# A/B: all per-segment s_setprio flips deleted from the GEMM K-loops and their peeled first trips (barrier structure untouched)
# speedup vs baseline: 1.0067x; 1.0067x over previous
; #define PG8_STAGE(bufoff, gbase, o0, o1) do { \
;         __builtin_amdgcn_global_load_lds((const unsigned*)((const char*)(gbase) + (o0)), (LAS unsigned*)(lds + (bufoff) + ldsw), 16, 0, 0); \
;         __builtin_amdgcn_global_load_lds((const unsigned*)((const char*)(gbase) + (o1)), (LAS unsigned*)(lds + (bufoff) + ldsw + 8192), 16, 0, 0); } while (0)
; #define PG8_LDA(dst, b, h) do { _Pragma("unroll") for (int m = 0; m < 4; ++m) _Pragma("unroll") for (int k = 0; k < 2; ++k) dst[m][k] = *(const LAS bf16x8*)(lds + PG8_SA(b, h) + aoff + m * 2048 + k * 1024); } while (0)
; template <class Epi, class Sched, class Prob>
; __device__ __forceinline__ void gemm_phase(LAS unsigned char* lds, LAS unsigned char* lds_epi, const Prob g, const Sched& S, const Epi& E, int wid) {
;     ...
;         const bool has_next = S.next(ui + 1, nxt);
;         const char* nA = has_next ? g.a_base(nxt) : cA; const char* nB = has_next ? g.b_base(nxt) : cB;
; _Pragma("clang loop unroll(disable)")
;         for (int t = 0; t < nt; t += 2) {
;             const bool last = (t == nt - 2);
;             const char* a1 = cA + (size_t)(t + 1) * kstep;
;             const char* a2 = last ? nA : cA + (size_t)(t + 2) * kstep; const char* b2 = last ? nB : cB + (size_t)(t + 2) * kstep;
;             const char* a3 = a2 + kstep; const char* b3 = b2 + kstep;
;             PG8_LDB(B0, 0, 0); PG8_LDB(B1, 0, 1); PG8_SCHED; PG8_LDA(At, 0, 0); PG8_STAGE(PG8_SA(1, 1), a1, cA10, cA11);
;             PG8_WAIT_V(8); PG8_WAIT_L(0); PG8_BAR; PG8_MMA(0, 0, At, B0); PG8_MMA(0, 1, At, B1); PG8_BAR; PG8_SCHED;
;             PG8_LDA(At, 0, 1); PG8_STAGE(PG8_SB(0, 0), b2, vB0, vB1); PG8_STAGE(PG8_SB(0, 1), b2 + hstepB, vB0, vB1); PG8_STAGE(PG8_SA(0, 0), a2, cA00, cA01);
;             PG8_WAIT_V(8); PG8_WAIT_L(0); PG8_BAR; PG8_MMA(1, 0, At, B0); PG8_MMA(1, 1, At, B1); PG8_BAR; PG8_SCHED;
;             PG8_LDB(B0, 1, 0); PG8_LDB(B1, 1, 1); PG8_SCHED; PG8_LDA(At, 1, 0); PG8_STAGE(PG8_SA(0, 1), a2, cA10, cA11);
;             PG8_WAIT_V(8); PG8_WAIT_L(0); PG8_BAR; PG8_MMA(0, 0, At, B0); PG8_MMA(0, 1, At, B1); PG8_BAR; PG8_SCHED;
;             PG8_LDA(At, 1, 1); PG8_STAGE(PG8_SB(1, 0), b3, vB0, vB1); PG8_STAGE(PG8_SB(1, 1), b3 + hstepB, vB0, vB1); PG8_STAGE(PG8_SA(1, 0), a3, cA00, cA01);
;             PG8_WAIT_V(8); PG8_WAIT_L(0); PG8_BAR; PG8_MMA(1, 0, At, B0); PG8_MMA(1, 1, At, B1); PG8_BAR; PG8_SCHED;
.LBB0_261:
	s_ashr_i32 s3, s2, 31
	s_lshl_b64 s[48:49], s[2:3], 20
	s_add_u32 s48, s33, s48
	s_addc_u32 s49, s39, s49
	s_and_b64 s[50:51], s[46:47], exec
	s_cselect_b32 s3, s49, s15
	s_cselect_b32 s77, s48, s14
	s_ashr_i32 s45, s44, 31
	s_lshl_b64 s[50:51], s[44:45], 20
	s_add_u32 s50, s56, s50
	s_addc_u32 s51, s57, s51
	s_and_b64 s[54:55], s[46:47], exec
	s_cselect_b32 s45, s51, s53
	s_cselect_b32 s78, s50, s52
	s_add_u32 s14, s14, 0x80
	s_addc_u32 s15, s15, 0
	s_add_u32 s79, s52, 0x100
	v_mov_b32_e32 v44, 0
	s_addc_u32 s80, s53, 0
	s_mov_b32 s81, -2
	v_add_u32_e32 v140, s72, v194
	v_add_u32_e32 v156, s73, v194
	ds_read_b128 v[128:131], v140
	ds_read_b128 v[132:135], v140 offset:1024
	ds_read_b128 v[136:139], v140 offset:2048
	ds_read_b128 v[140:143], v140 offset:3072
	ds_read_b128 v[174:177], v156
	ds_read_b128 v[178:181], v156 offset:1024
	ds_read_b128 v[182:185], v156 offset:2048
	ds_read_b128 v[186:189], v156 offset:3072
	s_add_u32 s52, s14, 0x80
	s_addc_u32 s53, s15, 0
	s_cmp_eq_u32 s81, 28
	s_cselect_b32 s55, s3, s53
	s_cselect_b32 s54, s77, s52
	s_cselect_b32 s53, s45, s80
	s_cselect_b32 s52, s78, s79
	v_lshl_add_u64 v[190:191], s[14:15], 0, v[170:171]
	s_add_i32 m0, s25, 0xc000
	ds_read_b128 v[208:211], v204
	ds_read_b128 v[212:215], v204 offset:1024
	ds_read_b128 v[216:219], v204 offset:2048
	ds_read_b128 v[220:223], v204 offset:3072
	ds_read_b128 v[224:227], v204 offset:4096
	ds_read_b128 v[228:231], v204 offset:5120
	ds_read_b128 v[232:235], v204 offset:6144
	ds_read_b128 v[238:241], v204 offset:7168
	global_load_lds_dwordx4 v[190:191], off
	v_lshl_add_u64 v[190:191], s[14:15], 0, v[168:169]
	s_add_i32 m0, s25, 0xe000
	s_nop 0
	global_load_lds_dwordx4 v[190:191], off
	s_waitcnt vmcnt(8)
	s_waitcnt lgkmcnt(0)
	s_barrier
	s_waitcnt lgkmcnt(0)
	v_mfma_f32_16x16x32_bf16 v[80:83], v[128:131], v[208:211], 0
	v_mfma_f32_16x16x32_bf16 v[92:95], v[136:139], v[208:211], 0
	v_mfma_f32_16x16x32_bf16 v[52:55], v[128:131], v[216:219], 0
	v_mfma_f32_16x16x32_bf16 v[68:71], v[136:139], v[216:219], 0
	v_mfma_f32_16x16x32_bf16 v[28:31], v[128:131], v[224:227], 0
	v_mfma_f32_16x16x32_bf16 v[36:39], v[136:139], v[224:227], 0
	v_mfma_f32_16x16x32_bf16 v[8:11], v[128:131], v[232:235], 0
	v_mfma_f32_16x16x32_bf16 v[16:19], v[136:139], v[232:235], 0
	v_mfma_f32_16x16x32_bf16 v[80:83], v[132:135], v[212:215], v[80:83]
	v_mfma_f32_16x16x32_bf16 v[92:95], v[140:143], v[212:215], v[92:95]
	v_mfma_f32_16x16x32_bf16 v[52:55], v[132:135], v[220:223], v[52:55]
	v_mfma_f32_16x16x32_bf16 v[68:71], v[140:143], v[220:223], v[68:71]
	v_mfma_f32_16x16x32_bf16 v[28:31], v[132:135], v[228:231], v[28:31]
	v_mfma_f32_16x16x32_bf16 v[36:39], v[140:143], v[228:231], v[36:39]
	v_mfma_f32_16x16x32_bf16 v[8:11], v[132:135], v[238:241], v[8:11]
	v_mfma_f32_16x16x32_bf16 v[16:19], v[140:143], v[238:241], v[16:19]
	v_mfma_f32_16x16x32_bf16 v[120:123], v[174:177], v[208:211], 0
	v_mfma_f32_16x16x32_bf16 v[124:127], v[182:185], v[208:211], 0
	v_mfma_f32_16x16x32_bf16 v[104:107], v[174:177], v[216:219], 0
	v_mfma_f32_16x16x32_bf16 v[112:115], v[182:185], v[216:219], 0
	v_mfma_f32_16x16x32_bf16 v[84:87], v[174:177], v[224:227], 0
	v_mfma_f32_16x16x32_bf16 v[96:99], v[182:185], v[224:227], 0
	v_mfma_f32_16x16x32_bf16 v[48:51], v[174:177], v[232:235], 0
	v_mfma_f32_16x16x32_bf16 v[64:67], v[182:185], v[232:235], 0
	v_mfma_f32_16x16x32_bf16 v[120:123], v[178:181], v[212:215], v[120:123]
	v_mfma_f32_16x16x32_bf16 v[124:127], v[186:189], v[212:215], v[124:127]
	v_mfma_f32_16x16x32_bf16 v[104:107], v[178:181], v[220:223], v[104:107]
	v_mfma_f32_16x16x32_bf16 v[112:115], v[186:189], v[220:223], v[112:115]
	v_mfma_f32_16x16x32_bf16 v[84:87], v[178:181], v[228:231], v[84:87]
	v_mfma_f32_16x16x32_bf16 v[96:99], v[186:189], v[228:231], v[96:99]
	v_mfma_f32_16x16x32_bf16 v[48:51], v[178:181], v[238:241], v[48:51]
	v_mfma_f32_16x16x32_bf16 v[64:67], v[186:189], v[238:241], v[64:67]
	s_barrier
	s_add_i32 s82, s72, s97
	v_lshl_add_u64 v[190:191], s[52:53], 0, v[144:145]
	s_mov_b32 m0, s82
	ds_read_b128 v[208:211], v204 offset:16384
	ds_read_b128 v[212:215], v204 offset:17408
	ds_read_b128 v[216:219], v204 offset:18432
	ds_read_b128 v[220:223], v204 offset:19456
	ds_read_b128 v[224:227], v204 offset:20480
	ds_read_b128 v[228:231], v204 offset:21504
	ds_read_b128 v[232:235], v204 offset:22528
	ds_read_b128 v[238:241], v204 offset:23552
	global_load_lds_dwordx4 v[190:191], off
	s_add_i32 m0, s82, 0x2000
	s_add_u32 s82, s52, 0x80000
	v_lshl_add_u64 v[236:237], s[52:53], 0, v[146:147]
	s_addc_u32 s83, s53, 0
	s_add_i32 s84, s73, s97
	global_load_lds_dwordx4 v[236:237], off
	v_lshl_add_u64 v[242:243], s[82:83], 0, v[144:145]
	s_mov_b32 m0, s84
	v_lshl_add_u64 v[244:245], s[54:55], 0, v[152:153]
	global_load_lds_dwordx4 v[242:243], off
	v_lshl_add_u64 v[242:243], s[82:83], 0, v[146:147]
	s_add_i32 m0, s84, 0x2000
	s_nop 0
	global_load_lds_dwordx4 v[242:243], off
	v_lshl_add_u64 v[242:243], s[54:55], 0, v[148:149]
	s_mov_b32 m0, s25
	s_nop 0
	global_load_lds_dwordx4 v[242:243], off
	s_mov_b32 m0, s58
	s_nop 0
	global_load_lds_dwordx4 v[244:245], off
	s_waitcnt vmcnt(8)
	s_waitcnt lgkmcnt(0)
	s_barrier
; #define PG8_STAGE(bufoff, gbase, o0, o1) do { \
;         __builtin_amdgcn_global_load_lds((const unsigned*)((const char*)(gbase) + (o0)), (LAS unsigned*)(lds + (bufoff) + ldsw), 16, 0, 0); \
;         __builtin_amdgcn_global_load_lds((const unsigned*)((const char*)(gbase) + (o1)), (LAS unsigned*)(lds + (bufoff) + ldsw + 8192), 16, 0, 0); } while (0)
; #define PG8_LDA(dst, b, h) do { _Pragma("unroll") for (int m = 0; m < 4; ++m) _Pragma("unroll") for (int k = 0; k < 2; ++k) dst[m][k] = *(const LAS bf16x8*)(lds + PG8_SA(b, h) + aoff + m * 2048 + k * 1024); } while (0)
; #define PG8_LDB(dst, b, h) do { _Pragma("unroll") for (int n = 0; n < 2; ++n) _Pragma("unroll") for (int k = 0; k < 2; ++k) dst[n][k] = *(const LAS bf16x8*)(lds + PG8_SB(b, h) + boff + n * 2048 + k * 1024); } while (0)
; template <class Epi, class Sched, class Prob>
; __device__ __forceinline__ void gemm_phase(LAS unsigned char* lds, LAS unsigned char* lds_epi, const Prob g, const Sched& S, const Epi& E, int wid) {
;     ...
;         for (int t = 0; t < nt; t += 2) {
;             const bool last = (t == nt - 2);
;             const char* a1 = cA + (size_t)(t + 1) * kstep;
;             const char* a2 = last ? nA : cA + (size_t)(t + 2) * kstep; const char* b2 = last ? nB : cB + (size_t)(t + 2) * kstep;
;             const char* a3 = a2 + kstep; const char* b3 = b2 + kstep;
;             PG8_LDB(B0, 0, 0); PG8_LDB(B1, 0, 1); PG8_SCHED; PG8_LDA(At, 0, 0); PG8_STAGE(PG8_SA(1, 1), a1, cA10, cA11);
;             PG8_WAIT_V(8); PG8_WAIT_L(0); PG8_BAR; PG8_MMA(0, 0, At, B0); PG8_MMA(0, 1, At, B1); PG8_BAR; PG8_SCHED;
;             PG8_LDA(At, 0, 1); PG8_STAGE(PG8_SB(0, 0), b2, vB0, vB1); PG8_STAGE(PG8_SB(0, 1), b2 + hstepB, vB0, vB1); PG8_STAGE(PG8_SA(0, 0), a2, cA00, cA01);
;             PG8_WAIT_V(8); PG8_WAIT_L(0); PG8_BAR; PG8_MMA(1, 0, At, B0); PG8_MMA(1, 1, At, B1); PG8_BAR; PG8_SCHED;
;             PG8_LDB(B0, 1, 0); PG8_LDB(B1, 1, 1); PG8_SCHED; PG8_LDA(At, 1, 0); PG8_STAGE(PG8_SA(0, 1), a2, cA10, cA11);
;             PG8_WAIT_V(8); PG8_WAIT_L(0); PG8_BAR; PG8_MMA(0, 0, At, B0); PG8_MMA(0, 1, At, B1); PG8_BAR; PG8_SCHED;
;             PG8_LDA(At, 1, 1); PG8_STAGE(PG8_SB(1, 0), b3, vB0, vB1); PG8_STAGE(PG8_SB(1, 1), b3 + hstepB, vB0, vB1); PG8_STAGE(PG8_SA(1, 0), a3, cA00, cA01);
;             PG8_WAIT_V(8); PG8_WAIT_L(0); PG8_BAR; PG8_MMA(1, 0, At, B0); PG8_MMA(1, 1, At, B1); PG8_BAR; PG8_SCHED;
	s_waitcnt lgkmcnt(0)
	v_mfma_f32_16x16x32_bf16 v[56:59], v[128:131], v[208:211], 0
	v_mfma_f32_16x16x32_bf16 v[72:75], v[136:139], v[208:211], 0
	v_mfma_f32_16x16x32_bf16 v[32:35], v[128:131], v[216:219], 0
	v_mfma_f32_16x16x32_bf16 v[40:43], v[136:139], v[216:219], 0
	v_mfma_f32_16x16x32_bf16 v[12:15], v[128:131], v[224:227], 0
	v_mfma_f32_16x16x32_bf16 v[20:23], v[136:139], v[224:227], 0
	v_mfma_f32_16x16x32_bf16 v[0:3], v[128:131], v[232:235], 0
	v_mfma_f32_16x16x32_bf16 v[4:7], v[136:139], v[232:235], 0
	v_mfma_f32_16x16x32_bf16 v[56:59], v[132:135], v[212:215], v[56:59]
	v_mfma_f32_16x16x32_bf16 v[72:75], v[140:143], v[212:215], v[72:75]
	v_mfma_f32_16x16x32_bf16 v[32:35], v[132:135], v[220:223], v[32:35]
	v_mfma_f32_16x16x32_bf16 v[40:43], v[140:143], v[220:223], v[40:43]
	v_mfma_f32_16x16x32_bf16 v[12:15], v[132:135], v[228:231], v[12:15]
	v_mfma_f32_16x16x32_bf16 v[20:23], v[140:143], v[228:231], v[20:23]
	v_mfma_f32_16x16x32_bf16 v[0:3], v[132:135], v[238:241], v[0:3]
	v_mfma_f32_16x16x32_bf16 v[4:7], v[140:143], v[238:241], v[4:7]
	v_mfma_f32_16x16x32_bf16 v[108:111], v[174:177], v[208:211], 0
	v_mfma_f32_16x16x32_bf16 v[116:119], v[182:185], v[208:211], 0
	v_mfma_f32_16x16x32_bf16 v[88:91], v[174:177], v[216:219], 0
	v_mfma_f32_16x16x32_bf16 v[100:103], v[182:185], v[216:219], 0
	v_mfma_f32_16x16x32_bf16 v[60:63], v[174:177], v[224:227], 0
	v_mfma_f32_16x16x32_bf16 v[76:79], v[182:185], v[224:227], 0
	v_mfma_f32_16x16x32_bf16 v[24:27], v[174:177], v[232:235], 0
	v_mfma_f32_16x16x32_bf16 v[44:47], v[182:185], v[232:235], 0
	v_mfma_f32_16x16x32_bf16 v[108:111], v[178:181], v[212:215], v[108:111]
	v_mfma_f32_16x16x32_bf16 v[116:119], v[186:189], v[212:215], v[116:119]
	v_mfma_f32_16x16x32_bf16 v[88:91], v[178:181], v[220:223], v[88:91]
	v_mfma_f32_16x16x32_bf16 v[100:103], v[186:189], v[220:223], v[100:103]
	v_mfma_f32_16x16x32_bf16 v[60:63], v[178:181], v[228:231], v[60:63]
	v_mfma_f32_16x16x32_bf16 v[76:79], v[186:189], v[228:231], v[76:79]
	v_mfma_f32_16x16x32_bf16 v[24:27], v[178:181], v[238:241], v[24:27]
	v_mfma_f32_16x16x32_bf16 v[44:47], v[186:189], v[238:241], v[44:47]
	s_barrier
	s_add_i32 s82, 0, 0x18000
	s_add_i32 s83, 0, 0x1c000
	v_add_u32_e32 v140, s82, v194
	v_add_u32_e32 v156, s83, v194
	ds_read_b128 v[128:131], v140
	ds_read_b128 v[132:135], v140 offset:1024
	ds_read_b128 v[136:139], v140 offset:2048
	ds_read_b128 v[140:143], v140 offset:3072
	ds_read_b128 v[174:177], v156
	ds_read_b128 v[178:181], v156 offset:1024
	ds_read_b128 v[182:185], v156 offset:2048
	ds_read_b128 v[186:189], v156 offset:3072
	s_mov_b32 m0, s59
	v_lshl_add_u64 v[246:247], s[54:55], 0, v[150:151]
	ds_read_b128 v[208:211], v204 offset:32768
	ds_read_b128 v[212:215], v204 offset:33792
	ds_read_b128 v[216:219], v204 offset:34816
	ds_read_b128 v[220:223], v204 offset:35840
	ds_read_b128 v[224:227], v204 offset:36864
	ds_read_b128 v[228:231], v204 offset:37888
	ds_read_b128 v[232:235], v204 offset:38912
	ds_read_b128 v[238:241], v204 offset:39936
	global_load_lds_dwordx4 v[246:247], off
	v_lshl_add_u64 v[246:247], s[54:55], 0, v[154:155]
	s_mov_b32 m0, s60
	s_nop 0
	global_load_lds_dwordx4 v[246:247], off
	s_waitcnt vmcnt(8)
	s_waitcnt lgkmcnt(0)
	s_barrier
	s_waitcnt lgkmcnt(0)
	v_mfma_f32_16x16x32_bf16 v[80:83], v[128:131], v[208:211], v[80:83]
	v_mfma_f32_16x16x32_bf16 v[92:95], v[136:139], v[208:211], v[92:95]
	v_mfma_f32_16x16x32_bf16 v[52:55], v[128:131], v[216:219], v[52:55]
	v_mfma_f32_16x16x32_bf16 v[68:71], v[136:139], v[216:219], v[68:71]
	v_mfma_f32_16x16x32_bf16 v[28:31], v[128:131], v[224:227], v[28:31]
	v_mfma_f32_16x16x32_bf16 v[36:39], v[136:139], v[224:227], v[36:39]
	v_mfma_f32_16x16x32_bf16 v[8:11], v[128:131], v[232:235], v[8:11]
	v_mfma_f32_16x16x32_bf16 v[16:19], v[136:139], v[232:235], v[16:19]
	v_mfma_f32_16x16x32_bf16 v[80:83], v[132:135], v[212:215], v[80:83]
	v_mfma_f32_16x16x32_bf16 v[92:95], v[140:143], v[212:215], v[92:95]
	v_mfma_f32_16x16x32_bf16 v[52:55], v[132:135], v[220:223], v[52:55]
	v_mfma_f32_16x16x32_bf16 v[68:71], v[140:143], v[220:223], v[68:71]
	v_mfma_f32_16x16x32_bf16 v[28:31], v[132:135], v[228:231], v[28:31]
	v_mfma_f32_16x16x32_bf16 v[36:39], v[140:143], v[228:231], v[36:39]
	v_mfma_f32_16x16x32_bf16 v[8:11], v[132:135], v[238:241], v[8:11]
	v_mfma_f32_16x16x32_bf16 v[16:19], v[140:143], v[238:241], v[16:19]
	v_mfma_f32_16x16x32_bf16 v[120:123], v[174:177], v[208:211], v[120:123]
	v_mfma_f32_16x16x32_bf16 v[124:127], v[182:185], v[208:211], v[124:127]
	v_mfma_f32_16x16x32_bf16 v[104:107], v[174:177], v[216:219], v[104:107]
	v_mfma_f32_16x16x32_bf16 v[112:115], v[182:185], v[216:219], v[112:115]
	v_mfma_f32_16x16x32_bf16 v[84:87], v[174:177], v[224:227], v[84:87]
	v_mfma_f32_16x16x32_bf16 v[96:99], v[182:185], v[224:227], v[96:99]
	v_mfma_f32_16x16x32_bf16 v[48:51], v[174:177], v[232:235], v[48:51]
	v_mfma_f32_16x16x32_bf16 v[64:67], v[182:185], v[232:235], v[64:67]
	v_mfma_f32_16x16x32_bf16 v[120:123], v[178:181], v[212:215], v[120:123]
	v_mfma_f32_16x16x32_bf16 v[124:127], v[186:189], v[212:215], v[124:127]
	v_mfma_f32_16x16x32_bf16 v[104:107], v[178:181], v[220:223], v[104:107]
	v_mfma_f32_16x16x32_bf16 v[112:115], v[186:189], v[220:223], v[112:115]
	v_mfma_f32_16x16x32_bf16 v[84:87], v[178:181], v[228:231], v[84:87]
	v_mfma_f32_16x16x32_bf16 v[96:99], v[186:189], v[228:231], v[96:99]
	v_mfma_f32_16x16x32_bf16 v[48:51], v[178:181], v[238:241], v[48:51]
	v_mfma_f32_16x16x32_bf16 v[64:67], v[186:189], v[238:241], v[64:67]
	s_barrier
; #define PG8_STAGE(bufoff, gbase, o0, o1) do { \
;         __builtin_amdgcn_global_load_lds((const unsigned*)((const char*)(gbase) + (o0)), (LAS unsigned*)(lds + (bufoff) + ldsw), 16, 0, 0); \
;         __builtin_amdgcn_global_load_lds((const unsigned*)((const char*)(gbase) + (o1)), (LAS unsigned*)(lds + (bufoff) + ldsw + 8192), 16, 0, 0); } while (0)
; #define PG8_LDA(dst, b, h) do { _Pragma("unroll") for (int m = 0; m < 4; ++m) _Pragma("unroll") for (int k = 0; k < 2; ++k) dst[m][k] = *(const LAS bf16x8*)(lds + PG8_SA(b, h) + aoff + m * 2048 + k * 1024); } while (0)
; #define PG8_LDB(dst, b, h) do { _Pragma("unroll") for (int n = 0; n < 2; ++n) _Pragma("unroll") for (int k = 0; k < 2; ++k) dst[n][k] = *(const LAS bf16x8*)(lds + PG8_SB(b, h) + boff + n * 2048 + k * 1024); } while (0)
; template <class Epi, class Sched, class Prob>
; __device__ __forceinline__ void gemm_phase(LAS unsigned char* lds, LAS unsigned char* lds_epi, const Prob g, const Sched& S, const Epi& E, int wid) {
;     ...
;         for (int t = 0; t < nt; t += 2) {
;             const bool last = (t == nt - 2);
;             const char* a1 = cA + (size_t)(t + 1) * kstep;
;             const char* a2 = last ? nA : cA + (size_t)(t + 2) * kstep; const char* b2 = last ? nB : cB + (size_t)(t + 2) * kstep;
;             const char* a3 = a2 + kstep; const char* b3 = b2 + kstep;
;             PG8_LDB(B0, 0, 0); PG8_LDB(B1, 0, 1); PG8_SCHED; PG8_LDA(At, 0, 0); PG8_STAGE(PG8_SA(1, 1), a1, cA10, cA11);
;             PG8_WAIT_V(8); PG8_WAIT_L(0); PG8_BAR; PG8_MMA(0, 0, At, B0); PG8_MMA(0, 1, At, B1); PG8_BAR; PG8_SCHED;
;             PG8_LDA(At, 0, 1); PG8_STAGE(PG8_SB(0, 0), b2, vB0, vB1); PG8_STAGE(PG8_SB(0, 1), b2 + hstepB, vB0, vB1); PG8_STAGE(PG8_SA(0, 0), a2, cA00, cA01);
;             PG8_WAIT_V(8); PG8_WAIT_L(0); PG8_BAR; PG8_MMA(1, 0, At, B0); PG8_MMA(1, 1, At, B1); PG8_BAR; PG8_SCHED;
;             PG8_LDB(B0, 1, 0); PG8_LDB(B1, 1, 1); PG8_SCHED; PG8_LDA(At, 1, 0); PG8_STAGE(PG8_SA(0, 1), a2, cA10, cA11);
;             PG8_WAIT_V(8); PG8_WAIT_L(0); PG8_BAR; PG8_MMA(0, 0, At, B0); PG8_MMA(0, 1, At, B1); PG8_BAR; PG8_SCHED;
;             PG8_LDA(At, 1, 1); PG8_STAGE(PG8_SB(1, 0), b3, vB0, vB1); PG8_STAGE(PG8_SB(1, 1), b3 + hstepB, vB0, vB1); PG8_STAGE(PG8_SA(1, 0), a3, cA00, cA01);
;             PG8_WAIT_V(8); PG8_WAIT_L(0); PG8_BAR; PG8_MMA(1, 0, At, B0); PG8_MMA(1, 1, At, B1); PG8_BAR; PG8_SCHED;
	s_add_i32 s54, s82, s97
	v_lshl_add_u64 v[190:191], v[190:191], 0, s[20:21]
	s_mov_b32 m0, s54
	ds_read_b128 v[208:211], v204 offset:49152
	ds_read_b128 v[212:215], v204 offset:50176
	ds_read_b128 v[216:219], v204 offset:51200
	ds_read_b128 v[220:223], v204 offset:52224
	ds_read_b128 v[224:227], v204 offset:53248
	ds_read_b128 v[228:231], v204 offset:54272
	ds_read_b128 v[232:235], v204 offset:55296
	ds_read_b128 v[238:241], v204 offset:56320
	global_load_lds_dwordx4 v[190:191], off
	s_add_i32 m0, s54, 0x2000
	s_add_u32 s52, s52, 0x80080
	v_lshl_add_u64 v[190:191], v[236:237], 0, s[20:21]
	s_addc_u32 s53, s53, 0
	s_add_i32 s54, s83, s97
	global_load_lds_dwordx4 v[190:191], off
	v_lshl_add_u64 v[190:191], s[52:53], 0, v[144:145]
	s_mov_b32 m0, s54
	s_nop 0
	global_load_lds_dwordx4 v[190:191], off
	v_lshl_add_u64 v[190:191], s[52:53], 0, v[146:147]
	s_add_i32 m0, s54, 0x2000
	s_nop 0
	global_load_lds_dwordx4 v[190:191], off
	v_lshl_add_u64 v[190:191], v[242:243], 0, s[20:21]
	s_mov_b32 m0, s70
	s_nop 0
	global_load_lds_dwordx4 v[190:191], off
	v_lshl_add_u64 v[190:191], v[244:245], 0, s[20:21]
	s_mov_b32 m0, s71
	s_nop 0
	global_load_lds_dwordx4 v[190:191], off
	s_waitcnt vmcnt(8)
	s_waitcnt lgkmcnt(0)
	s_barrier
	s_waitcnt lgkmcnt(0)
	v_mfma_f32_16x16x32_bf16 v[56:59], v[128:131], v[208:211], v[56:59]
	v_mfma_f32_16x16x32_bf16 v[72:75], v[136:139], v[208:211], v[72:75]
	v_mfma_f32_16x16x32_bf16 v[32:35], v[128:131], v[216:219], v[32:35]
	v_mfma_f32_16x16x32_bf16 v[40:43], v[136:139], v[216:219], v[40:43]
	v_mfma_f32_16x16x32_bf16 v[12:15], v[128:131], v[224:227], v[12:15]
	v_mfma_f32_16x16x32_bf16 v[20:23], v[136:139], v[224:227], v[20:23]
	v_mfma_f32_16x16x32_bf16 v[0:3], v[128:131], v[232:235], v[0:3]
	v_mfma_f32_16x16x32_bf16 v[4:7], v[136:139], v[232:235], v[4:7]
	v_mfma_f32_16x16x32_bf16 v[56:59], v[132:135], v[212:215], v[56:59]
	v_mfma_f32_16x16x32_bf16 v[72:75], v[140:143], v[212:215], v[72:75]
	v_mfma_f32_16x16x32_bf16 v[32:35], v[132:135], v[220:223], v[32:35]
	v_mfma_f32_16x16x32_bf16 v[40:43], v[140:143], v[220:223], v[40:43]
	v_mfma_f32_16x16x32_bf16 v[12:15], v[132:135], v[228:231], v[12:15]
	v_mfma_f32_16x16x32_bf16 v[20:23], v[140:143], v[228:231], v[20:23]
	v_mfma_f32_16x16x32_bf16 v[0:3], v[132:135], v[238:241], v[0:3]
	v_mfma_f32_16x16x32_bf16 v[4:7], v[140:143], v[238:241], v[4:7]
	v_mfma_f32_16x16x32_bf16 v[108:111], v[174:177], v[208:211], v[108:111]
	v_mfma_f32_16x16x32_bf16 v[116:119], v[182:185], v[208:211], v[116:119]
	v_mfma_f32_16x16x32_bf16 v[88:91], v[174:177], v[216:219], v[88:91]
	v_mfma_f32_16x16x32_bf16 v[100:103], v[182:185], v[216:219], v[100:103]
	v_mfma_f32_16x16x32_bf16 v[60:63], v[174:177], v[224:227], v[60:63]
	v_mfma_f32_16x16x32_bf16 v[76:79], v[182:185], v[224:227], v[76:79]
	v_mfma_f32_16x16x32_bf16 v[24:27], v[174:177], v[232:235], v[24:27]
	v_mfma_f32_16x16x32_bf16 v[44:47], v[182:185], v[232:235], v[44:47]
	v_mfma_f32_16x16x32_bf16 v[108:111], v[178:181], v[212:215], v[108:111]
	v_mfma_f32_16x16x32_bf16 v[116:119], v[186:189], v[212:215], v[116:119]
	v_mfma_f32_16x16x32_bf16 v[88:91], v[178:181], v[220:223], v[88:91]
	v_mfma_f32_16x16x32_bf16 v[100:103], v[186:189], v[220:223], v[100:103]
	v_mfma_f32_16x16x32_bf16 v[60:63], v[178:181], v[228:231], v[60:63]
	v_mfma_f32_16x16x32_bf16 v[76:79], v[186:189], v[228:231], v[76:79]
	v_mfma_f32_16x16x32_bf16 v[24:27], v[178:181], v[238:241], v[24:27]
	v_mfma_f32_16x16x32_bf16 v[44:47], v[186:189], v[238:241], v[44:47]
	s_barrier
	s_add_i32 s81, s81, 2
	s_add_u32 s14, s14, 0x100
	s_addc_u32 s15, s15, 0
	s_add_u32 s79, s79, 0x100
	s_addc_u32 s80, s80, 0
	s_cmp_gt_u32 s81, 29
.LBB0_262:
	v_add_u32_e32 v140, s72, v194
	v_add_u32_e32 v156, s73, v194
	ds_read_b128 v[128:131], v140
	ds_read_b128 v[132:135], v140 offset:1024
	ds_read_b128 v[136:139], v140 offset:2048
	ds_read_b128 v[140:143], v140 offset:3072
	ds_read_b128 v[174:177], v156
	ds_read_b128 v[178:181], v156 offset:1024
	ds_read_b128 v[182:185], v156 offset:2048
	ds_read_b128 v[186:189], v156 offset:3072
	s_add_u32 s52, s14, 0x80
	s_addc_u32 s53, s15, 0
	s_cmp_eq_u32 s81, 28
	s_cselect_b32 s55, s3, s53
	s_cselect_b32 s54, s77, s52
	s_cselect_b32 s53, s45, s80
	s_cselect_b32 s52, s78, s79
	v_lshl_add_u64 v[190:191], s[14:15], 0, v[170:171]
	s_add_i32 m0, s25, 0xc000
	ds_read_b128 v[208:211], v204
	ds_read_b128 v[212:215], v204 offset:1024
	ds_read_b128 v[216:219], v204 offset:2048
	ds_read_b128 v[220:223], v204 offset:3072
	ds_read_b128 v[224:227], v204 offset:4096
	ds_read_b128 v[228:231], v204 offset:5120
	ds_read_b128 v[232:235], v204 offset:6144
	ds_read_b128 v[238:241], v204 offset:7168
	global_load_lds_dwordx4 v[190:191], off
	v_lshl_add_u64 v[190:191], s[14:15], 0, v[168:169]
	s_add_i32 m0, s25, 0xe000
	s_nop 0
	global_load_lds_dwordx4 v[190:191], off
	s_waitcnt vmcnt(8)
	s_waitcnt lgkmcnt(0)
	s_barrier
; #define PG8_STAGE(bufoff, gbase, o0, o1) do { \
;         __builtin_amdgcn_global_load_lds((const unsigned*)((const char*)(gbase) + (o0)), (LAS unsigned*)(lds + (bufoff) + ldsw), 16, 0, 0); \
;         __builtin_amdgcn_global_load_lds((const unsigned*)((const char*)(gbase) + (o1)), (LAS unsigned*)(lds + (bufoff) + ldsw + 8192), 16, 0, 0); } while (0)
; #define PG8_LDA(dst, b, h) do { _Pragma("unroll") for (int m = 0; m < 4; ++m) _Pragma("unroll") for (int k = 0; k < 2; ++k) dst[m][k] = *(const LAS bf16x8*)(lds + PG8_SA(b, h) + aoff + m * 2048 + k * 1024); } while (0)
; #define PG8_LDB(dst, b, h) do { _Pragma("unroll") for (int n = 0; n < 2; ++n) _Pragma("unroll") for (int k = 0; k < 2; ++k) dst[n][k] = *(const LAS bf16x8*)(lds + PG8_SB(b, h) + boff + n * 2048 + k * 1024); } while (0)
; template <class Epi, class Sched, class Prob>
; __device__ __forceinline__ void gemm_phase(LAS unsigned char* lds, LAS unsigned char* lds_epi, const Prob g, const Sched& S, const Epi& E, int wid) {
;     ...
;         for (int t = 0; t < nt; t += 2) {
;             const bool last = (t == nt - 2);
;             const char* a1 = cA + (size_t)(t + 1) * kstep;
;             const char* a2 = last ? nA : cA + (size_t)(t + 2) * kstep; const char* b2 = last ? nB : cB + (size_t)(t + 2) * kstep;
;             const char* a3 = a2 + kstep; const char* b3 = b2 + kstep;
;             PG8_LDB(B0, 0, 0); PG8_LDB(B1, 0, 1); PG8_SCHED; PG8_LDA(At, 0, 0); PG8_STAGE(PG8_SA(1, 1), a1, cA10, cA11);
;             PG8_WAIT_V(8); PG8_WAIT_L(0); PG8_BAR; PG8_MMA(0, 0, At, B0); PG8_MMA(0, 1, At, B1); PG8_BAR; PG8_SCHED;
;             PG8_LDA(At, 0, 1); PG8_STAGE(PG8_SB(0, 0), b2, vB0, vB1); PG8_STAGE(PG8_SB(0, 1), b2 + hstepB, vB0, vB1); PG8_STAGE(PG8_SA(0, 0), a2, cA00, cA01);
;             PG8_WAIT_V(8); PG8_WAIT_L(0); PG8_BAR; PG8_MMA(1, 0, At, B0); PG8_MMA(1, 1, At, B1); PG8_BAR; PG8_SCHED;
;             PG8_LDB(B0, 1, 0); PG8_LDB(B1, 1, 1); PG8_SCHED; PG8_LDA(At, 1, 0); PG8_STAGE(PG8_SA(0, 1), a2, cA10, cA11);
;             PG8_WAIT_V(8); PG8_WAIT_L(0); PG8_BAR; PG8_MMA(0, 0, At, B0); PG8_MMA(0, 1, At, B1); PG8_BAR; PG8_SCHED;
;             PG8_LDA(At, 1, 1); PG8_STAGE(PG8_SB(1, 0), b3, vB0, vB1); PG8_STAGE(PG8_SB(1, 1), b3 + hstepB, vB0, vB1); PG8_STAGE(PG8_SA(1, 0), a3, cA00, cA01);
;             PG8_WAIT_V(8); PG8_WAIT_L(0); PG8_BAR; PG8_MMA(1, 0, At, B0); PG8_MMA(1, 1, At, B1); PG8_BAR; PG8_SCHED;
	s_waitcnt lgkmcnt(0)
	v_mfma_f32_16x16x32_bf16 v[80:83], v[128:131], v[208:211], v[80:83]
	v_mfma_f32_16x16x32_bf16 v[92:95], v[136:139], v[208:211], v[92:95]
	v_mfma_f32_16x16x32_bf16 v[52:55], v[128:131], v[216:219], v[52:55]
	v_mfma_f32_16x16x32_bf16 v[68:71], v[136:139], v[216:219], v[68:71]
	v_mfma_f32_16x16x32_bf16 v[28:31], v[128:131], v[224:227], v[28:31]
	v_mfma_f32_16x16x32_bf16 v[36:39], v[136:139], v[224:227], v[36:39]
	v_mfma_f32_16x16x32_bf16 v[8:11], v[128:131], v[232:235], v[8:11]
	v_mfma_f32_16x16x32_bf16 v[16:19], v[136:139], v[232:235], v[16:19]
	v_mfma_f32_16x16x32_bf16 v[80:83], v[132:135], v[212:215], v[80:83]
	v_mfma_f32_16x16x32_bf16 v[92:95], v[140:143], v[212:215], v[92:95]
	v_mfma_f32_16x16x32_bf16 v[52:55], v[132:135], v[220:223], v[52:55]
	v_mfma_f32_16x16x32_bf16 v[68:71], v[140:143], v[220:223], v[68:71]
	v_mfma_f32_16x16x32_bf16 v[28:31], v[132:135], v[228:231], v[28:31]
	v_mfma_f32_16x16x32_bf16 v[36:39], v[140:143], v[228:231], v[36:39]
	v_mfma_f32_16x16x32_bf16 v[8:11], v[132:135], v[238:241], v[8:11]
	v_mfma_f32_16x16x32_bf16 v[16:19], v[140:143], v[238:241], v[16:19]
	v_mfma_f32_16x16x32_bf16 v[120:123], v[174:177], v[208:211], v[120:123]
	v_mfma_f32_16x16x32_bf16 v[124:127], v[182:185], v[208:211], v[124:127]
	v_mfma_f32_16x16x32_bf16 v[104:107], v[174:177], v[216:219], v[104:107]
	v_mfma_f32_16x16x32_bf16 v[112:115], v[182:185], v[216:219], v[112:115]
	v_mfma_f32_16x16x32_bf16 v[84:87], v[174:177], v[224:227], v[84:87]
	v_mfma_f32_16x16x32_bf16 v[96:99], v[182:185], v[224:227], v[96:99]
	v_mfma_f32_16x16x32_bf16 v[48:51], v[174:177], v[232:235], v[48:51]
	v_mfma_f32_16x16x32_bf16 v[64:67], v[182:185], v[232:235], v[64:67]
	v_mfma_f32_16x16x32_bf16 v[120:123], v[178:181], v[212:215], v[120:123]
	v_mfma_f32_16x16x32_bf16 v[124:127], v[186:189], v[212:215], v[124:127]
	v_mfma_f32_16x16x32_bf16 v[104:107], v[178:181], v[220:223], v[104:107]
	v_mfma_f32_16x16x32_bf16 v[112:115], v[186:189], v[220:223], v[112:115]
	v_mfma_f32_16x16x32_bf16 v[84:87], v[178:181], v[228:231], v[84:87]
	v_mfma_f32_16x16x32_bf16 v[96:99], v[186:189], v[228:231], v[96:99]
	v_mfma_f32_16x16x32_bf16 v[48:51], v[178:181], v[238:241], v[48:51]
	v_mfma_f32_16x16x32_bf16 v[64:67], v[186:189], v[238:241], v[64:67]
	s_barrier
	s_add_i32 s82, s72, s97
	v_lshl_add_u64 v[190:191], s[52:53], 0, v[144:145]
	s_mov_b32 m0, s82
	ds_read_b128 v[208:211], v204 offset:16384
	ds_read_b128 v[212:215], v204 offset:17408
	ds_read_b128 v[216:219], v204 offset:18432
	ds_read_b128 v[220:223], v204 offset:19456
	ds_read_b128 v[224:227], v204 offset:20480
	ds_read_b128 v[228:231], v204 offset:21504
	ds_read_b128 v[232:235], v204 offset:22528
	ds_read_b128 v[238:241], v204 offset:23552
	global_load_lds_dwordx4 v[190:191], off
	s_add_i32 m0, s82, 0x2000
	s_add_u32 s82, s52, 0x80000
	v_lshl_add_u64 v[236:237], s[52:53], 0, v[146:147]
	s_addc_u32 s83, s53, 0
	s_add_i32 s84, s73, s97
	global_load_lds_dwordx4 v[236:237], off
	v_lshl_add_u64 v[242:243], s[82:83], 0, v[144:145]
	s_mov_b32 m0, s84
	v_lshl_add_u64 v[244:245], s[54:55], 0, v[152:153]
	global_load_lds_dwordx4 v[242:243], off
	v_lshl_add_u64 v[242:243], s[82:83], 0, v[146:147]
	s_add_i32 m0, s84, 0x2000
	s_nop 0
	global_load_lds_dwordx4 v[242:243], off
	v_lshl_add_u64 v[242:243], s[54:55], 0, v[148:149]
	s_mov_b32 m0, s25
	s_nop 0
	global_load_lds_dwordx4 v[242:243], off
	s_mov_b32 m0, s58
	s_nop 0
	global_load_lds_dwordx4 v[244:245], off
	s_waitcnt vmcnt(8)
	s_waitcnt lgkmcnt(0)
	s_barrier
	s_waitcnt lgkmcnt(0)
	v_mfma_f32_16x16x32_bf16 v[56:59], v[128:131], v[208:211], v[56:59]
	v_mfma_f32_16x16x32_bf16 v[72:75], v[136:139], v[208:211], v[72:75]
	v_mfma_f32_16x16x32_bf16 v[32:35], v[128:131], v[216:219], v[32:35]
	v_mfma_f32_16x16x32_bf16 v[40:43], v[136:139], v[216:219], v[40:43]
	v_mfma_f32_16x16x32_bf16 v[12:15], v[128:131], v[224:227], v[12:15]
	v_mfma_f32_16x16x32_bf16 v[20:23], v[136:139], v[224:227], v[20:23]
	v_mfma_f32_16x16x32_bf16 v[0:3], v[128:131], v[232:235], v[0:3]
	v_mfma_f32_16x16x32_bf16 v[4:7], v[136:139], v[232:235], v[4:7]
	v_mfma_f32_16x16x32_bf16 v[56:59], v[132:135], v[212:215], v[56:59]
	v_mfma_f32_16x16x32_bf16 v[72:75], v[140:143], v[212:215], v[72:75]
	v_mfma_f32_16x16x32_bf16 v[32:35], v[132:135], v[220:223], v[32:35]
	v_mfma_f32_16x16x32_bf16 v[40:43], v[140:143], v[220:223], v[40:43]
	v_mfma_f32_16x16x32_bf16 v[12:15], v[132:135], v[228:231], v[12:15]
	v_mfma_f32_16x16x32_bf16 v[20:23], v[140:143], v[228:231], v[20:23]
	v_mfma_f32_16x16x32_bf16 v[0:3], v[132:135], v[238:241], v[0:3]
	v_mfma_f32_16x16x32_bf16 v[4:7], v[140:143], v[238:241], v[4:7]
	v_mfma_f32_16x16x32_bf16 v[108:111], v[174:177], v[208:211], v[108:111]
	v_mfma_f32_16x16x32_bf16 v[116:119], v[182:185], v[208:211], v[116:119]
	v_mfma_f32_16x16x32_bf16 v[88:91], v[174:177], v[216:219], v[88:91]
	v_mfma_f32_16x16x32_bf16 v[100:103], v[182:185], v[216:219], v[100:103]
	v_mfma_f32_16x16x32_bf16 v[60:63], v[174:177], v[224:227], v[60:63]
	v_mfma_f32_16x16x32_bf16 v[76:79], v[182:185], v[224:227], v[76:79]
	v_mfma_f32_16x16x32_bf16 v[24:27], v[174:177], v[232:235], v[24:27]
	v_mfma_f32_16x16x32_bf16 v[44:47], v[182:185], v[232:235], v[44:47]
	v_mfma_f32_16x16x32_bf16 v[108:111], v[178:181], v[212:215], v[108:111]
	v_mfma_f32_16x16x32_bf16 v[116:119], v[186:189], v[212:215], v[116:119]
	v_mfma_f32_16x16x32_bf16 v[88:91], v[178:181], v[220:223], v[88:91]
	v_mfma_f32_16x16x32_bf16 v[100:103], v[186:189], v[220:223], v[100:103]
	v_mfma_f32_16x16x32_bf16 v[60:63], v[178:181], v[228:231], v[60:63]
	v_mfma_f32_16x16x32_bf16 v[76:79], v[186:189], v[228:231], v[76:79]
	v_mfma_f32_16x16x32_bf16 v[24:27], v[178:181], v[238:241], v[24:27]
	v_mfma_f32_16x16x32_bf16 v[44:47], v[186:189], v[238:241], v[44:47]
	s_barrier
; #define PG8_STAGE(bufoff, gbase, o0, o1) do { \
;         __builtin_amdgcn_global_load_lds((const unsigned*)((const char*)(gbase) + (o0)), (LAS unsigned*)(lds + (bufoff) + ldsw), 16, 0, 0); \
;         __builtin_amdgcn_global_load_lds((const unsigned*)((const char*)(gbase) + (o1)), (LAS unsigned*)(lds + (bufoff) + ldsw + 8192), 16, 0, 0); } while (0)
; #define PG8_LDA(dst, b, h) do { _Pragma("unroll") for (int m = 0; m < 4; ++m) _Pragma("unroll") for (int k = 0; k < 2; ++k) dst[m][k] = *(const LAS bf16x8*)(lds + PG8_SA(b, h) + aoff + m * 2048 + k * 1024); } while (0)
; #define PG8_LDB(dst, b, h) do { _Pragma("unroll") for (int n = 0; n < 2; ++n) _Pragma("unroll") for (int k = 0; k < 2; ++k) dst[n][k] = *(const LAS bf16x8*)(lds + PG8_SB(b, h) + boff + n * 2048 + k * 1024); } while (0)
; template <class Epi, class Sched, class Prob>
; __device__ __forceinline__ void gemm_phase(LAS unsigned char* lds, LAS unsigned char* lds_epi, const Prob g, const Sched& S, const Epi& E, int wid) {
;     ...
;         for (int t = 0; t < nt; t += 2) {
;             const bool last = (t == nt - 2);
;             const char* a1 = cA + (size_t)(t + 1) * kstep;
;             const char* a2 = last ? nA : cA + (size_t)(t + 2) * kstep; const char* b2 = last ? nB : cB + (size_t)(t + 2) * kstep;
;             const char* a3 = a2 + kstep; const char* b3 = b2 + kstep;
;             PG8_LDB(B0, 0, 0); PG8_LDB(B1, 0, 1); PG8_SCHED; PG8_LDA(At, 0, 0); PG8_STAGE(PG8_SA(1, 1), a1, cA10, cA11);
;             PG8_WAIT_V(8); PG8_WAIT_L(0); PG8_BAR; PG8_MMA(0, 0, At, B0); PG8_MMA(0, 1, At, B1); PG8_BAR; PG8_SCHED;
;             PG8_LDA(At, 0, 1); PG8_STAGE(PG8_SB(0, 0), b2, vB0, vB1); PG8_STAGE(PG8_SB(0, 1), b2 + hstepB, vB0, vB1); PG8_STAGE(PG8_SA(0, 0), a2, cA00, cA01);
;             PG8_WAIT_V(8); PG8_WAIT_L(0); PG8_BAR; PG8_MMA(1, 0, At, B0); PG8_MMA(1, 1, At, B1); PG8_BAR; PG8_SCHED;
;             PG8_LDB(B0, 1, 0); PG8_LDB(B1, 1, 1); PG8_SCHED; PG8_LDA(At, 1, 0); PG8_STAGE(PG8_SA(0, 1), a2, cA10, cA11);
;             PG8_WAIT_V(8); PG8_WAIT_L(0); PG8_BAR; PG8_MMA(0, 0, At, B0); PG8_MMA(0, 1, At, B1); PG8_BAR; PG8_SCHED;
;             PG8_LDA(At, 1, 1); PG8_STAGE(PG8_SB(1, 0), b3, vB0, vB1); PG8_STAGE(PG8_SB(1, 1), b3 + hstepB, vB0, vB1); PG8_STAGE(PG8_SA(1, 0), a3, cA00, cA01);
;             PG8_WAIT_V(8); PG8_WAIT_L(0); PG8_BAR; PG8_MMA(1, 0, At, B0); PG8_MMA(1, 1, At, B1); PG8_BAR; PG8_SCHED;
	s_add_i32 s82, 0, 0x18000
	s_add_i32 s83, 0, 0x1c000
	v_add_u32_e32 v140, s82, v194
	v_add_u32_e32 v156, s83, v194
	ds_read_b128 v[128:131], v140
	ds_read_b128 v[132:135], v140 offset:1024
	ds_read_b128 v[136:139], v140 offset:2048
	ds_read_b128 v[140:143], v140 offset:3072
	ds_read_b128 v[174:177], v156
	ds_read_b128 v[178:181], v156 offset:1024
	ds_read_b128 v[182:185], v156 offset:2048
	ds_read_b128 v[186:189], v156 offset:3072
	s_mov_b32 m0, s59
	v_lshl_add_u64 v[246:247], s[54:55], 0, v[150:151]
	ds_read_b128 v[208:211], v204 offset:32768
	ds_read_b128 v[212:215], v204 offset:33792
	ds_read_b128 v[216:219], v204 offset:34816
	ds_read_b128 v[220:223], v204 offset:35840
	ds_read_b128 v[224:227], v204 offset:36864
	ds_read_b128 v[228:231], v204 offset:37888
	ds_read_b128 v[232:235], v204 offset:38912
	ds_read_b128 v[238:241], v204 offset:39936
	global_load_lds_dwordx4 v[246:247], off
	v_lshl_add_u64 v[246:247], s[54:55], 0, v[154:155]
	s_mov_b32 m0, s60
	s_nop 0
	global_load_lds_dwordx4 v[246:247], off
	s_waitcnt vmcnt(8)
	s_waitcnt lgkmcnt(0)
	s_barrier
	s_waitcnt lgkmcnt(0)
	v_mfma_f32_16x16x32_bf16 v[80:83], v[128:131], v[208:211], v[80:83]
	v_mfma_f32_16x16x32_bf16 v[92:95], v[136:139], v[208:211], v[92:95]
	v_mfma_f32_16x16x32_bf16 v[52:55], v[128:131], v[216:219], v[52:55]
	v_mfma_f32_16x16x32_bf16 v[68:71], v[136:139], v[216:219], v[68:71]
	v_mfma_f32_16x16x32_bf16 v[28:31], v[128:131], v[224:227], v[28:31]
	v_mfma_f32_16x16x32_bf16 v[36:39], v[136:139], v[224:227], v[36:39]
	v_mfma_f32_16x16x32_bf16 v[8:11], v[128:131], v[232:235], v[8:11]
	v_mfma_f32_16x16x32_bf16 v[16:19], v[136:139], v[232:235], v[16:19]
	v_mfma_f32_16x16x32_bf16 v[80:83], v[132:135], v[212:215], v[80:83]
	v_mfma_f32_16x16x32_bf16 v[92:95], v[140:143], v[212:215], v[92:95]
	v_mfma_f32_16x16x32_bf16 v[52:55], v[132:135], v[220:223], v[52:55]
	v_mfma_f32_16x16x32_bf16 v[68:71], v[140:143], v[220:223], v[68:71]
	v_mfma_f32_16x16x32_bf16 v[28:31], v[132:135], v[228:231], v[28:31]
	v_mfma_f32_16x16x32_bf16 v[36:39], v[140:143], v[228:231], v[36:39]
	v_mfma_f32_16x16x32_bf16 v[8:11], v[132:135], v[238:241], v[8:11]
	v_mfma_f32_16x16x32_bf16 v[16:19], v[140:143], v[238:241], v[16:19]
	v_mfma_f32_16x16x32_bf16 v[120:123], v[174:177], v[208:211], v[120:123]
	v_mfma_f32_16x16x32_bf16 v[124:127], v[182:185], v[208:211], v[124:127]
	v_mfma_f32_16x16x32_bf16 v[104:107], v[174:177], v[216:219], v[104:107]
	v_mfma_f32_16x16x32_bf16 v[112:115], v[182:185], v[216:219], v[112:115]
	v_mfma_f32_16x16x32_bf16 v[84:87], v[174:177], v[224:227], v[84:87]
	v_mfma_f32_16x16x32_bf16 v[96:99], v[182:185], v[224:227], v[96:99]
	v_mfma_f32_16x16x32_bf16 v[48:51], v[174:177], v[232:235], v[48:51]
	v_mfma_f32_16x16x32_bf16 v[64:67], v[182:185], v[232:235], v[64:67]
	v_mfma_f32_16x16x32_bf16 v[120:123], v[178:181], v[212:215], v[120:123]
	v_mfma_f32_16x16x32_bf16 v[124:127], v[186:189], v[212:215], v[124:127]
	v_mfma_f32_16x16x32_bf16 v[104:107], v[178:181], v[220:223], v[104:107]
	v_mfma_f32_16x16x32_bf16 v[112:115], v[186:189], v[220:223], v[112:115]
	v_mfma_f32_16x16x32_bf16 v[84:87], v[178:181], v[228:231], v[84:87]
	v_mfma_f32_16x16x32_bf16 v[96:99], v[186:189], v[228:231], v[96:99]
	v_mfma_f32_16x16x32_bf16 v[48:51], v[178:181], v[238:241], v[48:51]
	v_mfma_f32_16x16x32_bf16 v[64:67], v[186:189], v[238:241], v[64:67]
	s_barrier
; #define PG8_STAGE(bufoff, gbase, o0, o1) do { \
;         __builtin_amdgcn_global_load_lds((const unsigned*)((const char*)(gbase) + (o0)), (LAS unsigned*)(lds + (bufoff) + ldsw), 16, 0, 0); \
;         __builtin_amdgcn_global_load_lds((const unsigned*)((const char*)(gbase) + (o1)), (LAS unsigned*)(lds + (bufoff) + ldsw + 8192), 16, 0, 0); } while (0)
; #define PG8_LDA(dst, b, h) do { _Pragma("unroll") for (int m = 0; m < 4; ++m) _Pragma("unroll") for (int k = 0; k < 2; ++k) dst[m][k] = *(const LAS bf16x8*)(lds + PG8_SA(b, h) + aoff + m * 2048 + k * 1024); } while (0)
; #define PG8_WAIT_V(n) asm volatile("s_waitcnt vmcnt(" #n ")" ::: "memory")
; template <class Epi, class Sched, class Prob>
; __device__ __forceinline__ void gemm_phase(LAS unsigned char* lds, LAS unsigned char* lds_epi, const Prob g, const Sched& S, const Epi& E, int wid) {
;     ...
;         for (int t = 0; t < nt; t += 2) {
;             const bool last = (t == nt - 2);
;             const char* a1 = cA + (size_t)(t + 1) * kstep;
;             const char* a2 = last ? nA : cA + (size_t)(t + 2) * kstep; const char* b2 = last ? nB : cB + (size_t)(t + 2) * kstep;
;             const char* a3 = a2 + kstep; const char* b3 = b2 + kstep;
;             PG8_LDB(B0, 0, 0); PG8_LDB(B1, 0, 1); PG8_SCHED; PG8_LDA(At, 0, 0); PG8_STAGE(PG8_SA(1, 1), a1, cA10, cA11);
;             PG8_WAIT_V(8); PG8_WAIT_L(0); PG8_BAR; PG8_MMA(0, 0, At, B0); PG8_MMA(0, 1, At, B1); PG8_BAR; PG8_SCHED;
;             PG8_LDA(At, 0, 1); PG8_STAGE(PG8_SB(0, 0), b2, vB0, vB1); PG8_STAGE(PG8_SB(0, 1), b2 + hstepB, vB0, vB1); PG8_STAGE(PG8_SA(0, 0), a2, cA00, cA01);
;             PG8_WAIT_V(8); PG8_WAIT_L(0); PG8_BAR; PG8_MMA(1, 0, At, B0); PG8_MMA(1, 1, At, B1); PG8_BAR; PG8_SCHED;
;             PG8_LDB(B0, 1, 0); PG8_LDB(B1, 1, 1); PG8_SCHED; PG8_LDA(At, 1, 0); PG8_STAGE(PG8_SA(0, 1), a2, cA10, cA11);
;             PG8_WAIT_V(8); PG8_WAIT_L(0); PG8_BAR; PG8_MMA(0, 0, At, B0); PG8_MMA(0, 1, At, B1); PG8_BAR; PG8_SCHED;
;             PG8_LDA(At, 1, 1); PG8_STAGE(PG8_SB(1, 0), b3, vB0, vB1); PG8_STAGE(PG8_SB(1, 1), b3 + hstepB, vB0, vB1); PG8_STAGE(PG8_SA(1, 0), a3, cA00, cA01);
;             PG8_WAIT_V(8); PG8_WAIT_L(0); PG8_BAR; PG8_MMA(1, 0, At, B0); PG8_MMA(1, 1, At, B1); PG8_BAR; PG8_SCHED;
;         }
;         if constexpr (Prob::FP8) asm volatile("s_nop 7\n\ts_nop 7\n\ts_nop 7" ::: "memory");
;         if (wr == 0) PG8_BAR;
	s_add_i32 s54, s82, s97
	v_lshl_add_u64 v[190:191], v[190:191], 0, s[20:21]
	s_mov_b32 m0, s54
	ds_read_b128 v[208:211], v204 offset:49152
	ds_read_b128 v[212:215], v204 offset:50176
	ds_read_b128 v[216:219], v204 offset:51200
	ds_read_b128 v[220:223], v204 offset:52224
	ds_read_b128 v[224:227], v204 offset:53248
	ds_read_b128 v[228:231], v204 offset:54272
	ds_read_b128 v[232:235], v204 offset:55296
	ds_read_b128 v[238:241], v204 offset:56320
	global_load_lds_dwordx4 v[190:191], off
	s_add_i32 m0, s54, 0x2000
	s_add_u32 s52, s52, 0x80080
	v_lshl_add_u64 v[190:191], v[236:237], 0, s[20:21]
	s_addc_u32 s53, s53, 0
	s_add_i32 s54, s83, s97
	global_load_lds_dwordx4 v[190:191], off
	v_lshl_add_u64 v[190:191], s[52:53], 0, v[144:145]
	s_mov_b32 m0, s54
	s_nop 0
	global_load_lds_dwordx4 v[190:191], off
	v_lshl_add_u64 v[190:191], s[52:53], 0, v[146:147]
	s_add_i32 m0, s54, 0x2000
	s_nop 0
	global_load_lds_dwordx4 v[190:191], off
	v_lshl_add_u64 v[190:191], v[242:243], 0, s[20:21]
	s_mov_b32 m0, s70
	s_nop 0
	global_load_lds_dwordx4 v[190:191], off
	v_lshl_add_u64 v[190:191], v[244:245], 0, s[20:21]
	s_mov_b32 m0, s71
	s_nop 0
	global_load_lds_dwordx4 v[190:191], off
	s_waitcnt vmcnt(8)
	s_waitcnt lgkmcnt(0)
	s_barrier
	s_waitcnt lgkmcnt(0)
	v_mfma_f32_16x16x32_bf16 v[56:59], v[128:131], v[208:211], v[56:59]
	v_mfma_f32_16x16x32_bf16 v[72:75], v[136:139], v[208:211], v[72:75]
	v_mfma_f32_16x16x32_bf16 v[32:35], v[128:131], v[216:219], v[32:35]
	v_mfma_f32_16x16x32_bf16 v[40:43], v[136:139], v[216:219], v[40:43]
	v_mfma_f32_16x16x32_bf16 v[12:15], v[128:131], v[224:227], v[12:15]
	v_mfma_f32_16x16x32_bf16 v[20:23], v[136:139], v[224:227], v[20:23]
	v_mfma_f32_16x16x32_bf16 v[0:3], v[128:131], v[232:235], v[0:3]
	v_mfma_f32_16x16x32_bf16 v[4:7], v[136:139], v[232:235], v[4:7]
	v_mfma_f32_16x16x32_bf16 v[56:59], v[132:135], v[212:215], v[56:59]
	v_mfma_f32_16x16x32_bf16 v[72:75], v[140:143], v[212:215], v[72:75]
	v_mfma_f32_16x16x32_bf16 v[32:35], v[132:135], v[220:223], v[32:35]
	v_mfma_f32_16x16x32_bf16 v[40:43], v[140:143], v[220:223], v[40:43]
	v_mfma_f32_16x16x32_bf16 v[12:15], v[132:135], v[228:231], v[12:15]
	v_mfma_f32_16x16x32_bf16 v[20:23], v[140:143], v[228:231], v[20:23]
	v_mfma_f32_16x16x32_bf16 v[0:3], v[132:135], v[238:241], v[0:3]
	v_mfma_f32_16x16x32_bf16 v[4:7], v[140:143], v[238:241], v[4:7]
	v_mfma_f32_16x16x32_bf16 v[108:111], v[174:177], v[208:211], v[108:111]
	v_mfma_f32_16x16x32_bf16 v[116:119], v[182:185], v[208:211], v[116:119]
	v_mfma_f32_16x16x32_bf16 v[88:91], v[174:177], v[216:219], v[88:91]
	v_mfma_f32_16x16x32_bf16 v[100:103], v[182:185], v[216:219], v[100:103]
	v_mfma_f32_16x16x32_bf16 v[60:63], v[174:177], v[224:227], v[60:63]
	v_mfma_f32_16x16x32_bf16 v[76:79], v[182:185], v[224:227], v[76:79]
	v_mfma_f32_16x16x32_bf16 v[24:27], v[174:177], v[232:235], v[24:27]
	v_mfma_f32_16x16x32_bf16 v[44:47], v[182:185], v[232:235], v[44:47]
	v_mfma_f32_16x16x32_bf16 v[108:111], v[178:181], v[212:215], v[108:111]
	v_mfma_f32_16x16x32_bf16 v[116:119], v[186:189], v[212:215], v[116:119]
	v_mfma_f32_16x16x32_bf16 v[88:91], v[178:181], v[220:223], v[88:91]
	v_mfma_f32_16x16x32_bf16 v[100:103], v[186:189], v[220:223], v[100:103]
	v_mfma_f32_16x16x32_bf16 v[60:63], v[178:181], v[228:231], v[60:63]
	v_mfma_f32_16x16x32_bf16 v[76:79], v[186:189], v[228:231], v[76:79]
	v_mfma_f32_16x16x32_bf16 v[24:27], v[178:181], v[238:241], v[24:27]
	v_mfma_f32_16x16x32_bf16 v[44:47], v[186:189], v[238:241], v[44:47]
	s_barrier
	s_add_i32 s81, s81, 2
	s_add_u32 s14, s14, 0x100
	s_addc_u32 s15, s15, 0
	s_add_u32 s79, s79, 0x100
	s_addc_u32 s80, s80, 0
	s_cmp_gt_u32 s81, 29
	s_cbranch_scc0 .LBB0_262
	v_readlane_b32 s14, v254, 27
	v_readlane_b32 s15, v254, 28
	s_and_b64 vcc, exec, s[14:15]
	s_cbranch_vccz .LBB0_265
	s_barrier

; #define PG8_STAGE(bufoff, gbase, o0, o1) do { \
;         __builtin_amdgcn_global_load_lds((const unsigned*)((const char*)(gbase) + (o0)), (LAS unsigned*)(lds + (bufoff) + ldsw), 16, 0, 0); \
;         __builtin_amdgcn_global_load_lds((const unsigned*)((const char*)(gbase) + (o1)), (LAS unsigned*)(lds + (bufoff) + ldsw + 8192), 16, 0, 0); } while (0)
; #define PG8_LDA(dst, b, h) do { _Pragma("unroll") for (int m = 0; m < 4; ++m) _Pragma("unroll") for (int k = 0; k < 2; ++k) dst[m][k] = *(const LAS bf16x8*)(lds + PG8_SA(b, h) + aoff + m * 2048 + k * 1024); } while (0)
; #define PG8_LDB(dst, b, h) do { _Pragma("unroll") for (int n = 0; n < 2; ++n) _Pragma("unroll") for (int k = 0; k < 2; ++k) dst[n][k] = *(const LAS bf16x8*)(lds + PG8_SB(b, h) + boff + n * 2048 + k * 1024); } while (0)
; template <class Epi, class Sched, class Prob>
; __device__ __forceinline__ void gemm_phase(LAS unsigned char* lds, LAS unsigned char* lds_epi, const Prob g, const Sched& S, const Epi& E, int wid) {
;     ...
;         for (int t = 0; t < nt; t += 2) {
;             const bool last = (t == nt - 2);
;             const char* a1 = cA + (size_t)(t + 1) * kstep;
;             const char* a2 = last ? nA : cA + (size_t)(t + 2) * kstep; const char* b2 = last ? nB : cB + (size_t)(t + 2) * kstep;
;             const char* a3 = a2 + kstep; const char* b3 = b2 + kstep;
;             PG8_LDB(B0, 0, 0); PG8_LDB(B1, 0, 1); PG8_SCHED; PG8_LDA(At, 0, 0); PG8_STAGE(PG8_SA(1, 1), a1, cA10, cA11);
;             PG8_WAIT_V(8); PG8_WAIT_L(0); PG8_BAR; PG8_MMA(0, 0, At, B0); PG8_MMA(0, 1, At, B1); PG8_BAR; PG8_SCHED;
;             PG8_LDA(At, 0, 1); PG8_STAGE(PG8_SB(0, 0), b2, vB0, vB1); PG8_STAGE(PG8_SB(0, 1), b2 + hstepB, vB0, vB1); PG8_STAGE(PG8_SA(0, 0), a2, cA00, cA01);
;             PG8_WAIT_V(8); PG8_WAIT_L(0); PG8_BAR; PG8_MMA(1, 0, At, B0); PG8_MMA(1, 1, At, B1); PG8_BAR; PG8_SCHED;
;             PG8_LDB(B0, 1, 0); PG8_LDB(B1, 1, 1); PG8_SCHED; PG8_LDA(At, 1, 0); PG8_STAGE(PG8_SA(0, 1), a2, cA10, cA11);
;             PG8_WAIT_V(8); PG8_WAIT_L(0); PG8_BAR; PG8_MMA(0, 0, At, B0); PG8_MMA(0, 1, At, B1); PG8_BAR; PG8_SCHED;
;             PG8_LDA(At, 1, 1); PG8_STAGE(PG8_SB(1, 0), b3, vB0, vB1); PG8_STAGE(PG8_SB(1, 1), b3 + hstepB, vB0, vB1); PG8_STAGE(PG8_SA(1, 0), a3, cA00, cA01);
;             PG8_WAIT_V(8); PG8_WAIT_L(0); PG8_BAR; PG8_MMA(1, 0, At, B0); PG8_MMA(1, 1, At, B1); PG8_BAR; PG8_SCHED;
.LBB0_1156:
	v_add_u32_e32 v146, s62, v149
	ds_read_b128 v[158:161], v146
	ds_read_b128 v[162:165], v146 offset:1024
	ds_read_b128 v[166:169], v146 offset:2048
	ds_read_b128 v[170:173], v146 offset:3072
	v_add_u32_e32 v146, s63, v149
	ds_read_b128 v[174:177], v146
	ds_read_b128 v[178:181], v146 offset:1024
	ds_read_b128 v[182:185], v146 offset:2048
	ds_read_b128 v[186:189], v146 offset:3072
	s_add_u32 s40, s38, 0x80
	s_addc_u32 s41, s39, 0
	s_cmp_eq_u32 s68, 28
	s_cselect_b32 s43, s25, s41
	s_cselect_b32 s42, s27, s40
	s_cselect_b32 s41, s23, s67
	s_cselect_b32 s40, s37, s66
	v_lshl_add_u64 v[146:147], s[38:39], 0, v[140:141]
	s_add_i32 m0, s53, 0xc000
	ds_read_b128 v[190:193], v153
	ds_read_b128 v[194:197], v153 offset:1024
	ds_read_b128 v[198:201], v153 offset:2048
	ds_read_b128 v[202:205], v153 offset:3072
	ds_read_b128 v[206:209], v153 offset:4096
	ds_read_b128 v[210:213], v153 offset:5120
	ds_read_b128 v[214:217], v153 offset:6144
	ds_read_b128 v[218:221], v153 offset:7168
	global_load_lds_dwordx4 v[146:147], off
	v_lshl_add_u64 v[146:147], s[38:39], 0, v[142:143]
	s_add_i32 m0, s53, 0xe000
	s_nop 0
	global_load_lds_dwordx4 v[146:147], off
	s_waitcnt vmcnt(8)
	s_waitcnt lgkmcnt(0)
	s_barrier
	s_waitcnt lgkmcnt(0)
	v_mfma_f32_16x16x32_bf16 v[124:127], v[158:161], v[190:193], v[124:127]
	v_mfma_f32_16x16x32_bf16 v[120:123], v[166:169], v[190:193], v[120:123]
	v_mfma_f32_16x16x32_bf16 v[108:111], v[158:161], v[198:201], v[108:111]
	v_mfma_f32_16x16x32_bf16 v[104:107], v[166:169], v[198:201], v[104:107]
	v_mfma_f32_16x16x32_bf16 v[92:95], v[158:161], v[206:209], v[92:95]
	v_mfma_f32_16x16x32_bf16 v[88:91], v[166:169], v[206:209], v[88:91]
	v_mfma_f32_16x16x32_bf16 v[76:79], v[158:161], v[214:217], v[76:79]
	v_mfma_f32_16x16x32_bf16 v[72:75], v[166:169], v[214:217], v[72:75]
	v_mfma_f32_16x16x32_bf16 v[124:127], v[162:165], v[194:197], v[124:127]
	v_mfma_f32_16x16x32_bf16 v[120:123], v[170:173], v[194:197], v[120:123]
	v_mfma_f32_16x16x32_bf16 v[108:111], v[162:165], v[202:205], v[108:111]
	v_mfma_f32_16x16x32_bf16 v[104:107], v[170:173], v[202:205], v[104:107]
	v_mfma_f32_16x16x32_bf16 v[92:95], v[162:165], v[210:213], v[92:95]
	v_mfma_f32_16x16x32_bf16 v[88:91], v[170:173], v[210:213], v[88:91]
	v_mfma_f32_16x16x32_bf16 v[76:79], v[162:165], v[218:221], v[76:79]
	v_mfma_f32_16x16x32_bf16 v[72:75], v[170:173], v[218:221], v[72:75]
	v_mfma_f32_16x16x32_bf16 v[116:119], v[174:177], v[190:193], v[116:119]
	v_mfma_f32_16x16x32_bf16 v[112:115], v[182:185], v[190:193], v[112:115]
	v_mfma_f32_16x16x32_bf16 v[100:103], v[174:177], v[198:201], v[100:103]
	v_mfma_f32_16x16x32_bf16 v[96:99], v[182:185], v[198:201], v[96:99]
	v_mfma_f32_16x16x32_bf16 v[84:87], v[174:177], v[206:209], v[84:87]
	v_mfma_f32_16x16x32_bf16 v[80:83], v[182:185], v[206:209], v[80:83]
	v_mfma_f32_16x16x32_bf16 v[68:71], v[174:177], v[214:217], v[68:71]
	v_mfma_f32_16x16x32_bf16 v[64:67], v[182:185], v[214:217], v[64:67]
	v_mfma_f32_16x16x32_bf16 v[116:119], v[178:181], v[194:197], v[116:119]
	v_mfma_f32_16x16x32_bf16 v[112:115], v[186:189], v[194:197], v[112:115]
	v_mfma_f32_16x16x32_bf16 v[100:103], v[178:181], v[202:205], v[100:103]
	v_mfma_f32_16x16x32_bf16 v[96:99], v[186:189], v[202:205], v[96:99]
	v_mfma_f32_16x16x32_bf16 v[84:87], v[178:181], v[210:213], v[84:87]
	v_mfma_f32_16x16x32_bf16 v[80:83], v[186:189], v[210:213], v[80:83]
	v_mfma_f32_16x16x32_bf16 v[68:71], v[178:181], v[218:221], v[68:71]
	v_mfma_f32_16x16x32_bf16 v[64:67], v[186:189], v[218:221], v[64:67]
	s_barrier
	s_add_i32 s69, s62, s97
	v_lshl_add_u64 v[146:147], s[40:41], 0, v[130:131]
	s_mov_b32 m0, s69
	ds_read_b128 v[190:193], v153 offset:16384
	ds_read_b128 v[194:197], v153 offset:17408
	ds_read_b128 v[198:201], v153 offset:18432
	ds_read_b128 v[202:205], v153 offset:19456
	ds_read_b128 v[206:209], v153 offset:20480
	ds_read_b128 v[210:213], v153 offset:21504
	ds_read_b128 v[214:217], v153 offset:22528
	ds_read_b128 v[218:221], v153 offset:23552
	global_load_lds_dwordx4 v[146:147], off
	s_add_i32 m0, s69, 0x2000
	s_add_u32 s70, s40, 0x80000
	v_lshl_add_u64 v[222:223], s[40:41], 0, v[128:129]
	s_addc_u32 s71, s41, 0
	s_add_i32 s69, s63, s97
	global_load_lds_dwordx4 v[222:223], off
	v_lshl_add_u64 v[224:225], s[70:71], 0, v[130:131]
	s_mov_b32 m0, s69
	v_lshl_add_u64 v[226:227], s[42:43], 0, v[128:129]
	global_load_lds_dwordx4 v[224:225], off
	v_lshl_add_u64 v[224:225], s[70:71], 0, v[128:129]
	s_add_i32 m0, s69, 0x2000
	s_nop 0
	global_load_lds_dwordx4 v[224:225], off
	v_lshl_add_u64 v[224:225], s[42:43], 0, v[130:131]
	s_mov_b32 m0, s53
	s_nop 0
	global_load_lds_dwordx4 v[224:225], off
	s_mov_b32 m0, s54
	s_nop 0
	global_load_lds_dwordx4 v[226:227], off
	s_waitcnt vmcnt(8)
	s_waitcnt lgkmcnt(0)
	s_barrier
; #define PG8_STAGE(bufoff, gbase, o0, o1) do { \
;         __builtin_amdgcn_global_load_lds((const unsigned*)((const char*)(gbase) + (o0)), (LAS unsigned*)(lds + (bufoff) + ldsw), 16, 0, 0); \
;         __builtin_amdgcn_global_load_lds((const unsigned*)((const char*)(gbase) + (o1)), (LAS unsigned*)(lds + (bufoff) + ldsw + 8192), 16, 0, 0); } while (0)
; #define PG8_LDA(dst, b, h) do { _Pragma("unroll") for (int m = 0; m < 4; ++m) _Pragma("unroll") for (int k = 0; k < 2; ++k) dst[m][k] = *(const LAS bf16x8*)(lds + PG8_SA(b, h) + aoff + m * 2048 + k * 1024); } while (0)
; #define PG8_LDB(dst, b, h) do { _Pragma("unroll") for (int n = 0; n < 2; ++n) _Pragma("unroll") for (int k = 0; k < 2; ++k) dst[n][k] = *(const LAS bf16x8*)(lds + PG8_SB(b, h) + boff + n * 2048 + k * 1024); } while (0)
; template <class Epi, class Sched, class Prob>
; __device__ __forceinline__ void gemm_phase(LAS unsigned char* lds, LAS unsigned char* lds_epi, const Prob g, const Sched& S, const Epi& E, int wid) {
;     ...
;         for (int t = 0; t < nt; t += 2) {
;             const bool last = (t == nt - 2);
;             const char* a1 = cA + (size_t)(t + 1) * kstep;
;             const char* a2 = last ? nA : cA + (size_t)(t + 2) * kstep; const char* b2 = last ? nB : cB + (size_t)(t + 2) * kstep;
;             const char* a3 = a2 + kstep; const char* b3 = b2 + kstep;
;             PG8_LDB(B0, 0, 0); PG8_LDB(B1, 0, 1); PG8_SCHED; PG8_LDA(At, 0, 0); PG8_STAGE(PG8_SA(1, 1), a1, cA10, cA11);
;             PG8_WAIT_V(8); PG8_WAIT_L(0); PG8_BAR; PG8_MMA(0, 0, At, B0); PG8_MMA(0, 1, At, B1); PG8_BAR; PG8_SCHED;
;             PG8_LDA(At, 0, 1); PG8_STAGE(PG8_SB(0, 0), b2, vB0, vB1); PG8_STAGE(PG8_SB(0, 1), b2 + hstepB, vB0, vB1); PG8_STAGE(PG8_SA(0, 0), a2, cA00, cA01);
;             PG8_WAIT_V(8); PG8_WAIT_L(0); PG8_BAR; PG8_MMA(1, 0, At, B0); PG8_MMA(1, 1, At, B1); PG8_BAR; PG8_SCHED;
;             PG8_LDB(B0, 1, 0); PG8_LDB(B1, 1, 1); PG8_SCHED; PG8_LDA(At, 1, 0); PG8_STAGE(PG8_SA(0, 1), a2, cA10, cA11);
;             PG8_WAIT_V(8); PG8_WAIT_L(0); PG8_BAR; PG8_MMA(0, 0, At, B0); PG8_MMA(0, 1, At, B1); PG8_BAR; PG8_SCHED;
;             PG8_LDA(At, 1, 1); PG8_STAGE(PG8_SB(1, 0), b3, vB0, vB1); PG8_STAGE(PG8_SB(1, 1), b3 + hstepB, vB0, vB1); PG8_STAGE(PG8_SA(1, 0), a3, cA00, cA01);
;             PG8_WAIT_V(8); PG8_WAIT_L(0); PG8_BAR; PG8_MMA(1, 0, At, B0); PG8_MMA(1, 1, At, B1); PG8_BAR; PG8_SCHED;
	s_waitcnt lgkmcnt(0)
	v_mfma_f32_16x16x32_bf16 v[60:63], v[158:161], v[190:193], v[60:63]
	v_mfma_f32_16x16x32_bf16 v[56:59], v[166:169], v[190:193], v[56:59]
	v_mfma_f32_16x16x32_bf16 v[44:47], v[158:161], v[198:201], v[44:47]
	v_mfma_f32_16x16x32_bf16 v[40:43], v[166:169], v[198:201], v[40:43]
	v_mfma_f32_16x16x32_bf16 v[28:31], v[158:161], v[206:209], v[28:31]
	v_mfma_f32_16x16x32_bf16 v[24:27], v[166:169], v[206:209], v[24:27]
	v_mfma_f32_16x16x32_bf16 v[0:3], v[158:161], v[214:217], v[0:3]
	v_mfma_f32_16x16x32_bf16 v[12:15], v[166:169], v[214:217], v[12:15]
	v_mfma_f32_16x16x32_bf16 v[60:63], v[162:165], v[194:197], v[60:63]
	v_mfma_f32_16x16x32_bf16 v[56:59], v[170:173], v[194:197], v[56:59]
	v_mfma_f32_16x16x32_bf16 v[44:47], v[162:165], v[202:205], v[44:47]
	v_mfma_f32_16x16x32_bf16 v[40:43], v[170:173], v[202:205], v[40:43]
	v_mfma_f32_16x16x32_bf16 v[28:31], v[162:165], v[210:213], v[28:31]
	v_mfma_f32_16x16x32_bf16 v[24:27], v[170:173], v[210:213], v[24:27]
	v_mfma_f32_16x16x32_bf16 v[0:3], v[162:165], v[218:221], v[0:3]
	v_mfma_f32_16x16x32_bf16 v[12:15], v[170:173], v[218:221], v[12:15]
	v_mfma_f32_16x16x32_bf16 v[52:55], v[174:177], v[190:193], v[52:55]
	v_mfma_f32_16x16x32_bf16 v[48:51], v[182:185], v[190:193], v[48:51]
	v_mfma_f32_16x16x32_bf16 v[36:39], v[174:177], v[198:201], v[36:39]
	v_mfma_f32_16x16x32_bf16 v[32:35], v[182:185], v[198:201], v[32:35]
	v_mfma_f32_16x16x32_bf16 v[20:23], v[174:177], v[206:209], v[20:23]
	v_mfma_f32_16x16x32_bf16 v[16:19], v[182:185], v[206:209], v[16:19]
	v_mfma_f32_16x16x32_bf16 v[8:11], v[174:177], v[214:217], v[8:11]
	v_mfma_f32_16x16x32_bf16 v[4:7], v[182:185], v[214:217], v[4:7]
	v_mfma_f32_16x16x32_bf16 v[52:55], v[178:181], v[194:197], v[52:55]
	v_mfma_f32_16x16x32_bf16 v[48:51], v[186:189], v[194:197], v[48:51]
	v_mfma_f32_16x16x32_bf16 v[36:39], v[178:181], v[202:205], v[36:39]
	v_mfma_f32_16x16x32_bf16 v[32:35], v[186:189], v[202:205], v[32:35]
	v_mfma_f32_16x16x32_bf16 v[20:23], v[178:181], v[210:213], v[20:23]
	v_mfma_f32_16x16x32_bf16 v[16:19], v[186:189], v[210:213], v[16:19]
	v_mfma_f32_16x16x32_bf16 v[8:11], v[178:181], v[218:221], v[8:11]
	v_mfma_f32_16x16x32_bf16 v[4:7], v[186:189], v[218:221], v[4:7]
	s_barrier
	s_add_i32 s69, 0, 0x18000
	v_add_u32_e32 v157, s69, v149
	s_add_i32 s70, 0, 0x1c000
	ds_read_b128 v[158:161], v157
	ds_read_b128 v[162:165], v157 offset:1024
	ds_read_b128 v[166:169], v157 offset:2048
	ds_read_b128 v[170:173], v157 offset:3072
	v_add_u32_e32 v157, s70, v149
	ds_read_b128 v[174:177], v157
	ds_read_b128 v[178:181], v157 offset:1024
	ds_read_b128 v[182:185], v157 offset:2048
	ds_read_b128 v[186:189], v157 offset:3072
	s_mov_b32 m0, s55
	v_lshl_add_u64 v[228:229], s[42:43], 0, v[132:133]
	ds_read_b128 v[190:193], v153 offset:32768
	ds_read_b128 v[194:197], v153 offset:33792
	ds_read_b128 v[198:201], v153 offset:34816
	ds_read_b128 v[202:205], v153 offset:35840
	ds_read_b128 v[206:209], v153 offset:36864
	ds_read_b128 v[210:213], v153 offset:37888
	ds_read_b128 v[214:217], v153 offset:38912
	ds_read_b128 v[218:221], v153 offset:39936
	global_load_lds_dwordx4 v[228:229], off
	v_lshl_add_u64 v[228:229], s[42:43], 0, v[134:135]
	s_mov_b32 m0, s56
	s_nop 0
	global_load_lds_dwordx4 v[228:229], off
	s_waitcnt vmcnt(8)
	s_waitcnt lgkmcnt(0)
	s_barrier
	s_waitcnt lgkmcnt(0)
	v_mfma_f32_16x16x32_bf16 v[124:127], v[158:161], v[190:193], v[124:127]
	v_mfma_f32_16x16x32_bf16 v[120:123], v[166:169], v[190:193], v[120:123]
	v_mfma_f32_16x16x32_bf16 v[108:111], v[158:161], v[198:201], v[108:111]
	v_mfma_f32_16x16x32_bf16 v[104:107], v[166:169], v[198:201], v[104:107]
	v_mfma_f32_16x16x32_bf16 v[92:95], v[158:161], v[206:209], v[92:95]
	v_mfma_f32_16x16x32_bf16 v[88:91], v[166:169], v[206:209], v[88:91]
	v_mfma_f32_16x16x32_bf16 v[76:79], v[158:161], v[214:217], v[76:79]
	v_mfma_f32_16x16x32_bf16 v[72:75], v[166:169], v[214:217], v[72:75]
	v_mfma_f32_16x16x32_bf16 v[124:127], v[162:165], v[194:197], v[124:127]
	v_mfma_f32_16x16x32_bf16 v[120:123], v[170:173], v[194:197], v[120:123]
	v_mfma_f32_16x16x32_bf16 v[108:111], v[162:165], v[202:205], v[108:111]
	v_mfma_f32_16x16x32_bf16 v[104:107], v[170:173], v[202:205], v[104:107]
	v_mfma_f32_16x16x32_bf16 v[92:95], v[162:165], v[210:213], v[92:95]
	v_mfma_f32_16x16x32_bf16 v[88:91], v[170:173], v[210:213], v[88:91]
	v_mfma_f32_16x16x32_bf16 v[76:79], v[162:165], v[218:221], v[76:79]
	v_mfma_f32_16x16x32_bf16 v[72:75], v[170:173], v[218:221], v[72:75]
	v_mfma_f32_16x16x32_bf16 v[116:119], v[174:177], v[190:193], v[116:119]
	v_mfma_f32_16x16x32_bf16 v[112:115], v[182:185], v[190:193], v[112:115]
	v_mfma_f32_16x16x32_bf16 v[100:103], v[174:177], v[198:201], v[100:103]
	v_mfma_f32_16x16x32_bf16 v[96:99], v[182:185], v[198:201], v[96:99]
	v_mfma_f32_16x16x32_bf16 v[84:87], v[174:177], v[206:209], v[84:87]
	v_mfma_f32_16x16x32_bf16 v[80:83], v[182:185], v[206:209], v[80:83]
	v_mfma_f32_16x16x32_bf16 v[68:71], v[174:177], v[214:217], v[68:71]
	v_mfma_f32_16x16x32_bf16 v[64:67], v[182:185], v[214:217], v[64:67]
	v_mfma_f32_16x16x32_bf16 v[116:119], v[178:181], v[194:197], v[116:119]
	v_mfma_f32_16x16x32_bf16 v[112:115], v[186:189], v[194:197], v[112:115]
	v_mfma_f32_16x16x32_bf16 v[100:103], v[178:181], v[202:205], v[100:103]
	v_mfma_f32_16x16x32_bf16 v[96:99], v[186:189], v[202:205], v[96:99]
	v_mfma_f32_16x16x32_bf16 v[84:87], v[178:181], v[210:213], v[84:87]
	v_mfma_f32_16x16x32_bf16 v[80:83], v[186:189], v[210:213], v[80:83]
	v_mfma_f32_16x16x32_bf16 v[68:71], v[178:181], v[218:221], v[68:71]
	v_mfma_f32_16x16x32_bf16 v[64:67], v[186:189], v[218:221], v[64:67]
	s_barrier
; #define PG8_STAGE(bufoff, gbase, o0, o1) do { \
;         __builtin_amdgcn_global_load_lds((const unsigned*)((const char*)(gbase) + (o0)), (LAS unsigned*)(lds + (bufoff) + ldsw), 16, 0, 0); \
;         __builtin_amdgcn_global_load_lds((const unsigned*)((const char*)(gbase) + (o1)), (LAS unsigned*)(lds + (bufoff) + ldsw + 8192), 16, 0, 0); } while (0)
; #define PG8_LDA(dst, b, h) do { _Pragma("unroll") for (int m = 0; m < 4; ++m) _Pragma("unroll") for (int k = 0; k < 2; ++k) dst[m][k] = *(const LAS bf16x8*)(lds + PG8_SA(b, h) + aoff + m * 2048 + k * 1024); } while (0)
; #define PG8_WAIT_V(n) asm volatile("s_waitcnt vmcnt(" #n ")" ::: "memory")
; template <class Epi, class Sched, class Prob>
; __device__ __forceinline__ void gemm_phase(LAS unsigned char* lds, LAS unsigned char* lds_epi, const Prob g, const Sched& S, const Epi& E, int wid) {
;     ...
;         for (int t = 0; t < nt; t += 2) {
;             const bool last = (t == nt - 2);
;             const char* a1 = cA + (size_t)(t + 1) * kstep;
;             const char* a2 = last ? nA : cA + (size_t)(t + 2) * kstep; const char* b2 = last ? nB : cB + (size_t)(t + 2) * kstep;
;             const char* a3 = a2 + kstep; const char* b3 = b2 + kstep;
;             PG8_LDB(B0, 0, 0); PG8_LDB(B1, 0, 1); PG8_SCHED; PG8_LDA(At, 0, 0); PG8_STAGE(PG8_SA(1, 1), a1, cA10, cA11);
;             PG8_WAIT_V(8); PG8_WAIT_L(0); PG8_BAR; PG8_MMA(0, 0, At, B0); PG8_MMA(0, 1, At, B1); PG8_BAR; PG8_SCHED;
;             PG8_LDA(At, 0, 1); PG8_STAGE(PG8_SB(0, 0), b2, vB0, vB1); PG8_STAGE(PG8_SB(0, 1), b2 + hstepB, vB0, vB1); PG8_STAGE(PG8_SA(0, 0), a2, cA00, cA01);
;             PG8_WAIT_V(8); PG8_WAIT_L(0); PG8_BAR; PG8_MMA(1, 0, At, B0); PG8_MMA(1, 1, At, B1); PG8_BAR; PG8_SCHED;
;             PG8_LDB(B0, 1, 0); PG8_LDB(B1, 1, 1); PG8_SCHED; PG8_LDA(At, 1, 0); PG8_STAGE(PG8_SA(0, 1), a2, cA10, cA11);
;             PG8_WAIT_V(8); PG8_WAIT_L(0); PG8_BAR; PG8_MMA(0, 0, At, B0); PG8_MMA(0, 1, At, B1); PG8_BAR; PG8_SCHED;
;             PG8_LDA(At, 1, 1); PG8_STAGE(PG8_SB(1, 0), b3, vB0, vB1); PG8_STAGE(PG8_SB(1, 1), b3 + hstepB, vB0, vB1); PG8_STAGE(PG8_SA(1, 0), a3, cA00, cA01);
;             PG8_WAIT_V(8); PG8_WAIT_L(0); PG8_BAR; PG8_MMA(1, 0, At, B0); PG8_MMA(1, 1, At, B1); PG8_BAR; PG8_SCHED;
;         }
;         if constexpr (Prob::FP8) asm volatile("s_nop 7\n\ts_nop 7\n\ts_nop 7" ::: "memory");
;         if (wr == 0) PG8_BAR;
	s_add_i32 s42, s69, s97
	v_lshl_add_u64 v[146:147], v[146:147], 0, s[16:17]
	s_mov_b32 m0, s42
	ds_read_b128 v[190:193], v153 offset:49152
	ds_read_b128 v[194:197], v153 offset:50176
	ds_read_b128 v[198:201], v153 offset:51200
	ds_read_b128 v[202:205], v153 offset:52224
	ds_read_b128 v[206:209], v153 offset:53248
	ds_read_b128 v[210:213], v153 offset:54272
	ds_read_b128 v[214:217], v153 offset:55296
	ds_read_b128 v[218:221], v153 offset:56320
	global_load_lds_dwordx4 v[146:147], off
	s_add_i32 m0, s42, 0x2000
	s_add_u32 s40, s40, 0x80080
	v_lshl_add_u64 v[146:147], v[222:223], 0, s[16:17]
	s_addc_u32 s41, s41, 0
	s_add_i32 s42, s70, s97
	global_load_lds_dwordx4 v[146:147], off
	v_lshl_add_u64 v[146:147], s[40:41], 0, v[130:131]
	s_mov_b32 m0, s42
	s_nop 0
	global_load_lds_dwordx4 v[146:147], off
	v_lshl_add_u64 v[146:147], s[40:41], 0, v[128:129]
	s_add_i32 m0, s42, 0x2000
	s_nop 0
	global_load_lds_dwordx4 v[146:147], off
	v_lshl_add_u64 v[146:147], v[224:225], 0, s[16:17]
	s_mov_b32 m0, s60
	s_nop 0
	global_load_lds_dwordx4 v[146:147], off
	v_lshl_add_u64 v[146:147], v[226:227], 0, s[16:17]
	s_mov_b32 m0, s61
	s_nop 0
	global_load_lds_dwordx4 v[146:147], off
	s_waitcnt vmcnt(8)
	s_waitcnt lgkmcnt(0)
	s_barrier
	s_waitcnt lgkmcnt(0)
	v_mfma_f32_16x16x32_bf16 v[60:63], v[158:161], v[190:193], v[60:63]
	v_mfma_f32_16x16x32_bf16 v[56:59], v[166:169], v[190:193], v[56:59]
	v_mfma_f32_16x16x32_bf16 v[44:47], v[158:161], v[198:201], v[44:47]
	v_mfma_f32_16x16x32_bf16 v[40:43], v[166:169], v[198:201], v[40:43]
	v_mfma_f32_16x16x32_bf16 v[28:31], v[158:161], v[206:209], v[28:31]
	v_mfma_f32_16x16x32_bf16 v[24:27], v[166:169], v[206:209], v[24:27]
	v_mfma_f32_16x16x32_bf16 v[0:3], v[158:161], v[214:217], v[0:3]
	v_mfma_f32_16x16x32_bf16 v[12:15], v[166:169], v[214:217], v[12:15]
	v_mfma_f32_16x16x32_bf16 v[60:63], v[162:165], v[194:197], v[60:63]
	v_mfma_f32_16x16x32_bf16 v[56:59], v[170:173], v[194:197], v[56:59]
	v_mfma_f32_16x16x32_bf16 v[44:47], v[162:165], v[202:205], v[44:47]
	v_mfma_f32_16x16x32_bf16 v[40:43], v[170:173], v[202:205], v[40:43]
	v_mfma_f32_16x16x32_bf16 v[28:31], v[162:165], v[210:213], v[28:31]
	v_mfma_f32_16x16x32_bf16 v[24:27], v[170:173], v[210:213], v[24:27]
	v_mfma_f32_16x16x32_bf16 v[0:3], v[162:165], v[218:221], v[0:3]
	v_mfma_f32_16x16x32_bf16 v[12:15], v[170:173], v[218:221], v[12:15]
	v_mfma_f32_16x16x32_bf16 v[52:55], v[174:177], v[190:193], v[52:55]
	v_mfma_f32_16x16x32_bf16 v[48:51], v[182:185], v[190:193], v[48:51]
	v_mfma_f32_16x16x32_bf16 v[36:39], v[174:177], v[198:201], v[36:39]
	v_mfma_f32_16x16x32_bf16 v[32:35], v[182:185], v[198:201], v[32:35]
	v_mfma_f32_16x16x32_bf16 v[20:23], v[174:177], v[206:209], v[20:23]
	v_mfma_f32_16x16x32_bf16 v[16:19], v[182:185], v[206:209], v[16:19]
	v_mfma_f32_16x16x32_bf16 v[8:11], v[174:177], v[214:217], v[8:11]
	v_mfma_f32_16x16x32_bf16 v[4:7], v[182:185], v[214:217], v[4:7]
	v_mfma_f32_16x16x32_bf16 v[52:55], v[178:181], v[194:197], v[52:55]
	v_mfma_f32_16x16x32_bf16 v[48:51], v[186:189], v[194:197], v[48:51]
	v_mfma_f32_16x16x32_bf16 v[36:39], v[178:181], v[202:205], v[36:39]
	v_mfma_f32_16x16x32_bf16 v[32:35], v[186:189], v[202:205], v[32:35]
	v_mfma_f32_16x16x32_bf16 v[20:23], v[178:181], v[210:213], v[20:23]
	v_mfma_f32_16x16x32_bf16 v[16:19], v[186:189], v[210:213], v[16:19]
	v_mfma_f32_16x16x32_bf16 v[8:11], v[178:181], v[218:221], v[8:11]
	v_mfma_f32_16x16x32_bf16 v[4:7], v[186:189], v[218:221], v[4:7]
	s_barrier
	s_add_i32 s68, s68, 2
	s_add_u32 s38, s38, 0x100
	s_addc_u32 s39, s39, 0
	s_add_u32 s66, s66, 0x100
	s_addc_u32 s67, s67, 0
	s_cmp_gt_u32 s68, 29
	s_cbranch_scc0 .LBB0_1156
	v_readlane_b32 s38, v254, 27
	v_readlane_b32 s39, v254, 28
	s_and_b64 vcc, exec, s[38:39]
	s_cbranch_vccz .LBB0_1159
	s_barrier

; #define PG8_STAGE(bufoff, gbase, o0, o1) do { \
;         __builtin_amdgcn_global_load_lds((const unsigned*)((const char*)(gbase) + (o0)), (LAS unsigned*)(lds + (bufoff) + ldsw), 16, 0, 0); \
;         __builtin_amdgcn_global_load_lds((const unsigned*)((const char*)(gbase) + (o1)), (LAS unsigned*)(lds + (bufoff) + ldsw + 8192), 16, 0, 0); } while (0)
; #define PG8_LDA(dst, b, h) do { _Pragma("unroll") for (int m = 0; m < 4; ++m) _Pragma("unroll") for (int k = 0; k < 2; ++k) dst[m][k] = *(const LAS bf16x8*)(lds + PG8_SA(b, h) + aoff + m * 2048 + k * 1024); } while (0)
; template <class Epi, class Sched, class Prob>
; __device__ __forceinline__ void gemm_phase(LAS unsigned char* lds, LAS unsigned char* lds_epi, const Prob g, const Sched& S, const Epi& E, int wid) {
;     ...
;         const bool has_next = S.next(ui + 1, nxt);
;         const char* nA = has_next ? g.a_base(nxt) : cA; const char* nB = has_next ? g.b_base(nxt) : cB;
; _Pragma("clang loop unroll(disable)")
;         for (int t = 0; t < nt; t += 2) {
;             const bool last = (t == nt - 2);
;             const char* a1 = cA + (size_t)(t + 1) * kstep;
;             const char* a2 = last ? nA : cA + (size_t)(t + 2) * kstep; const char* b2 = last ? nB : cB + (size_t)(t + 2) * kstep;
;             const char* a3 = a2 + kstep; const char* b3 = b2 + kstep;
;             PG8_LDB(B0, 0, 0); PG8_LDB(B1, 0, 1); PG8_SCHED; PG8_LDA(At, 0, 0); PG8_STAGE(PG8_SA(1, 1), a1, cA10, cA11);
;             PG8_WAIT_V(8); PG8_WAIT_L(0); PG8_BAR; PG8_MMA(0, 0, At, B0); PG8_MMA(0, 1, At, B1); PG8_BAR; PG8_SCHED;
;             PG8_LDA(At, 0, 1); PG8_STAGE(PG8_SB(0, 0), b2, vB0, vB1); PG8_STAGE(PG8_SB(0, 1), b2 + hstepB, vB0, vB1); PG8_STAGE(PG8_SA(0, 0), a2, cA00, cA01);
;             PG8_WAIT_V(8); PG8_WAIT_L(0); PG8_BAR; PG8_MMA(1, 0, At, B0); PG8_MMA(1, 1, At, B1); PG8_BAR; PG8_SCHED;
;             PG8_LDB(B0, 1, 0); PG8_LDB(B1, 1, 1); PG8_SCHED; PG8_LDA(At, 1, 0); PG8_STAGE(PG8_SA(0, 1), a2, cA10, cA11);
;             PG8_WAIT_V(8); PG8_WAIT_L(0); PG8_BAR; PG8_MMA(0, 0, At, B0); PG8_MMA(0, 1, At, B1); PG8_BAR; PG8_SCHED;
;             PG8_LDA(At, 1, 1); PG8_STAGE(PG8_SB(1, 0), b3, vB0, vB1); PG8_STAGE(PG8_SB(1, 1), b3 + hstepB, vB0, vB1); PG8_STAGE(PG8_SA(1, 0), a3, cA00, cA01);
;             PG8_WAIT_V(8); PG8_WAIT_L(0); PG8_BAR; PG8_MMA(1, 0, At, B0); PG8_MMA(1, 1, At, B1); PG8_BAR; PG8_SCHED;
.LBB0_1247:
	s_ashr_i32 s3, s2, 31
	s_lshl_b64 s[24:25], s[2:3], 19
	s_add_u32 s24, s36, s24
	s_addc_u32 s25, s37, s25
	s_and_b64 s[26:27], s[22:23], exec
	s_cselect_b32 s3, s25, s11
	s_cselect_b32 s54, s24, s10
	s_ashr_i32 s21, s20, 31
	s_lshl_b64 s[26:27], s[20:21], 19
	s_add_u32 s26, s40, s26
	s_addc_u32 s27, s41, s27
	s_and_b64 s[34:35], s[22:23], exec
	s_cselect_b32 s21, s27, s31
	s_cselect_b32 s55, s26, s30
	s_add_u32 s10, s10, 0x80
	s_addc_u32 s11, s11, 0
	s_add_u32 s56, s30, 0x100
	v_mov_b32_e32 v32, 0
	s_addc_u32 s58, s31, 0
	s_mov_b32 s59, -2
	ds_read_b128 v[24:27], v194
	ds_read_b128 v[28:31], v194 offset:1024
	ds_read_b128 v[16:19], v194 offset:2048
	ds_read_b128 v[20:23], v194 offset:3072
	ds_read_b128 v[8:11], v195
	ds_read_b128 v[12:15], v195 offset:1024
	ds_read_b128 v[0:3], v195 offset:2048
	ds_read_b128 v[4:7], v195 offset:3072
	s_add_u32 s30, s10, 0x80
	s_addc_u32 s31, s11, 0
	s_cmp_eq_u32 s59, 12
	s_cselect_b32 s35, s3, s31
	s_cselect_b32 s34, s54, s30
	s_cselect_b32 s31, s21, s58
	s_cselect_b32 s30, s55, s56
	v_lshl_add_u64 v[224:225], s[10:11], 0, v[178:179]
	s_add_i32 m0, s29, 0xc000
	ds_read_b128 v[182:185], v196
	ds_read_b128 v[186:189], v196 offset:1024
	ds_read_b128 v[200:203], v196 offset:2048
	ds_read_b128 v[204:207], v196 offset:3072
	ds_read_b128 v[208:211], v196 offset:4096
	ds_read_b128 v[212:215], v196 offset:5120
	ds_read_b128 v[216:219], v196 offset:6144
	ds_read_b128 v[220:223], v196 offset:7168
	global_load_lds_dwordx4 v[224:225], off
	v_lshl_add_u64 v[224:225], s[10:11], 0, v[176:177]
	s_add_i32 m0, s29, 0xe000
	s_nop 0
	global_load_lds_dwordx4 v[224:225], off
	s_waitcnt vmcnt(8)
	s_waitcnt lgkmcnt(0)
	s_barrier
	s_waitcnt lgkmcnt(0)
	v_mfma_f32_16x16x128_f8f6f4 v[156:159], v[24:31], v[182:189], 0
	v_mfma_f32_16x16x128_f8f6f4 v[144:147], v[16:23], v[182:189], 0
	v_mfma_f32_16x16x128_f8f6f4 v[140:143], v[24:31], v[200:207], 0
	v_mfma_f32_16x16x128_f8f6f4 v[132:135], v[16:23], v[200:207], 0
	v_mfma_f32_16x16x128_f8f6f4 v[124:127], v[24:31], v[208:215], 0
	v_mfma_f32_16x16x128_f8f6f4 v[116:119], v[16:23], v[208:215], 0
	v_mfma_f32_16x16x128_f8f6f4 v[108:111], v[24:31], v[216:223], 0
	v_mfma_f32_16x16x128_f8f6f4 v[100:103], v[16:23], v[216:223], 0
	v_mfma_f32_16x16x128_f8f6f4 v[152:155], v[8:15], v[182:189], 0
	v_mfma_f32_16x16x128_f8f6f4 v[148:151], v[0:7], v[182:189], 0
	v_mfma_f32_16x16x128_f8f6f4 v[136:139], v[8:15], v[200:207], 0
	v_mfma_f32_16x16x128_f8f6f4 v[128:131], v[0:7], v[200:207], 0
	v_mfma_f32_16x16x128_f8f6f4 v[120:123], v[8:15], v[208:215], 0
	v_mfma_f32_16x16x128_f8f6f4 v[112:115], v[0:7], v[208:215], 0
	v_mfma_f32_16x16x128_f8f6f4 v[104:107], v[8:15], v[216:223], 0
	v_mfma_f32_16x16x128_f8f6f4 v[96:99], v[0:7], v[216:223], 0
	s_barrier
	s_add_i32 s60, s50, s97
	v_lshl_add_u64 v[182:183], s[30:31], 0, v[162:163]
	s_mov_b32 m0, s60
	ds_read_b128 v[200:203], v196 offset:16384
	ds_read_b128 v[204:207], v196 offset:17408
	ds_read_b128 v[208:211], v196 offset:18432
	ds_read_b128 v[212:215], v196 offset:19456
	ds_read_b128 v[216:219], v196 offset:20480
	ds_read_b128 v[220:223], v196 offset:21504
	ds_read_b128 v[224:227], v196 offset:22528
	ds_read_b128 v[228:231], v196 offset:23552
	global_load_lds_dwordx4 v[182:183], off
	s_add_i32 m0, s60, 0x2000
	s_add_u32 s60, s30, 0x40000
	v_lshl_add_u64 v[184:185], s[30:31], 0, v[160:161]
	s_addc_u32 s61, s31, 0
	s_add_i32 s62, s51, s97
	global_load_lds_dwordx4 v[184:185], off
	v_lshl_add_u64 v[186:187], s[60:61], 0, v[162:163]
	s_mov_b32 m0, s62
	v_lshl_add_u64 v[188:189], s[34:35], 0, v[168:169]
	global_load_lds_dwordx4 v[186:187], off
	v_lshl_add_u64 v[186:187], s[60:61], 0, v[160:161]
	s_add_i32 m0, s62, 0x2000
	s_nop 0
	global_load_lds_dwordx4 v[186:187], off
	v_lshl_add_u64 v[186:187], s[34:35], 0, v[164:165]
	s_mov_b32 m0, s29
	s_nop 0
	global_load_lds_dwordx4 v[186:187], off
	s_mov_b32 m0, s43
	s_nop 0
	global_load_lds_dwordx4 v[188:189], off
	s_waitcnt vmcnt(8)
	s_waitcnt lgkmcnt(0)
	s_barrier
	s_waitcnt lgkmcnt(0)
	v_mfma_f32_16x16x128_f8f6f4 v[92:95], v[24:31], v[200:207], 0
	v_mfma_f32_16x16x128_f8f6f4 v[84:87], v[16:23], v[200:207], 0
	v_mfma_f32_16x16x128_f8f6f4 v[76:79], v[24:31], v[208:215], 0
	v_mfma_f32_16x16x128_f8f6f4 v[68:71], v[16:23], v[208:215], 0
	v_mfma_f32_16x16x128_f8f6f4 v[60:63], v[24:31], v[216:223], 0
	v_mfma_f32_16x16x128_f8f6f4 v[52:55], v[16:23], v[216:223], 0
	v_mfma_f32_16x16x128_f8f6f4 v[44:47], v[24:31], v[224:231], 0
	v_mfma_f32_16x16x128_f8f6f4 v[36:39], v[16:23], v[224:231], 0
	v_mfma_f32_16x16x128_f8f6f4 v[88:91], v[8:15], v[200:207], 0
	v_mfma_f32_16x16x128_f8f6f4 v[80:83], v[0:7], v[200:207], 0
	v_mfma_f32_16x16x128_f8f6f4 v[72:75], v[8:15], v[208:215], 0
	v_mfma_f32_16x16x128_f8f6f4 v[64:67], v[0:7], v[208:215], 0
	v_mfma_f32_16x16x128_f8f6f4 v[56:59], v[8:15], v[216:223], 0
	v_mfma_f32_16x16x128_f8f6f4 v[48:51], v[0:7], v[216:223], 0
	v_mfma_f32_16x16x128_f8f6f4 v[40:43], v[8:15], v[224:231], 0
	v_mfma_f32_16x16x128_f8f6f4 v[32:35], v[0:7], v[224:231], 0
	s_barrier
	s_add_i32 s60, 0, 0x18000
	s_add_i32 s61, 0, 0x1c000
	v_add_u32_e32 v12, s60, v191
	v_add_u32_e32 v28, s61, v191
	ds_read_b128 v[0:3], v12
	ds_read_b128 v[4:7], v12 offset:1024
	ds_read_b128 v[8:11], v12 offset:2048
	ds_read_b128 v[12:15], v12 offset:3072
	ds_read_b128 v[16:19], v28
	ds_read_b128 v[20:23], v28 offset:1024
	ds_read_b128 v[24:27], v28 offset:2048
	ds_read_b128 v[28:31], v28 offset:3072
	s_mov_b32 m0, s44
	v_lshl_add_u64 v[232:233], s[34:35], 0, v[166:167]
	ds_read_b128 v[200:203], v196 offset:32768
	ds_read_b128 v[204:207], v196 offset:33792
	ds_read_b128 v[208:211], v196 offset:34816
	ds_read_b128 v[212:215], v196 offset:35840
	ds_read_b128 v[216:219], v196 offset:36864
	ds_read_b128 v[220:223], v196 offset:37888
	ds_read_b128 v[224:227], v196 offset:38912
	ds_read_b128 v[228:231], v196 offset:39936
	global_load_lds_dwordx4 v[232:233], off
	v_lshl_add_u64 v[232:233], s[34:35], 0, v[170:171]
	s_mov_b32 m0, s45
	s_nop 0
	global_load_lds_dwordx4 v[232:233], off
	s_waitcnt vmcnt(8)
	s_waitcnt lgkmcnt(0)
	s_barrier
; #define PG8_STAGE(bufoff, gbase, o0, o1) do { \
;         __builtin_amdgcn_global_load_lds((const unsigned*)((const char*)(gbase) + (o0)), (LAS unsigned*)(lds + (bufoff) + ldsw), 16, 0, 0); \
;         __builtin_amdgcn_global_load_lds((const unsigned*)((const char*)(gbase) + (o1)), (LAS unsigned*)(lds + (bufoff) + ldsw + 8192), 16, 0, 0); } while (0)
; #define PG8_LDA(dst, b, h) do { _Pragma("unroll") for (int m = 0; m < 4; ++m) _Pragma("unroll") for (int k = 0; k < 2; ++k) dst[m][k] = *(const LAS bf16x8*)(lds + PG8_SA(b, h) + aoff + m * 2048 + k * 1024); } while (0)
; #define PG8_LDB(dst, b, h) do { _Pragma("unroll") for (int n = 0; n < 2; ++n) _Pragma("unroll") for (int k = 0; k < 2; ++k) dst[n][k] = *(const LAS bf16x8*)(lds + PG8_SB(b, h) + boff + n * 2048 + k * 1024); } while (0)
; template <class Epi, class Sched, class Prob>
; __device__ __forceinline__ void gemm_phase(LAS unsigned char* lds, LAS unsigned char* lds_epi, const Prob g, const Sched& S, const Epi& E, int wid) {
;     ...
;         for (int t = 0; t < nt; t += 2) {
;             const bool last = (t == nt - 2);
;             const char* a1 = cA + (size_t)(t + 1) * kstep;
;             const char* a2 = last ? nA : cA + (size_t)(t + 2) * kstep; const char* b2 = last ? nB : cB + (size_t)(t + 2) * kstep;
;             const char* a3 = a2 + kstep; const char* b3 = b2 + kstep;
;             PG8_LDB(B0, 0, 0); PG8_LDB(B1, 0, 1); PG8_SCHED; PG8_LDA(At, 0, 0); PG8_STAGE(PG8_SA(1, 1), a1, cA10, cA11);
;             PG8_WAIT_V(8); PG8_WAIT_L(0); PG8_BAR; PG8_MMA(0, 0, At, B0); PG8_MMA(0, 1, At, B1); PG8_BAR; PG8_SCHED;
;             PG8_LDA(At, 0, 1); PG8_STAGE(PG8_SB(0, 0), b2, vB0, vB1); PG8_STAGE(PG8_SB(0, 1), b2 + hstepB, vB0, vB1); PG8_STAGE(PG8_SA(0, 0), a2, cA00, cA01);
;             PG8_WAIT_V(8); PG8_WAIT_L(0); PG8_BAR; PG8_MMA(1, 0, At, B0); PG8_MMA(1, 1, At, B1); PG8_BAR; PG8_SCHED;
;             PG8_LDB(B0, 1, 0); PG8_LDB(B1, 1, 1); PG8_SCHED; PG8_LDA(At, 1, 0); PG8_STAGE(PG8_SA(0, 1), a2, cA10, cA11);
;             PG8_WAIT_V(8); PG8_WAIT_L(0); PG8_BAR; PG8_MMA(0, 0, At, B0); PG8_MMA(0, 1, At, B1); PG8_BAR; PG8_SCHED;
;             PG8_LDA(At, 1, 1); PG8_STAGE(PG8_SB(1, 0), b3, vB0, vB1); PG8_STAGE(PG8_SB(1, 1), b3 + hstepB, vB0, vB1); PG8_STAGE(PG8_SA(1, 0), a3, cA00, cA01);
;             PG8_WAIT_V(8); PG8_WAIT_L(0); PG8_BAR; PG8_MMA(1, 0, At, B0); PG8_MMA(1, 1, At, B1); PG8_BAR; PG8_SCHED;
	s_waitcnt lgkmcnt(0)
	v_mfma_f32_16x16x128_f8f6f4 v[156:159], v[0:7], v[200:207], v[156:159]
	v_mfma_f32_16x16x128_f8f6f4 v[144:147], v[8:15], v[200:207], v[144:147]
	v_mfma_f32_16x16x128_f8f6f4 v[140:143], v[0:7], v[208:215], v[140:143]
	v_mfma_f32_16x16x128_f8f6f4 v[132:135], v[8:15], v[208:215], v[132:135]
	v_mfma_f32_16x16x128_f8f6f4 v[124:127], v[0:7], v[216:223], v[124:127]
	v_mfma_f32_16x16x128_f8f6f4 v[116:119], v[8:15], v[216:223], v[116:119]
	v_mfma_f32_16x16x128_f8f6f4 v[108:111], v[0:7], v[224:231], v[108:111]
	v_mfma_f32_16x16x128_f8f6f4 v[100:103], v[8:15], v[224:231], v[100:103]
	v_mfma_f32_16x16x128_f8f6f4 v[152:155], v[16:23], v[200:207], v[152:155]
	v_mfma_f32_16x16x128_f8f6f4 v[148:151], v[24:31], v[200:207], v[148:151]
	v_mfma_f32_16x16x128_f8f6f4 v[136:139], v[16:23], v[208:215], v[136:139]
	v_mfma_f32_16x16x128_f8f6f4 v[128:131], v[24:31], v[208:215], v[128:131]
	v_mfma_f32_16x16x128_f8f6f4 v[120:123], v[16:23], v[216:223], v[120:123]
	v_mfma_f32_16x16x128_f8f6f4 v[112:115], v[24:31], v[216:223], v[112:115]
	v_mfma_f32_16x16x128_f8f6f4 v[104:107], v[16:23], v[224:231], v[104:107]
	v_mfma_f32_16x16x128_f8f6f4 v[96:99], v[24:31], v[224:231], v[96:99]
	s_barrier
	s_add_i32 s34, s60, s97
	v_lshl_add_u64 v[182:183], v[182:183], 0, s[14:15]
	s_mov_b32 m0, s34
	ds_read_b128 v[200:203], v196 offset:49152
	ds_read_b128 v[204:207], v196 offset:50176
	ds_read_b128 v[208:211], v196 offset:51200
	ds_read_b128 v[212:215], v196 offset:52224
	ds_read_b128 v[216:219], v196 offset:53248
	ds_read_b128 v[220:223], v196 offset:54272
	ds_read_b128 v[224:227], v196 offset:55296
	ds_read_b128 v[228:231], v196 offset:56320
	global_load_lds_dwordx4 v[182:183], off
	s_add_i32 m0, s34, 0x2000
	s_add_u32 s30, s30, 0x40080
	v_lshl_add_u64 v[182:183], v[184:185], 0, s[14:15]
	s_addc_u32 s31, s31, 0
	s_add_i32 s34, s61, s97
	global_load_lds_dwordx4 v[182:183], off
	v_lshl_add_u64 v[182:183], s[30:31], 0, v[162:163]
	s_mov_b32 m0, s34
	s_nop 0
	global_load_lds_dwordx4 v[182:183], off
	v_lshl_add_u64 v[182:183], s[30:31], 0, v[160:161]
	s_add_i32 m0, s34, 0x2000
	s_nop 0
	global_load_lds_dwordx4 v[182:183], off
	v_lshl_add_u64 v[182:183], v[186:187], 0, s[14:15]
	s_mov_b32 m0, s48
	s_nop 0
	global_load_lds_dwordx4 v[182:183], off
	v_lshl_add_u64 v[182:183], v[188:189], 0, s[14:15]
	s_mov_b32 m0, s49
	s_nop 0
	global_load_lds_dwordx4 v[182:183], off
	s_waitcnt vmcnt(8)
	s_waitcnt lgkmcnt(0)
	s_barrier
	s_waitcnt lgkmcnt(0)
	v_mfma_f32_16x16x128_f8f6f4 v[92:95], v[0:7], v[200:207], v[92:95]
	v_mfma_f32_16x16x128_f8f6f4 v[84:87], v[8:15], v[200:207], v[84:87]
	v_mfma_f32_16x16x128_f8f6f4 v[76:79], v[0:7], v[208:215], v[76:79]
	v_mfma_f32_16x16x128_f8f6f4 v[68:71], v[8:15], v[208:215], v[68:71]
	v_mfma_f32_16x16x128_f8f6f4 v[60:63], v[0:7], v[216:223], v[60:63]
	v_mfma_f32_16x16x128_f8f6f4 v[52:55], v[8:15], v[216:223], v[52:55]
	v_mfma_f32_16x16x128_f8f6f4 v[44:47], v[0:7], v[224:231], v[44:47]
	v_mfma_f32_16x16x128_f8f6f4 v[36:39], v[8:15], v[224:231], v[36:39]
	v_mfma_f32_16x16x128_f8f6f4 v[88:91], v[16:23], v[200:207], v[88:91]
	v_mfma_f32_16x16x128_f8f6f4 v[80:83], v[24:31], v[200:207], v[80:83]
	v_mfma_f32_16x16x128_f8f6f4 v[72:75], v[16:23], v[208:215], v[72:75]
	v_mfma_f32_16x16x128_f8f6f4 v[64:67], v[24:31], v[208:215], v[64:67]
	v_mfma_f32_16x16x128_f8f6f4 v[56:59], v[16:23], v[216:223], v[56:59]
	v_mfma_f32_16x16x128_f8f6f4 v[48:51], v[24:31], v[216:223], v[48:51]
	v_mfma_f32_16x16x128_f8f6f4 v[40:43], v[16:23], v[224:231], v[40:43]
	v_mfma_f32_16x16x128_f8f6f4 v[32:35], v[24:31], v[224:231], v[32:35]
	s_barrier
	s_add_i32 s59, s59, 2
	s_add_u32 s10, s10, 0x100
	s_addc_u32 s11, s11, 0
	s_add_u32 s56, s56, 0x100
	s_addc_u32 s58, s58, 0
	s_cmp_gt_u32 s59, 13
.LBB0_1248:
	ds_read_b128 v[24:27], v194
	ds_read_b128 v[28:31], v194 offset:1024
	ds_read_b128 v[16:19], v194 offset:2048
	ds_read_b128 v[20:23], v194 offset:3072
	ds_read_b128 v[8:11], v195
	ds_read_b128 v[12:15], v195 offset:1024
	ds_read_b128 v[0:3], v195 offset:2048
	ds_read_b128 v[4:7], v195 offset:3072
	s_add_u32 s30, s10, 0x80
	s_addc_u32 s31, s11, 0
	s_cmp_eq_u32 s59, 12
	s_cselect_b32 s35, s3, s31
	s_cselect_b32 s34, s54, s30
	s_cselect_b32 s31, s21, s58
	s_cselect_b32 s30, s55, s56
	v_lshl_add_u64 v[224:225], s[10:11], 0, v[178:179]
	s_add_i32 m0, s29, 0xc000
	ds_read_b128 v[182:185], v196
	ds_read_b128 v[186:189], v196 offset:1024
	ds_read_b128 v[200:203], v196 offset:2048
	ds_read_b128 v[204:207], v196 offset:3072
	ds_read_b128 v[208:211], v196 offset:4096
	ds_read_b128 v[212:215], v196 offset:5120
	ds_read_b128 v[216:219], v196 offset:6144
	ds_read_b128 v[220:223], v196 offset:7168
	global_load_lds_dwordx4 v[224:225], off
	v_lshl_add_u64 v[224:225], s[10:11], 0, v[176:177]
	s_add_i32 m0, s29, 0xe000
	s_nop 0
	global_load_lds_dwordx4 v[224:225], off
	s_waitcnt vmcnt(8)
	s_waitcnt lgkmcnt(0)
	s_barrier
	s_waitcnt lgkmcnt(0)
	v_mfma_f32_16x16x128_f8f6f4 v[156:159], v[24:31], v[182:189], v[156:159]
	v_mfma_f32_16x16x128_f8f6f4 v[144:147], v[16:23], v[182:189], v[144:147]
	v_mfma_f32_16x16x128_f8f6f4 v[140:143], v[24:31], v[200:207], v[140:143]
	v_mfma_f32_16x16x128_f8f6f4 v[132:135], v[16:23], v[200:207], v[132:135]
	v_mfma_f32_16x16x128_f8f6f4 v[124:127], v[24:31], v[208:215], v[124:127]
	v_mfma_f32_16x16x128_f8f6f4 v[116:119], v[16:23], v[208:215], v[116:119]
	v_mfma_f32_16x16x128_f8f6f4 v[108:111], v[24:31], v[216:223], v[108:111]
	v_mfma_f32_16x16x128_f8f6f4 v[100:103], v[16:23], v[216:223], v[100:103]
	v_mfma_f32_16x16x128_f8f6f4 v[152:155], v[8:15], v[182:189], v[152:155]
	v_mfma_f32_16x16x128_f8f6f4 v[148:151], v[0:7], v[182:189], v[148:151]
	v_mfma_f32_16x16x128_f8f6f4 v[136:139], v[8:15], v[200:207], v[136:139]
	v_mfma_f32_16x16x128_f8f6f4 v[128:131], v[0:7], v[200:207], v[128:131]
	v_mfma_f32_16x16x128_f8f6f4 v[120:123], v[8:15], v[208:215], v[120:123]
	v_mfma_f32_16x16x128_f8f6f4 v[112:115], v[0:7], v[208:215], v[112:115]
	v_mfma_f32_16x16x128_f8f6f4 v[104:107], v[8:15], v[216:223], v[104:107]
	v_mfma_f32_16x16x128_f8f6f4 v[96:99], v[0:7], v[216:223], v[96:99]
	s_barrier
; #define PG8_STAGE(bufoff, gbase, o0, o1) do { \
;         __builtin_amdgcn_global_load_lds((const unsigned*)((const char*)(gbase) + (o0)), (LAS unsigned*)(lds + (bufoff) + ldsw), 16, 0, 0); \
;         __builtin_amdgcn_global_load_lds((const unsigned*)((const char*)(gbase) + (o1)), (LAS unsigned*)(lds + (bufoff) + ldsw + 8192), 16, 0, 0); } while (0)
; #define PG8_LDA(dst, b, h) do { _Pragma("unroll") for (int m = 0; m < 4; ++m) _Pragma("unroll") for (int k = 0; k < 2; ++k) dst[m][k] = *(const LAS bf16x8*)(lds + PG8_SA(b, h) + aoff + m * 2048 + k * 1024); } while (0)
; #define PG8_LDB(dst, b, h) do { _Pragma("unroll") for (int n = 0; n < 2; ++n) _Pragma("unroll") for (int k = 0; k < 2; ++k) dst[n][k] = *(const LAS bf16x8*)(lds + PG8_SB(b, h) + boff + n * 2048 + k * 1024); } while (0)
; template <class Epi, class Sched, class Prob>
; __device__ __forceinline__ void gemm_phase(LAS unsigned char* lds, LAS unsigned char* lds_epi, const Prob g, const Sched& S, const Epi& E, int wid) {
;     ...
;         for (int t = 0; t < nt; t += 2) {
;             const bool last = (t == nt - 2);
;             const char* a1 = cA + (size_t)(t + 1) * kstep;
;             const char* a2 = last ? nA : cA + (size_t)(t + 2) * kstep; const char* b2 = last ? nB : cB + (size_t)(t + 2) * kstep;
;             const char* a3 = a2 + kstep; const char* b3 = b2 + kstep;
;             PG8_LDB(B0, 0, 0); PG8_LDB(B1, 0, 1); PG8_SCHED; PG8_LDA(At, 0, 0); PG8_STAGE(PG8_SA(1, 1), a1, cA10, cA11);
;             PG8_WAIT_V(8); PG8_WAIT_L(0); PG8_BAR; PG8_MMA(0, 0, At, B0); PG8_MMA(0, 1, At, B1); PG8_BAR; PG8_SCHED;
;             PG8_LDA(At, 0, 1); PG8_STAGE(PG8_SB(0, 0), b2, vB0, vB1); PG8_STAGE(PG8_SB(0, 1), b2 + hstepB, vB0, vB1); PG8_STAGE(PG8_SA(0, 0), a2, cA00, cA01);
;             PG8_WAIT_V(8); PG8_WAIT_L(0); PG8_BAR; PG8_MMA(1, 0, At, B0); PG8_MMA(1, 1, At, B1); PG8_BAR; PG8_SCHED;
;             PG8_LDB(B0, 1, 0); PG8_LDB(B1, 1, 1); PG8_SCHED; PG8_LDA(At, 1, 0); PG8_STAGE(PG8_SA(0, 1), a2, cA10, cA11);
;             PG8_WAIT_V(8); PG8_WAIT_L(0); PG8_BAR; PG8_MMA(0, 0, At, B0); PG8_MMA(0, 1, At, B1); PG8_BAR; PG8_SCHED;
;             PG8_LDA(At, 1, 1); PG8_STAGE(PG8_SB(1, 0), b3, vB0, vB1); PG8_STAGE(PG8_SB(1, 1), b3 + hstepB, vB0, vB1); PG8_STAGE(PG8_SA(1, 0), a3, cA00, cA01);
;             PG8_WAIT_V(8); PG8_WAIT_L(0); PG8_BAR; PG8_MMA(1, 0, At, B0); PG8_MMA(1, 1, At, B1); PG8_BAR; PG8_SCHED;
	s_add_i32 s60, s50, s97
	v_lshl_add_u64 v[182:183], s[30:31], 0, v[162:163]
	s_mov_b32 m0, s60
	ds_read_b128 v[200:203], v196 offset:16384
	ds_read_b128 v[204:207], v196 offset:17408
	ds_read_b128 v[208:211], v196 offset:18432
	ds_read_b128 v[212:215], v196 offset:19456
	ds_read_b128 v[216:219], v196 offset:20480
	ds_read_b128 v[220:223], v196 offset:21504
	ds_read_b128 v[224:227], v196 offset:22528
	ds_read_b128 v[228:231], v196 offset:23552
	global_load_lds_dwordx4 v[182:183], off
	s_add_i32 m0, s60, 0x2000
	s_add_u32 s60, s30, 0x40000
	v_lshl_add_u64 v[184:185], s[30:31], 0, v[160:161]
	s_addc_u32 s61, s31, 0
	s_add_i32 s62, s51, s97
	global_load_lds_dwordx4 v[184:185], off
	v_lshl_add_u64 v[186:187], s[60:61], 0, v[162:163]
	s_mov_b32 m0, s62
	v_lshl_add_u64 v[188:189], s[34:35], 0, v[168:169]
	global_load_lds_dwordx4 v[186:187], off
	v_lshl_add_u64 v[186:187], s[60:61], 0, v[160:161]
	s_add_i32 m0, s62, 0x2000
	s_nop 0
	global_load_lds_dwordx4 v[186:187], off
	v_lshl_add_u64 v[186:187], s[34:35], 0, v[164:165]
	s_mov_b32 m0, s29
	s_nop 0
	global_load_lds_dwordx4 v[186:187], off
	s_mov_b32 m0, s43
	s_nop 0
	global_load_lds_dwordx4 v[188:189], off
	s_waitcnt vmcnt(8)
	s_waitcnt lgkmcnt(0)
	s_barrier
	s_waitcnt lgkmcnt(0)
	v_mfma_f32_16x16x128_f8f6f4 v[92:95], v[24:31], v[200:207], v[92:95]
	v_mfma_f32_16x16x128_f8f6f4 v[84:87], v[16:23], v[200:207], v[84:87]
	v_mfma_f32_16x16x128_f8f6f4 v[76:79], v[24:31], v[208:215], v[76:79]
	v_mfma_f32_16x16x128_f8f6f4 v[68:71], v[16:23], v[208:215], v[68:71]
	v_mfma_f32_16x16x128_f8f6f4 v[60:63], v[24:31], v[216:223], v[60:63]
	v_mfma_f32_16x16x128_f8f6f4 v[52:55], v[16:23], v[216:223], v[52:55]
	v_mfma_f32_16x16x128_f8f6f4 v[44:47], v[24:31], v[224:231], v[44:47]
	v_mfma_f32_16x16x128_f8f6f4 v[36:39], v[16:23], v[224:231], v[36:39]
	v_mfma_f32_16x16x128_f8f6f4 v[88:91], v[8:15], v[200:207], v[88:91]
	v_mfma_f32_16x16x128_f8f6f4 v[80:83], v[0:7], v[200:207], v[80:83]
	v_mfma_f32_16x16x128_f8f6f4 v[72:75], v[8:15], v[208:215], v[72:75]
	v_mfma_f32_16x16x128_f8f6f4 v[64:67], v[0:7], v[208:215], v[64:67]
	v_mfma_f32_16x16x128_f8f6f4 v[56:59], v[8:15], v[216:223], v[56:59]
	v_mfma_f32_16x16x128_f8f6f4 v[48:51], v[0:7], v[216:223], v[48:51]
	v_mfma_f32_16x16x128_f8f6f4 v[40:43], v[8:15], v[224:231], v[40:43]
	v_mfma_f32_16x16x128_f8f6f4 v[32:35], v[0:7], v[224:231], v[32:35]
	s_barrier
	s_add_i32 s60, 0, 0x18000
	s_add_i32 s61, 0, 0x1c000
	v_add_u32_e32 v12, s60, v191
	v_add_u32_e32 v28, s61, v191
	ds_read_b128 v[0:3], v12
	ds_read_b128 v[4:7], v12 offset:1024
	ds_read_b128 v[8:11], v12 offset:2048
	ds_read_b128 v[12:15], v12 offset:3072
	ds_read_b128 v[16:19], v28
	ds_read_b128 v[20:23], v28 offset:1024
	ds_read_b128 v[24:27], v28 offset:2048
	ds_read_b128 v[28:31], v28 offset:3072
	s_mov_b32 m0, s44
	v_lshl_add_u64 v[232:233], s[34:35], 0, v[166:167]
	ds_read_b128 v[200:203], v196 offset:32768
	ds_read_b128 v[204:207], v196 offset:33792
	ds_read_b128 v[208:211], v196 offset:34816
	ds_read_b128 v[212:215], v196 offset:35840
	ds_read_b128 v[216:219], v196 offset:36864
	ds_read_b128 v[220:223], v196 offset:37888
	ds_read_b128 v[224:227], v196 offset:38912
	ds_read_b128 v[228:231], v196 offset:39936
	global_load_lds_dwordx4 v[232:233], off
	v_lshl_add_u64 v[232:233], s[34:35], 0, v[170:171]
	s_mov_b32 m0, s45
	s_nop 0
	global_load_lds_dwordx4 v[232:233], off
	s_waitcnt vmcnt(8)
	s_waitcnt lgkmcnt(0)
	s_barrier
; #define PG8_STAGE(bufoff, gbase, o0, o1) do { \
;         __builtin_amdgcn_global_load_lds((const unsigned*)((const char*)(gbase) + (o0)), (LAS unsigned*)(lds + (bufoff) + ldsw), 16, 0, 0); \
;         __builtin_amdgcn_global_load_lds((const unsigned*)((const char*)(gbase) + (o1)), (LAS unsigned*)(lds + (bufoff) + ldsw + 8192), 16, 0, 0); } while (0)
; #define PG8_LDA(dst, b, h) do { _Pragma("unroll") for (int m = 0; m < 4; ++m) _Pragma("unroll") for (int k = 0; k < 2; ++k) dst[m][k] = *(const LAS bf16x8*)(lds + PG8_SA(b, h) + aoff + m * 2048 + k * 1024); } while (0)
; #define PG8_WAIT_V(n) asm volatile("s_waitcnt vmcnt(" #n ")" ::: "memory")
; template <class Epi, class Sched, class Prob>
; __device__ __forceinline__ void gemm_phase(LAS unsigned char* lds, LAS unsigned char* lds_epi, const Prob g, const Sched& S, const Epi& E, int wid) {
;     ...
;         for (int t = 0; t < nt; t += 2) {
;             const bool last = (t == nt - 2);
;             const char* a1 = cA + (size_t)(t + 1) * kstep;
;             const char* a2 = last ? nA : cA + (size_t)(t + 2) * kstep; const char* b2 = last ? nB : cB + (size_t)(t + 2) * kstep;
;             const char* a3 = a2 + kstep; const char* b3 = b2 + kstep;
;             PG8_LDB(B0, 0, 0); PG8_LDB(B1, 0, 1); PG8_SCHED; PG8_LDA(At, 0, 0); PG8_STAGE(PG8_SA(1, 1), a1, cA10, cA11);
;             PG8_WAIT_V(8); PG8_WAIT_L(0); PG8_BAR; PG8_MMA(0, 0, At, B0); PG8_MMA(0, 1, At, B1); PG8_BAR; PG8_SCHED;
;             PG8_LDA(At, 0, 1); PG8_STAGE(PG8_SB(0, 0), b2, vB0, vB1); PG8_STAGE(PG8_SB(0, 1), b2 + hstepB, vB0, vB1); PG8_STAGE(PG8_SA(0, 0), a2, cA00, cA01);
;             PG8_WAIT_V(8); PG8_WAIT_L(0); PG8_BAR; PG8_MMA(1, 0, At, B0); PG8_MMA(1, 1, At, B1); PG8_BAR; PG8_SCHED;
;             PG8_LDB(B0, 1, 0); PG8_LDB(B1, 1, 1); PG8_SCHED; PG8_LDA(At, 1, 0); PG8_STAGE(PG8_SA(0, 1), a2, cA10, cA11);
;             PG8_WAIT_V(8); PG8_WAIT_L(0); PG8_BAR; PG8_MMA(0, 0, At, B0); PG8_MMA(0, 1, At, B1); PG8_BAR; PG8_SCHED;
;             PG8_LDA(At, 1, 1); PG8_STAGE(PG8_SB(1, 0), b3, vB0, vB1); PG8_STAGE(PG8_SB(1, 1), b3 + hstepB, vB0, vB1); PG8_STAGE(PG8_SA(1, 0), a3, cA00, cA01);
;             PG8_WAIT_V(8); PG8_WAIT_L(0); PG8_BAR; PG8_MMA(1, 0, At, B0); PG8_MMA(1, 1, At, B1); PG8_BAR; PG8_SCHED;
;         }
;         if constexpr (Prob::FP8) asm volatile("s_nop 7\n\ts_nop 7\n\ts_nop 7" ::: "memory");
;         if (wr == 0) PG8_BAR;
	s_waitcnt lgkmcnt(0)
	v_mfma_f32_16x16x128_f8f6f4 v[156:159], v[0:7], v[200:207], v[156:159]
	v_mfma_f32_16x16x128_f8f6f4 v[144:147], v[8:15], v[200:207], v[144:147]
	v_mfma_f32_16x16x128_f8f6f4 v[140:143], v[0:7], v[208:215], v[140:143]
	v_mfma_f32_16x16x128_f8f6f4 v[132:135], v[8:15], v[208:215], v[132:135]
	v_mfma_f32_16x16x128_f8f6f4 v[124:127], v[0:7], v[216:223], v[124:127]
	v_mfma_f32_16x16x128_f8f6f4 v[116:119], v[8:15], v[216:223], v[116:119]
	v_mfma_f32_16x16x128_f8f6f4 v[108:111], v[0:7], v[224:231], v[108:111]
	v_mfma_f32_16x16x128_f8f6f4 v[100:103], v[8:15], v[224:231], v[100:103]
	v_mfma_f32_16x16x128_f8f6f4 v[152:155], v[16:23], v[200:207], v[152:155]
	v_mfma_f32_16x16x128_f8f6f4 v[148:151], v[24:31], v[200:207], v[148:151]
	v_mfma_f32_16x16x128_f8f6f4 v[136:139], v[16:23], v[208:215], v[136:139]
	v_mfma_f32_16x16x128_f8f6f4 v[128:131], v[24:31], v[208:215], v[128:131]
	v_mfma_f32_16x16x128_f8f6f4 v[120:123], v[16:23], v[216:223], v[120:123]
	v_mfma_f32_16x16x128_f8f6f4 v[112:115], v[24:31], v[216:223], v[112:115]
	v_mfma_f32_16x16x128_f8f6f4 v[104:107], v[16:23], v[224:231], v[104:107]
	v_mfma_f32_16x16x128_f8f6f4 v[96:99], v[24:31], v[224:231], v[96:99]
	s_barrier
	s_add_i32 s34, s60, s97
	v_lshl_add_u64 v[182:183], v[182:183], 0, s[14:15]
	s_mov_b32 m0, s34
	ds_read_b128 v[200:203], v196 offset:49152
	ds_read_b128 v[204:207], v196 offset:50176
	ds_read_b128 v[208:211], v196 offset:51200
	ds_read_b128 v[212:215], v196 offset:52224
	ds_read_b128 v[216:219], v196 offset:53248
	ds_read_b128 v[220:223], v196 offset:54272
	ds_read_b128 v[224:227], v196 offset:55296
	ds_read_b128 v[228:231], v196 offset:56320
	global_load_lds_dwordx4 v[182:183], off
	s_add_i32 m0, s34, 0x2000
	s_add_u32 s30, s30, 0x40080
	v_lshl_add_u64 v[182:183], v[184:185], 0, s[14:15]
	s_addc_u32 s31, s31, 0
	s_add_i32 s34, s61, s97
	global_load_lds_dwordx4 v[182:183], off
	v_lshl_add_u64 v[182:183], s[30:31], 0, v[162:163]
	s_mov_b32 m0, s34
	s_nop 0
	global_load_lds_dwordx4 v[182:183], off
	v_lshl_add_u64 v[182:183], s[30:31], 0, v[160:161]
	s_add_i32 m0, s34, 0x2000
	s_nop 0
	global_load_lds_dwordx4 v[182:183], off
	v_lshl_add_u64 v[182:183], v[186:187], 0, s[14:15]
	s_mov_b32 m0, s48
	s_nop 0
	global_load_lds_dwordx4 v[182:183], off
	v_lshl_add_u64 v[182:183], v[188:189], 0, s[14:15]
	s_mov_b32 m0, s49
	s_nop 0
	global_load_lds_dwordx4 v[182:183], off
	s_waitcnt vmcnt(8)
	s_waitcnt lgkmcnt(0)
	s_barrier
	s_waitcnt lgkmcnt(0)
	v_mfma_f32_16x16x128_f8f6f4 v[92:95], v[0:7], v[200:207], v[92:95]
	v_mfma_f32_16x16x128_f8f6f4 v[84:87], v[8:15], v[200:207], v[84:87]
	v_mfma_f32_16x16x128_f8f6f4 v[76:79], v[0:7], v[208:215], v[76:79]
	v_mfma_f32_16x16x128_f8f6f4 v[68:71], v[8:15], v[208:215], v[68:71]
	v_mfma_f32_16x16x128_f8f6f4 v[60:63], v[0:7], v[216:223], v[60:63]
	v_mfma_f32_16x16x128_f8f6f4 v[52:55], v[8:15], v[216:223], v[52:55]
	v_mfma_f32_16x16x128_f8f6f4 v[44:47], v[0:7], v[224:231], v[44:47]
	v_mfma_f32_16x16x128_f8f6f4 v[36:39], v[8:15], v[224:231], v[36:39]
	v_mfma_f32_16x16x128_f8f6f4 v[88:91], v[16:23], v[200:207], v[88:91]
	v_mfma_f32_16x16x128_f8f6f4 v[80:83], v[24:31], v[200:207], v[80:83]
	v_mfma_f32_16x16x128_f8f6f4 v[72:75], v[16:23], v[208:215], v[72:75]
	v_mfma_f32_16x16x128_f8f6f4 v[64:67], v[24:31], v[208:215], v[64:67]
	v_mfma_f32_16x16x128_f8f6f4 v[56:59], v[16:23], v[216:223], v[56:59]
	v_mfma_f32_16x16x128_f8f6f4 v[48:51], v[24:31], v[216:223], v[48:51]
	v_mfma_f32_16x16x128_f8f6f4 v[40:43], v[16:23], v[224:231], v[40:43]
	v_mfma_f32_16x16x128_f8f6f4 v[32:35], v[24:31], v[224:231], v[32:35]
	s_barrier
	s_add_i32 s59, s59, 2
	s_add_u32 s10, s10, 0x100
	s_addc_u32 s11, s11, 0
	s_add_u32 s56, s56, 0x100
	s_addc_u32 s58, s58, 0
	s_cmp_gt_u32 s59, 13
	s_cbranch_scc0 .LBB0_1248
	v_readlane_b32 s10, v254, 27
	v_readlane_b32 s11, v254, 28
	s_and_b64 vcc, exec, s[10:11]
	s_cbranch_vccz .LBB0_1251
	s_barrier

; #define PG8_STAGE(bufoff, gbase, o0, o1) do { \
;         __builtin_amdgcn_global_load_lds((const unsigned*)((const char*)(gbase) + (o0)), (LAS unsigned*)(lds + (bufoff) + ldsw), 16, 0, 0); \
;         __builtin_amdgcn_global_load_lds((const unsigned*)((const char*)(gbase) + (o1)), (LAS unsigned*)(lds + (bufoff) + ldsw + 8192), 16, 0, 0); } while (0)
; #define PG8_LDA(dst, b, h) do { _Pragma("unroll") for (int m = 0; m < 4; ++m) _Pragma("unroll") for (int k = 0; k < 2; ++k) dst[m][k] = *(const LAS bf16x8*)(lds + PG8_SA(b, h) + aoff + m * 2048 + k * 1024); } while (0)
; #define PG8_LDB(dst, b, h) do { _Pragma("unroll") for (int n = 0; n < 2; ++n) _Pragma("unroll") for (int k = 0; k < 2; ++k) dst[n][k] = *(const LAS bf16x8*)(lds + PG8_SB(b, h) + boff + n * 2048 + k * 1024); } while (0)
; template <class Epi, class Sched, class Prob>
; __device__ __forceinline__ void gemm_phase(LAS unsigned char* lds, LAS unsigned char* lds_epi, const Prob g, const Sched& S, const Epi& E, int wid) {
;     ...
;         for (int t = 0; t < nt; t += 2) {
;             const bool last = (t == nt - 2);
;             const char* a1 = cA + (size_t)(t + 1) * kstep;
;             const char* a2 = last ? nA : cA + (size_t)(t + 2) * kstep; const char* b2 = last ? nB : cB + (size_t)(t + 2) * kstep;
;             const char* a3 = a2 + kstep; const char* b3 = b2 + kstep;
;             PG8_LDB(B0, 0, 0); PG8_LDB(B1, 0, 1); PG8_SCHED; PG8_LDA(At, 0, 0); PG8_STAGE(PG8_SA(1, 1), a1, cA10, cA11);
;             PG8_WAIT_V(8); PG8_WAIT_L(0); PG8_BAR; PG8_MMA(0, 0, At, B0); PG8_MMA(0, 1, At, B1); PG8_BAR; PG8_SCHED;
;             PG8_LDA(At, 0, 1); PG8_STAGE(PG8_SB(0, 0), b2, vB0, vB1); PG8_STAGE(PG8_SB(0, 1), b2 + hstepB, vB0, vB1); PG8_STAGE(PG8_SA(0, 0), a2, cA00, cA01);
;             PG8_WAIT_V(8); PG8_WAIT_L(0); PG8_BAR; PG8_MMA(1, 0, At, B0); PG8_MMA(1, 1, At, B1); PG8_BAR; PG8_SCHED;
;             PG8_LDB(B0, 1, 0); PG8_LDB(B1, 1, 1); PG8_SCHED; PG8_LDA(At, 1, 0); PG8_STAGE(PG8_SA(0, 1), a2, cA10, cA11);
;             PG8_WAIT_V(8); PG8_WAIT_L(0); PG8_BAR; PG8_MMA(0, 0, At, B0); PG8_MMA(0, 1, At, B1); PG8_BAR; PG8_SCHED;
;             PG8_LDA(At, 1, 1); PG8_STAGE(PG8_SB(1, 0), b3, vB0, vB1); PG8_STAGE(PG8_SB(1, 1), b3 + hstepB, vB0, vB1); PG8_STAGE(PG8_SA(1, 0), a3, cA00, cA01);
;             PG8_WAIT_V(8); PG8_WAIT_L(0); PG8_BAR; PG8_MMA(1, 0, At, B0); PG8_MMA(1, 1, At, B1); PG8_BAR; PG8_SCHED;
.LBB0_1336:
	v_add_u32_e32 v146, s55, v149
	ds_read_b128 v[156:159], v146
	ds_read_b128 v[160:163], v146 offset:1024
	ds_read_b128 v[164:167], v146 offset:2048
	ds_read_b128 v[168:171], v146 offset:3072
	v_add_u32_e32 v146, s56, v149
	ds_read_b128 v[172:175], v146
	ds_read_b128 v[176:179], v146 offset:1024
	ds_read_b128 v[180:183], v146 offset:2048
	ds_read_b128 v[184:187], v146 offset:3072
	s_add_u32 s30, s28, 0x80
	s_addc_u32 s31, s29, 0
	s_cmpk_eq_i32 s62, 0x6c
	s_cselect_b32 s35, s25, s31
	s_cselect_b32 s34, s24, s30
	s_cselect_b32 s31, s27, s61
	s_cselect_b32 s30, s26, s60
	v_lshl_add_u64 v[146:147], s[28:29], 0, v[140:141]
	s_add_i32 m0, s47, 0xc000
	ds_read_b128 v[188:191], v153
	ds_read_b128 v[192:195], v153 offset:1024
	ds_read_b128 v[196:199], v153 offset:2048
	ds_read_b128 v[200:203], v153 offset:3072
	ds_read_b128 v[204:207], v153 offset:4096
	ds_read_b128 v[208:211], v153 offset:5120
	ds_read_b128 v[212:215], v153 offset:6144
	ds_read_b128 v[216:219], v153 offset:7168
	global_load_lds_dwordx4 v[146:147], off
	v_lshl_add_u64 v[146:147], s[28:29], 0, v[142:143]
	s_add_i32 m0, s47, 0xe000
	s_nop 0
	global_load_lds_dwordx4 v[146:147], off
	s_waitcnt vmcnt(8)
	s_waitcnt lgkmcnt(0)
	s_barrier
	s_waitcnt lgkmcnt(0)
	v_mfma_f32_16x16x32_bf16 v[120:123], v[156:159], v[188:191], v[120:123]
	v_mfma_f32_16x16x32_bf16 v[112:115], v[164:167], v[188:191], v[112:115]
	v_mfma_f32_16x16x32_bf16 v[104:107], v[156:159], v[196:199], v[104:107]
	v_mfma_f32_16x16x32_bf16 v[96:99], v[164:167], v[196:199], v[96:99]
	v_mfma_f32_16x16x32_bf16 v[88:91], v[156:159], v[204:207], v[88:91]
	v_mfma_f32_16x16x32_bf16 v[80:83], v[164:167], v[204:207], v[80:83]
	v_mfma_f32_16x16x32_bf16 v[72:75], v[156:159], v[212:215], v[72:75]
	v_mfma_f32_16x16x32_bf16 v[64:67], v[164:167], v[212:215], v[64:67]
	v_mfma_f32_16x16x32_bf16 v[120:123], v[160:163], v[192:195], v[120:123]
	v_mfma_f32_16x16x32_bf16 v[112:115], v[168:171], v[192:195], v[112:115]
	v_mfma_f32_16x16x32_bf16 v[104:107], v[160:163], v[200:203], v[104:107]
	v_mfma_f32_16x16x32_bf16 v[96:99], v[168:171], v[200:203], v[96:99]
	v_mfma_f32_16x16x32_bf16 v[88:91], v[160:163], v[208:211], v[88:91]
	v_mfma_f32_16x16x32_bf16 v[80:83], v[168:171], v[208:211], v[80:83]
	v_mfma_f32_16x16x32_bf16 v[72:75], v[160:163], v[216:219], v[72:75]
	v_mfma_f32_16x16x32_bf16 v[64:67], v[168:171], v[216:219], v[64:67]
	v_mfma_f32_16x16x32_bf16 v[124:127], v[172:175], v[188:191], v[124:127]
	v_mfma_f32_16x16x32_bf16 v[116:119], v[180:183], v[188:191], v[116:119]
	v_mfma_f32_16x16x32_bf16 v[108:111], v[172:175], v[196:199], v[108:111]
	v_mfma_f32_16x16x32_bf16 v[100:103], v[180:183], v[196:199], v[100:103]
	v_mfma_f32_16x16x32_bf16 v[92:95], v[172:175], v[204:207], v[92:95]
	v_mfma_f32_16x16x32_bf16 v[84:87], v[180:183], v[204:207], v[84:87]
	v_mfma_f32_16x16x32_bf16 v[76:79], v[172:175], v[212:215], v[76:79]
	v_mfma_f32_16x16x32_bf16 v[68:71], v[180:183], v[212:215], v[68:71]
	v_mfma_f32_16x16x32_bf16 v[124:127], v[176:179], v[192:195], v[124:127]
	v_mfma_f32_16x16x32_bf16 v[116:119], v[184:187], v[192:195], v[116:119]
	v_mfma_f32_16x16x32_bf16 v[108:111], v[176:179], v[200:203], v[108:111]
	v_mfma_f32_16x16x32_bf16 v[100:103], v[184:187], v[200:203], v[100:103]
	v_mfma_f32_16x16x32_bf16 v[92:95], v[176:179], v[208:211], v[92:95]
	v_mfma_f32_16x16x32_bf16 v[84:87], v[184:187], v[208:211], v[84:87]
	v_mfma_f32_16x16x32_bf16 v[76:79], v[176:179], v[216:219], v[76:79]
	v_mfma_f32_16x16x32_bf16 v[68:71], v[184:187], v[216:219], v[68:71]
	s_barrier
	s_add_i32 s63, s55, s97
	v_lshl_add_u64 v[146:147], s[30:31], 0, v[130:131]
	s_mov_b32 m0, s63
	ds_read_b128 v[188:191], v153 offset:16384
	ds_read_b128 v[192:195], v153 offset:17408
	ds_read_b128 v[196:199], v153 offset:18432
	ds_read_b128 v[200:203], v153 offset:19456
	ds_read_b128 v[204:207], v153 offset:20480
	ds_read_b128 v[208:211], v153 offset:21504
	ds_read_b128 v[212:215], v153 offset:22528
	ds_read_b128 v[216:219], v153 offset:23552
	global_load_lds_dwordx4 v[146:147], off
	s_add_i32 m0, s63, 0x2000
	s_add_u32 s64, s30, 0x1c0000
	v_lshl_add_u64 v[220:221], s[30:31], 0, v[128:129]
	s_addc_u32 s65, s31, 0
	s_add_i32 s63, s56, s97
	global_load_lds_dwordx4 v[220:221], off
	v_lshl_add_u64 v[222:223], s[64:65], 0, v[130:131]
	s_mov_b32 m0, s63
	v_lshl_add_u64 v[224:225], s[34:35], 0, v[128:129]
	global_load_lds_dwordx4 v[222:223], off
	v_lshl_add_u64 v[222:223], s[64:65], 0, v[128:129]
	s_add_i32 m0, s63, 0x2000
	s_nop 0
	global_load_lds_dwordx4 v[222:223], off
	v_lshl_add_u64 v[222:223], s[34:35], 0, v[130:131]
	s_mov_b32 m0, s47
	s_nop 0
	global_load_lds_dwordx4 v[222:223], off
	s_mov_b32 m0, s48
	s_nop 0
	global_load_lds_dwordx4 v[224:225], off
	s_waitcnt vmcnt(8)
	s_waitcnt lgkmcnt(0)
	s_barrier
; #define PG8_STAGE(bufoff, gbase, o0, o1) do { \
;         __builtin_amdgcn_global_load_lds((const unsigned*)((const char*)(gbase) + (o0)), (LAS unsigned*)(lds + (bufoff) + ldsw), 16, 0, 0); \
;         __builtin_amdgcn_global_load_lds((const unsigned*)((const char*)(gbase) + (o1)), (LAS unsigned*)(lds + (bufoff) + ldsw + 8192), 16, 0, 0); } while (0)
; #define PG8_LDA(dst, b, h) do { _Pragma("unroll") for (int m = 0; m < 4; ++m) _Pragma("unroll") for (int k = 0; k < 2; ++k) dst[m][k] = *(const LAS bf16x8*)(lds + PG8_SA(b, h) + aoff + m * 2048 + k * 1024); } while (0)
; #define PG8_LDB(dst, b, h) do { _Pragma("unroll") for (int n = 0; n < 2; ++n) _Pragma("unroll") for (int k = 0; k < 2; ++k) dst[n][k] = *(const LAS bf16x8*)(lds + PG8_SB(b, h) + boff + n * 2048 + k * 1024); } while (0)
; #define PG8_WAIT_V(n) asm volatile("s_waitcnt vmcnt(" #n ")" ::: "memory")
; #define PG8_WAIT_L(n) asm volatile("s_waitcnt lgkmcnt(" #n ")" ::: "memory")
; #define PG8_BAR __builtin_amdgcn_s_barrier()
; #define PG8_SCHED __builtin_amdgcn_sched_barrier(0)
; template <class Epi, class Sched, class Prob>
; __device__ __forceinline__ void gemm_phase(LAS unsigned char* lds, LAS unsigned char* lds_epi, const Prob g, const Sched& S, const Epi& E, int wid) {
;     ...
;             PG8_WAIT_V(8); PG8_WAIT_L(0); PG8_BAR; PG8_MMA(0, 0, At, B0); PG8_MMA(0, 1, At, B1); PG8_BAR; PG8_SCHED;
;             PG8_LDA(At, 0, 1); PG8_STAGE(PG8_SB(0, 0), b2, vB0, vB1); PG8_STAGE(PG8_SB(0, 1), b2 + hstepB, vB0, vB1); PG8_STAGE(PG8_SA(0, 0), a2, cA00, cA01);
;             PG8_WAIT_V(8); PG8_WAIT_L(0); PG8_BAR; PG8_MMA(1, 0, At, B0); PG8_MMA(1, 1, At, B1); PG8_BAR; PG8_SCHED;
;             PG8_LDB(B0, 1, 0); PG8_LDB(B1, 1, 1); PG8_SCHED; PG8_LDA(At, 1, 0); PG8_STAGE(PG8_SA(0, 1), a2, cA10, cA11);
;             PG8_WAIT_V(8); PG8_WAIT_L(0); PG8_BAR; PG8_MMA(0, 0, At, B0); PG8_MMA(0, 1, At, B1); PG8_BAR; PG8_SCHED;
	s_waitcnt lgkmcnt(0)
	v_mfma_f32_16x16x32_bf16 v[56:59], v[156:159], v[188:191], v[56:59]
	v_mfma_f32_16x16x32_bf16 v[48:51], v[164:167], v[188:191], v[48:51]
	v_mfma_f32_16x16x32_bf16 v[40:43], v[156:159], v[196:199], v[40:43]
	v_mfma_f32_16x16x32_bf16 v[32:35], v[164:167], v[196:199], v[32:35]
	v_mfma_f32_16x16x32_bf16 v[20:23], v[156:159], v[204:207], v[20:23]
	v_mfma_f32_16x16x32_bf16 v[8:11], v[164:167], v[204:207], v[8:11]
	v_mfma_f32_16x16x32_bf16 v[4:7], v[156:159], v[212:215], v[4:7]
	v_mfma_f32_16x16x32_bf16 v[0:3], v[164:167], v[212:215], v[0:3]
	v_mfma_f32_16x16x32_bf16 v[56:59], v[160:163], v[192:195], v[56:59]
	v_mfma_f32_16x16x32_bf16 v[48:51], v[168:171], v[192:195], v[48:51]
	v_mfma_f32_16x16x32_bf16 v[40:43], v[160:163], v[200:203], v[40:43]
	v_mfma_f32_16x16x32_bf16 v[32:35], v[168:171], v[200:203], v[32:35]
	v_mfma_f32_16x16x32_bf16 v[20:23], v[160:163], v[208:211], v[20:23]
	v_mfma_f32_16x16x32_bf16 v[8:11], v[168:171], v[208:211], v[8:11]
	v_mfma_f32_16x16x32_bf16 v[4:7], v[160:163], v[216:219], v[4:7]
	v_mfma_f32_16x16x32_bf16 v[0:3], v[168:171], v[216:219], v[0:3]
	v_mfma_f32_16x16x32_bf16 v[60:63], v[172:175], v[188:191], v[60:63]
	v_mfma_f32_16x16x32_bf16 v[52:55], v[180:183], v[188:191], v[52:55]
	v_mfma_f32_16x16x32_bf16 v[44:47], v[172:175], v[196:199], v[44:47]
	v_mfma_f32_16x16x32_bf16 v[36:39], v[180:183], v[196:199], v[36:39]
	v_mfma_f32_16x16x32_bf16 v[28:31], v[172:175], v[204:207], v[28:31]
	v_mfma_f32_16x16x32_bf16 v[16:19], v[180:183], v[204:207], v[16:19]
	v_mfma_f32_16x16x32_bf16 v[24:27], v[172:175], v[212:215], v[24:27]
	v_mfma_f32_16x16x32_bf16 v[12:15], v[180:183], v[212:215], v[12:15]
	v_mfma_f32_16x16x32_bf16 v[60:63], v[176:179], v[192:195], v[60:63]
	v_mfma_f32_16x16x32_bf16 v[52:55], v[184:187], v[192:195], v[52:55]
	v_mfma_f32_16x16x32_bf16 v[44:47], v[176:179], v[200:203], v[44:47]
	v_mfma_f32_16x16x32_bf16 v[36:39], v[184:187], v[200:203], v[36:39]
	v_mfma_f32_16x16x32_bf16 v[28:31], v[176:179], v[208:211], v[28:31]
	v_mfma_f32_16x16x32_bf16 v[16:19], v[184:187], v[208:211], v[16:19]
	v_mfma_f32_16x16x32_bf16 v[24:27], v[176:179], v[216:219], v[24:27]
	v_mfma_f32_16x16x32_bf16 v[12:15], v[184:187], v[216:219], v[12:15]
	s_barrier
	s_add_i32 s63, 0, 0x18000
	s_add_i32 s64, 0, 0x1c000
	v_add_u32_e32 v168, s63, v149
	v_add_u32_e32 v184, s64, v149
	ds_read_b128 v[156:159], v168
	ds_read_b128 v[160:163], v168 offset:1024
	ds_read_b128 v[164:167], v168 offset:2048
	ds_read_b128 v[168:171], v168 offset:3072
	ds_read_b128 v[172:175], v184
	ds_read_b128 v[176:179], v184 offset:1024
	ds_read_b128 v[180:183], v184 offset:2048
	ds_read_b128 v[184:187], v184 offset:3072
	s_mov_b32 m0, s49
	v_lshl_add_u64 v[226:227], s[34:35], 0, v[132:133]
	ds_read_b128 v[188:191], v153 offset:32768
	ds_read_b128 v[192:195], v153 offset:33792
	ds_read_b128 v[196:199], v153 offset:34816
	ds_read_b128 v[200:203], v153 offset:35840
	ds_read_b128 v[204:207], v153 offset:36864
	ds_read_b128 v[208:211], v153 offset:37888
	ds_read_b128 v[212:215], v153 offset:38912
	ds_read_b128 v[216:219], v153 offset:39936
	global_load_lds_dwordx4 v[226:227], off
	v_lshl_add_u64 v[226:227], s[34:35], 0, v[134:135]
	s_mov_b32 m0, s50
	s_nop 0
	global_load_lds_dwordx4 v[226:227], off
	s_waitcnt vmcnt(8)
	s_waitcnt lgkmcnt(0)
	s_barrier
	s_waitcnt lgkmcnt(0)
	v_mfma_f32_16x16x32_bf16 v[120:123], v[156:159], v[188:191], v[120:123]
	v_mfma_f32_16x16x32_bf16 v[112:115], v[164:167], v[188:191], v[112:115]
	v_mfma_f32_16x16x32_bf16 v[104:107], v[156:159], v[196:199], v[104:107]
	v_mfma_f32_16x16x32_bf16 v[96:99], v[164:167], v[196:199], v[96:99]
	v_mfma_f32_16x16x32_bf16 v[88:91], v[156:159], v[204:207], v[88:91]
	v_mfma_f32_16x16x32_bf16 v[80:83], v[164:167], v[204:207], v[80:83]
	v_mfma_f32_16x16x32_bf16 v[72:75], v[156:159], v[212:215], v[72:75]
	v_mfma_f32_16x16x32_bf16 v[64:67], v[164:167], v[212:215], v[64:67]
	v_mfma_f32_16x16x32_bf16 v[120:123], v[160:163], v[192:195], v[120:123]
	v_mfma_f32_16x16x32_bf16 v[112:115], v[168:171], v[192:195], v[112:115]
	v_mfma_f32_16x16x32_bf16 v[104:107], v[160:163], v[200:203], v[104:107]
	v_mfma_f32_16x16x32_bf16 v[96:99], v[168:171], v[200:203], v[96:99]
	v_mfma_f32_16x16x32_bf16 v[88:91], v[160:163], v[208:211], v[88:91]
	v_mfma_f32_16x16x32_bf16 v[80:83], v[168:171], v[208:211], v[80:83]
	v_mfma_f32_16x16x32_bf16 v[72:75], v[160:163], v[216:219], v[72:75]
	v_mfma_f32_16x16x32_bf16 v[64:67], v[168:171], v[216:219], v[64:67]
	v_mfma_f32_16x16x32_bf16 v[124:127], v[172:175], v[188:191], v[124:127]
	v_mfma_f32_16x16x32_bf16 v[116:119], v[180:183], v[188:191], v[116:119]
	v_mfma_f32_16x16x32_bf16 v[108:111], v[172:175], v[196:199], v[108:111]
	v_mfma_f32_16x16x32_bf16 v[100:103], v[180:183], v[196:199], v[100:103]
	v_mfma_f32_16x16x32_bf16 v[92:95], v[172:175], v[204:207], v[92:95]
	v_mfma_f32_16x16x32_bf16 v[84:87], v[180:183], v[204:207], v[84:87]
	v_mfma_f32_16x16x32_bf16 v[76:79], v[172:175], v[212:215], v[76:79]
	v_mfma_f32_16x16x32_bf16 v[68:71], v[180:183], v[212:215], v[68:71]
	v_mfma_f32_16x16x32_bf16 v[124:127], v[176:179], v[192:195], v[124:127]
	v_mfma_f32_16x16x32_bf16 v[116:119], v[184:187], v[192:195], v[116:119]
	v_mfma_f32_16x16x32_bf16 v[108:111], v[176:179], v[200:203], v[108:111]
	v_mfma_f32_16x16x32_bf16 v[100:103], v[184:187], v[200:203], v[100:103]
	v_mfma_f32_16x16x32_bf16 v[92:95], v[176:179], v[208:211], v[92:95]
	v_mfma_f32_16x16x32_bf16 v[84:87], v[184:187], v[208:211], v[84:87]
	v_mfma_f32_16x16x32_bf16 v[76:79], v[176:179], v[216:219], v[76:79]
	v_mfma_f32_16x16x32_bf16 v[68:71], v[184:187], v[216:219], v[68:71]
	s_barrier
; #define PG8_STAGE(bufoff, gbase, o0, o1) do { \
;         __builtin_amdgcn_global_load_lds((const unsigned*)((const char*)(gbase) + (o0)), (LAS unsigned*)(lds + (bufoff) + ldsw), 16, 0, 0); \
;         __builtin_amdgcn_global_load_lds((const unsigned*)((const char*)(gbase) + (o1)), (LAS unsigned*)(lds + (bufoff) + ldsw + 8192), 16, 0, 0); } while (0)
; #define PG8_LDA(dst, b, h) do { _Pragma("unroll") for (int m = 0; m < 4; ++m) _Pragma("unroll") for (int k = 0; k < 2; ++k) dst[m][k] = *(const LAS bf16x8*)(lds + PG8_SA(b, h) + aoff + m * 2048 + k * 1024); } while (0)
; #define PG8_WAIT_V(n) asm volatile("s_waitcnt vmcnt(" #n ")" ::: "memory")
; #define PG8_WAIT_L(n) asm volatile("s_waitcnt lgkmcnt(" #n ")" ::: "memory")
; #define PG8_BAR __builtin_amdgcn_s_barrier()
; #define PG8_SCHED __builtin_amdgcn_sched_barrier(0)
; template <class Epi, class Sched, class Prob>
; __device__ __forceinline__ void gemm_phase(LAS unsigned char* lds, LAS unsigned char* lds_epi, const Prob g, const Sched& S, const Epi& E, int wid) {
;     ...
;             PG8_LDA(At, 1, 1); PG8_STAGE(PG8_SB(1, 0), b3, vB0, vB1); PG8_STAGE(PG8_SB(1, 1), b3 + hstepB, vB0, vB1); PG8_STAGE(PG8_SA(1, 0), a3, cA00, cA01);
;             PG8_WAIT_V(8); PG8_WAIT_L(0); PG8_BAR; PG8_MMA(1, 0, At, B0); PG8_MMA(1, 1, At, B1); PG8_BAR; PG8_SCHED;
;         }
	s_add_i32 s34, s63, s97
	v_lshl_add_u64 v[146:147], v[146:147], 0, s[16:17]
	s_mov_b32 m0, s34
	ds_read_b128 v[188:191], v153 offset:49152
	ds_read_b128 v[192:195], v153 offset:50176
	ds_read_b128 v[196:199], v153 offset:51200
	ds_read_b128 v[200:203], v153 offset:52224
	ds_read_b128 v[204:207], v153 offset:53248
	ds_read_b128 v[208:211], v153 offset:54272
	ds_read_b128 v[212:215], v153 offset:55296
	ds_read_b128 v[216:219], v153 offset:56320
	global_load_lds_dwordx4 v[146:147], off
	s_add_i32 m0, s34, 0x2000
	s_add_u32 s30, s30, 0x1c0080
	v_lshl_add_u64 v[146:147], v[220:221], 0, s[16:17]
	s_addc_u32 s31, s31, 0
	s_add_i32 s34, s64, s97
	global_load_lds_dwordx4 v[146:147], off
	v_lshl_add_u64 v[146:147], s[30:31], 0, v[130:131]
	s_mov_b32 m0, s34
	s_nop 0
	global_load_lds_dwordx4 v[146:147], off
	v_lshl_add_u64 v[146:147], s[30:31], 0, v[128:129]
	s_add_i32 m0, s34, 0x2000
	s_nop 0
	global_load_lds_dwordx4 v[146:147], off
	v_lshl_add_u64 v[146:147], v[222:223], 0, s[16:17]
	s_mov_b32 m0, s53
	s_nop 0
	global_load_lds_dwordx4 v[146:147], off
	v_lshl_add_u64 v[146:147], v[224:225], 0, s[16:17]
	s_mov_b32 m0, s54
	s_nop 0
	global_load_lds_dwordx4 v[146:147], off
	s_waitcnt vmcnt(8)
	s_waitcnt lgkmcnt(0)
	s_barrier
	s_waitcnt lgkmcnt(0)
	v_mfma_f32_16x16x32_bf16 v[56:59], v[156:159], v[188:191], v[56:59]
	v_mfma_f32_16x16x32_bf16 v[48:51], v[164:167], v[188:191], v[48:51]
	v_mfma_f32_16x16x32_bf16 v[40:43], v[156:159], v[196:199], v[40:43]
	v_mfma_f32_16x16x32_bf16 v[32:35], v[164:167], v[196:199], v[32:35]
	v_mfma_f32_16x16x32_bf16 v[20:23], v[156:159], v[204:207], v[20:23]
	v_mfma_f32_16x16x32_bf16 v[8:11], v[164:167], v[204:207], v[8:11]
	v_mfma_f32_16x16x32_bf16 v[4:7], v[156:159], v[212:215], v[4:7]
	v_mfma_f32_16x16x32_bf16 v[0:3], v[164:167], v[212:215], v[0:3]
	v_mfma_f32_16x16x32_bf16 v[56:59], v[160:163], v[192:195], v[56:59]
	v_mfma_f32_16x16x32_bf16 v[48:51], v[168:171], v[192:195], v[48:51]
	v_mfma_f32_16x16x32_bf16 v[40:43], v[160:163], v[200:203], v[40:43]
	v_mfma_f32_16x16x32_bf16 v[32:35], v[168:171], v[200:203], v[32:35]
	v_mfma_f32_16x16x32_bf16 v[20:23], v[160:163], v[208:211], v[20:23]
	v_mfma_f32_16x16x32_bf16 v[8:11], v[168:171], v[208:211], v[8:11]
	v_mfma_f32_16x16x32_bf16 v[4:7], v[160:163], v[216:219], v[4:7]
	v_mfma_f32_16x16x32_bf16 v[0:3], v[168:171], v[216:219], v[0:3]
	v_mfma_f32_16x16x32_bf16 v[60:63], v[172:175], v[188:191], v[60:63]
	v_mfma_f32_16x16x32_bf16 v[52:55], v[180:183], v[188:191], v[52:55]
	v_mfma_f32_16x16x32_bf16 v[44:47], v[172:175], v[196:199], v[44:47]
	v_mfma_f32_16x16x32_bf16 v[36:39], v[180:183], v[196:199], v[36:39]
	v_mfma_f32_16x16x32_bf16 v[28:31], v[172:175], v[204:207], v[28:31]
	v_mfma_f32_16x16x32_bf16 v[16:19], v[180:183], v[204:207], v[16:19]
	v_mfma_f32_16x16x32_bf16 v[24:27], v[172:175], v[212:215], v[24:27]
	v_mfma_f32_16x16x32_bf16 v[12:15], v[180:183], v[212:215], v[12:15]
	v_mfma_f32_16x16x32_bf16 v[60:63], v[176:179], v[192:195], v[60:63]
	v_mfma_f32_16x16x32_bf16 v[52:55], v[184:187], v[192:195], v[52:55]
	v_mfma_f32_16x16x32_bf16 v[44:47], v[176:179], v[200:203], v[44:47]
	v_mfma_f32_16x16x32_bf16 v[36:39], v[184:187], v[200:203], v[36:39]
	v_mfma_f32_16x16x32_bf16 v[28:31], v[176:179], v[208:211], v[28:31]
	v_mfma_f32_16x16x32_bf16 v[16:19], v[184:187], v[208:211], v[16:19]
	v_mfma_f32_16x16x32_bf16 v[24:27], v[176:179], v[216:219], v[24:27]
	v_mfma_f32_16x16x32_bf16 v[12:15], v[184:187], v[216:219], v[12:15]
	s_barrier
	s_add_i32 s62, s62, 2
	s_add_u32 s28, s28, 0x100
	s_addc_u32 s29, s29, 0
	s_add_u32 s60, s60, 0x100
	s_addc_u32 s61, s61, 0
	s_cmpk_gt_u32 s62, 0x6d
	s_cbranch_scc0 .LBB0_1336
	v_readlane_b32 s28, v254, 27
	v_readlane_b32 s29, v254, 28
	s_and_b64 vcc, exec, s[28:29]
	s_cbranch_vccz .LBB0_1339
	s_barrier

; #define PG8_STAGE(bufoff, gbase, o0, o1) do { \
;         __builtin_amdgcn_global_load_lds((const unsigned*)((const char*)(gbase) + (o0)), (LAS unsigned*)(lds + (bufoff) + ldsw), 16, 0, 0); \
;         __builtin_amdgcn_global_load_lds((const unsigned*)((const char*)(gbase) + (o1)), (LAS unsigned*)(lds + (bufoff) + ldsw + 8192), 16, 0, 0); } while (0)
; #define PG8_LDA(dst, b, h) do { _Pragma("unroll") for (int m = 0; m < 4; ++m) _Pragma("unroll") for (int k = 0; k < 2; ++k) dst[m][k] = *(const LAS bf16x8*)(lds + PG8_SA(b, h) + aoff + m * 2048 + k * 1024); } while (0)
; #define PG8_LDB(dst, b, h) do { _Pragma("unroll") for (int n = 0; n < 2; ++n) _Pragma("unroll") for (int k = 0; k < 2; ++k) dst[n][k] = *(const LAS bf16x8*)(lds + PG8_SB(b, h) + boff + n * 2048 + k * 1024); } while (0)
; #define PG8_WAIT_V(n) asm volatile("s_waitcnt vmcnt(" #n ")" ::: "memory")
; #define PG8_WAIT_L(n) asm volatile("s_waitcnt lgkmcnt(" #n ")" ::: "memory")
; #define PG8_BAR __builtin_amdgcn_s_barrier()
; #define PG8_SCHED __builtin_amdgcn_sched_barrier(0)
; template <class Epi, class Sched, class Prob>
; __device__ __forceinline__ void gemm_phase(LAS unsigned char* lds, LAS unsigned char* lds_epi, const Prob g, const Sched& S, const Epi& E, int wid) {
;     ...
;         const bool has_next = S.next(ui + 1, nxt);
;         const char* nA = has_next ? g.a_base(nxt) : cA; const char* nB = has_next ? g.b_base(nxt) : cB;
; _Pragma("clang loop unroll(disable)")
;         for (int t = 0; t < nt; t += 2) {
;             const bool last = (t == nt - 2);
;             const char* a1 = cA + (size_t)(t + 1) * kstep;
;             const char* a2 = last ? nA : cA + (size_t)(t + 2) * kstep; const char* b2 = last ? nB : cB + (size_t)(t + 2) * kstep;
;             const char* a3 = a2 + kstep; const char* b3 = b2 + kstep;
;             PG8_LDB(B0, 0, 0); PG8_LDB(B1, 0, 1); PG8_SCHED; PG8_LDA(At, 0, 0); PG8_STAGE(PG8_SA(1, 1), a1, cA10, cA11);
;             PG8_WAIT_V(8); PG8_WAIT_L(0); PG8_BAR; PG8_MMA(0, 0, At, B0); PG8_MMA(0, 1, At, B1); PG8_BAR; PG8_SCHED;
;             PG8_LDA(At, 0, 1); PG8_STAGE(PG8_SB(0, 0), b2, vB0, vB1); PG8_STAGE(PG8_SB(0, 1), b2 + hstepB, vB0, vB1); PG8_STAGE(PG8_SA(0, 0), a2, cA00, cA01);
;             PG8_WAIT_V(8); PG8_WAIT_L(0); PG8_BAR; PG8_MMA(1, 0, At, B0); PG8_MMA(1, 1, At, B1); PG8_BAR; PG8_SCHED;
.LBB0_1433:
	s_ashr_i32 s17, s16, 31
	s_lshl_b64 s[40:41], s[16:17], 20
	s_add_u32 s40, s58, s40
	s_addc_u32 s41, s59, s41
	s_and_b64 s[42:43], s[36:37], exec
	s_cselect_b32 s17, s41, s11
	s_cselect_b32 s52, s40, s10
	s_ashr_i32 s35, s34, 31
	s_lshl_b64 s[42:43], s[34:35], 20
	s_add_u32 s42, s60, s42
	s_addc_u32 s43, s61, s43
	s_and_b64 s[48:49], s[36:37], exec
	s_cselect_b32 s35, s43, s47
	s_cselect_b32 s53, s42, s46
	s_add_u32 s54, s46, 0x100
	v_mov_b32_e32 v0, 0
	s_addc_u32 s55, s47, 0
	s_mov_b32 s87, -2
	ds_read_b128 v[146:149], v240
	ds_read_b128 v[150:153], v240 offset:1024
	ds_read_b128 v[154:157], v240 offset:2048
	ds_read_b128 v[158:161], v240 offset:3072
	ds_read_b128 v[162:165], v241
	ds_read_b128 v[166:169], v241 offset:1024
	ds_read_b128 v[170:173], v241 offset:2048
	ds_read_b128 v[174:177], v241 offset:3072
	s_add_u32 s46, s10, 0x100
	s_addc_u32 s47, s11, 0
	s_cmp_eq_u32 s87, 28
	s_cselect_b32 s51, s17, s47
	s_cselect_b32 s50, s52, s46
	s_cselect_b32 s49, s35, s55
	s_cselect_b32 s48, s53, s54
	v_lshl_add_u64 v[210:211], s[10:11], 0, v[142:143]
	s_add_i32 m0, s62, 0xc000
	ds_read_b128 v[178:181], v242
	ds_read_b128 v[182:185], v242 offset:1024
	ds_read_b128 v[186:189], v242 offset:2048
	ds_read_b128 v[190:193], v242 offset:3072
	ds_read_b128 v[194:197], v242 offset:4096
	ds_read_b128 v[198:201], v242 offset:5120
	ds_read_b128 v[202:205], v242 offset:6144
	ds_read_b128 v[206:209], v242 offset:7168
	global_load_lds_dwordx4 v[210:211], off
	v_lshl_add_u64 v[210:211], s[10:11], 0, v[140:141]
	s_add_i32 m0, s62, 0xe000
	s_nop 0
	global_load_lds_dwordx4 v[210:211], off
	s_waitcnt vmcnt(8)
	s_waitcnt lgkmcnt(0)
	s_barrier
	s_waitcnt lgkmcnt(0)
	v_mfma_f32_16x16x32_bf16 v[124:127], v[146:149], v[178:181], 0
	v_mfma_f32_16x16x32_bf16 v[120:123], v[154:157], v[178:181], 0
	v_mfma_f32_16x16x32_bf16 v[116:119], v[146:149], v[186:189], 0
	v_mfma_f32_16x16x32_bf16 v[112:115], v[154:157], v[186:189], 0
	v_mfma_f32_16x16x32_bf16 v[108:111], v[146:149], v[194:197], 0
	v_mfma_f32_16x16x32_bf16 v[100:103], v[154:157], v[194:197], 0
	v_mfma_f32_16x16x32_bf16 v[92:95], v[146:149], v[202:205], 0
	v_mfma_f32_16x16x32_bf16 v[84:87], v[154:157], v[202:205], 0
	v_mfma_f32_16x16x32_bf16 v[124:127], v[150:153], v[182:185], v[124:127]
	v_mfma_f32_16x16x32_bf16 v[120:123], v[158:161], v[182:185], v[120:123]
	v_mfma_f32_16x16x32_bf16 v[116:119], v[150:153], v[190:193], v[116:119]
	v_mfma_f32_16x16x32_bf16 v[112:115], v[158:161], v[190:193], v[112:115]
	v_mfma_f32_16x16x32_bf16 v[108:111], v[150:153], v[198:201], v[108:111]
	v_mfma_f32_16x16x32_bf16 v[100:103], v[158:161], v[198:201], v[100:103]
	v_mfma_f32_16x16x32_bf16 v[92:95], v[150:153], v[206:209], v[92:95]
	v_mfma_f32_16x16x32_bf16 v[84:87], v[158:161], v[206:209], v[84:87]
	v_mfma_f32_16x16x32_bf16 v[104:107], v[162:165], v[178:181], 0
	v_mfma_f32_16x16x32_bf16 v[96:99], v[170:173], v[178:181], 0
	v_mfma_f32_16x16x32_bf16 v[88:91], v[162:165], v[186:189], 0
	v_mfma_f32_16x16x32_bf16 v[80:83], v[170:173], v[186:189], 0
	v_mfma_f32_16x16x32_bf16 v[76:79], v[162:165], v[194:197], 0
	v_mfma_f32_16x16x32_bf16 v[72:75], v[170:173], v[194:197], 0
	v_mfma_f32_16x16x32_bf16 v[68:71], v[162:165], v[202:205], 0
	v_mfma_f32_16x16x32_bf16 v[64:67], v[170:173], v[202:205], 0
	v_mfma_f32_16x16x32_bf16 v[104:107], v[166:169], v[182:185], v[104:107]
	v_mfma_f32_16x16x32_bf16 v[96:99], v[174:177], v[182:185], v[96:99]
	v_mfma_f32_16x16x32_bf16 v[88:91], v[166:169], v[190:193], v[88:91]
	v_mfma_f32_16x16x32_bf16 v[80:83], v[174:177], v[190:193], v[80:83]
	v_mfma_f32_16x16x32_bf16 v[76:79], v[166:169], v[198:201], v[76:79]
	v_mfma_f32_16x16x32_bf16 v[72:75], v[174:177], v[198:201], v[72:75]
	v_mfma_f32_16x16x32_bf16 v[68:71], v[166:169], v[206:209], v[68:71]
	v_mfma_f32_16x16x32_bf16 v[64:67], v[174:177], v[206:209], v[64:67]
	s_barrier
	s_add_i32 s10, s80, s97
	v_lshl_add_u64 v[210:211], s[48:49], 0, v[128:129]
	s_mov_b32 m0, s10
	ds_read_b128 v[178:181], v242 offset:16384
	ds_read_b128 v[182:185], v242 offset:17408
	ds_read_b128 v[186:189], v242 offset:18432
	ds_read_b128 v[190:193], v242 offset:19456
	ds_read_b128 v[194:197], v242 offset:20480
	ds_read_b128 v[198:201], v242 offset:21504
	ds_read_b128 v[202:205], v242 offset:22528
	ds_read_b128 v[206:209], v242 offset:23552
	global_load_lds_dwordx4 v[210:211], off
	s_add_i32 m0, s10, 0x2000
	s_add_u32 s10, s48, 0x80000
	v_lshl_add_u64 v[212:213], s[48:49], 0, v[130:131]
	s_addc_u32 s11, s49, 0
	s_add_i32 s88, s81, s97
	global_load_lds_dwordx4 v[212:213], off
	v_lshl_add_u64 v[214:215], s[10:11], 0, v[128:129]
	s_mov_b32 m0, s88
	v_lshl_add_u64 v[216:217], s[50:51], 0, v[136:137]
	global_load_lds_dwordx4 v[214:215], off
	v_lshl_add_u64 v[214:215], s[10:11], 0, v[130:131]
	s_add_i32 m0, s88, 0x2000
	s_nop 0
	global_load_lds_dwordx4 v[214:215], off
	v_lshl_add_u64 v[214:215], s[50:51], 0, v[132:133]
	s_mov_b32 m0, s62
	s_nop 0
	global_load_lds_dwordx4 v[214:215], off
	s_mov_b32 m0, s63
	s_nop 0
	global_load_lds_dwordx4 v[216:217], off
	s_waitcnt vmcnt(8)
	s_waitcnt lgkmcnt(0)
	s_barrier
; #define PG8_STAGE(bufoff, gbase, o0, o1) do { \
;         __builtin_amdgcn_global_load_lds((const unsigned*)((const char*)(gbase) + (o0)), (LAS unsigned*)(lds + (bufoff) + ldsw), 16, 0, 0); \
;         __builtin_amdgcn_global_load_lds((const unsigned*)((const char*)(gbase) + (o1)), (LAS unsigned*)(lds + (bufoff) + ldsw + 8192), 16, 0, 0); } while (0)
; #define PG8_LDA(dst, b, h) do { _Pragma("unroll") for (int m = 0; m < 4; ++m) _Pragma("unroll") for (int k = 0; k < 2; ++k) dst[m][k] = *(const LAS bf16x8*)(lds + PG8_SA(b, h) + aoff + m * 2048 + k * 1024); } while (0)
; #define PG8_LDB(dst, b, h) do { _Pragma("unroll") for (int n = 0; n < 2; ++n) _Pragma("unroll") for (int k = 0; k < 2; ++k) dst[n][k] = *(const LAS bf16x8*)(lds + PG8_SB(b, h) + boff + n * 2048 + k * 1024); } while (0)
; #define PG8_WAIT_V(n) asm volatile("s_waitcnt vmcnt(" #n ")" ::: "memory")
; #define PG8_WAIT_L(n) asm volatile("s_waitcnt lgkmcnt(" #n ")" ::: "memory")
; #define PG8_BAR __builtin_amdgcn_s_barrier()
; #define PG8_SCHED __builtin_amdgcn_sched_barrier(0)
; template <class Epi, class Sched, class Prob>
; __device__ __forceinline__ void gemm_phase(LAS unsigned char* lds, LAS unsigned char* lds_epi, const Prob g, const Sched& S, const Epi& E, int wid) {
;     ...
;             PG8_WAIT_V(8); PG8_WAIT_L(0); PG8_BAR; PG8_MMA(1, 0, At, B0); PG8_MMA(1, 1, At, B1); PG8_BAR; PG8_SCHED;
;             PG8_LDB(B0, 1, 0); PG8_LDB(B1, 1, 1); PG8_SCHED; PG8_LDA(At, 1, 0); PG8_STAGE(PG8_SA(0, 1), a2, cA10, cA11);
;             PG8_WAIT_V(8); PG8_WAIT_L(0); PG8_BAR; PG8_MMA(0, 0, At, B0); PG8_MMA(0, 1, At, B1); PG8_BAR; PG8_SCHED;
	s_waitcnt lgkmcnt(0)
	v_mfma_f32_16x16x32_bf16 v[60:63], v[146:149], v[178:181], 0
	v_mfma_f32_16x16x32_bf16 v[56:59], v[154:157], v[178:181], 0
	v_mfma_f32_16x16x32_bf16 v[52:55], v[146:149], v[186:189], 0
	v_mfma_f32_16x16x32_bf16 v[48:51], v[154:157], v[186:189], 0
	v_mfma_f32_16x16x32_bf16 v[36:39], v[146:149], v[194:197], 0
	v_mfma_f32_16x16x32_bf16 v[32:35], v[154:157], v[194:197], 0
	v_mfma_f32_16x16x32_bf16 v[20:23], v[146:149], v[202:205], 0
	v_mfma_f32_16x16x32_bf16 v[16:19], v[154:157], v[202:205], 0
	v_mfma_f32_16x16x32_bf16 v[60:63], v[150:153], v[182:185], v[60:63]
	v_mfma_f32_16x16x32_bf16 v[56:59], v[158:161], v[182:185], v[56:59]
	v_mfma_f32_16x16x32_bf16 v[52:55], v[150:153], v[190:193], v[52:55]
	v_mfma_f32_16x16x32_bf16 v[48:51], v[158:161], v[190:193], v[48:51]
	v_mfma_f32_16x16x32_bf16 v[36:39], v[150:153], v[198:201], v[36:39]
	v_mfma_f32_16x16x32_bf16 v[32:35], v[158:161], v[198:201], v[32:35]
	v_mfma_f32_16x16x32_bf16 v[20:23], v[150:153], v[206:209], v[20:23]
	v_mfma_f32_16x16x32_bf16 v[16:19], v[158:161], v[206:209], v[16:19]
	v_mfma_f32_16x16x32_bf16 v[44:47], v[162:165], v[178:181], 0
	v_mfma_f32_16x16x32_bf16 v[40:43], v[170:173], v[178:181], 0
	v_mfma_f32_16x16x32_bf16 v[28:31], v[162:165], v[186:189], 0
	v_mfma_f32_16x16x32_bf16 v[24:27], v[170:173], v[186:189], 0
	v_mfma_f32_16x16x32_bf16 v[12:15], v[162:165], v[194:197], 0
	v_mfma_f32_16x16x32_bf16 v[8:11], v[170:173], v[194:197], 0
	v_mfma_f32_16x16x32_bf16 v[4:7], v[162:165], v[202:205], 0
	v_mfma_f32_16x16x32_bf16 v[0:3], v[170:173], v[202:205], 0
	v_mfma_f32_16x16x32_bf16 v[44:47], v[166:169], v[182:185], v[44:47]
	v_mfma_f32_16x16x32_bf16 v[40:43], v[174:177], v[182:185], v[40:43]
	v_mfma_f32_16x16x32_bf16 v[28:31], v[166:169], v[190:193], v[28:31]
	v_mfma_f32_16x16x32_bf16 v[24:27], v[174:177], v[190:193], v[24:27]
	v_mfma_f32_16x16x32_bf16 v[12:15], v[166:169], v[198:201], v[12:15]
	v_mfma_f32_16x16x32_bf16 v[8:11], v[174:177], v[198:201], v[8:11]
	v_mfma_f32_16x16x32_bf16 v[4:7], v[166:169], v[206:209], v[4:7]
	v_mfma_f32_16x16x32_bf16 v[0:3], v[174:177], v[206:209], v[0:3]
	s_barrier
	s_add_i32 s10, 0, 0x18000
	s_add_i32 s88, 0, 0x1c000
	v_add_u32_e32 v158, s10, v239
	v_add_u32_e32 v174, s88, v239
	ds_read_b128 v[146:149], v158
	ds_read_b128 v[150:153], v158 offset:1024
	ds_read_b128 v[154:157], v158 offset:2048
	ds_read_b128 v[158:161], v158 offset:3072
	ds_read_b128 v[162:165], v174
	ds_read_b128 v[166:169], v174 offset:1024
	ds_read_b128 v[170:173], v174 offset:2048
	ds_read_b128 v[174:177], v174 offset:3072
	s_mov_b32 m0, s64
	v_lshl_add_u64 v[218:219], s[50:51], 0, v[134:135]
	ds_read_b128 v[178:181], v242 offset:32768
	ds_read_b128 v[182:185], v242 offset:33792
	ds_read_b128 v[186:189], v242 offset:34816
	ds_read_b128 v[190:193], v242 offset:35840
	ds_read_b128 v[194:197], v242 offset:36864
	ds_read_b128 v[198:201], v242 offset:37888
	ds_read_b128 v[202:205], v242 offset:38912
	ds_read_b128 v[206:209], v242 offset:39936
	global_load_lds_dwordx4 v[218:219], off
	v_lshl_add_u64 v[218:219], s[50:51], 0, v[138:139]
	s_mov_b32 m0, s65
	s_nop 0
	global_load_lds_dwordx4 v[218:219], off
	s_waitcnt vmcnt(8)
	s_waitcnt lgkmcnt(0)
	s_barrier
	s_waitcnt lgkmcnt(0)
	v_mfma_f32_16x16x32_bf16 v[124:127], v[146:149], v[178:181], v[124:127]
	v_mfma_f32_16x16x32_bf16 v[120:123], v[154:157], v[178:181], v[120:123]
	v_mfma_f32_16x16x32_bf16 v[116:119], v[146:149], v[186:189], v[116:119]
	v_mfma_f32_16x16x32_bf16 v[112:115], v[154:157], v[186:189], v[112:115]
	v_mfma_f32_16x16x32_bf16 v[108:111], v[146:149], v[194:197], v[108:111]
	v_mfma_f32_16x16x32_bf16 v[100:103], v[154:157], v[194:197], v[100:103]
	v_mfma_f32_16x16x32_bf16 v[92:95], v[146:149], v[202:205], v[92:95]
	v_mfma_f32_16x16x32_bf16 v[84:87], v[154:157], v[202:205], v[84:87]
	v_mfma_f32_16x16x32_bf16 v[124:127], v[150:153], v[182:185], v[124:127]
	v_mfma_f32_16x16x32_bf16 v[120:123], v[158:161], v[182:185], v[120:123]
	v_mfma_f32_16x16x32_bf16 v[116:119], v[150:153], v[190:193], v[116:119]
	v_mfma_f32_16x16x32_bf16 v[112:115], v[158:161], v[190:193], v[112:115]
	v_mfma_f32_16x16x32_bf16 v[108:111], v[150:153], v[198:201], v[108:111]
	v_mfma_f32_16x16x32_bf16 v[100:103], v[158:161], v[198:201], v[100:103]
	v_mfma_f32_16x16x32_bf16 v[92:95], v[150:153], v[206:209], v[92:95]
	v_mfma_f32_16x16x32_bf16 v[84:87], v[158:161], v[206:209], v[84:87]
	v_mfma_f32_16x16x32_bf16 v[104:107], v[162:165], v[178:181], v[104:107]
	v_mfma_f32_16x16x32_bf16 v[96:99], v[170:173], v[178:181], v[96:99]
	v_mfma_f32_16x16x32_bf16 v[88:91], v[162:165], v[186:189], v[88:91]
	v_mfma_f32_16x16x32_bf16 v[80:83], v[170:173], v[186:189], v[80:83]
	v_mfma_f32_16x16x32_bf16 v[76:79], v[162:165], v[194:197], v[76:79]
	v_mfma_f32_16x16x32_bf16 v[72:75], v[170:173], v[194:197], v[72:75]
	v_mfma_f32_16x16x32_bf16 v[68:71], v[162:165], v[202:205], v[68:71]
	v_mfma_f32_16x16x32_bf16 v[64:67], v[170:173], v[202:205], v[64:67]
	v_mfma_f32_16x16x32_bf16 v[104:107], v[166:169], v[182:185], v[104:107]
	v_mfma_f32_16x16x32_bf16 v[96:99], v[174:177], v[182:185], v[96:99]
	v_mfma_f32_16x16x32_bf16 v[88:91], v[166:169], v[190:193], v[88:91]
	v_mfma_f32_16x16x32_bf16 v[80:83], v[174:177], v[190:193], v[80:83]
	v_mfma_f32_16x16x32_bf16 v[76:79], v[166:169], v[198:201], v[76:79]
	v_mfma_f32_16x16x32_bf16 v[72:75], v[174:177], v[198:201], v[72:75]
	v_mfma_f32_16x16x32_bf16 v[68:71], v[166:169], v[206:209], v[68:71]
	v_mfma_f32_16x16x32_bf16 v[64:67], v[174:177], v[206:209], v[64:67]
	s_barrier
; #define PG8_STAGE(bufoff, gbase, o0, o1) do { \
;         __builtin_amdgcn_global_load_lds((const unsigned*)((const char*)(gbase) + (o0)), (LAS unsigned*)(lds + (bufoff) + ldsw), 16, 0, 0); \
;         __builtin_amdgcn_global_load_lds((const unsigned*)((const char*)(gbase) + (o1)), (LAS unsigned*)(lds + (bufoff) + ldsw + 8192), 16, 0, 0); } while (0)
; #define PG8_LDA(dst, b, h) do { _Pragma("unroll") for (int m = 0; m < 4; ++m) _Pragma("unroll") for (int k = 0; k < 2; ++k) dst[m][k] = *(const LAS bf16x8*)(lds + PG8_SA(b, h) + aoff + m * 2048 + k * 1024); } while (0)
; #define PG8_LDB(dst, b, h) do { _Pragma("unroll") for (int n = 0; n < 2; ++n) _Pragma("unroll") for (int k = 0; k < 2; ++k) dst[n][k] = *(const LAS bf16x8*)(lds + PG8_SB(b, h) + boff + n * 2048 + k * 1024); } while (0)
; #define PG8_WAIT_V(n) asm volatile("s_waitcnt vmcnt(" #n ")" ::: "memory")
; #define PG8_WAIT_L(n) asm volatile("s_waitcnt lgkmcnt(" #n ")" ::: "memory")
; #define PG8_BAR __builtin_amdgcn_s_barrier()
; #define PG8_SCHED __builtin_amdgcn_sched_barrier(0)
; template <class Epi, class Sched, class Prob>
; __device__ __forceinline__ void gemm_phase(LAS unsigned char* lds, LAS unsigned char* lds_epi, const Prob g, const Sched& S, const Epi& E, int wid) {
;     ...
;             PG8_LDB(B0, 0, 0); PG8_LDB(B1, 0, 1); PG8_SCHED; PG8_LDA(At, 0, 0); PG8_STAGE(PG8_SA(1, 1), a1, cA10, cA11);
;             PG8_WAIT_V(8); PG8_WAIT_L(0); PG8_BAR; PG8_MMA(0, 0, At, B0); PG8_MMA(0, 1, At, B1); PG8_BAR; PG8_SCHED;
;             PG8_LDA(At, 0, 1); PG8_STAGE(PG8_SB(0, 0), b2, vB0, vB1); PG8_STAGE(PG8_SB(0, 1), b2 + hstepB, vB0, vB1); PG8_STAGE(PG8_SA(0, 0), a2, cA00, cA01);
;             PG8_WAIT_V(8); PG8_WAIT_L(0); PG8_BAR; PG8_MMA(1, 0, At, B0); PG8_MMA(1, 1, At, B1); PG8_BAR; PG8_SCHED;
;             PG8_LDB(B0, 1, 0); PG8_LDB(B1, 1, 1); PG8_SCHED; PG8_LDA(At, 1, 0); PG8_STAGE(PG8_SA(0, 1), a2, cA10, cA11);
;             PG8_WAIT_V(8); PG8_WAIT_L(0); PG8_BAR; PG8_MMA(0, 0, At, B0); PG8_MMA(0, 1, At, B1); PG8_BAR; PG8_SCHED;
;             PG8_LDA(At, 1, 1); PG8_STAGE(PG8_SB(1, 0), b3, vB0, vB1); PG8_STAGE(PG8_SB(1, 1), b3 + hstepB, vB0, vB1); PG8_STAGE(PG8_SA(1, 0), a3, cA00, cA01);
;             PG8_WAIT_V(8); PG8_WAIT_L(0); PG8_BAR; PG8_MMA(1, 0, At, B0); PG8_MMA(1, 1, At, B1); PG8_BAR; PG8_SCHED;
	s_add_i32 s10, s10, s97
	v_lshl_add_u64 v[210:211], v[210:211], 0, s[24:25]
	s_mov_b32 m0, s10
	ds_read_b128 v[178:181], v242 offset:49152
	ds_read_b128 v[182:185], v242 offset:50176
	ds_read_b128 v[186:189], v242 offset:51200
	ds_read_b128 v[190:193], v242 offset:52224
	ds_read_b128 v[194:197], v242 offset:53248
	ds_read_b128 v[198:201], v242 offset:54272
	ds_read_b128 v[202:205], v242 offset:55296
	ds_read_b128 v[206:209], v242 offset:56320
	global_load_lds_dwordx4 v[210:211], off
	s_add_i32 m0, s10, 0x2000
	s_add_u32 s10, s48, 0x80080
	v_lshl_add_u64 v[210:211], v[212:213], 0, s[24:25]
	s_addc_u32 s11, s49, 0
	s_add_i32 s48, s88, s97
	global_load_lds_dwordx4 v[210:211], off
	v_lshl_add_u64 v[210:211], s[10:11], 0, v[128:129]
	s_mov_b32 m0, s48
	s_nop 0
	global_load_lds_dwordx4 v[210:211], off
	v_lshl_add_u64 v[210:211], s[10:11], 0, v[130:131]
	s_add_i32 m0, s48, 0x2000
	s_nop 0
	global_load_lds_dwordx4 v[210:211], off
	v_lshl_add_u64 v[210:211], v[214:215], 0, s[24:25]
	s_mov_b32 m0, s78
	s_nop 0
	global_load_lds_dwordx4 v[210:211], off
	v_lshl_add_u64 v[210:211], v[216:217], 0, s[24:25]
	s_mov_b32 m0, s79
	s_nop 0
	global_load_lds_dwordx4 v[210:211], off
	s_waitcnt vmcnt(8)
	s_waitcnt lgkmcnt(0)
	s_barrier
	s_waitcnt lgkmcnt(0)
	v_mfma_f32_16x16x32_bf16 v[60:63], v[146:149], v[178:181], v[60:63]
	v_mfma_f32_16x16x32_bf16 v[56:59], v[154:157], v[178:181], v[56:59]
	v_mfma_f32_16x16x32_bf16 v[52:55], v[146:149], v[186:189], v[52:55]
	v_mfma_f32_16x16x32_bf16 v[48:51], v[154:157], v[186:189], v[48:51]
	v_mfma_f32_16x16x32_bf16 v[36:39], v[146:149], v[194:197], v[36:39]
	v_mfma_f32_16x16x32_bf16 v[32:35], v[154:157], v[194:197], v[32:35]
	v_mfma_f32_16x16x32_bf16 v[20:23], v[146:149], v[202:205], v[20:23]
	v_mfma_f32_16x16x32_bf16 v[16:19], v[154:157], v[202:205], v[16:19]
	v_mfma_f32_16x16x32_bf16 v[60:63], v[150:153], v[182:185], v[60:63]
	v_mfma_f32_16x16x32_bf16 v[56:59], v[158:161], v[182:185], v[56:59]
	v_mfma_f32_16x16x32_bf16 v[52:55], v[150:153], v[190:193], v[52:55]
	v_mfma_f32_16x16x32_bf16 v[48:51], v[158:161], v[190:193], v[48:51]
	v_mfma_f32_16x16x32_bf16 v[36:39], v[150:153], v[198:201], v[36:39]
	v_mfma_f32_16x16x32_bf16 v[32:35], v[158:161], v[198:201], v[32:35]
	v_mfma_f32_16x16x32_bf16 v[20:23], v[150:153], v[206:209], v[20:23]
	v_mfma_f32_16x16x32_bf16 v[16:19], v[158:161], v[206:209], v[16:19]
	v_mfma_f32_16x16x32_bf16 v[44:47], v[162:165], v[178:181], v[44:47]
	v_mfma_f32_16x16x32_bf16 v[40:43], v[170:173], v[178:181], v[40:43]
	v_mfma_f32_16x16x32_bf16 v[28:31], v[162:165], v[186:189], v[28:31]
	v_mfma_f32_16x16x32_bf16 v[24:27], v[170:173], v[186:189], v[24:27]
	v_mfma_f32_16x16x32_bf16 v[12:15], v[162:165], v[194:197], v[12:15]
	v_mfma_f32_16x16x32_bf16 v[8:11], v[170:173], v[194:197], v[8:11]
	v_mfma_f32_16x16x32_bf16 v[4:7], v[162:165], v[202:205], v[4:7]
	v_mfma_f32_16x16x32_bf16 v[0:3], v[170:173], v[202:205], v[0:3]
	v_mfma_f32_16x16x32_bf16 v[44:47], v[166:169], v[182:185], v[44:47]
	v_mfma_f32_16x16x32_bf16 v[40:43], v[174:177], v[182:185], v[40:43]
	v_mfma_f32_16x16x32_bf16 v[28:31], v[166:169], v[190:193], v[28:31]
	v_mfma_f32_16x16x32_bf16 v[24:27], v[174:177], v[190:193], v[24:27]
	v_mfma_f32_16x16x32_bf16 v[12:15], v[166:169], v[198:201], v[12:15]
	v_mfma_f32_16x16x32_bf16 v[8:11], v[174:177], v[198:201], v[8:11]
	v_mfma_f32_16x16x32_bf16 v[4:7], v[166:169], v[206:209], v[4:7]
	v_mfma_f32_16x16x32_bf16 v[0:3], v[174:177], v[206:209], v[0:3]
	s_barrier
	s_add_i32 s87, s87, 2
	s_add_u32 s54, s54, 0x100
	s_addc_u32 s55, s55, 0
	s_cmp_gt_u32 s87, 29
	s_mov_b64 s[10:11], s[46:47]
.LBB0_1434:
	ds_read_b128 v[146:149], v240
	ds_read_b128 v[150:153], v240 offset:1024
	ds_read_b128 v[154:157], v240 offset:2048
	ds_read_b128 v[158:161], v240 offset:3072
	ds_read_b128 v[162:165], v241
	ds_read_b128 v[166:169], v241 offset:1024
	ds_read_b128 v[170:173], v241 offset:2048
	ds_read_b128 v[174:177], v241 offset:3072
	s_add_u32 s46, s10, 0x100
	s_addc_u32 s47, s11, 0
	s_cmp_eq_u32 s87, 28
	s_cselect_b32 s51, s17, s47
	s_cselect_b32 s50, s52, s46
	s_cselect_b32 s49, s35, s55
	s_cselect_b32 s48, s53, s54
	v_lshl_add_u64 v[210:211], s[10:11], 0, v[142:143]
	s_add_i32 m0, s62, 0xc000
	ds_read_b128 v[178:181], v242
	ds_read_b128 v[182:185], v242 offset:1024
	ds_read_b128 v[186:189], v242 offset:2048
	ds_read_b128 v[190:193], v242 offset:3072
	ds_read_b128 v[194:197], v242 offset:4096
	ds_read_b128 v[198:201], v242 offset:5120
	ds_read_b128 v[202:205], v242 offset:6144
	ds_read_b128 v[206:209], v242 offset:7168
	global_load_lds_dwordx4 v[210:211], off
	v_lshl_add_u64 v[210:211], s[10:11], 0, v[140:141]
	s_add_i32 m0, s62, 0xe000
	s_nop 0
	global_load_lds_dwordx4 v[210:211], off
	s_waitcnt vmcnt(8)
	s_waitcnt lgkmcnt(0)
	s_barrier
; #define PG8_STAGE(bufoff, gbase, o0, o1) do { \
;         __builtin_amdgcn_global_load_lds((const unsigned*)((const char*)(gbase) + (o0)), (LAS unsigned*)(lds + (bufoff) + ldsw), 16, 0, 0); \
;         __builtin_amdgcn_global_load_lds((const unsigned*)((const char*)(gbase) + (o1)), (LAS unsigned*)(lds + (bufoff) + ldsw + 8192), 16, 0, 0); } while (0)
; #define PG8_LDA(dst, b, h) do { _Pragma("unroll") for (int m = 0; m < 4; ++m) _Pragma("unroll") for (int k = 0; k < 2; ++k) dst[m][k] = *(const LAS bf16x8*)(lds + PG8_SA(b, h) + aoff + m * 2048 + k * 1024); } while (0)
; #define PG8_WAIT_V(n) asm volatile("s_waitcnt vmcnt(" #n ")" ::: "memory")
; #define PG8_WAIT_L(n) asm volatile("s_waitcnt lgkmcnt(" #n ")" ::: "memory")
; #define PG8_BAR __builtin_amdgcn_s_barrier()
; #define PG8_SCHED __builtin_amdgcn_sched_barrier(0)
; template <class Epi, class Sched, class Prob>
; __device__ __forceinline__ void gemm_phase(LAS unsigned char* lds, LAS unsigned char* lds_epi, const Prob g, const Sched& S, const Epi& E, int wid) {
;     ...
;             PG8_WAIT_V(8); PG8_WAIT_L(0); PG8_BAR; PG8_MMA(0, 0, At, B0); PG8_MMA(0, 1, At, B1); PG8_BAR; PG8_SCHED;
;             PG8_LDA(At, 0, 1); PG8_STAGE(PG8_SB(0, 0), b2, vB0, vB1); PG8_STAGE(PG8_SB(0, 1), b2 + hstepB, vB0, vB1); PG8_STAGE(PG8_SA(0, 0), a2, cA00, cA01);
;             PG8_WAIT_V(8); PG8_WAIT_L(0); PG8_BAR; PG8_MMA(1, 0, At, B0); PG8_MMA(1, 1, At, B1); PG8_BAR; PG8_SCHED;
	s_waitcnt lgkmcnt(0)
	v_mfma_f32_16x16x32_bf16 v[124:127], v[146:149], v[178:181], v[124:127]
	v_mfma_f32_16x16x32_bf16 v[120:123], v[154:157], v[178:181], v[120:123]
	v_mfma_f32_16x16x32_bf16 v[116:119], v[146:149], v[186:189], v[116:119]
	v_mfma_f32_16x16x32_bf16 v[112:115], v[154:157], v[186:189], v[112:115]
	v_mfma_f32_16x16x32_bf16 v[108:111], v[146:149], v[194:197], v[108:111]
	v_mfma_f32_16x16x32_bf16 v[100:103], v[154:157], v[194:197], v[100:103]
	v_mfma_f32_16x16x32_bf16 v[92:95], v[146:149], v[202:205], v[92:95]
	v_mfma_f32_16x16x32_bf16 v[84:87], v[154:157], v[202:205], v[84:87]
	v_mfma_f32_16x16x32_bf16 v[124:127], v[150:153], v[182:185], v[124:127]
	v_mfma_f32_16x16x32_bf16 v[120:123], v[158:161], v[182:185], v[120:123]
	v_mfma_f32_16x16x32_bf16 v[116:119], v[150:153], v[190:193], v[116:119]
	v_mfma_f32_16x16x32_bf16 v[112:115], v[158:161], v[190:193], v[112:115]
	v_mfma_f32_16x16x32_bf16 v[108:111], v[150:153], v[198:201], v[108:111]
	v_mfma_f32_16x16x32_bf16 v[100:103], v[158:161], v[198:201], v[100:103]
	v_mfma_f32_16x16x32_bf16 v[92:95], v[150:153], v[206:209], v[92:95]
	v_mfma_f32_16x16x32_bf16 v[84:87], v[158:161], v[206:209], v[84:87]
	v_mfma_f32_16x16x32_bf16 v[104:107], v[162:165], v[178:181], v[104:107]
	v_mfma_f32_16x16x32_bf16 v[96:99], v[170:173], v[178:181], v[96:99]
	v_mfma_f32_16x16x32_bf16 v[88:91], v[162:165], v[186:189], v[88:91]
	v_mfma_f32_16x16x32_bf16 v[80:83], v[170:173], v[186:189], v[80:83]
	v_mfma_f32_16x16x32_bf16 v[76:79], v[162:165], v[194:197], v[76:79]
	v_mfma_f32_16x16x32_bf16 v[72:75], v[170:173], v[194:197], v[72:75]
	v_mfma_f32_16x16x32_bf16 v[68:71], v[162:165], v[202:205], v[68:71]
	v_mfma_f32_16x16x32_bf16 v[64:67], v[170:173], v[202:205], v[64:67]
	v_mfma_f32_16x16x32_bf16 v[104:107], v[166:169], v[182:185], v[104:107]
	v_mfma_f32_16x16x32_bf16 v[96:99], v[174:177], v[182:185], v[96:99]
	v_mfma_f32_16x16x32_bf16 v[88:91], v[166:169], v[190:193], v[88:91]
	v_mfma_f32_16x16x32_bf16 v[80:83], v[174:177], v[190:193], v[80:83]
	v_mfma_f32_16x16x32_bf16 v[76:79], v[166:169], v[198:201], v[76:79]
	v_mfma_f32_16x16x32_bf16 v[72:75], v[174:177], v[198:201], v[72:75]
	v_mfma_f32_16x16x32_bf16 v[68:71], v[166:169], v[206:209], v[68:71]
	v_mfma_f32_16x16x32_bf16 v[64:67], v[174:177], v[206:209], v[64:67]
	s_barrier
	s_add_i32 s10, s80, s97
	v_lshl_add_u64 v[210:211], s[48:49], 0, v[128:129]
	s_mov_b32 m0, s10
	ds_read_b128 v[178:181], v242 offset:16384
	ds_read_b128 v[182:185], v242 offset:17408
	ds_read_b128 v[186:189], v242 offset:18432
	ds_read_b128 v[190:193], v242 offset:19456
	ds_read_b128 v[194:197], v242 offset:20480
	ds_read_b128 v[198:201], v242 offset:21504
	ds_read_b128 v[202:205], v242 offset:22528
	ds_read_b128 v[206:209], v242 offset:23552
	global_load_lds_dwordx4 v[210:211], off
	s_add_i32 m0, s10, 0x2000
	s_add_u32 s10, s48, 0x80000
	v_lshl_add_u64 v[212:213], s[48:49], 0, v[130:131]
	s_addc_u32 s11, s49, 0
	s_add_i32 s88, s81, s97
	global_load_lds_dwordx4 v[212:213], off
	v_lshl_add_u64 v[214:215], s[10:11], 0, v[128:129]
	s_mov_b32 m0, s88
	v_lshl_add_u64 v[216:217], s[50:51], 0, v[136:137]
	global_load_lds_dwordx4 v[214:215], off
	v_lshl_add_u64 v[214:215], s[10:11], 0, v[130:131]
	s_add_i32 m0, s88, 0x2000
	s_nop 0
	global_load_lds_dwordx4 v[214:215], off
	v_lshl_add_u64 v[214:215], s[50:51], 0, v[132:133]
	s_mov_b32 m0, s62
	s_nop 0
	global_load_lds_dwordx4 v[214:215], off
	s_mov_b32 m0, s63
	s_nop 0
	global_load_lds_dwordx4 v[216:217], off
	s_waitcnt vmcnt(8)
	s_waitcnt lgkmcnt(0)
	s_barrier
	s_waitcnt lgkmcnt(0)
	v_mfma_f32_16x16x32_bf16 v[60:63], v[146:149], v[178:181], v[60:63]
	v_mfma_f32_16x16x32_bf16 v[56:59], v[154:157], v[178:181], v[56:59]
	v_mfma_f32_16x16x32_bf16 v[52:55], v[146:149], v[186:189], v[52:55]
	v_mfma_f32_16x16x32_bf16 v[48:51], v[154:157], v[186:189], v[48:51]
	v_mfma_f32_16x16x32_bf16 v[36:39], v[146:149], v[194:197], v[36:39]
	v_mfma_f32_16x16x32_bf16 v[32:35], v[154:157], v[194:197], v[32:35]
	v_mfma_f32_16x16x32_bf16 v[20:23], v[146:149], v[202:205], v[20:23]
	v_mfma_f32_16x16x32_bf16 v[16:19], v[154:157], v[202:205], v[16:19]
	v_mfma_f32_16x16x32_bf16 v[60:63], v[150:153], v[182:185], v[60:63]
	v_mfma_f32_16x16x32_bf16 v[56:59], v[158:161], v[182:185], v[56:59]
	v_mfma_f32_16x16x32_bf16 v[52:55], v[150:153], v[190:193], v[52:55]
	v_mfma_f32_16x16x32_bf16 v[48:51], v[158:161], v[190:193], v[48:51]
	v_mfma_f32_16x16x32_bf16 v[36:39], v[150:153], v[198:201], v[36:39]
	v_mfma_f32_16x16x32_bf16 v[32:35], v[158:161], v[198:201], v[32:35]
	v_mfma_f32_16x16x32_bf16 v[20:23], v[150:153], v[206:209], v[20:23]
	v_mfma_f32_16x16x32_bf16 v[16:19], v[158:161], v[206:209], v[16:19]
	v_mfma_f32_16x16x32_bf16 v[44:47], v[162:165], v[178:181], v[44:47]
	v_mfma_f32_16x16x32_bf16 v[40:43], v[170:173], v[178:181], v[40:43]
	v_mfma_f32_16x16x32_bf16 v[28:31], v[162:165], v[186:189], v[28:31]
	v_mfma_f32_16x16x32_bf16 v[24:27], v[170:173], v[186:189], v[24:27]
	v_mfma_f32_16x16x32_bf16 v[12:15], v[162:165], v[194:197], v[12:15]
	v_mfma_f32_16x16x32_bf16 v[8:11], v[170:173], v[194:197], v[8:11]
	v_mfma_f32_16x16x32_bf16 v[4:7], v[162:165], v[202:205], v[4:7]
	v_mfma_f32_16x16x32_bf16 v[0:3], v[170:173], v[202:205], v[0:3]
	v_mfma_f32_16x16x32_bf16 v[44:47], v[166:169], v[182:185], v[44:47]
	v_mfma_f32_16x16x32_bf16 v[40:43], v[174:177], v[182:185], v[40:43]
	v_mfma_f32_16x16x32_bf16 v[28:31], v[166:169], v[190:193], v[28:31]
	v_mfma_f32_16x16x32_bf16 v[24:27], v[174:177], v[190:193], v[24:27]
	v_mfma_f32_16x16x32_bf16 v[12:15], v[166:169], v[198:201], v[12:15]
	v_mfma_f32_16x16x32_bf16 v[8:11], v[174:177], v[198:201], v[8:11]
	v_mfma_f32_16x16x32_bf16 v[4:7], v[166:169], v[206:209], v[4:7]
	v_mfma_f32_16x16x32_bf16 v[0:3], v[174:177], v[206:209], v[0:3]
	s_barrier
; #define PG8_STAGE(bufoff, gbase, o0, o1) do { \
;         __builtin_amdgcn_global_load_lds((const unsigned*)((const char*)(gbase) + (o0)), (LAS unsigned*)(lds + (bufoff) + ldsw), 16, 0, 0); \
;         __builtin_amdgcn_global_load_lds((const unsigned*)((const char*)(gbase) + (o1)), (LAS unsigned*)(lds + (bufoff) + ldsw + 8192), 16, 0, 0); } while (0)
; #define PG8_LDA(dst, b, h) do { _Pragma("unroll") for (int m = 0; m < 4; ++m) _Pragma("unroll") for (int k = 0; k < 2; ++k) dst[m][k] = *(const LAS bf16x8*)(lds + PG8_SA(b, h) + aoff + m * 2048 + k * 1024); } while (0)
; #define PG8_LDB(dst, b, h) do { _Pragma("unroll") for (int n = 0; n < 2; ++n) _Pragma("unroll") for (int k = 0; k < 2; ++k) dst[n][k] = *(const LAS bf16x8*)(lds + PG8_SB(b, h) + boff + n * 2048 + k * 1024); } while (0)
; #define PG8_WAIT_V(n) asm volatile("s_waitcnt vmcnt(" #n ")" ::: "memory")
; #define PG8_WAIT_L(n) asm volatile("s_waitcnt lgkmcnt(" #n ")" ::: "memory")
; #define PG8_BAR __builtin_amdgcn_s_barrier()
; #define PG8_SCHED __builtin_amdgcn_sched_barrier(0)
; template <class Epi, class Sched, class Prob>
; __device__ __forceinline__ void gemm_phase(LAS unsigned char* lds, LAS unsigned char* lds_epi, const Prob g, const Sched& S, const Epi& E, int wid) {
;     ...
;             PG8_LDB(B0, 1, 0); PG8_LDB(B1, 1, 1); PG8_SCHED; PG8_LDA(At, 1, 0); PG8_STAGE(PG8_SA(0, 1), a2, cA10, cA11);
;             PG8_WAIT_V(8); PG8_WAIT_L(0); PG8_BAR; PG8_MMA(0, 0, At, B0); PG8_MMA(0, 1, At, B1); PG8_BAR; PG8_SCHED;
	s_add_i32 s10, 0, 0x18000
	s_add_i32 s88, 0, 0x1c000
	v_add_u32_e32 v158, s10, v239
	v_add_u32_e32 v174, s88, v239
	ds_read_b128 v[146:149], v158
	ds_read_b128 v[150:153], v158 offset:1024
	ds_read_b128 v[154:157], v158 offset:2048
	ds_read_b128 v[158:161], v158 offset:3072
	ds_read_b128 v[162:165], v174
	ds_read_b128 v[166:169], v174 offset:1024
	ds_read_b128 v[170:173], v174 offset:2048
	ds_read_b128 v[174:177], v174 offset:3072
	s_mov_b32 m0, s64
	v_lshl_add_u64 v[218:219], s[50:51], 0, v[134:135]
	ds_read_b128 v[178:181], v242 offset:32768
	ds_read_b128 v[182:185], v242 offset:33792
	ds_read_b128 v[186:189], v242 offset:34816
	ds_read_b128 v[190:193], v242 offset:35840
	ds_read_b128 v[194:197], v242 offset:36864
	ds_read_b128 v[198:201], v242 offset:37888
	ds_read_b128 v[202:205], v242 offset:38912
	ds_read_b128 v[206:209], v242 offset:39936
	global_load_lds_dwordx4 v[218:219], off
	v_lshl_add_u64 v[218:219], s[50:51], 0, v[138:139]
	s_mov_b32 m0, s65
	s_nop 0
	global_load_lds_dwordx4 v[218:219], off
	s_waitcnt vmcnt(8)
	s_waitcnt lgkmcnt(0)
	s_barrier
	s_waitcnt lgkmcnt(0)
	v_mfma_f32_16x16x32_bf16 v[124:127], v[146:149], v[178:181], v[124:127]
	v_mfma_f32_16x16x32_bf16 v[120:123], v[154:157], v[178:181], v[120:123]
	v_mfma_f32_16x16x32_bf16 v[116:119], v[146:149], v[186:189], v[116:119]
	v_mfma_f32_16x16x32_bf16 v[112:115], v[154:157], v[186:189], v[112:115]
	v_mfma_f32_16x16x32_bf16 v[108:111], v[146:149], v[194:197], v[108:111]
	v_mfma_f32_16x16x32_bf16 v[100:103], v[154:157], v[194:197], v[100:103]
	v_mfma_f32_16x16x32_bf16 v[92:95], v[146:149], v[202:205], v[92:95]
	v_mfma_f32_16x16x32_bf16 v[84:87], v[154:157], v[202:205], v[84:87]
	v_mfma_f32_16x16x32_bf16 v[124:127], v[150:153], v[182:185], v[124:127]
	v_mfma_f32_16x16x32_bf16 v[120:123], v[158:161], v[182:185], v[120:123]
	v_mfma_f32_16x16x32_bf16 v[116:119], v[150:153], v[190:193], v[116:119]
	v_mfma_f32_16x16x32_bf16 v[112:115], v[158:161], v[190:193], v[112:115]
	v_mfma_f32_16x16x32_bf16 v[108:111], v[150:153], v[198:201], v[108:111]
	v_mfma_f32_16x16x32_bf16 v[100:103], v[158:161], v[198:201], v[100:103]
	v_mfma_f32_16x16x32_bf16 v[92:95], v[150:153], v[206:209], v[92:95]
	v_mfma_f32_16x16x32_bf16 v[84:87], v[158:161], v[206:209], v[84:87]
	v_mfma_f32_16x16x32_bf16 v[104:107], v[162:165], v[178:181], v[104:107]
	v_mfma_f32_16x16x32_bf16 v[96:99], v[170:173], v[178:181], v[96:99]
	v_mfma_f32_16x16x32_bf16 v[88:91], v[162:165], v[186:189], v[88:91]
	v_mfma_f32_16x16x32_bf16 v[80:83], v[170:173], v[186:189], v[80:83]
	v_mfma_f32_16x16x32_bf16 v[76:79], v[162:165], v[194:197], v[76:79]
	v_mfma_f32_16x16x32_bf16 v[72:75], v[170:173], v[194:197], v[72:75]
	v_mfma_f32_16x16x32_bf16 v[68:71], v[162:165], v[202:205], v[68:71]
	v_mfma_f32_16x16x32_bf16 v[64:67], v[170:173], v[202:205], v[64:67]
	v_mfma_f32_16x16x32_bf16 v[104:107], v[166:169], v[182:185], v[104:107]
	v_mfma_f32_16x16x32_bf16 v[96:99], v[174:177], v[182:185], v[96:99]
	v_mfma_f32_16x16x32_bf16 v[88:91], v[166:169], v[190:193], v[88:91]
	v_mfma_f32_16x16x32_bf16 v[80:83], v[174:177], v[190:193], v[80:83]
	v_mfma_f32_16x16x32_bf16 v[76:79], v[166:169], v[198:201], v[76:79]
	v_mfma_f32_16x16x32_bf16 v[72:75], v[174:177], v[198:201], v[72:75]
	v_mfma_f32_16x16x32_bf16 v[68:71], v[166:169], v[206:209], v[68:71]
	v_mfma_f32_16x16x32_bf16 v[64:67], v[174:177], v[206:209], v[64:67]
	s_barrier
; #define PG8_STAGE(bufoff, gbase, o0, o1) do { \
;         __builtin_amdgcn_global_load_lds((const unsigned*)((const char*)(gbase) + (o0)), (LAS unsigned*)(lds + (bufoff) + ldsw), 16, 0, 0); \
;         __builtin_amdgcn_global_load_lds((const unsigned*)((const char*)(gbase) + (o1)), (LAS unsigned*)(lds + (bufoff) + ldsw + 8192), 16, 0, 0); } while (0)
; #define PG8_LDA(dst, b, h) do { _Pragma("unroll") for (int m = 0; m < 4; ++m) _Pragma("unroll") for (int k = 0; k < 2; ++k) dst[m][k] = *(const LAS bf16x8*)(lds + PG8_SA(b, h) + aoff + m * 2048 + k * 1024); } while (0)
; #define PG8_WAIT_V(n) asm volatile("s_waitcnt vmcnt(" #n ")" ::: "memory")
; #define PG8_WAIT_L(n) asm volatile("s_waitcnt lgkmcnt(" #n ")" ::: "memory")
; #define PG8_BAR __builtin_amdgcn_s_barrier()
; #define PG8_SCHED __builtin_amdgcn_sched_barrier(0)
; template <class Epi, class Sched, class Prob>
; __device__ __forceinline__ void gemm_phase(LAS unsigned char* lds, LAS unsigned char* lds_epi, const Prob g, const Sched& S, const Epi& E, int wid) {
;     ...
;             PG8_LDA(At, 1, 1); PG8_STAGE(PG8_SB(1, 0), b3, vB0, vB1); PG8_STAGE(PG8_SB(1, 1), b3 + hstepB, vB0, vB1); PG8_STAGE(PG8_SA(1, 0), a3, cA00, cA01);
;             PG8_WAIT_V(8); PG8_WAIT_L(0); PG8_BAR; PG8_MMA(1, 0, At, B0); PG8_MMA(1, 1, At, B1); PG8_BAR; PG8_SCHED;
;         }
	s_add_i32 s10, s10, s97
	v_lshl_add_u64 v[210:211], v[210:211], 0, s[24:25]
	s_mov_b32 m0, s10
	ds_read_b128 v[178:181], v242 offset:49152
	ds_read_b128 v[182:185], v242 offset:50176
	ds_read_b128 v[186:189], v242 offset:51200
	ds_read_b128 v[190:193], v242 offset:52224
	ds_read_b128 v[194:197], v242 offset:53248
	ds_read_b128 v[198:201], v242 offset:54272
	ds_read_b128 v[202:205], v242 offset:55296
	ds_read_b128 v[206:209], v242 offset:56320
	global_load_lds_dwordx4 v[210:211], off
	s_add_i32 m0, s10, 0x2000
	s_add_u32 s10, s48, 0x80080
	v_lshl_add_u64 v[210:211], v[212:213], 0, s[24:25]
	s_addc_u32 s11, s49, 0
	s_add_i32 s48, s88, s97
	global_load_lds_dwordx4 v[210:211], off
	v_lshl_add_u64 v[210:211], s[10:11], 0, v[128:129]
	s_mov_b32 m0, s48
	s_nop 0
	global_load_lds_dwordx4 v[210:211], off
	v_lshl_add_u64 v[210:211], s[10:11], 0, v[130:131]
	s_add_i32 m0, s48, 0x2000
	s_nop 0
	global_load_lds_dwordx4 v[210:211], off
	v_lshl_add_u64 v[210:211], v[214:215], 0, s[24:25]
	s_mov_b32 m0, s78
	s_nop 0
	global_load_lds_dwordx4 v[210:211], off
	v_lshl_add_u64 v[210:211], v[216:217], 0, s[24:25]
	s_mov_b32 m0, s79
	s_nop 0
	global_load_lds_dwordx4 v[210:211], off
	s_waitcnt vmcnt(8)
	s_waitcnt lgkmcnt(0)
	s_barrier
	s_waitcnt lgkmcnt(0)
	v_mfma_f32_16x16x32_bf16 v[60:63], v[146:149], v[178:181], v[60:63]
	v_mfma_f32_16x16x32_bf16 v[56:59], v[154:157], v[178:181], v[56:59]
	v_mfma_f32_16x16x32_bf16 v[52:55], v[146:149], v[186:189], v[52:55]
	v_mfma_f32_16x16x32_bf16 v[48:51], v[154:157], v[186:189], v[48:51]
	v_mfma_f32_16x16x32_bf16 v[36:39], v[146:149], v[194:197], v[36:39]
	v_mfma_f32_16x16x32_bf16 v[32:35], v[154:157], v[194:197], v[32:35]
	v_mfma_f32_16x16x32_bf16 v[20:23], v[146:149], v[202:205], v[20:23]
	v_mfma_f32_16x16x32_bf16 v[16:19], v[154:157], v[202:205], v[16:19]
	v_mfma_f32_16x16x32_bf16 v[60:63], v[150:153], v[182:185], v[60:63]
	v_mfma_f32_16x16x32_bf16 v[56:59], v[158:161], v[182:185], v[56:59]
	v_mfma_f32_16x16x32_bf16 v[52:55], v[150:153], v[190:193], v[52:55]
	v_mfma_f32_16x16x32_bf16 v[48:51], v[158:161], v[190:193], v[48:51]
	v_mfma_f32_16x16x32_bf16 v[36:39], v[150:153], v[198:201], v[36:39]
	v_mfma_f32_16x16x32_bf16 v[32:35], v[158:161], v[198:201], v[32:35]
	v_mfma_f32_16x16x32_bf16 v[20:23], v[150:153], v[206:209], v[20:23]
	v_mfma_f32_16x16x32_bf16 v[16:19], v[158:161], v[206:209], v[16:19]
	v_mfma_f32_16x16x32_bf16 v[44:47], v[162:165], v[178:181], v[44:47]
	v_mfma_f32_16x16x32_bf16 v[40:43], v[170:173], v[178:181], v[40:43]
	v_mfma_f32_16x16x32_bf16 v[28:31], v[162:165], v[186:189], v[28:31]
	v_mfma_f32_16x16x32_bf16 v[24:27], v[170:173], v[186:189], v[24:27]
	v_mfma_f32_16x16x32_bf16 v[12:15], v[162:165], v[194:197], v[12:15]
	v_mfma_f32_16x16x32_bf16 v[8:11], v[170:173], v[194:197], v[8:11]
	v_mfma_f32_16x16x32_bf16 v[4:7], v[162:165], v[202:205], v[4:7]
	v_mfma_f32_16x16x32_bf16 v[0:3], v[170:173], v[202:205], v[0:3]
	v_mfma_f32_16x16x32_bf16 v[44:47], v[166:169], v[182:185], v[44:47]
	v_mfma_f32_16x16x32_bf16 v[40:43], v[174:177], v[182:185], v[40:43]
	v_mfma_f32_16x16x32_bf16 v[28:31], v[166:169], v[190:193], v[28:31]
	v_mfma_f32_16x16x32_bf16 v[24:27], v[174:177], v[190:193], v[24:27]
	v_mfma_f32_16x16x32_bf16 v[12:15], v[166:169], v[198:201], v[12:15]
	v_mfma_f32_16x16x32_bf16 v[8:11], v[174:177], v[198:201], v[8:11]
	v_mfma_f32_16x16x32_bf16 v[4:7], v[166:169], v[206:209], v[4:7]
	v_mfma_f32_16x16x32_bf16 v[0:3], v[174:177], v[206:209], v[0:3]
	s_barrier
	s_add_i32 s87, s87, 2
	s_add_u32 s54, s54, 0x100
	s_addc_u32 s55, s55, 0
	s_cmp_gt_u32 s87, 29
	s_mov_b64 s[10:11], s[46:47]
	s_cbranch_scc0 .LBB0_1434
	v_readlane_b32 s10, v254, 27
	v_readlane_b32 s11, v254, 28
	s_and_b64 vcc, exec, s[10:11]
	s_cbranch_vccz .LBB0_1437
	s_barrier

; #define PG8_STAGE(bufoff, gbase, o0, o1) do { \
;         __builtin_amdgcn_global_load_lds((const unsigned*)((const char*)(gbase) + (o0)), (LAS unsigned*)(lds + (bufoff) + ldsw), 16, 0, 0); \
;         __builtin_amdgcn_global_load_lds((const unsigned*)((const char*)(gbase) + (o1)), (LAS unsigned*)(lds + (bufoff) + ldsw + 8192), 16, 0, 0); } while (0)
; #define PG8_LDA(dst, b, h) do { _Pragma("unroll") for (int m = 0; m < 4; ++m) _Pragma("unroll") for (int k = 0; k < 2; ++k) dst[m][k] = *(const LAS bf16x8*)(lds + PG8_SA(b, h) + aoff + m * 2048 + k * 1024); } while (0)
; #define PG8_LDB(dst, b, h) do { _Pragma("unroll") for (int n = 0; n < 2; ++n) _Pragma("unroll") for (int k = 0; k < 2; ++k) dst[n][k] = *(const LAS bf16x8*)(lds + PG8_SB(b, h) + boff + n * 2048 + k * 1024); } while (0)
; #define PG8_WAIT_V(n) asm volatile("s_waitcnt vmcnt(" #n ")" ::: "memory")
; #define PG8_WAIT_L(n) asm volatile("s_waitcnt lgkmcnt(" #n ")" ::: "memory")
; #define PG8_BAR __builtin_amdgcn_s_barrier()
; #define PG8_SCHED __builtin_amdgcn_sched_barrier(0)
; template <class Epi, class Sched, class Prob>
; __device__ __forceinline__ void gemm_phase(LAS unsigned char* lds, LAS unsigned char* lds_epi, const Prob g, const Sched& S, const Epi& E, int wid) {
;     ...
;         const bool has_next = S.next(ui + 1, nxt);
;         const char* nA = has_next ? g.a_base(nxt) : cA; const char* nB = has_next ? g.b_base(nxt) : cB;
; _Pragma("clang loop unroll(disable)")
;         for (int t = 0; t < nt; t += 2) {
;             const bool last = (t == nt - 2);
;             const char* a1 = cA + (size_t)(t + 1) * kstep;
;             const char* a2 = last ? nA : cA + (size_t)(t + 2) * kstep; const char* b2 = last ? nB : cB + (size_t)(t + 2) * kstep;
;             const char* a3 = a2 + kstep; const char* b3 = b2 + kstep;
;             PG8_LDB(B0, 0, 0); PG8_LDB(B1, 0, 1); PG8_SCHED; PG8_LDA(At, 0, 0); PG8_STAGE(PG8_SA(1, 1), a1, cA10, cA11);
;             PG8_WAIT_V(8); PG8_WAIT_L(0); PG8_BAR; PG8_MMA(0, 0, At, B0); PG8_MMA(0, 1, At, B1); PG8_BAR; PG8_SCHED;
;             PG8_LDA(At, 0, 1); PG8_STAGE(PG8_SB(0, 0), b2, vB0, vB1); PG8_STAGE(PG8_SB(0, 1), b2 + hstepB, vB0, vB1); PG8_STAGE(PG8_SA(0, 0), a2, cA00, cA01);
;             PG8_WAIT_V(8); PG8_WAIT_L(0); PG8_BAR; PG8_MMA(1, 0, At, B0); PG8_MMA(1, 1, At, B1); PG8_BAR; PG8_SCHED;
.LBB0_1594:
	s_ashr_i32 s65, s64, 31
	s_lshl_b64 s[14:15], s[64:65], 20
	s_add_u32 s17, s40, s14
	s_addc_u32 s19, s41, s15
	s_ashr_i32 s14, s62, 1
	s_ashr_i32 s15, s14, 31
	s_lshl_b64 s[14:15], s[14:15], 9
	s_add_u32 s68, s17, s14
	s_addc_u32 s69, s19, s15
	s_and_b64 s[14:15], s[66:67], exec
	s_cselect_b32 s17, s69, s9
	s_cselect_b32 s19, s68, s8
	s_ashr_i32 s63, s62, 31
	s_lshl_b64 s[14:15], s[62:63], 17
	s_add_u32 s70, s33, s14
	s_addc_u32 s71, s76, s15
	s_and_b64 s[14:15], s[66:67], exec
	v_mov_b32_e32 v0, 0
	s_cselect_b32 s26, s71, s11
	s_cselect_b32 s27, s70, s10
	s_mov_b64 s[20:21], -1
	s_mov_b64 s[14:15], 0
	s_add_u32 s24, s8, s14
	s_addc_u32 s25, s9, s15
	s_add_u32 s22, s24, 0x100
	s_addc_u32 s23, s25, 0
	v_cndmask_b32_e64 v56, 0, 1, s[20:21]
	s_and_b64 s[20:21], s[12:13], exec
	s_cselect_b32 s20, s19, s22
	s_cselect_b32 s21, s17, s23
	s_add_u32 s14, s10, s14
	s_addc_u32 s15, s11, s15
	s_add_u32 s14, s14, 0x100
	v_cmp_ne_u32_e32 vcc, 1, v56
	ds_read_b128 v[56:59], v221
	ds_read_b128 v[68:71], v221 offset:1024
	ds_read_b128 v[72:75], v221 offset:2048
	ds_read_b128 v[88:91], v221 offset:3072
	ds_read_b128 v[100:103], v222
	ds_read_b128 v[104:107], v222 offset:1024
	ds_read_b128 v[166:169], v222 offset:2048
	ds_read_b128 v[170:173], v222 offset:3072
	s_addc_u32 s15, s15, 0
	s_and_b64 s[12:13], s[12:13], exec
	s_cselect_b32 s15, s26, s15
	s_cselect_b32 s14, s27, s14
	s_add_i32 s65, s85, s97
	s_add_i32 m0, s77, 0xc000
	s_add_i32 s72, s77, 0xe000
	s_add_i32 s36, s65, 0x2000
	s_add_u32 s22, s14, 0x10000
	s_addc_u32 s23, s15, 0
	s_add_i32 s35, 0, 0x18000
	s_add_i32 s63, s86, s97
	s_add_i32 s31, s35, s97
	s_add_i32 s37, s63, 0x2000
	s_add_i32 s34, 0, 0x1c000
	s_add_i32 s29, s31, 0x2000
	s_add_u32 s12, s14, 0x10080
	s_addc_u32 s13, s15, 0
	s_add_i32 s30, s34, s97
	s_add_i32 s28, s30, 0x2000
	v_lshl_add_u64 v[206:207], s[24:25], 0, v[158:159]
	v_lshl_add_u64 v[206:207], v[206:207], 0, s[54:55]
	ds_read_b128 v[174:177], v223
	ds_read_b128 v[178:181], v223 offset:1024
	ds_read_b128 v[182:185], v223 offset:2048
	ds_read_b128 v[186:189], v223 offset:3072
	ds_read_b128 v[190:193], v223 offset:4096
	ds_read_b128 v[194:197], v223 offset:5120
	ds_read_b128 v[198:201], v223 offset:6144
	ds_read_b128 v[202:205], v223 offset:7168
	global_load_lds_dwordx4 v[206:207], off
	v_lshl_add_u64 v[206:207], s[24:25], 0, v[162:163]
	v_lshl_add_u64 v[206:207], v[206:207], 0, s[54:55]
	s_mov_b32 m0, s72
	s_nop 0
	global_load_lds_dwordx4 v[206:207], off
	s_waitcnt vmcnt(8)
	s_waitcnt lgkmcnt(0)
	s_barrier
	s_waitcnt lgkmcnt(0)
	v_mfma_f32_16x16x32_bf16 v[148:151], v[56:59], v[174:177], 0
	v_mfma_f32_16x16x32_bf16 v[116:119], v[72:75], v[174:177], 0
	v_mfma_f32_16x16x32_bf16 v[144:147], v[56:59], v[182:185], 0
	v_mfma_f32_16x16x32_bf16 v[112:115], v[72:75], v[182:185], 0
	v_mfma_f32_16x16x32_bf16 v[140:143], v[56:59], v[190:193], 0
	v_mfma_f32_16x16x32_bf16 v[108:111], v[72:75], v[190:193], 0
	v_mfma_f32_16x16x32_bf16 v[136:139], v[56:59], v[198:201], 0
	v_mfma_f32_16x16x32_bf16 v[96:99], v[72:75], v[198:201], 0
	v_mfma_f32_16x16x32_bf16 v[148:151], v[68:71], v[178:181], v[148:151]
	v_mfma_f32_16x16x32_bf16 v[116:119], v[88:91], v[178:181], v[116:119]
	v_mfma_f32_16x16x32_bf16 v[144:147], v[68:71], v[186:189], v[144:147]
	v_mfma_f32_16x16x32_bf16 v[112:115], v[88:91], v[186:189], v[112:115]
	v_mfma_f32_16x16x32_bf16 v[140:143], v[68:71], v[194:197], v[140:143]
	v_mfma_f32_16x16x32_bf16 v[108:111], v[88:91], v[194:197], v[108:111]
	v_mfma_f32_16x16x32_bf16 v[136:139], v[68:71], v[202:205], v[136:139]
	v_mfma_f32_16x16x32_bf16 v[96:99], v[88:91], v[202:205], v[96:99]
	v_mfma_f32_16x16x32_bf16 v[132:135], v[100:103], v[174:177], 0
	v_mfma_f32_16x16x32_bf16 v[92:95], v[166:169], v[174:177], 0
	v_mfma_f32_16x16x32_bf16 v[128:131], v[100:103], v[182:185], 0
	v_mfma_f32_16x16x32_bf16 v[84:87], v[166:169], v[182:185], 0
	v_mfma_f32_16x16x32_bf16 v[124:127], v[100:103], v[190:193], 0
	v_mfma_f32_16x16x32_bf16 v[80:83], v[166:169], v[190:193], 0
	v_mfma_f32_16x16x32_bf16 v[120:123], v[100:103], v[198:201], 0
	v_mfma_f32_16x16x32_bf16 v[76:79], v[166:169], v[198:201], 0
	v_mfma_f32_16x16x32_bf16 v[132:135], v[104:107], v[178:181], v[132:135]
	v_mfma_f32_16x16x32_bf16 v[92:95], v[170:173], v[178:181], v[92:95]
	v_mfma_f32_16x16x32_bf16 v[128:131], v[104:107], v[186:189], v[128:131]
	v_mfma_f32_16x16x32_bf16 v[84:87], v[170:173], v[186:189], v[84:87]
	v_mfma_f32_16x16x32_bf16 v[124:127], v[104:107], v[194:197], v[124:127]
	v_mfma_f32_16x16x32_bf16 v[80:83], v[170:173], v[194:197], v[80:83]
	v_mfma_f32_16x16x32_bf16 v[120:123], v[104:107], v[202:205], v[120:123]
	v_mfma_f32_16x16x32_bf16 v[76:79], v[170:173], v[202:205], v[76:79]
	s_barrier
	s_mov_b32 m0, s65
	v_lshl_add_u64 v[206:207], s[14:15], 0, v[152:153]
	ds_read_b128 v[174:177], v223 offset:16384
	ds_read_b128 v[178:181], v223 offset:17408
	ds_read_b128 v[182:185], v223 offset:18432
	ds_read_b128 v[186:189], v223 offset:19456
	ds_read_b128 v[190:193], v223 offset:20480
	ds_read_b128 v[194:197], v223 offset:21504
	ds_read_b128 v[198:201], v223 offset:22528
	ds_read_b128 v[202:205], v223 offset:23552
	global_load_lds_dwordx4 v[206:207], off
	v_lshl_add_u64 v[208:209], s[14:15], 0, v[154:155]
	s_mov_b32 m0, s36
	v_lshl_add_u64 v[210:211], s[22:23], 0, v[152:153]
	global_load_lds_dwordx4 v[208:209], off
	s_mov_b32 m0, s63
	v_lshl_add_u64 v[212:213], s[20:21], 0, v[160:161]
	global_load_lds_dwordx4 v[210:211], off
	v_lshl_add_u64 v[210:211], s[22:23], 0, v[154:155]
	s_mov_b32 m0, s37
	s_nop 0
	global_load_lds_dwordx4 v[210:211], off
	v_lshl_add_u64 v[210:211], s[20:21], 0, v[156:157]
	s_mov_b32 m0, s77
	s_nop 0
	global_load_lds_dwordx4 v[210:211], off
	s_mov_b32 m0, s78
	s_nop 0
	global_load_lds_dwordx4 v[212:213], off
	s_waitcnt vmcnt(8)
	s_waitcnt lgkmcnt(0)
	s_barrier
; #define PG8_STAGE(bufoff, gbase, o0, o1) do { \
;         __builtin_amdgcn_global_load_lds((const unsigned*)((const char*)(gbase) + (o0)), (LAS unsigned*)(lds + (bufoff) + ldsw), 16, 0, 0); \
;         __builtin_amdgcn_global_load_lds((const unsigned*)((const char*)(gbase) + (o1)), (LAS unsigned*)(lds + (bufoff) + ldsw + 8192), 16, 0, 0); } while (0)
; #define PG8_LDA(dst, b, h) do { _Pragma("unroll") for (int m = 0; m < 4; ++m) _Pragma("unroll") for (int k = 0; k < 2; ++k) dst[m][k] = *(const LAS bf16x8*)(lds + PG8_SA(b, h) + aoff + m * 2048 + k * 1024); } while (0)
; #define PG8_LDB(dst, b, h) do { _Pragma("unroll") for (int n = 0; n < 2; ++n) _Pragma("unroll") for (int k = 0; k < 2; ++k) dst[n][k] = *(const LAS bf16x8*)(lds + PG8_SB(b, h) + boff + n * 2048 + k * 1024); } while (0)
; #define PG8_WAIT_V(n) asm volatile("s_waitcnt vmcnt(" #n ")" ::: "memory")
; #define PG8_WAIT_L(n) asm volatile("s_waitcnt lgkmcnt(" #n ")" ::: "memory")
; #define PG8_BAR __builtin_amdgcn_s_barrier()
; #define PG8_SCHED __builtin_amdgcn_sched_barrier(0)
; template <class Epi, class Sched, class Prob>
; __device__ __forceinline__ void gemm_phase(LAS unsigned char* lds, LAS unsigned char* lds_epi, const Prob g, const Sched& S, const Epi& E, int wid) {
;     ...
;             PG8_WAIT_V(8); PG8_WAIT_L(0); PG8_BAR; PG8_MMA(1, 0, At, B0); PG8_MMA(1, 1, At, B1); PG8_BAR; PG8_SCHED;
;             PG8_LDB(B0, 1, 0); PG8_LDB(B1, 1, 1); PG8_SCHED; PG8_LDA(At, 1, 0); PG8_STAGE(PG8_SA(0, 1), a2, cA10, cA11);
;             PG8_WAIT_V(8); PG8_WAIT_L(0); PG8_BAR; PG8_MMA(0, 0, At, B0); PG8_MMA(0, 1, At, B1); PG8_BAR; PG8_SCHED;
	s_waitcnt lgkmcnt(0)
	v_mfma_f32_16x16x32_bf16 v[64:67], v[56:59], v[174:177], 0
	v_mfma_f32_16x16x32_bf16 v[28:31], v[72:75], v[174:177], 0
	v_mfma_f32_16x16x32_bf16 v[60:63], v[56:59], v[182:185], 0
	v_mfma_f32_16x16x32_bf16 v[24:27], v[72:75], v[182:185], 0
	v_mfma_f32_16x16x32_bf16 v[52:55], v[56:59], v[190:193], 0
	v_mfma_f32_16x16x32_bf16 v[20:23], v[72:75], v[190:193], 0
	v_mfma_f32_16x16x32_bf16 v[48:51], v[56:59], v[198:201], 0
	v_mfma_f32_16x16x32_bf16 v[16:19], v[72:75], v[198:201], 0
	v_mfma_f32_16x16x32_bf16 v[64:67], v[68:71], v[178:181], v[64:67]
	v_mfma_f32_16x16x32_bf16 v[28:31], v[88:91], v[178:181], v[28:31]
	v_mfma_f32_16x16x32_bf16 v[60:63], v[68:71], v[186:189], v[60:63]
	v_mfma_f32_16x16x32_bf16 v[24:27], v[88:91], v[186:189], v[24:27]
	v_mfma_f32_16x16x32_bf16 v[52:55], v[68:71], v[194:197], v[52:55]
	v_mfma_f32_16x16x32_bf16 v[20:23], v[88:91], v[194:197], v[20:23]
	v_mfma_f32_16x16x32_bf16 v[48:51], v[68:71], v[202:205], v[48:51]
	v_mfma_f32_16x16x32_bf16 v[16:19], v[88:91], v[202:205], v[16:19]
	v_mfma_f32_16x16x32_bf16 v[44:47], v[100:103], v[174:177], 0
	v_mfma_f32_16x16x32_bf16 v[12:15], v[166:169], v[174:177], 0
	v_mfma_f32_16x16x32_bf16 v[40:43], v[100:103], v[182:185], 0
	v_mfma_f32_16x16x32_bf16 v[8:11], v[166:169], v[182:185], 0
	v_mfma_f32_16x16x32_bf16 v[36:39], v[100:103], v[190:193], 0
	v_mfma_f32_16x16x32_bf16 v[4:7], v[166:169], v[190:193], 0
	v_mfma_f32_16x16x32_bf16 v[32:35], v[100:103], v[198:201], 0
	v_mfma_f32_16x16x32_bf16 v[0:3], v[166:169], v[198:201], 0
	v_mfma_f32_16x16x32_bf16 v[44:47], v[104:107], v[178:181], v[44:47]
	v_mfma_f32_16x16x32_bf16 v[12:15], v[170:173], v[178:181], v[12:15]
	v_mfma_f32_16x16x32_bf16 v[40:43], v[104:107], v[186:189], v[40:43]
	v_mfma_f32_16x16x32_bf16 v[8:11], v[170:173], v[186:189], v[8:11]
	v_mfma_f32_16x16x32_bf16 v[36:39], v[104:107], v[194:197], v[36:39]
	v_mfma_f32_16x16x32_bf16 v[4:7], v[170:173], v[194:197], v[4:7]
	v_mfma_f32_16x16x32_bf16 v[32:35], v[104:107], v[202:205], v[32:35]
	v_mfma_f32_16x16x32_bf16 v[0:3], v[170:173], v[202:205], v[0:3]
	s_barrier
	v_add_u32_e32 v88, s35, v220
	v_add_u32_e32 v170, s34, v220
	ds_read_b128 v[56:59], v88
	ds_read_b128 v[68:71], v88 offset:1024
	ds_read_b128 v[72:75], v88 offset:2048
	ds_read_b128 v[88:91], v88 offset:3072
	ds_read_b128 v[100:103], v170
	ds_read_b128 v[104:107], v170 offset:1024
	ds_read_b128 v[166:169], v170 offset:2048
	ds_read_b128 v[170:173], v170 offset:3072
	s_mov_b32 m0, s79
	v_lshl_add_u64 v[214:215], s[20:21], 0, v[158:159]
	ds_read_b128 v[174:177], v223 offset:32768
	ds_read_b128 v[178:181], v223 offset:33792
	ds_read_b128 v[182:185], v223 offset:34816
	ds_read_b128 v[186:189], v223 offset:35840
	ds_read_b128 v[190:193], v223 offset:36864
	ds_read_b128 v[194:197], v223 offset:37888
	ds_read_b128 v[198:201], v223 offset:38912
	ds_read_b128 v[202:205], v223 offset:39936
	global_load_lds_dwordx4 v[214:215], off
	v_lshl_add_u64 v[214:215], s[20:21], 0, v[162:163]
	s_mov_b32 m0, s80
	s_nop 0
	global_load_lds_dwordx4 v[214:215], off
	s_waitcnt vmcnt(8)
	s_waitcnt lgkmcnt(0)
	s_barrier
	s_waitcnt lgkmcnt(0)
	v_mfma_f32_16x16x32_bf16 v[148:151], v[56:59], v[174:177], v[148:151]
	v_mfma_f32_16x16x32_bf16 v[116:119], v[72:75], v[174:177], v[116:119]
	v_mfma_f32_16x16x32_bf16 v[144:147], v[56:59], v[182:185], v[144:147]
	v_mfma_f32_16x16x32_bf16 v[112:115], v[72:75], v[182:185], v[112:115]
	v_mfma_f32_16x16x32_bf16 v[140:143], v[56:59], v[190:193], v[140:143]
	v_mfma_f32_16x16x32_bf16 v[108:111], v[72:75], v[190:193], v[108:111]
	v_mfma_f32_16x16x32_bf16 v[136:139], v[56:59], v[198:201], v[136:139]
	v_mfma_f32_16x16x32_bf16 v[96:99], v[72:75], v[198:201], v[96:99]
	v_mfma_f32_16x16x32_bf16 v[148:151], v[68:71], v[178:181], v[148:151]
	v_mfma_f32_16x16x32_bf16 v[116:119], v[88:91], v[178:181], v[116:119]
	v_mfma_f32_16x16x32_bf16 v[144:147], v[68:71], v[186:189], v[144:147]
	v_mfma_f32_16x16x32_bf16 v[112:115], v[88:91], v[186:189], v[112:115]
	v_mfma_f32_16x16x32_bf16 v[140:143], v[68:71], v[194:197], v[140:143]
	v_mfma_f32_16x16x32_bf16 v[108:111], v[88:91], v[194:197], v[108:111]
	v_mfma_f32_16x16x32_bf16 v[136:139], v[68:71], v[202:205], v[136:139]
	v_mfma_f32_16x16x32_bf16 v[96:99], v[88:91], v[202:205], v[96:99]
	v_mfma_f32_16x16x32_bf16 v[132:135], v[100:103], v[174:177], v[132:135]
	v_mfma_f32_16x16x32_bf16 v[92:95], v[166:169], v[174:177], v[92:95]
	v_mfma_f32_16x16x32_bf16 v[128:131], v[100:103], v[182:185], v[128:131]
	v_mfma_f32_16x16x32_bf16 v[84:87], v[166:169], v[182:185], v[84:87]
	v_mfma_f32_16x16x32_bf16 v[124:127], v[100:103], v[190:193], v[124:127]
	v_mfma_f32_16x16x32_bf16 v[80:83], v[166:169], v[190:193], v[80:83]
	v_mfma_f32_16x16x32_bf16 v[120:123], v[100:103], v[198:201], v[120:123]
	v_mfma_f32_16x16x32_bf16 v[76:79], v[166:169], v[198:201], v[76:79]
	v_mfma_f32_16x16x32_bf16 v[132:135], v[104:107], v[178:181], v[132:135]
	v_mfma_f32_16x16x32_bf16 v[92:95], v[170:173], v[178:181], v[92:95]
	v_mfma_f32_16x16x32_bf16 v[128:131], v[104:107], v[186:189], v[128:131]
	v_mfma_f32_16x16x32_bf16 v[84:87], v[170:173], v[186:189], v[84:87]
	v_mfma_f32_16x16x32_bf16 v[124:127], v[104:107], v[194:197], v[124:127]
	v_mfma_f32_16x16x32_bf16 v[80:83], v[170:173], v[194:197], v[80:83]
	v_mfma_f32_16x16x32_bf16 v[120:123], v[104:107], v[202:205], v[120:123]
	v_mfma_f32_16x16x32_bf16 v[76:79], v[170:173], v[202:205], v[76:79]
	s_barrier
; #define PG8_STAGE(bufoff, gbase, o0, o1) do { \
;         __builtin_amdgcn_global_load_lds((const unsigned*)((const char*)(gbase) + (o0)), (LAS unsigned*)(lds + (bufoff) + ldsw), 16, 0, 0); \
;         __builtin_amdgcn_global_load_lds((const unsigned*)((const char*)(gbase) + (o1)), (LAS unsigned*)(lds + (bufoff) + ldsw + 8192), 16, 0, 0); } while (0)
; #define PG8_LDA(dst, b, h) do { _Pragma("unroll") for (int m = 0; m < 4; ++m) _Pragma("unroll") for (int k = 0; k < 2; ++k) dst[m][k] = *(const LAS bf16x8*)(lds + PG8_SA(b, h) + aoff + m * 2048 + k * 1024); } while (0)
; #define PG8_LDB(dst, b, h) do { _Pragma("unroll") for (int n = 0; n < 2; ++n) _Pragma("unroll") for (int k = 0; k < 2; ++k) dst[n][k] = *(const LAS bf16x8*)(lds + PG8_SB(b, h) + boff + n * 2048 + k * 1024); } while (0)
; #define PG8_WAIT_V(n) asm volatile("s_waitcnt vmcnt(" #n ")" ::: "memory")
; #define PG8_WAIT_L(n) asm volatile("s_waitcnt lgkmcnt(" #n ")" ::: "memory")
; #define PG8_BAR __builtin_amdgcn_s_barrier()
; #define PG8_SCHED __builtin_amdgcn_sched_barrier(0)
; template <class Epi, class Sched, class Prob>
; __device__ __forceinline__ void gemm_phase(LAS unsigned char* lds, LAS unsigned char* lds_epi, const Prob g, const Sched& S, const Epi& E, int wid) {
;     ...
;             PG8_LDB(B0, 0, 0); PG8_LDB(B1, 0, 1); PG8_SCHED; PG8_LDA(At, 0, 0); PG8_STAGE(PG8_SA(1, 1), a1, cA10, cA11);
;             PG8_WAIT_V(8); PG8_WAIT_L(0); PG8_BAR; PG8_MMA(0, 0, At, B0); PG8_MMA(0, 1, At, B1); PG8_BAR; PG8_SCHED;
;             PG8_LDA(At, 0, 1); PG8_STAGE(PG8_SB(0, 0), b2, vB0, vB1); PG8_STAGE(PG8_SB(0, 1), b2 + hstepB, vB0, vB1); PG8_STAGE(PG8_SA(0, 0), a2, cA00, cA01);
;             PG8_WAIT_V(8); PG8_WAIT_L(0); PG8_BAR; PG8_MMA(1, 0, At, B0); PG8_MMA(1, 1, At, B1); PG8_BAR; PG8_SCHED;
;             PG8_LDB(B0, 1, 0); PG8_LDB(B1, 1, 1); PG8_SCHED; PG8_LDA(At, 1, 0); PG8_STAGE(PG8_SA(0, 1), a2, cA10, cA11);
;             PG8_WAIT_V(8); PG8_WAIT_L(0); PG8_BAR; PG8_MMA(0, 0, At, B0); PG8_MMA(0, 1, At, B1); PG8_BAR; PG8_SCHED;
;             PG8_LDA(At, 1, 1); PG8_STAGE(PG8_SB(1, 0), b3, vB0, vB1); PG8_STAGE(PG8_SB(1, 1), b3 + hstepB, vB0, vB1); PG8_STAGE(PG8_SA(1, 0), a3, cA00, cA01);
;             PG8_WAIT_V(8); PG8_WAIT_L(0); PG8_BAR; PG8_MMA(1, 0, At, B0); PG8_MMA(1, 1, At, B1); PG8_BAR; PG8_SCHED;
	s_mov_b32 m0, s31
	v_lshl_add_u64 v[206:207], v[206:207], 0, s[54:55]
	ds_read_b128 v[174:177], v223 offset:49152
	ds_read_b128 v[178:181], v223 offset:50176
	ds_read_b128 v[182:185], v223 offset:51200
	ds_read_b128 v[186:189], v223 offset:52224
	ds_read_b128 v[190:193], v223 offset:53248
	ds_read_b128 v[194:197], v223 offset:54272
	ds_read_b128 v[198:201], v223 offset:55296
	ds_read_b128 v[202:205], v223 offset:56320
	global_load_lds_dwordx4 v[206:207], off
	v_lshl_add_u64 v[206:207], v[208:209], 0, s[54:55]
	s_mov_b32 m0, s29
	s_nop 0
	global_load_lds_dwordx4 v[206:207], off
	v_lshl_add_u64 v[206:207], s[12:13], 0, v[152:153]
	s_mov_b32 m0, s30
	s_nop 0
	global_load_lds_dwordx4 v[206:207], off
	v_lshl_add_u64 v[206:207], s[12:13], 0, v[154:155]
	s_mov_b32 m0, s28
	s_nop 0
	global_load_lds_dwordx4 v[206:207], off
	v_lshl_add_u64 v[206:207], v[210:211], 0, s[54:55]
	s_mov_b32 m0, s83
	s_nop 0
	global_load_lds_dwordx4 v[206:207], off
	v_lshl_add_u64 v[206:207], v[212:213], 0, s[54:55]
	s_mov_b32 m0, s84
	s_nop 0
	global_load_lds_dwordx4 v[206:207], off
	s_waitcnt vmcnt(8)
	s_waitcnt lgkmcnt(0)
	s_barrier
	s_waitcnt lgkmcnt(0)
	v_mfma_f32_16x16x32_bf16 v[64:67], v[56:59], v[174:177], v[64:67]
	v_mfma_f32_16x16x32_bf16 v[28:31], v[72:75], v[174:177], v[28:31]
	v_mfma_f32_16x16x32_bf16 v[60:63], v[56:59], v[182:185], v[60:63]
	v_mfma_f32_16x16x32_bf16 v[24:27], v[72:75], v[182:185], v[24:27]
	v_mfma_f32_16x16x32_bf16 v[52:55], v[56:59], v[190:193], v[52:55]
	v_mfma_f32_16x16x32_bf16 v[20:23], v[72:75], v[190:193], v[20:23]
	v_mfma_f32_16x16x32_bf16 v[48:51], v[56:59], v[198:201], v[48:51]
	v_mfma_f32_16x16x32_bf16 v[16:19], v[72:75], v[198:201], v[16:19]
	v_mfma_f32_16x16x32_bf16 v[64:67], v[68:71], v[178:181], v[64:67]
	v_mfma_f32_16x16x32_bf16 v[28:31], v[88:91], v[178:181], v[28:31]
	v_mfma_f32_16x16x32_bf16 v[60:63], v[68:71], v[186:189], v[60:63]
	v_mfma_f32_16x16x32_bf16 v[24:27], v[88:91], v[186:189], v[24:27]
	v_mfma_f32_16x16x32_bf16 v[52:55], v[68:71], v[194:197], v[52:55]
	v_mfma_f32_16x16x32_bf16 v[20:23], v[88:91], v[194:197], v[20:23]
	v_mfma_f32_16x16x32_bf16 v[48:51], v[68:71], v[202:205], v[48:51]
	v_mfma_f32_16x16x32_bf16 v[16:19], v[88:91], v[202:205], v[16:19]
	v_mfma_f32_16x16x32_bf16 v[44:47], v[100:103], v[174:177], v[44:47]
	v_mfma_f32_16x16x32_bf16 v[12:15], v[166:169], v[174:177], v[12:15]
	v_mfma_f32_16x16x32_bf16 v[40:43], v[100:103], v[182:185], v[40:43]
	v_mfma_f32_16x16x32_bf16 v[8:11], v[166:169], v[182:185], v[8:11]
	v_mfma_f32_16x16x32_bf16 v[36:39], v[100:103], v[190:193], v[36:39]
	v_mfma_f32_16x16x32_bf16 v[4:7], v[166:169], v[190:193], v[4:7]
	v_mfma_f32_16x16x32_bf16 v[32:35], v[100:103], v[198:201], v[32:35]
	v_mfma_f32_16x16x32_bf16 v[0:3], v[166:169], v[198:201], v[0:3]
	v_mfma_f32_16x16x32_bf16 v[44:47], v[104:107], v[178:181], v[44:47]
	v_mfma_f32_16x16x32_bf16 v[12:15], v[170:173], v[178:181], v[12:15]
	v_mfma_f32_16x16x32_bf16 v[40:43], v[104:107], v[186:189], v[40:43]
	v_mfma_f32_16x16x32_bf16 v[8:11], v[170:173], v[186:189], v[8:11]
	v_mfma_f32_16x16x32_bf16 v[36:39], v[104:107], v[194:197], v[36:39]
	v_mfma_f32_16x16x32_bf16 v[4:7], v[170:173], v[194:197], v[4:7]
	v_mfma_f32_16x16x32_bf16 v[32:35], v[104:107], v[202:205], v[32:35]
	v_mfma_f32_16x16x32_bf16 v[0:3], v[170:173], v[202:205], v[0:3]
	s_barrier
	s_mov_b64 s[20:21], 0
	s_mov_b64 s[12:13], -1
	s_mov_b64 s[14:15], 0x100
.LBB0_1595:
	s_add_u32 s24, s8, s14
	s_addc_u32 s25, s9, s15
	s_add_u32 s22, s24, 0x100
	s_addc_u32 s23, s25, 0
	v_cndmask_b32_e64 v56, 0, 1, s[20:21]
	s_and_b64 s[20:21], s[12:13], exec
	s_cselect_b32 s20, s19, s22
	s_cselect_b32 s21, s17, s23
	s_add_u32 s14, s10, s14
	s_addc_u32 s15, s11, s15
	s_add_u32 s14, s14, 0x100
	v_cmp_ne_u32_e32 vcc, 1, v56
	ds_read_b128 v[56:59], v221
	ds_read_b128 v[68:71], v221 offset:1024
	ds_read_b128 v[72:75], v221 offset:2048
	ds_read_b128 v[88:91], v221 offset:3072
	ds_read_b128 v[100:103], v222
	ds_read_b128 v[104:107], v222 offset:1024
	ds_read_b128 v[166:169], v222 offset:2048
	ds_read_b128 v[170:173], v222 offset:3072
	s_addc_u32 s15, s15, 0
	s_and_b64 s[12:13], s[12:13], exec
	s_cselect_b32 s15, s26, s15
	s_cselect_b32 s14, s27, s14
	s_add_i32 s65, s85, s97
	s_add_i32 m0, s77, 0xc000
	s_add_i32 s72, s77, 0xe000
	s_add_i32 s36, s65, 0x2000
	s_add_u32 s22, s14, 0x10000
	s_addc_u32 s23, s15, 0
	s_add_i32 s35, 0, 0x18000
	s_add_i32 s63, s86, s97
	s_add_i32 s31, s35, s97
	s_add_i32 s37, s63, 0x2000
	s_add_i32 s34, 0, 0x1c000
	s_add_i32 s29, s31, 0x2000
	s_add_u32 s12, s14, 0x10080
	s_addc_u32 s13, s15, 0
	s_add_i32 s30, s34, s97
	s_add_i32 s28, s30, 0x2000
	v_lshl_add_u64 v[206:207], s[24:25], 0, v[158:159]
	v_lshl_add_u64 v[206:207], v[206:207], 0, s[54:55]
	ds_read_b128 v[174:177], v223
	ds_read_b128 v[178:181], v223 offset:1024
	ds_read_b128 v[182:185], v223 offset:2048
	ds_read_b128 v[186:189], v223 offset:3072
	ds_read_b128 v[190:193], v223 offset:4096
	ds_read_b128 v[194:197], v223 offset:5120
	ds_read_b128 v[198:201], v223 offset:6144
	ds_read_b128 v[202:205], v223 offset:7168
	global_load_lds_dwordx4 v[206:207], off
	v_lshl_add_u64 v[206:207], s[24:25], 0, v[162:163]
	v_lshl_add_u64 v[206:207], v[206:207], 0, s[54:55]
	s_mov_b32 m0, s72
	s_nop 0
	global_load_lds_dwordx4 v[206:207], off
	s_waitcnt vmcnt(8)
	s_waitcnt lgkmcnt(0)
	s_barrier
; #define PG8_STAGE(bufoff, gbase, o0, o1) do { \
;         __builtin_amdgcn_global_load_lds((const unsigned*)((const char*)(gbase) + (o0)), (LAS unsigned*)(lds + (bufoff) + ldsw), 16, 0, 0); \
;         __builtin_amdgcn_global_load_lds((const unsigned*)((const char*)(gbase) + (o1)), (LAS unsigned*)(lds + (bufoff) + ldsw + 8192), 16, 0, 0); } while (0)
; #define PG8_LDA(dst, b, h) do { _Pragma("unroll") for (int m = 0; m < 4; ++m) _Pragma("unroll") for (int k = 0; k < 2; ++k) dst[m][k] = *(const LAS bf16x8*)(lds + PG8_SA(b, h) + aoff + m * 2048 + k * 1024); } while (0)
; #define PG8_WAIT_V(n) asm volatile("s_waitcnt vmcnt(" #n ")" ::: "memory")
; #define PG8_WAIT_L(n) asm volatile("s_waitcnt lgkmcnt(" #n ")" ::: "memory")
; #define PG8_BAR __builtin_amdgcn_s_barrier()
; #define PG8_SCHED __builtin_amdgcn_sched_barrier(0)
; template <class Epi, class Sched, class Prob>
; __device__ __forceinline__ void gemm_phase(LAS unsigned char* lds, LAS unsigned char* lds_epi, const Prob g, const Sched& S, const Epi& E, int wid) {
;     ...
;             PG8_WAIT_V(8); PG8_WAIT_L(0); PG8_BAR; PG8_MMA(0, 0, At, B0); PG8_MMA(0, 1, At, B1); PG8_BAR; PG8_SCHED;
;             PG8_LDA(At, 0, 1); PG8_STAGE(PG8_SB(0, 0), b2, vB0, vB1); PG8_STAGE(PG8_SB(0, 1), b2 + hstepB, vB0, vB1); PG8_STAGE(PG8_SA(0, 0), a2, cA00, cA01);
;             PG8_WAIT_V(8); PG8_WAIT_L(0); PG8_BAR; PG8_MMA(1, 0, At, B0); PG8_MMA(1, 1, At, B1); PG8_BAR; PG8_SCHED;
	s_waitcnt lgkmcnt(0)
	v_mfma_f32_16x16x32_bf16 v[148:151], v[56:59], v[174:177], v[148:151]
	v_mfma_f32_16x16x32_bf16 v[116:119], v[72:75], v[174:177], v[116:119]
	v_mfma_f32_16x16x32_bf16 v[144:147], v[56:59], v[182:185], v[144:147]
	v_mfma_f32_16x16x32_bf16 v[112:115], v[72:75], v[182:185], v[112:115]
	v_mfma_f32_16x16x32_bf16 v[140:143], v[56:59], v[190:193], v[140:143]
	v_mfma_f32_16x16x32_bf16 v[108:111], v[72:75], v[190:193], v[108:111]
	v_mfma_f32_16x16x32_bf16 v[136:139], v[56:59], v[198:201], v[136:139]
	v_mfma_f32_16x16x32_bf16 v[96:99], v[72:75], v[198:201], v[96:99]
	v_mfma_f32_16x16x32_bf16 v[148:151], v[68:71], v[178:181], v[148:151]
	v_mfma_f32_16x16x32_bf16 v[116:119], v[88:91], v[178:181], v[116:119]
	v_mfma_f32_16x16x32_bf16 v[144:147], v[68:71], v[186:189], v[144:147]
	v_mfma_f32_16x16x32_bf16 v[112:115], v[88:91], v[186:189], v[112:115]
	v_mfma_f32_16x16x32_bf16 v[140:143], v[68:71], v[194:197], v[140:143]
	v_mfma_f32_16x16x32_bf16 v[108:111], v[88:91], v[194:197], v[108:111]
	v_mfma_f32_16x16x32_bf16 v[136:139], v[68:71], v[202:205], v[136:139]
	v_mfma_f32_16x16x32_bf16 v[96:99], v[88:91], v[202:205], v[96:99]
	v_mfma_f32_16x16x32_bf16 v[132:135], v[100:103], v[174:177], v[132:135]
	v_mfma_f32_16x16x32_bf16 v[92:95], v[166:169], v[174:177], v[92:95]
	v_mfma_f32_16x16x32_bf16 v[128:131], v[100:103], v[182:185], v[128:131]
	v_mfma_f32_16x16x32_bf16 v[84:87], v[166:169], v[182:185], v[84:87]
	v_mfma_f32_16x16x32_bf16 v[124:127], v[100:103], v[190:193], v[124:127]
	v_mfma_f32_16x16x32_bf16 v[80:83], v[166:169], v[190:193], v[80:83]
	v_mfma_f32_16x16x32_bf16 v[120:123], v[100:103], v[198:201], v[120:123]
	v_mfma_f32_16x16x32_bf16 v[76:79], v[166:169], v[198:201], v[76:79]
	v_mfma_f32_16x16x32_bf16 v[132:135], v[104:107], v[178:181], v[132:135]
	v_mfma_f32_16x16x32_bf16 v[92:95], v[170:173], v[178:181], v[92:95]
	v_mfma_f32_16x16x32_bf16 v[128:131], v[104:107], v[186:189], v[128:131]
	v_mfma_f32_16x16x32_bf16 v[84:87], v[170:173], v[186:189], v[84:87]
	v_mfma_f32_16x16x32_bf16 v[124:127], v[104:107], v[194:197], v[124:127]
	v_mfma_f32_16x16x32_bf16 v[80:83], v[170:173], v[194:197], v[80:83]
	v_mfma_f32_16x16x32_bf16 v[120:123], v[104:107], v[202:205], v[120:123]
	v_mfma_f32_16x16x32_bf16 v[76:79], v[170:173], v[202:205], v[76:79]
	s_barrier
	s_mov_b32 m0, s65
	v_lshl_add_u64 v[206:207], s[14:15], 0, v[152:153]
	ds_read_b128 v[174:177], v223 offset:16384
	ds_read_b128 v[178:181], v223 offset:17408
	ds_read_b128 v[182:185], v223 offset:18432
	ds_read_b128 v[186:189], v223 offset:19456
	ds_read_b128 v[190:193], v223 offset:20480
	ds_read_b128 v[194:197], v223 offset:21504
	ds_read_b128 v[198:201], v223 offset:22528
	ds_read_b128 v[202:205], v223 offset:23552
	global_load_lds_dwordx4 v[206:207], off
	v_lshl_add_u64 v[208:209], s[14:15], 0, v[154:155]
	s_mov_b32 m0, s36
	v_lshl_add_u64 v[210:211], s[22:23], 0, v[152:153]
	global_load_lds_dwordx4 v[208:209], off
	s_mov_b32 m0, s63
	v_lshl_add_u64 v[212:213], s[20:21], 0, v[160:161]
	global_load_lds_dwordx4 v[210:211], off
	v_lshl_add_u64 v[210:211], s[22:23], 0, v[154:155]
	s_mov_b32 m0, s37
	s_nop 0
	global_load_lds_dwordx4 v[210:211], off
	v_lshl_add_u64 v[210:211], s[20:21], 0, v[156:157]
	s_mov_b32 m0, s77
	s_nop 0
	global_load_lds_dwordx4 v[210:211], off
	s_mov_b32 m0, s78
	s_nop 0
	global_load_lds_dwordx4 v[212:213], off
	s_waitcnt vmcnt(8)
	s_waitcnt lgkmcnt(0)
	s_barrier
	s_waitcnt lgkmcnt(0)
	v_mfma_f32_16x16x32_bf16 v[64:67], v[56:59], v[174:177], v[64:67]
	v_mfma_f32_16x16x32_bf16 v[28:31], v[72:75], v[174:177], v[28:31]
	v_mfma_f32_16x16x32_bf16 v[60:63], v[56:59], v[182:185], v[60:63]
	v_mfma_f32_16x16x32_bf16 v[24:27], v[72:75], v[182:185], v[24:27]
	v_mfma_f32_16x16x32_bf16 v[52:55], v[56:59], v[190:193], v[52:55]
	v_mfma_f32_16x16x32_bf16 v[20:23], v[72:75], v[190:193], v[20:23]
	v_mfma_f32_16x16x32_bf16 v[48:51], v[56:59], v[198:201], v[48:51]
	v_mfma_f32_16x16x32_bf16 v[16:19], v[72:75], v[198:201], v[16:19]
	v_mfma_f32_16x16x32_bf16 v[64:67], v[68:71], v[178:181], v[64:67]
	v_mfma_f32_16x16x32_bf16 v[28:31], v[88:91], v[178:181], v[28:31]
	v_mfma_f32_16x16x32_bf16 v[60:63], v[68:71], v[186:189], v[60:63]
	v_mfma_f32_16x16x32_bf16 v[24:27], v[88:91], v[186:189], v[24:27]
	v_mfma_f32_16x16x32_bf16 v[52:55], v[68:71], v[194:197], v[52:55]
	v_mfma_f32_16x16x32_bf16 v[20:23], v[88:91], v[194:197], v[20:23]
	v_mfma_f32_16x16x32_bf16 v[48:51], v[68:71], v[202:205], v[48:51]
	v_mfma_f32_16x16x32_bf16 v[16:19], v[88:91], v[202:205], v[16:19]
	v_mfma_f32_16x16x32_bf16 v[44:47], v[100:103], v[174:177], v[44:47]
	v_mfma_f32_16x16x32_bf16 v[12:15], v[166:169], v[174:177], v[12:15]
	v_mfma_f32_16x16x32_bf16 v[40:43], v[100:103], v[182:185], v[40:43]
	v_mfma_f32_16x16x32_bf16 v[8:11], v[166:169], v[182:185], v[8:11]
	v_mfma_f32_16x16x32_bf16 v[36:39], v[100:103], v[190:193], v[36:39]
	v_mfma_f32_16x16x32_bf16 v[4:7], v[166:169], v[190:193], v[4:7]
	v_mfma_f32_16x16x32_bf16 v[32:35], v[100:103], v[198:201], v[32:35]
	v_mfma_f32_16x16x32_bf16 v[0:3], v[166:169], v[198:201], v[0:3]
	v_mfma_f32_16x16x32_bf16 v[44:47], v[104:107], v[178:181], v[44:47]
	v_mfma_f32_16x16x32_bf16 v[12:15], v[170:173], v[178:181], v[12:15]
	v_mfma_f32_16x16x32_bf16 v[40:43], v[104:107], v[186:189], v[40:43]
	v_mfma_f32_16x16x32_bf16 v[8:11], v[170:173], v[186:189], v[8:11]
	v_mfma_f32_16x16x32_bf16 v[36:39], v[104:107], v[194:197], v[36:39]
	v_mfma_f32_16x16x32_bf16 v[4:7], v[170:173], v[194:197], v[4:7]
	v_mfma_f32_16x16x32_bf16 v[32:35], v[104:107], v[202:205], v[32:35]
	v_mfma_f32_16x16x32_bf16 v[0:3], v[170:173], v[202:205], v[0:3]
	s_barrier
; #define PG8_STAGE(bufoff, gbase, o0, o1) do { \
;         __builtin_amdgcn_global_load_lds((const unsigned*)((const char*)(gbase) + (o0)), (LAS unsigned*)(lds + (bufoff) + ldsw), 16, 0, 0); \
;         __builtin_amdgcn_global_load_lds((const unsigned*)((const char*)(gbase) + (o1)), (LAS unsigned*)(lds + (bufoff) + ldsw + 8192), 16, 0, 0); } while (0)
; #define PG8_LDA(dst, b, h) do { _Pragma("unroll") for (int m = 0; m < 4; ++m) _Pragma("unroll") for (int k = 0; k < 2; ++k) dst[m][k] = *(const LAS bf16x8*)(lds + PG8_SA(b, h) + aoff + m * 2048 + k * 1024); } while (0)
; #define PG8_LDB(dst, b, h) do { _Pragma("unroll") for (int n = 0; n < 2; ++n) _Pragma("unroll") for (int k = 0; k < 2; ++k) dst[n][k] = *(const LAS bf16x8*)(lds + PG8_SB(b, h) + boff + n * 2048 + k * 1024); } while (0)
; #define PG8_WAIT_V(n) asm volatile("s_waitcnt vmcnt(" #n ")" ::: "memory")
; #define PG8_WAIT_L(n) asm volatile("s_waitcnt lgkmcnt(" #n ")" ::: "memory")
; #define PG8_BAR __builtin_amdgcn_s_barrier()
; #define PG8_SCHED __builtin_amdgcn_sched_barrier(0)
; template <class Epi, class Sched, class Prob>
; __device__ __forceinline__ void gemm_phase(LAS unsigned char* lds, LAS unsigned char* lds_epi, const Prob g, const Sched& S, const Epi& E, int wid) {
;     ...
;             PG8_LDB(B0, 1, 0); PG8_LDB(B1, 1, 1); PG8_SCHED; PG8_LDA(At, 1, 0); PG8_STAGE(PG8_SA(0, 1), a2, cA10, cA11);
;             PG8_WAIT_V(8); PG8_WAIT_L(0); PG8_BAR; PG8_MMA(0, 0, At, B0); PG8_MMA(0, 1, At, B1); PG8_BAR; PG8_SCHED;
;             PG8_LDA(At, 1, 1); PG8_STAGE(PG8_SB(1, 0), b3, vB0, vB1); PG8_STAGE(PG8_SB(1, 1), b3 + hstepB, vB0, vB1); PG8_STAGE(PG8_SA(1, 0), a3, cA00, cA01);
;             PG8_WAIT_V(8); PG8_WAIT_L(0); PG8_BAR; PG8_MMA(1, 0, At, B0); PG8_MMA(1, 1, At, B1); PG8_BAR; PG8_SCHED;
;         }
	v_add_u32_e32 v88, s35, v220
	v_add_u32_e32 v170, s34, v220
	ds_read_b128 v[56:59], v88
	ds_read_b128 v[68:71], v88 offset:1024
	ds_read_b128 v[72:75], v88 offset:2048
	ds_read_b128 v[88:91], v88 offset:3072
	ds_read_b128 v[100:103], v170
	ds_read_b128 v[104:107], v170 offset:1024
	ds_read_b128 v[166:169], v170 offset:2048
	ds_read_b128 v[170:173], v170 offset:3072
	s_mov_b32 m0, s79
	v_lshl_add_u64 v[214:215], s[20:21], 0, v[158:159]
	ds_read_b128 v[174:177], v223 offset:32768
	ds_read_b128 v[178:181], v223 offset:33792
	ds_read_b128 v[182:185], v223 offset:34816
	ds_read_b128 v[186:189], v223 offset:35840
	ds_read_b128 v[190:193], v223 offset:36864
	ds_read_b128 v[194:197], v223 offset:37888
	ds_read_b128 v[198:201], v223 offset:38912
	ds_read_b128 v[202:205], v223 offset:39936
	global_load_lds_dwordx4 v[214:215], off
	v_lshl_add_u64 v[214:215], s[20:21], 0, v[162:163]
	s_mov_b32 m0, s80
	s_nop 0
	global_load_lds_dwordx4 v[214:215], off
	s_waitcnt vmcnt(8)
	s_waitcnt lgkmcnt(0)
	s_barrier
	s_waitcnt lgkmcnt(0)
	v_mfma_f32_16x16x32_bf16 v[148:151], v[56:59], v[174:177], v[148:151]
	v_mfma_f32_16x16x32_bf16 v[116:119], v[72:75], v[174:177], v[116:119]
	v_mfma_f32_16x16x32_bf16 v[144:147], v[56:59], v[182:185], v[144:147]
	v_mfma_f32_16x16x32_bf16 v[112:115], v[72:75], v[182:185], v[112:115]
	v_mfma_f32_16x16x32_bf16 v[140:143], v[56:59], v[190:193], v[140:143]
	v_mfma_f32_16x16x32_bf16 v[108:111], v[72:75], v[190:193], v[108:111]
	v_mfma_f32_16x16x32_bf16 v[136:139], v[56:59], v[198:201], v[136:139]
	v_mfma_f32_16x16x32_bf16 v[96:99], v[72:75], v[198:201], v[96:99]
	v_mfma_f32_16x16x32_bf16 v[148:151], v[68:71], v[178:181], v[148:151]
	v_mfma_f32_16x16x32_bf16 v[116:119], v[88:91], v[178:181], v[116:119]
	v_mfma_f32_16x16x32_bf16 v[144:147], v[68:71], v[186:189], v[144:147]
	v_mfma_f32_16x16x32_bf16 v[112:115], v[88:91], v[186:189], v[112:115]
	v_mfma_f32_16x16x32_bf16 v[140:143], v[68:71], v[194:197], v[140:143]
	v_mfma_f32_16x16x32_bf16 v[108:111], v[88:91], v[194:197], v[108:111]
	v_mfma_f32_16x16x32_bf16 v[136:139], v[68:71], v[202:205], v[136:139]
	v_mfma_f32_16x16x32_bf16 v[96:99], v[88:91], v[202:205], v[96:99]
	v_mfma_f32_16x16x32_bf16 v[132:135], v[100:103], v[174:177], v[132:135]
	v_mfma_f32_16x16x32_bf16 v[92:95], v[166:169], v[174:177], v[92:95]
	v_mfma_f32_16x16x32_bf16 v[128:131], v[100:103], v[182:185], v[128:131]
	v_mfma_f32_16x16x32_bf16 v[84:87], v[166:169], v[182:185], v[84:87]
	v_mfma_f32_16x16x32_bf16 v[124:127], v[100:103], v[190:193], v[124:127]
	v_mfma_f32_16x16x32_bf16 v[80:83], v[166:169], v[190:193], v[80:83]
	v_mfma_f32_16x16x32_bf16 v[120:123], v[100:103], v[198:201], v[120:123]
	v_mfma_f32_16x16x32_bf16 v[76:79], v[166:169], v[198:201], v[76:79]
	v_mfma_f32_16x16x32_bf16 v[132:135], v[104:107], v[178:181], v[132:135]
	v_mfma_f32_16x16x32_bf16 v[92:95], v[170:173], v[178:181], v[92:95]
	v_mfma_f32_16x16x32_bf16 v[128:131], v[104:107], v[186:189], v[128:131]
	v_mfma_f32_16x16x32_bf16 v[84:87], v[170:173], v[186:189], v[84:87]
	v_mfma_f32_16x16x32_bf16 v[124:127], v[104:107], v[194:197], v[124:127]
	v_mfma_f32_16x16x32_bf16 v[80:83], v[170:173], v[194:197], v[80:83]
	v_mfma_f32_16x16x32_bf16 v[120:123], v[104:107], v[202:205], v[120:123]
	v_mfma_f32_16x16x32_bf16 v[76:79], v[170:173], v[202:205], v[76:79]
	s_barrier
	s_mov_b32 m0, s31
	v_lshl_add_u64 v[206:207], v[206:207], 0, s[54:55]
	ds_read_b128 v[174:177], v223 offset:49152
	ds_read_b128 v[178:181], v223 offset:50176
	ds_read_b128 v[182:185], v223 offset:51200
	ds_read_b128 v[186:189], v223 offset:52224
	ds_read_b128 v[190:193], v223 offset:53248
	ds_read_b128 v[194:197], v223 offset:54272
	ds_read_b128 v[198:201], v223 offset:55296
	ds_read_b128 v[202:205], v223 offset:56320
	global_load_lds_dwordx4 v[206:207], off
	v_lshl_add_u64 v[206:207], v[208:209], 0, s[54:55]
	s_mov_b32 m0, s29
	s_nop 0
	global_load_lds_dwordx4 v[206:207], off
	v_lshl_add_u64 v[206:207], s[12:13], 0, v[152:153]
	s_mov_b32 m0, s30
	s_nop 0
	global_load_lds_dwordx4 v[206:207], off
	v_lshl_add_u64 v[206:207], s[12:13], 0, v[154:155]
	s_mov_b32 m0, s28
	s_nop 0
	global_load_lds_dwordx4 v[206:207], off
	v_lshl_add_u64 v[206:207], v[210:211], 0, s[54:55]
	s_mov_b32 m0, s83
	s_nop 0
	global_load_lds_dwordx4 v[206:207], off
	v_lshl_add_u64 v[206:207], v[212:213], 0, s[54:55]
	s_mov_b32 m0, s84
	s_nop 0
	global_load_lds_dwordx4 v[206:207], off
	s_waitcnt vmcnt(8)
	s_waitcnt lgkmcnt(0)
	s_barrier
	s_waitcnt lgkmcnt(0)
	v_mfma_f32_16x16x32_bf16 v[64:67], v[56:59], v[174:177], v[64:67]
	v_mfma_f32_16x16x32_bf16 v[28:31], v[72:75], v[174:177], v[28:31]
	v_mfma_f32_16x16x32_bf16 v[60:63], v[56:59], v[182:185], v[60:63]
	v_mfma_f32_16x16x32_bf16 v[24:27], v[72:75], v[182:185], v[24:27]
	v_mfma_f32_16x16x32_bf16 v[52:55], v[56:59], v[190:193], v[52:55]
	v_mfma_f32_16x16x32_bf16 v[20:23], v[72:75], v[190:193], v[20:23]
	v_mfma_f32_16x16x32_bf16 v[48:51], v[56:59], v[198:201], v[48:51]
	v_mfma_f32_16x16x32_bf16 v[16:19], v[72:75], v[198:201], v[16:19]
	v_mfma_f32_16x16x32_bf16 v[64:67], v[68:71], v[178:181], v[64:67]
	v_mfma_f32_16x16x32_bf16 v[28:31], v[88:91], v[178:181], v[28:31]
	v_mfma_f32_16x16x32_bf16 v[60:63], v[68:71], v[186:189], v[60:63]
	v_mfma_f32_16x16x32_bf16 v[24:27], v[88:91], v[186:189], v[24:27]
	v_mfma_f32_16x16x32_bf16 v[52:55], v[68:71], v[194:197], v[52:55]
	v_mfma_f32_16x16x32_bf16 v[20:23], v[88:91], v[194:197], v[20:23]
	v_mfma_f32_16x16x32_bf16 v[48:51], v[68:71], v[202:205], v[48:51]
	v_mfma_f32_16x16x32_bf16 v[16:19], v[88:91], v[202:205], v[16:19]
	v_mfma_f32_16x16x32_bf16 v[44:47], v[100:103], v[174:177], v[44:47]
	v_mfma_f32_16x16x32_bf16 v[12:15], v[166:169], v[174:177], v[12:15]
	v_mfma_f32_16x16x32_bf16 v[40:43], v[100:103], v[182:185], v[40:43]
	v_mfma_f32_16x16x32_bf16 v[8:11], v[166:169], v[182:185], v[8:11]
	v_mfma_f32_16x16x32_bf16 v[36:39], v[100:103], v[190:193], v[36:39]
	v_mfma_f32_16x16x32_bf16 v[4:7], v[166:169], v[190:193], v[4:7]
	v_mfma_f32_16x16x32_bf16 v[32:35], v[100:103], v[198:201], v[32:35]
	v_mfma_f32_16x16x32_bf16 v[0:3], v[166:169], v[198:201], v[0:3]
	v_mfma_f32_16x16x32_bf16 v[44:47], v[104:107], v[178:181], v[44:47]
	v_mfma_f32_16x16x32_bf16 v[12:15], v[170:173], v[178:181], v[12:15]
	v_mfma_f32_16x16x32_bf16 v[40:43], v[104:107], v[186:189], v[40:43]
	v_mfma_f32_16x16x32_bf16 v[8:11], v[170:173], v[186:189], v[8:11]
	v_mfma_f32_16x16x32_bf16 v[36:39], v[104:107], v[194:197], v[36:39]
	v_mfma_f32_16x16x32_bf16 v[4:7], v[170:173], v[194:197], v[4:7]
	v_mfma_f32_16x16x32_bf16 v[32:35], v[104:107], v[202:205], v[32:35]
	v_mfma_f32_16x16x32_bf16 v[0:3], v[170:173], v[202:205], v[0:3]
	s_barrier
	s_mov_b64 s[20:21], 0
	s_mov_b64 s[12:13], -1
	s_mov_b64 s[14:15], 0x100
	s_cbranch_vccz .LBB0_1595
	v_readlane_b32 s8, v254, 27
	v_readlane_b32 s9, v254, 28
	s_and_b64 vcc, exec, s[8:9]
	s_cbranch_vccz .LBB0_1598
	s_barrier

; #define PG8_STAGE(bufoff, gbase, o0, o1) do { \
;         __builtin_amdgcn_global_load_lds((const unsigned*)((const char*)(gbase) + (o0)), (LAS unsigned*)(lds + (bufoff) + ldsw), 16, 0, 0); \
;         __builtin_amdgcn_global_load_lds((const unsigned*)((const char*)(gbase) + (o1)), (LAS unsigned*)(lds + (bufoff) + ldsw + 8192), 16, 0, 0); } while (0)
; #define PG8_LDA(dst, b, h) do { _Pragma("unroll") for (int m = 0; m < 4; ++m) _Pragma("unroll") for (int k = 0; k < 2; ++k) dst[m][k] = *(const LAS bf16x8*)(lds + PG8_SA(b, h) + aoff + m * 2048 + k * 1024); } while (0)
; #define PG8_LDB(dst, b, h) do { _Pragma("unroll") for (int n = 0; n < 2; ++n) _Pragma("unroll") for (int k = 0; k < 2; ++k) dst[n][k] = *(const LAS bf16x8*)(lds + PG8_SB(b, h) + boff + n * 2048 + k * 1024); } while (0)
; #define PG8_WAIT_V(n) asm volatile("s_waitcnt vmcnt(" #n ")" ::: "memory")
; #define PG8_WAIT_L(n) asm volatile("s_waitcnt lgkmcnt(" #n ")" ::: "memory")
; #define PG8_BAR __builtin_amdgcn_s_barrier()
; #define PG8_SCHED __builtin_amdgcn_sched_barrier(0)
; template <class Epi, class Sched, class Prob>
; __device__ __forceinline__ void gemm_phase(LAS unsigned char* lds, LAS unsigned char* lds_epi, const Prob g, const Sched& S, const Epi& E, int wid) {
;     ...
;             PG8_LDB(B0, 0, 0); PG8_LDB(B1, 0, 1); PG8_SCHED; PG8_LDA(At, 0, 0); PG8_STAGE(PG8_SA(1, 1), a1, cA10, cA11);
;             PG8_WAIT_V(8); PG8_WAIT_L(0); PG8_BAR; PG8_MMA(0, 0, At, B0); PG8_MMA(0, 1, At, B1); PG8_BAR; PG8_SCHED;
;             PG8_LDA(At, 0, 1); PG8_STAGE(PG8_SB(0, 0), b2, vB0, vB1); PG8_STAGE(PG8_SB(0, 1), b2 + hstepB, vB0, vB1); PG8_STAGE(PG8_SA(0, 0), a2, cA00, cA01);
;             PG8_WAIT_V(8); PG8_WAIT_L(0); PG8_BAR; PG8_MMA(1, 0, At, B0); PG8_MMA(1, 1, At, B1); PG8_BAR; PG8_SCHED;
.LBB0_1749:
	v_add_u32_e32 v160, s51, v145
	v_add_u32_e32 v176, s52, v145
	ds_read_b128 v[148:151], v160
	ds_read_b128 v[152:155], v160 offset:1024
	ds_read_b128 v[156:159], v160 offset:2048
	ds_read_b128 v[160:163], v160 offset:3072
	ds_read_b128 v[164:167], v176
	ds_read_b128 v[168:171], v176 offset:1024
	ds_read_b128 v[172:175], v176 offset:2048
	ds_read_b128 v[176:179], v176 offset:3072
	s_add_u32 s28, s26, 0x80
	s_addc_u32 s29, s27, 0
	s_cmp_eq_u32 s57, 28
	s_cselect_b32 s35, s17, s29
	s_cselect_b32 s34, s19, s28
	s_cselect_b32 s29, s15, s56
	s_cselect_b32 s28, s54, s55
	v_lshl_add_u64 v[212:213], s[26:27], 0, v[140:141]
	s_add_i32 m0, s21, 0xc000
	ds_read_b128 v[180:183], v147
	ds_read_b128 v[184:187], v147 offset:1024
	ds_read_b128 v[188:191], v147 offset:2048
	ds_read_b128 v[192:195], v147 offset:3072
	ds_read_b128 v[196:199], v147 offset:4096
	ds_read_b128 v[200:203], v147 offset:5120
	ds_read_b128 v[204:207], v147 offset:6144
	ds_read_b128 v[208:211], v147 offset:7168
	global_load_lds_dwordx4 v[212:213], off
	v_lshl_add_u64 v[212:213], s[26:27], 0, v[138:139]
	s_add_i32 m0, s21, 0xe000
	s_nop 0
	global_load_lds_dwordx4 v[212:213], off
	s_waitcnt vmcnt(8)
	s_waitcnt lgkmcnt(0)
	s_barrier
	s_waitcnt lgkmcnt(0)
	v_mfma_f32_16x16x32_bf16 v[12:15], v[148:151], v[180:183], v[12:15]
	v_mfma_f32_16x16x32_bf16 v[28:31], v[156:159], v[180:183], v[28:31]
	v_mfma_f32_16x16x32_bf16 v[8:11], v[148:151], v[188:191], v[8:11]
	v_mfma_f32_16x16x32_bf16 v[24:27], v[156:159], v[188:191], v[24:27]
	v_mfma_f32_16x16x32_bf16 v[4:7], v[148:151], v[196:199], v[4:7]
	v_mfma_f32_16x16x32_bf16 v[20:23], v[156:159], v[196:199], v[20:23]
	v_mfma_f32_16x16x32_bf16 v[0:3], v[148:151], v[204:207], v[0:3]
	v_mfma_f32_16x16x32_bf16 v[16:19], v[156:159], v[204:207], v[16:19]
	v_mfma_f32_16x16x32_bf16 v[12:15], v[152:155], v[184:187], v[12:15]
	v_mfma_f32_16x16x32_bf16 v[28:31], v[160:163], v[184:187], v[28:31]
	v_mfma_f32_16x16x32_bf16 v[8:11], v[152:155], v[192:195], v[8:11]
	v_mfma_f32_16x16x32_bf16 v[24:27], v[160:163], v[192:195], v[24:27]
	v_mfma_f32_16x16x32_bf16 v[4:7], v[152:155], v[200:203], v[4:7]
	v_mfma_f32_16x16x32_bf16 v[20:23], v[160:163], v[200:203], v[20:23]
	v_mfma_f32_16x16x32_bf16 v[0:3], v[152:155], v[208:211], v[0:3]
	v_mfma_f32_16x16x32_bf16 v[16:19], v[160:163], v[208:211], v[16:19]
	v_mfma_f32_16x16x32_bf16 v[44:47], v[164:167], v[180:183], v[44:47]
	v_mfma_f32_16x16x32_bf16 v[68:71], v[172:175], v[180:183], v[68:71]
	v_mfma_f32_16x16x32_bf16 v[40:43], v[164:167], v[188:191], v[40:43]
	v_mfma_f32_16x16x32_bf16 v[64:67], v[172:175], v[188:191], v[64:67]
	v_mfma_f32_16x16x32_bf16 v[36:39], v[164:167], v[196:199], v[36:39]
	v_mfma_f32_16x16x32_bf16 v[60:63], v[172:175], v[196:199], v[60:63]
	v_mfma_f32_16x16x32_bf16 v[32:35], v[164:167], v[204:207], v[32:35]
	v_mfma_f32_16x16x32_bf16 v[56:59], v[172:175], v[204:207], v[56:59]
	v_mfma_f32_16x16x32_bf16 v[44:47], v[168:171], v[184:187], v[44:47]
	v_mfma_f32_16x16x32_bf16 v[68:71], v[176:179], v[184:187], v[68:71]
	v_mfma_f32_16x16x32_bf16 v[40:43], v[168:171], v[192:195], v[40:43]
	v_mfma_f32_16x16x32_bf16 v[64:67], v[176:179], v[192:195], v[64:67]
	v_mfma_f32_16x16x32_bf16 v[36:39], v[168:171], v[200:203], v[36:39]
	v_mfma_f32_16x16x32_bf16 v[60:63], v[176:179], v[200:203], v[60:63]
	v_mfma_f32_16x16x32_bf16 v[32:35], v[168:171], v[208:211], v[32:35]
	v_mfma_f32_16x16x32_bf16 v[56:59], v[176:179], v[208:211], v[56:59]
	s_barrier
	s_add_i32 s58, s51, s97
	v_lshl_add_u64 v[212:213], s[28:29], 0, v[130:131]
	s_mov_b32 m0, s58
	ds_read_b128 v[180:183], v147 offset:16384
	ds_read_b128 v[184:187], v147 offset:17408
	ds_read_b128 v[188:191], v147 offset:18432
	ds_read_b128 v[192:195], v147 offset:19456
	ds_read_b128 v[196:199], v147 offset:20480
	ds_read_b128 v[200:203], v147 offset:21504
	ds_read_b128 v[204:207], v147 offset:22528
	ds_read_b128 v[208:211], v147 offset:23552
	global_load_lds_dwordx4 v[212:213], off
	s_add_i32 m0, s58, 0x2000
	s_add_u32 s58, s28, 0x80000
	v_lshl_add_u64 v[214:215], s[28:29], 0, v[128:129]
	s_addc_u32 s59, s29, 0
	s_add_i32 s60, s52, s97
	global_load_lds_dwordx4 v[214:215], off
	v_lshl_add_u64 v[216:217], s[58:59], 0, v[130:131]
	s_mov_b32 m0, s60
	v_lshl_add_u64 v[218:219], s[34:35], 0, v[128:129]
	global_load_lds_dwordx4 v[216:217], off
	v_lshl_add_u64 v[216:217], s[58:59], 0, v[128:129]
	s_add_i32 m0, s60, 0x2000
	s_nop 0
	global_load_lds_dwordx4 v[216:217], off
	v_lshl_add_u64 v[216:217], s[34:35], 0, v[130:131]
	s_mov_b32 m0, s21
	s_nop 0
	global_load_lds_dwordx4 v[216:217], off
	s_mov_b32 m0, s46
	s_nop 0
	global_load_lds_dwordx4 v[218:219], off
	s_waitcnt vmcnt(8)
	s_waitcnt lgkmcnt(0)
	s_barrier
; #define PG8_STAGE(bufoff, gbase, o0, o1) do { \
;         __builtin_amdgcn_global_load_lds((const unsigned*)((const char*)(gbase) + (o0)), (LAS unsigned*)(lds + (bufoff) + ldsw), 16, 0, 0); \
;         __builtin_amdgcn_global_load_lds((const unsigned*)((const char*)(gbase) + (o1)), (LAS unsigned*)(lds + (bufoff) + ldsw + 8192), 16, 0, 0); } while (0)
; #define PG8_LDA(dst, b, h) do { _Pragma("unroll") for (int m = 0; m < 4; ++m) _Pragma("unroll") for (int k = 0; k < 2; ++k) dst[m][k] = *(const LAS bf16x8*)(lds + PG8_SA(b, h) + aoff + m * 2048 + k * 1024); } while (0)
; #define PG8_LDB(dst, b, h) do { _Pragma("unroll") for (int n = 0; n < 2; ++n) _Pragma("unroll") for (int k = 0; k < 2; ++k) dst[n][k] = *(const LAS bf16x8*)(lds + PG8_SB(b, h) + boff + n * 2048 + k * 1024); } while (0)
; #define PG8_WAIT_V(n) asm volatile("s_waitcnt vmcnt(" #n ")" ::: "memory")
; #define PG8_WAIT_L(n) asm volatile("s_waitcnt lgkmcnt(" #n ")" ::: "memory")
; #define PG8_BAR __builtin_amdgcn_s_barrier()
; #define PG8_SCHED __builtin_amdgcn_sched_barrier(0)
; template <class Epi, class Sched, class Prob>
; __device__ __forceinline__ void gemm_phase(LAS unsigned char* lds, LAS unsigned char* lds_epi, const Prob g, const Sched& S, const Epi& E, int wid) {
;     ...
;             PG8_WAIT_V(8); PG8_WAIT_L(0); PG8_BAR; PG8_MMA(1, 0, At, B0); PG8_MMA(1, 1, At, B1); PG8_BAR; PG8_SCHED;
;             PG8_LDB(B0, 1, 0); PG8_LDB(B1, 1, 1); PG8_SCHED; PG8_LDA(At, 1, 0); PG8_STAGE(PG8_SA(0, 1), a2, cA10, cA11);
;             PG8_WAIT_V(8); PG8_WAIT_L(0); PG8_BAR; PG8_MMA(0, 0, At, B0); PG8_MMA(0, 1, At, B1); PG8_BAR; PG8_SCHED;
	s_waitcnt lgkmcnt(0)
	v_mfma_f32_16x16x32_bf16 v[52:55], v[148:151], v[180:183], v[52:55]
	v_mfma_f32_16x16x32_bf16 v[76:79], v[156:159], v[180:183], v[76:79]
	v_mfma_f32_16x16x32_bf16 v[48:51], v[148:151], v[188:191], v[48:51]
	v_mfma_f32_16x16x32_bf16 v[72:75], v[156:159], v[188:191], v[72:75]
	v_mfma_f32_16x16x32_bf16 v[100:103], v[148:151], v[196:199], v[100:103]
	v_mfma_f32_16x16x32_bf16 v[108:111], v[156:159], v[196:199], v[108:111]
	v_mfma_f32_16x16x32_bf16 v[96:99], v[148:151], v[204:207], v[96:99]
	v_mfma_f32_16x16x32_bf16 v[104:107], v[156:159], v[204:207], v[104:107]
	v_mfma_f32_16x16x32_bf16 v[52:55], v[152:155], v[184:187], v[52:55]
	v_mfma_f32_16x16x32_bf16 v[76:79], v[160:163], v[184:187], v[76:79]
	v_mfma_f32_16x16x32_bf16 v[48:51], v[152:155], v[192:195], v[48:51]
	v_mfma_f32_16x16x32_bf16 v[72:75], v[160:163], v[192:195], v[72:75]
	v_mfma_f32_16x16x32_bf16 v[100:103], v[152:155], v[200:203], v[100:103]
	v_mfma_f32_16x16x32_bf16 v[108:111], v[160:163], v[200:203], v[108:111]
	v_mfma_f32_16x16x32_bf16 v[96:99], v[152:155], v[208:211], v[96:99]
	v_mfma_f32_16x16x32_bf16 v[104:107], v[160:163], v[208:211], v[104:107]
	v_mfma_f32_16x16x32_bf16 v[84:87], v[164:167], v[180:183], v[84:87]
	v_mfma_f32_16x16x32_bf16 v[92:95], v[172:175], v[180:183], v[92:95]
	v_mfma_f32_16x16x32_bf16 v[80:83], v[164:167], v[188:191], v[80:83]
	v_mfma_f32_16x16x32_bf16 v[88:91], v[172:175], v[188:191], v[88:91]
	v_mfma_f32_16x16x32_bf16 v[116:119], v[164:167], v[196:199], v[116:119]
	v_mfma_f32_16x16x32_bf16 v[124:127], v[172:175], v[196:199], v[124:127]
	v_mfma_f32_16x16x32_bf16 v[112:115], v[164:167], v[204:207], v[112:115]
	v_mfma_f32_16x16x32_bf16 v[120:123], v[172:175], v[204:207], v[120:123]
	v_mfma_f32_16x16x32_bf16 v[84:87], v[168:171], v[184:187], v[84:87]
	v_mfma_f32_16x16x32_bf16 v[92:95], v[176:179], v[184:187], v[92:95]
	v_mfma_f32_16x16x32_bf16 v[80:83], v[168:171], v[192:195], v[80:83]
	v_mfma_f32_16x16x32_bf16 v[88:91], v[176:179], v[192:195], v[88:91]
	v_mfma_f32_16x16x32_bf16 v[116:119], v[168:171], v[200:203], v[116:119]
	v_mfma_f32_16x16x32_bf16 v[124:127], v[176:179], v[200:203], v[124:127]
	v_mfma_f32_16x16x32_bf16 v[112:115], v[168:171], v[208:211], v[112:115]
	v_mfma_f32_16x16x32_bf16 v[120:123], v[176:179], v[208:211], v[120:123]
	s_barrier
	s_add_i32 s58, 0, 0x18000
	s_add_i32 s59, 0, 0x1c000
	v_add_u32_e32 v160, s58, v145
	v_add_u32_e32 v176, s59, v145
	ds_read_b128 v[148:151], v160
	ds_read_b128 v[152:155], v160 offset:1024
	ds_read_b128 v[156:159], v160 offset:2048
	ds_read_b128 v[160:163], v160 offset:3072
	ds_read_b128 v[164:167], v176
	ds_read_b128 v[168:171], v176 offset:1024
	ds_read_b128 v[172:175], v176 offset:2048
	ds_read_b128 v[176:179], v176 offset:3072
	s_mov_b32 m0, s47
	v_lshl_add_u64 v[220:221], s[34:35], 0, v[132:133]
	ds_read_b128 v[180:183], v147 offset:32768
	ds_read_b128 v[184:187], v147 offset:33792
	ds_read_b128 v[188:191], v147 offset:34816
	ds_read_b128 v[192:195], v147 offset:35840
	ds_read_b128 v[196:199], v147 offset:36864
	ds_read_b128 v[200:203], v147 offset:37888
	ds_read_b128 v[204:207], v147 offset:38912
	ds_read_b128 v[208:211], v147 offset:39936
	global_load_lds_dwordx4 v[220:221], off
	v_lshl_add_u64 v[220:221], s[34:35], 0, v[134:135]
	s_mov_b32 m0, s48
	s_nop 0
	global_load_lds_dwordx4 v[220:221], off
	s_waitcnt vmcnt(8)
	s_waitcnt lgkmcnt(0)
	s_barrier
	s_waitcnt lgkmcnt(0)
	v_mfma_f32_16x16x32_bf16 v[12:15], v[148:151], v[180:183], v[12:15]
	v_mfma_f32_16x16x32_bf16 v[28:31], v[156:159], v[180:183], v[28:31]
	v_mfma_f32_16x16x32_bf16 v[8:11], v[148:151], v[188:191], v[8:11]
	v_mfma_f32_16x16x32_bf16 v[24:27], v[156:159], v[188:191], v[24:27]
	v_mfma_f32_16x16x32_bf16 v[4:7], v[148:151], v[196:199], v[4:7]
	v_mfma_f32_16x16x32_bf16 v[20:23], v[156:159], v[196:199], v[20:23]
	v_mfma_f32_16x16x32_bf16 v[0:3], v[148:151], v[204:207], v[0:3]
	v_mfma_f32_16x16x32_bf16 v[16:19], v[156:159], v[204:207], v[16:19]
	v_mfma_f32_16x16x32_bf16 v[12:15], v[152:155], v[184:187], v[12:15]
	v_mfma_f32_16x16x32_bf16 v[28:31], v[160:163], v[184:187], v[28:31]
	v_mfma_f32_16x16x32_bf16 v[8:11], v[152:155], v[192:195], v[8:11]
	v_mfma_f32_16x16x32_bf16 v[24:27], v[160:163], v[192:195], v[24:27]
	v_mfma_f32_16x16x32_bf16 v[4:7], v[152:155], v[200:203], v[4:7]
	v_mfma_f32_16x16x32_bf16 v[20:23], v[160:163], v[200:203], v[20:23]
	v_mfma_f32_16x16x32_bf16 v[0:3], v[152:155], v[208:211], v[0:3]
	v_mfma_f32_16x16x32_bf16 v[16:19], v[160:163], v[208:211], v[16:19]
	v_mfma_f32_16x16x32_bf16 v[44:47], v[164:167], v[180:183], v[44:47]
	v_mfma_f32_16x16x32_bf16 v[68:71], v[172:175], v[180:183], v[68:71]
	v_mfma_f32_16x16x32_bf16 v[40:43], v[164:167], v[188:191], v[40:43]
	v_mfma_f32_16x16x32_bf16 v[64:67], v[172:175], v[188:191], v[64:67]
	v_mfma_f32_16x16x32_bf16 v[36:39], v[164:167], v[196:199], v[36:39]
	v_mfma_f32_16x16x32_bf16 v[60:63], v[172:175], v[196:199], v[60:63]
	v_mfma_f32_16x16x32_bf16 v[32:35], v[164:167], v[204:207], v[32:35]
	v_mfma_f32_16x16x32_bf16 v[56:59], v[172:175], v[204:207], v[56:59]
	v_mfma_f32_16x16x32_bf16 v[44:47], v[168:171], v[184:187], v[44:47]
	v_mfma_f32_16x16x32_bf16 v[68:71], v[176:179], v[184:187], v[68:71]
	v_mfma_f32_16x16x32_bf16 v[40:43], v[168:171], v[192:195], v[40:43]
	v_mfma_f32_16x16x32_bf16 v[64:67], v[176:179], v[192:195], v[64:67]
	v_mfma_f32_16x16x32_bf16 v[36:39], v[168:171], v[200:203], v[36:39]
	v_mfma_f32_16x16x32_bf16 v[60:63], v[176:179], v[200:203], v[60:63]
	v_mfma_f32_16x16x32_bf16 v[32:35], v[168:171], v[208:211], v[32:35]
	v_mfma_f32_16x16x32_bf16 v[56:59], v[176:179], v[208:211], v[56:59]
	s_barrier
; #define PG8_STAGE(bufoff, gbase, o0, o1) do { \
;         __builtin_amdgcn_global_load_lds((const unsigned*)((const char*)(gbase) + (o0)), (LAS unsigned*)(lds + (bufoff) + ldsw), 16, 0, 0); \
;         __builtin_amdgcn_global_load_lds((const unsigned*)((const char*)(gbase) + (o1)), (LAS unsigned*)(lds + (bufoff) + ldsw + 8192), 16, 0, 0); } while (0)
; #define PG8_LDA(dst, b, h) do { _Pragma("unroll") for (int m = 0; m < 4; ++m) _Pragma("unroll") for (int k = 0; k < 2; ++k) dst[m][k] = *(const LAS bf16x8*)(lds + PG8_SA(b, h) + aoff + m * 2048 + k * 1024); } while (0)
; #define PG8_WAIT_V(n) asm volatile("s_waitcnt vmcnt(" #n ")" ::: "memory")
; #define PG8_WAIT_L(n) asm volatile("s_waitcnt lgkmcnt(" #n ")" ::: "memory")
; #define PG8_BAR __builtin_amdgcn_s_barrier()
; #define PG8_SCHED __builtin_amdgcn_sched_barrier(0)
; template <class Epi, class Sched, class Prob>
; __device__ __forceinline__ void gemm_phase(LAS unsigned char* lds, LAS unsigned char* lds_epi, const Prob g, const Sched& S, const Epi& E, int wid) {
;     ...
;             PG8_LDA(At, 1, 1); PG8_STAGE(PG8_SB(1, 0), b3, vB0, vB1); PG8_STAGE(PG8_SB(1, 1), b3 + hstepB, vB0, vB1); PG8_STAGE(PG8_SA(1, 0), a3, cA00, cA01);
;             PG8_WAIT_V(8); PG8_WAIT_L(0); PG8_BAR; PG8_MMA(1, 0, At, B0); PG8_MMA(1, 1, At, B1); PG8_BAR; PG8_SCHED;
;         }
	s_add_i32 s34, s58, s97
	v_lshl_add_u64 v[212:213], v[212:213], 0, s[8:9]
	s_mov_b32 m0, s34
	ds_read_b128 v[180:183], v147 offset:49152
	ds_read_b128 v[184:187], v147 offset:50176
	ds_read_b128 v[188:191], v147 offset:51200
	ds_read_b128 v[192:195], v147 offset:52224
	ds_read_b128 v[196:199], v147 offset:53248
	ds_read_b128 v[200:203], v147 offset:54272
	ds_read_b128 v[204:207], v147 offset:55296
	ds_read_b128 v[208:211], v147 offset:56320
	global_load_lds_dwordx4 v[212:213], off
	s_add_i32 m0, s34, 0x2000
	s_add_u32 s28, s28, 0x80080
	v_lshl_add_u64 v[212:213], v[214:215], 0, s[8:9]
	s_addc_u32 s29, s29, 0
	s_add_i32 s34, s59, s97
	global_load_lds_dwordx4 v[212:213], off
	v_lshl_add_u64 v[212:213], s[28:29], 0, v[130:131]
	s_mov_b32 m0, s34
	s_nop 0
	global_load_lds_dwordx4 v[212:213], off
	v_lshl_add_u64 v[212:213], s[28:29], 0, v[128:129]
	s_add_i32 m0, s34, 0x2000
	s_nop 0
	global_load_lds_dwordx4 v[212:213], off
	v_lshl_add_u64 v[212:213], v[216:217], 0, s[8:9]
	s_mov_b32 m0, s49
	s_nop 0
	global_load_lds_dwordx4 v[212:213], off
	v_lshl_add_u64 v[212:213], v[218:219], 0, s[8:9]
	s_mov_b32 m0, s50
	s_nop 0
	global_load_lds_dwordx4 v[212:213], off
	s_waitcnt vmcnt(8)
	s_waitcnt lgkmcnt(0)
	s_barrier
	s_waitcnt lgkmcnt(0)
	v_mfma_f32_16x16x32_bf16 v[52:55], v[148:151], v[180:183], v[52:55]
	v_mfma_f32_16x16x32_bf16 v[76:79], v[156:159], v[180:183], v[76:79]
	v_mfma_f32_16x16x32_bf16 v[48:51], v[148:151], v[188:191], v[48:51]
	v_mfma_f32_16x16x32_bf16 v[72:75], v[156:159], v[188:191], v[72:75]
	v_mfma_f32_16x16x32_bf16 v[100:103], v[148:151], v[196:199], v[100:103]
	v_mfma_f32_16x16x32_bf16 v[108:111], v[156:159], v[196:199], v[108:111]
	v_mfma_f32_16x16x32_bf16 v[96:99], v[148:151], v[204:207], v[96:99]
	v_mfma_f32_16x16x32_bf16 v[104:107], v[156:159], v[204:207], v[104:107]
	v_mfma_f32_16x16x32_bf16 v[52:55], v[152:155], v[184:187], v[52:55]
	v_mfma_f32_16x16x32_bf16 v[76:79], v[160:163], v[184:187], v[76:79]
	v_mfma_f32_16x16x32_bf16 v[48:51], v[152:155], v[192:195], v[48:51]
	v_mfma_f32_16x16x32_bf16 v[72:75], v[160:163], v[192:195], v[72:75]
	v_mfma_f32_16x16x32_bf16 v[100:103], v[152:155], v[200:203], v[100:103]
	v_mfma_f32_16x16x32_bf16 v[108:111], v[160:163], v[200:203], v[108:111]
	v_mfma_f32_16x16x32_bf16 v[96:99], v[152:155], v[208:211], v[96:99]
	v_mfma_f32_16x16x32_bf16 v[104:107], v[160:163], v[208:211], v[104:107]
	v_mfma_f32_16x16x32_bf16 v[84:87], v[164:167], v[180:183], v[84:87]
	v_mfma_f32_16x16x32_bf16 v[92:95], v[172:175], v[180:183], v[92:95]
	v_mfma_f32_16x16x32_bf16 v[80:83], v[164:167], v[188:191], v[80:83]
	v_mfma_f32_16x16x32_bf16 v[88:91], v[172:175], v[188:191], v[88:91]
	v_mfma_f32_16x16x32_bf16 v[116:119], v[164:167], v[196:199], v[116:119]
	v_mfma_f32_16x16x32_bf16 v[124:127], v[172:175], v[196:199], v[124:127]
	v_mfma_f32_16x16x32_bf16 v[112:115], v[164:167], v[204:207], v[112:115]
	v_mfma_f32_16x16x32_bf16 v[120:123], v[172:175], v[204:207], v[120:123]
	v_mfma_f32_16x16x32_bf16 v[84:87], v[168:171], v[184:187], v[84:87]
	v_mfma_f32_16x16x32_bf16 v[92:95], v[176:179], v[184:187], v[92:95]
	v_mfma_f32_16x16x32_bf16 v[80:83], v[168:171], v[192:195], v[80:83]
	v_mfma_f32_16x16x32_bf16 v[88:91], v[176:179], v[192:195], v[88:91]
	v_mfma_f32_16x16x32_bf16 v[116:119], v[168:171], v[200:203], v[116:119]
	v_mfma_f32_16x16x32_bf16 v[124:127], v[176:179], v[200:203], v[124:127]
	v_mfma_f32_16x16x32_bf16 v[112:115], v[168:171], v[208:211], v[112:115]
	v_mfma_f32_16x16x32_bf16 v[120:123], v[176:179], v[208:211], v[120:123]
	s_barrier
	s_add_i32 s57, s57, 2
	s_add_u32 s26, s26, 0x100
	s_addc_u32 s27, s27, 0
	s_add_u32 s55, s55, 0x100
	s_addc_u32 s56, s56, 0
	s_cmp_gt_u32 s57, 29
	s_cbranch_scc0 .LBB0_1749
	v_readlane_b32 s26, v254, 27
	v_readlane_b32 s27, v254, 28
	s_and_b64 vcc, exec, s[26:27]
	s_cbranch_vccz .LBB0_1752
	s_barrier

; #define PG8_STAGE(bufoff, gbase, o0, o1) do { \
;         __builtin_amdgcn_global_load_lds((const unsigned*)((const char*)(gbase) + (o0)), (LAS unsigned*)(lds + (bufoff) + ldsw), 16, 0, 0); \
;         __builtin_amdgcn_global_load_lds((const unsigned*)((const char*)(gbase) + (o1)), (LAS unsigned*)(lds + (bufoff) + ldsw + 8192), 16, 0, 0); } while (0)
; #define PG8_LDA(dst, b, h) do { _Pragma("unroll") for (int m = 0; m < 4; ++m) _Pragma("unroll") for (int k = 0; k < 2; ++k) dst[m][k] = *(const LAS bf16x8*)(lds + PG8_SA(b, h) + aoff + m * 2048 + k * 1024); } while (0)
; #define PG8_LDB(dst, b, h) do { _Pragma("unroll") for (int n = 0; n < 2; ++n) _Pragma("unroll") for (int k = 0; k < 2; ++k) dst[n][k] = *(const LAS bf16x8*)(lds + PG8_SB(b, h) + boff + n * 2048 + k * 1024); } while (0)
; #define PG8_WAIT_V(n) asm volatile("s_waitcnt vmcnt(" #n ")" ::: "memory")
; #define PG8_WAIT_L(n) asm volatile("s_waitcnt lgkmcnt(" #n ")" ::: "memory")
; #define PG8_BAR __builtin_amdgcn_s_barrier()
; template <class Epi, class Sched, class Prob>
; __device__ __forceinline__ void gemm_phase(LAS unsigned char* lds, LAS unsigned char* lds_epi, const Prob g, const Sched& S, const Epi& E, int wid) {
;     ...
;         const bool has_next = S.next(ui + 1, nxt);
;         const char* nA = has_next ? g.a_base(nxt) : cA; const char* nB = has_next ? g.b_base(nxt) : cB;
; _Pragma("clang loop unroll(disable)")
;         for (int t = 0; t < nt; t += 2) {
;             const bool last = (t == nt - 2);
;             const char* a1 = cA + (size_t)(t + 1) * kstep;
;             const char* a2 = last ? nA : cA + (size_t)(t + 2) * kstep; const char* b2 = last ? nB : cB + (size_t)(t + 2) * kstep;
;             const char* a3 = a2 + kstep; const char* b3 = b2 + kstep;
;             PG8_LDB(B0, 0, 0); PG8_LDB(B1, 0, 1); PG8_SCHED; PG8_LDA(At, 0, 0); PG8_STAGE(PG8_SA(1, 1), a1, cA10, cA11);
;             PG8_WAIT_V(8); PG8_WAIT_L(0); PG8_BAR; PG8_MMA(0, 0, At, B0); PG8_MMA(0, 1, At, B1); PG8_BAR; PG8_SCHED;
;             PG8_LDA(At, 0, 1); PG8_STAGE(PG8_SB(0, 0), b2, vB0, vB1); PG8_STAGE(PG8_SB(0, 1), b2 + hstepB, vB0, vB1); PG8_STAGE(PG8_SA(0, 0), a2, cA00, cA01);
;             PG8_WAIT_V(8); PG8_WAIT_L(0); PG8_BAR; PG8_MMA(1, 0, At, B0); PG8_MMA(1, 1, At, B1); PG8_BAR; PG8_SCHED;
;             PG8_LDB(B0, 1, 0); PG8_LDB(B1, 1, 1); PG8_SCHED; PG8_LDA(At, 1, 0); PG8_STAGE(PG8_SA(0, 1), a2, cA10, cA11);
.LBB0_2090:
	s_ashr_i32 s11, s10, 31
	s_lshl_b64 s[30:31], s[10:11], 19
	s_add_u32 s30, s51, s30
	s_addc_u32 s31, s52, s31
	s_and_b64 s[40:41], s[40:41], exec
	s_cselect_b32 s11, s31, s37
	s_cselect_b32 s29, s30, s36
	s_add_u32 s36, s36, 0x80
	v_mov_b32_e32 v32, 0
	s_addc_u32 s37, s37, 0
	v_lshl_add_u64 v[182:183], v[0:1], 0, s[22:23]
	s_mov_b32 s69, -2
	ds_read_b128 v[24:27], v199
	ds_read_b128 v[28:31], v199 offset:1024
	ds_read_b128 v[16:19], v199 offset:2048
	ds_read_b128 v[20:23], v199 offset:3072
	ds_read_b128 v[8:11], v200
	ds_read_b128 v[12:15], v200 offset:1024
	ds_read_b128 v[0:3], v200 offset:2048
	ds_read_b128 v[4:7], v200 offset:3072
	s_add_u32 s40, s36, 0x80
	s_addc_u32 s41, s37, 0
	s_cmp_eq_u32 s69, 12
	s_cselect_b64 vcc, -1, 0
	s_cselect_b32 s41, s11, s41
	s_cselect_b32 s40, s29, s40
	v_cndmask_b32_e32 v185, v183, v181, vcc
	v_cndmask_b32_e32 v184, v182, v180, vcc
	v_lshl_add_u64 v[228:229], s[36:37], 0, v[176:177]
	s_add_i32 m0, s35, 0xc000
	ds_read_b128 v[186:189], v201
	ds_read_b128 v[190:193], v201 offset:1024
	ds_read_b128 v[204:207], v201 offset:2048
	ds_read_b128 v[208:211], v201 offset:3072
	ds_read_b128 v[212:215], v201 offset:4096
	ds_read_b128 v[216:219], v201 offset:5120
	ds_read_b128 v[220:223], v201 offset:6144
	ds_read_b128 v[224:227], v201 offset:7168
	global_load_lds_dwordx4 v[228:229], off
	v_lshl_add_u64 v[228:229], s[36:37], 0, v[174:175]
	s_add_i32 m0, s35, 0xe000
	s_nop 0
	global_load_lds_dwordx4 v[228:229], off
	s_waitcnt vmcnt(8)
	s_waitcnt lgkmcnt(0)
	s_barrier
	s_waitcnt lgkmcnt(0)
	v_mfma_f32_16x16x128_f8f6f4 v[156:159], v[24:31], v[186:193], 0
	v_mfma_f32_16x16x128_f8f6f4 v[152:155], v[16:23], v[186:193], 0
	v_mfma_f32_16x16x128_f8f6f4 v[140:143], v[24:31], v[204:211], 0
	v_mfma_f32_16x16x128_f8f6f4 v[136:139], v[16:23], v[204:211], 0
	v_mfma_f32_16x16x128_f8f6f4 v[124:127], v[24:31], v[212:219], 0
	v_mfma_f32_16x16x128_f8f6f4 v[120:123], v[16:23], v[212:219], 0
	v_mfma_f32_16x16x128_f8f6f4 v[108:111], v[24:31], v[220:227], 0
	v_mfma_f32_16x16x128_f8f6f4 v[104:107], v[16:23], v[220:227], 0
	v_mfma_f32_16x16x128_f8f6f4 v[148:151], v[8:15], v[186:193], 0
	v_mfma_f32_16x16x128_f8f6f4 v[144:147], v[0:7], v[186:193], 0
	v_mfma_f32_16x16x128_f8f6f4 v[132:135], v[8:15], v[204:211], 0
	v_mfma_f32_16x16x128_f8f6f4 v[128:131], v[0:7], v[204:211], 0
	v_mfma_f32_16x16x128_f8f6f4 v[116:119], v[8:15], v[212:219], 0
	v_mfma_f32_16x16x128_f8f6f4 v[112:115], v[0:7], v[212:219], 0
	v_mfma_f32_16x16x128_f8f6f4 v[100:103], v[8:15], v[220:227], 0
	v_mfma_f32_16x16x128_f8f6f4 v[96:99], v[0:7], v[220:227], 0
	s_barrier
	s_add_i32 s70, s63, s97
	v_lshl_add_u64 v[186:187], v[184:185], 0, v[160:161]
	s_mov_b32 m0, s70
	ds_read_b128 v[204:207], v201 offset:16384
	ds_read_b128 v[208:211], v201 offset:17408
	ds_read_b128 v[212:215], v201 offset:18432
	ds_read_b128 v[216:219], v201 offset:19456
	ds_read_b128 v[220:223], v201 offset:20480
	ds_read_b128 v[224:227], v201 offset:21504
	ds_read_b128 v[228:231], v201 offset:22528
	ds_read_b128 v[232:235], v201 offset:23552
	global_load_lds_dwordx4 v[186:187], off
	v_lshl_add_u64 v[188:189], v[184:185], 0, v[162:163]
	s_add_i32 m0, s70, 0x2000
	v_lshl_add_u64 v[190:191], v[184:185], 0, s[12:13]
	s_add_i32 s70, s64, s97
	global_load_lds_dwordx4 v[188:189], off
	v_lshl_add_u64 v[192:193], v[190:191], 0, v[160:161]
	s_mov_b32 m0, s70
	v_lshl_add_u64 v[190:191], v[190:191], 0, v[162:163]
	global_load_lds_dwordx4 v[192:193], off
	s_add_i32 m0, s70, 0x2000
	v_lshl_add_u64 v[192:193], s[40:41], 0, v[168:169]
	global_load_lds_dwordx4 v[190:191], off
	v_lshl_add_u64 v[190:191], s[40:41], 0, v[164:165]
	s_mov_b32 m0, s35
	s_nop 0
	global_load_lds_dwordx4 v[190:191], off
	s_mov_b32 m0, s58
	s_nop 0
	global_load_lds_dwordx4 v[192:193], off
	s_waitcnt vmcnt(8)
	s_waitcnt lgkmcnt(0)
	s_barrier
	s_waitcnt lgkmcnt(0)
	v_mfma_f32_16x16x128_f8f6f4 v[92:95], v[24:31], v[204:211], 0
	v_mfma_f32_16x16x128_f8f6f4 v[88:91], v[16:23], v[204:211], 0
	v_mfma_f32_16x16x128_f8f6f4 v[76:79], v[24:31], v[212:219], 0
	v_mfma_f32_16x16x128_f8f6f4 v[72:75], v[16:23], v[212:219], 0
	v_mfma_f32_16x16x128_f8f6f4 v[60:63], v[24:31], v[220:227], 0
	v_mfma_f32_16x16x128_f8f6f4 v[56:59], v[16:23], v[220:227], 0
	v_mfma_f32_16x16x128_f8f6f4 v[44:47], v[24:31], v[228:235], 0
	v_mfma_f32_16x16x128_f8f6f4 v[40:43], v[16:23], v[228:235], 0
	v_mfma_f32_16x16x128_f8f6f4 v[84:87], v[8:15], v[204:211], 0
	v_mfma_f32_16x16x128_f8f6f4 v[80:83], v[0:7], v[204:211], 0
	v_mfma_f32_16x16x128_f8f6f4 v[68:71], v[8:15], v[212:219], 0
	v_mfma_f32_16x16x128_f8f6f4 v[64:67], v[0:7], v[212:219], 0
	v_mfma_f32_16x16x128_f8f6f4 v[52:55], v[8:15], v[220:227], 0
	v_mfma_f32_16x16x128_f8f6f4 v[48:51], v[0:7], v[220:227], 0
	v_mfma_f32_16x16x128_f8f6f4 v[36:39], v[8:15], v[228:235], 0
	v_mfma_f32_16x16x128_f8f6f4 v[32:35], v[0:7], v[228:235], 0
	s_barrier
	s_add_i32 s70, 0, 0x18000
	s_add_i32 s71, 0, 0x1c000
	v_add_u32_e32 v12, s70, v195
	v_add_u32_e32 v28, s71, v195
	ds_read_b128 v[0:3], v12
	ds_read_b128 v[4:7], v12 offset:1024
	ds_read_b128 v[8:11], v12 offset:2048
	ds_read_b128 v[12:15], v12 offset:3072
	ds_read_b128 v[16:19], v28
	ds_read_b128 v[20:23], v28 offset:1024
	ds_read_b128 v[24:27], v28 offset:2048
	ds_read_b128 v[28:31], v28 offset:3072
	s_mov_b32 m0, s59
	v_lshl_add_u64 v[236:237], s[40:41], 0, v[166:167]
	ds_read_b128 v[204:207], v201 offset:32768
	ds_read_b128 v[208:211], v201 offset:33792
	ds_read_b128 v[212:215], v201 offset:34816
	ds_read_b128 v[216:219], v201 offset:35840
	ds_read_b128 v[220:223], v201 offset:36864
	ds_read_b128 v[224:227], v201 offset:37888
	ds_read_b128 v[228:231], v201 offset:38912
	ds_read_b128 v[232:235], v201 offset:39936
	global_load_lds_dwordx4 v[236:237], off
	v_lshl_add_u64 v[236:237], s[40:41], 0, v[170:171]
	s_mov_b32 m0, s60
	s_nop 0
	global_load_lds_dwordx4 v[236:237], off
	s_waitcnt vmcnt(8)
	s_waitcnt lgkmcnt(0)
	s_barrier
; #define PG8_STAGE(bufoff, gbase, o0, o1) do { \
;         __builtin_amdgcn_global_load_lds((const unsigned*)((const char*)(gbase) + (o0)), (LAS unsigned*)(lds + (bufoff) + ldsw), 16, 0, 0); \
;         __builtin_amdgcn_global_load_lds((const unsigned*)((const char*)(gbase) + (o1)), (LAS unsigned*)(lds + (bufoff) + ldsw + 8192), 16, 0, 0); } while (0)
; #define PG8_LDA(dst, b, h) do { _Pragma("unroll") for (int m = 0; m < 4; ++m) _Pragma("unroll") for (int k = 0; k < 2; ++k) dst[m][k] = *(const LAS bf16x8*)(lds + PG8_SA(b, h) + aoff + m * 2048 + k * 1024); } while (0)
; #define PG8_LDB(dst, b, h) do { _Pragma("unroll") for (int n = 0; n < 2; ++n) _Pragma("unroll") for (int k = 0; k < 2; ++k) dst[n][k] = *(const LAS bf16x8*)(lds + PG8_SB(b, h) + boff + n * 2048 + k * 1024); } while (0)
; #define PG8_WAIT_V(n) asm volatile("s_waitcnt vmcnt(" #n ")" ::: "memory")
; #define PG8_WAIT_L(n) asm volatile("s_waitcnt lgkmcnt(" #n ")" ::: "memory")
; #define PG8_BAR __builtin_amdgcn_s_barrier()
; #define PG8_SCHED __builtin_amdgcn_sched_barrier(0)
; template <class Epi, class Sched, class Prob>
; __device__ __forceinline__ void gemm_phase(LAS unsigned char* lds, LAS unsigned char* lds_epi, const Prob g, const Sched& S, const Epi& E, int wid) {
;     ...
;             PG8_LDB(B0, 0, 0); PG8_LDB(B1, 0, 1); PG8_SCHED; PG8_LDA(At, 0, 0); PG8_STAGE(PG8_SA(1, 1), a1, cA10, cA11);
;             PG8_WAIT_V(8); PG8_WAIT_L(0); PG8_BAR; PG8_MMA(0, 0, At, B0); PG8_MMA(0, 1, At, B1); PG8_BAR; PG8_SCHED;
;             PG8_LDA(At, 0, 1); PG8_STAGE(PG8_SB(0, 0), b2, vB0, vB1); PG8_STAGE(PG8_SB(0, 1), b2 + hstepB, vB0, vB1); PG8_STAGE(PG8_SA(0, 0), a2, cA00, cA01);
;             PG8_WAIT_V(8); PG8_WAIT_L(0); PG8_BAR; PG8_MMA(1, 0, At, B0); PG8_MMA(1, 1, At, B1); PG8_BAR; PG8_SCHED;
;             PG8_LDB(B0, 1, 0); PG8_LDB(B1, 1, 1); PG8_SCHED; PG8_LDA(At, 1, 0); PG8_STAGE(PG8_SA(0, 1), a2, cA10, cA11);
;             PG8_WAIT_V(8); PG8_WAIT_L(0); PG8_BAR; PG8_MMA(0, 0, At, B0); PG8_MMA(0, 1, At, B1); PG8_BAR; PG8_SCHED;
;             PG8_LDA(At, 1, 1); PG8_STAGE(PG8_SB(1, 0), b3, vB0, vB1); PG8_STAGE(PG8_SB(1, 1), b3 + hstepB, vB0, vB1); PG8_STAGE(PG8_SA(1, 0), a3, cA00, cA01);
;             PG8_WAIT_V(8); PG8_WAIT_L(0); PG8_BAR; PG8_MMA(1, 0, At, B0); PG8_MMA(1, 1, At, B1); PG8_BAR; PG8_SCHED;
	s_waitcnt lgkmcnt(0)
	v_mfma_f32_16x16x128_f8f6f4 v[156:159], v[0:7], v[204:211], v[156:159]
	v_mfma_f32_16x16x128_f8f6f4 v[152:155], v[8:15], v[204:211], v[152:155]
	v_mfma_f32_16x16x128_f8f6f4 v[140:143], v[0:7], v[212:219], v[140:143]
	v_mfma_f32_16x16x128_f8f6f4 v[136:139], v[8:15], v[212:219], v[136:139]
	v_mfma_f32_16x16x128_f8f6f4 v[124:127], v[0:7], v[220:227], v[124:127]
	v_mfma_f32_16x16x128_f8f6f4 v[120:123], v[8:15], v[220:227], v[120:123]
	v_mfma_f32_16x16x128_f8f6f4 v[108:111], v[0:7], v[228:235], v[108:111]
	v_mfma_f32_16x16x128_f8f6f4 v[104:107], v[8:15], v[228:235], v[104:107]
	v_mfma_f32_16x16x128_f8f6f4 v[148:151], v[16:23], v[204:211], v[148:151]
	v_mfma_f32_16x16x128_f8f6f4 v[144:147], v[24:31], v[204:211], v[144:147]
	v_mfma_f32_16x16x128_f8f6f4 v[132:135], v[16:23], v[212:219], v[132:135]
	v_mfma_f32_16x16x128_f8f6f4 v[128:131], v[24:31], v[212:219], v[128:131]
	v_mfma_f32_16x16x128_f8f6f4 v[116:119], v[16:23], v[220:227], v[116:119]
	v_mfma_f32_16x16x128_f8f6f4 v[112:115], v[24:31], v[220:227], v[112:115]
	v_mfma_f32_16x16x128_f8f6f4 v[100:103], v[16:23], v[228:235], v[100:103]
	v_mfma_f32_16x16x128_f8f6f4 v[96:99], v[24:31], v[228:235], v[96:99]
	s_barrier
	s_add_i32 s40, s70, s97
	v_lshl_add_u64 v[186:187], v[186:187], 0, s[18:19]
	s_mov_b32 m0, s40
	ds_read_b128 v[204:207], v201 offset:49152
	ds_read_b128 v[208:211], v201 offset:50176
	ds_read_b128 v[212:215], v201 offset:51200
	ds_read_b128 v[216:219], v201 offset:52224
	ds_read_b128 v[220:223], v201 offset:53248
	ds_read_b128 v[224:227], v201 offset:54272
	ds_read_b128 v[228:231], v201 offset:55296
	ds_read_b128 v[232:235], v201 offset:56320
	global_load_lds_dwordx4 v[186:187], off
	v_lshl_add_u64 v[186:187], v[188:189], 0, s[18:19]
	s_add_i32 m0, s40, 0x2000
	v_lshl_add_u64 v[184:185], v[184:185], 0, s[20:21]
	s_add_i32 s40, s71, s97
	global_load_lds_dwordx4 v[186:187], off
	v_lshl_add_u64 v[186:187], v[184:185], 0, v[160:161]
	s_mov_b32 m0, s40
	v_lshl_add_u64 v[184:185], v[184:185], 0, v[162:163]
	global_load_lds_dwordx4 v[186:187], off
	s_add_i32 m0, s40, 0x2000
	s_nop 0
	global_load_lds_dwordx4 v[184:185], off
	v_lshl_add_u64 v[184:185], v[190:191], 0, s[18:19]
	s_mov_b32 m0, s61
	s_nop 0
	global_load_lds_dwordx4 v[184:185], off
	v_lshl_add_u64 v[184:185], v[192:193], 0, s[18:19]
	s_mov_b32 m0, s62
	s_nop 0
	global_load_lds_dwordx4 v[184:185], off
	s_waitcnt vmcnt(8)
	s_waitcnt lgkmcnt(0)
	s_barrier
	s_waitcnt lgkmcnt(0)
	v_mfma_f32_16x16x128_f8f6f4 v[92:95], v[0:7], v[204:211], v[92:95]
	v_mfma_f32_16x16x128_f8f6f4 v[88:91], v[8:15], v[204:211], v[88:91]
	v_mfma_f32_16x16x128_f8f6f4 v[76:79], v[0:7], v[212:219], v[76:79]
	v_mfma_f32_16x16x128_f8f6f4 v[72:75], v[8:15], v[212:219], v[72:75]
	v_mfma_f32_16x16x128_f8f6f4 v[60:63], v[0:7], v[220:227], v[60:63]
	v_mfma_f32_16x16x128_f8f6f4 v[56:59], v[8:15], v[220:227], v[56:59]
	v_mfma_f32_16x16x128_f8f6f4 v[44:47], v[0:7], v[228:235], v[44:47]
	v_mfma_f32_16x16x128_f8f6f4 v[40:43], v[8:15], v[228:235], v[40:43]
	v_mfma_f32_16x16x128_f8f6f4 v[84:87], v[16:23], v[204:211], v[84:87]
	v_mfma_f32_16x16x128_f8f6f4 v[80:83], v[24:31], v[204:211], v[80:83]
	v_mfma_f32_16x16x128_f8f6f4 v[68:71], v[16:23], v[212:219], v[68:71]
	v_mfma_f32_16x16x128_f8f6f4 v[64:67], v[24:31], v[212:219], v[64:67]
	v_mfma_f32_16x16x128_f8f6f4 v[52:55], v[16:23], v[220:227], v[52:55]
	v_mfma_f32_16x16x128_f8f6f4 v[48:51], v[24:31], v[220:227], v[48:51]
	v_mfma_f32_16x16x128_f8f6f4 v[36:39], v[16:23], v[228:235], v[36:39]
	v_mfma_f32_16x16x128_f8f6f4 v[32:35], v[24:31], v[228:235], v[32:35]
	s_barrier
	s_add_i32 s69, s69, 2
	s_add_u32 s36, s36, 0x100
	s_addc_u32 s37, s37, 0
	s_cmp_gt_u32 s69, 13
	v_lshl_add_u64 v[182:183], v[182:183], 0, s[22:23]
.LBB0_2091:
	ds_read_b128 v[24:27], v199
	ds_read_b128 v[28:31], v199 offset:1024
	ds_read_b128 v[16:19], v199 offset:2048
	ds_read_b128 v[20:23], v199 offset:3072
	ds_read_b128 v[8:11], v200
	ds_read_b128 v[12:15], v200 offset:1024
	ds_read_b128 v[0:3], v200 offset:2048
	ds_read_b128 v[4:7], v200 offset:3072
	s_add_u32 s40, s36, 0x80
	s_addc_u32 s41, s37, 0
	s_cmp_eq_u32 s69, 12
	s_cselect_b64 vcc, -1, 0
	s_cselect_b32 s41, s11, s41
	s_cselect_b32 s40, s29, s40
	v_cndmask_b32_e32 v185, v183, v181, vcc
	v_cndmask_b32_e32 v184, v182, v180, vcc
	v_lshl_add_u64 v[228:229], s[36:37], 0, v[176:177]
	s_add_i32 m0, s35, 0xc000
	ds_read_b128 v[186:189], v201
	ds_read_b128 v[190:193], v201 offset:1024
	ds_read_b128 v[204:207], v201 offset:2048
	ds_read_b128 v[208:211], v201 offset:3072
	ds_read_b128 v[212:215], v201 offset:4096
	ds_read_b128 v[216:219], v201 offset:5120
	ds_read_b128 v[220:223], v201 offset:6144
	ds_read_b128 v[224:227], v201 offset:7168
	global_load_lds_dwordx4 v[228:229], off
	v_lshl_add_u64 v[228:229], s[36:37], 0, v[174:175]
	s_add_i32 m0, s35, 0xe000
	s_nop 0
	global_load_lds_dwordx4 v[228:229], off
	s_waitcnt vmcnt(8)
	s_waitcnt lgkmcnt(0)
	s_barrier
	s_waitcnt lgkmcnt(0)
	v_mfma_f32_16x16x128_f8f6f4 v[156:159], v[24:31], v[186:193], v[156:159]
	v_mfma_f32_16x16x128_f8f6f4 v[152:155], v[16:23], v[186:193], v[152:155]
	v_mfma_f32_16x16x128_f8f6f4 v[140:143], v[24:31], v[204:211], v[140:143]
	v_mfma_f32_16x16x128_f8f6f4 v[136:139], v[16:23], v[204:211], v[136:139]
	v_mfma_f32_16x16x128_f8f6f4 v[124:127], v[24:31], v[212:219], v[124:127]
	v_mfma_f32_16x16x128_f8f6f4 v[120:123], v[16:23], v[212:219], v[120:123]
	v_mfma_f32_16x16x128_f8f6f4 v[108:111], v[24:31], v[220:227], v[108:111]
	v_mfma_f32_16x16x128_f8f6f4 v[104:107], v[16:23], v[220:227], v[104:107]
	v_mfma_f32_16x16x128_f8f6f4 v[148:151], v[8:15], v[186:193], v[148:151]
	v_mfma_f32_16x16x128_f8f6f4 v[144:147], v[0:7], v[186:193], v[144:147]
	v_mfma_f32_16x16x128_f8f6f4 v[132:135], v[8:15], v[204:211], v[132:135]
	v_mfma_f32_16x16x128_f8f6f4 v[128:131], v[0:7], v[204:211], v[128:131]
	v_mfma_f32_16x16x128_f8f6f4 v[116:119], v[8:15], v[212:219], v[116:119]
	v_mfma_f32_16x16x128_f8f6f4 v[112:115], v[0:7], v[212:219], v[112:115]
	v_mfma_f32_16x16x128_f8f6f4 v[100:103], v[8:15], v[220:227], v[100:103]
	v_mfma_f32_16x16x128_f8f6f4 v[96:99], v[0:7], v[220:227], v[96:99]
	s_barrier
; #define PG8_STAGE(bufoff, gbase, o0, o1) do { \
;         __builtin_amdgcn_global_load_lds((const unsigned*)((const char*)(gbase) + (o0)), (LAS unsigned*)(lds + (bufoff) + ldsw), 16, 0, 0); \
;         __builtin_amdgcn_global_load_lds((const unsigned*)((const char*)(gbase) + (o1)), (LAS unsigned*)(lds + (bufoff) + ldsw + 8192), 16, 0, 0); } while (0)
; #define PG8_LDA(dst, b, h) do { _Pragma("unroll") for (int m = 0; m < 4; ++m) _Pragma("unroll") for (int k = 0; k < 2; ++k) dst[m][k] = *(const LAS bf16x8*)(lds + PG8_SA(b, h) + aoff + m * 2048 + k * 1024); } while (0)
; #define PG8_LDB(dst, b, h) do { _Pragma("unroll") for (int n = 0; n < 2; ++n) _Pragma("unroll") for (int k = 0; k < 2; ++k) dst[n][k] = *(const LAS bf16x8*)(lds + PG8_SB(b, h) + boff + n * 2048 + k * 1024); } while (0)
; #define PG8_WAIT_V(n) asm volatile("s_waitcnt vmcnt(" #n ")" ::: "memory")
; #define PG8_WAIT_L(n) asm volatile("s_waitcnt lgkmcnt(" #n ")" ::: "memory")
; #define PG8_BAR __builtin_amdgcn_s_barrier()
; #define PG8_SCHED __builtin_amdgcn_sched_barrier(0)
; template <class Epi, class Sched, class Prob>
; __device__ __forceinline__ void gemm_phase(LAS unsigned char* lds, LAS unsigned char* lds_epi, const Prob g, const Sched& S, const Epi& E, int wid) {
;     ...
;             PG8_LDA(At, 0, 1); PG8_STAGE(PG8_SB(0, 0), b2, vB0, vB1); PG8_STAGE(PG8_SB(0, 1), b2 + hstepB, vB0, vB1); PG8_STAGE(PG8_SA(0, 0), a2, cA00, cA01);
;             PG8_WAIT_V(8); PG8_WAIT_L(0); PG8_BAR; PG8_MMA(1, 0, At, B0); PG8_MMA(1, 1, At, B1); PG8_BAR; PG8_SCHED;
;             PG8_LDB(B0, 1, 0); PG8_LDB(B1, 1, 1); PG8_SCHED; PG8_LDA(At, 1, 0); PG8_STAGE(PG8_SA(0, 1), a2, cA10, cA11);
	s_add_i32 s70, s63, s97
	v_lshl_add_u64 v[186:187], v[184:185], 0, v[160:161]
	s_mov_b32 m0, s70
	ds_read_b128 v[204:207], v201 offset:16384
	ds_read_b128 v[208:211], v201 offset:17408
	ds_read_b128 v[212:215], v201 offset:18432
	ds_read_b128 v[216:219], v201 offset:19456
	ds_read_b128 v[220:223], v201 offset:20480
	ds_read_b128 v[224:227], v201 offset:21504
	ds_read_b128 v[228:231], v201 offset:22528
	ds_read_b128 v[232:235], v201 offset:23552
	global_load_lds_dwordx4 v[186:187], off
	v_lshl_add_u64 v[188:189], v[184:185], 0, v[162:163]
	s_add_i32 m0, s70, 0x2000
	v_lshl_add_u64 v[190:191], v[184:185], 0, s[12:13]
	s_add_i32 s70, s64, s97
	global_load_lds_dwordx4 v[188:189], off
	v_lshl_add_u64 v[192:193], v[190:191], 0, v[160:161]
	s_mov_b32 m0, s70
	v_lshl_add_u64 v[190:191], v[190:191], 0, v[162:163]
	global_load_lds_dwordx4 v[192:193], off
	s_add_i32 m0, s70, 0x2000
	v_lshl_add_u64 v[192:193], s[40:41], 0, v[168:169]
	global_load_lds_dwordx4 v[190:191], off
	v_lshl_add_u64 v[190:191], s[40:41], 0, v[164:165]
	s_mov_b32 m0, s35
	s_nop 0
	global_load_lds_dwordx4 v[190:191], off
	s_mov_b32 m0, s58
	s_nop 0
	global_load_lds_dwordx4 v[192:193], off
	s_waitcnt vmcnt(8)
	s_waitcnt lgkmcnt(0)
	s_barrier
	s_waitcnt lgkmcnt(0)
	v_mfma_f32_16x16x128_f8f6f4 v[92:95], v[24:31], v[204:211], v[92:95]
	v_mfma_f32_16x16x128_f8f6f4 v[88:91], v[16:23], v[204:211], v[88:91]
	v_mfma_f32_16x16x128_f8f6f4 v[76:79], v[24:31], v[212:219], v[76:79]
	v_mfma_f32_16x16x128_f8f6f4 v[72:75], v[16:23], v[212:219], v[72:75]
	v_mfma_f32_16x16x128_f8f6f4 v[60:63], v[24:31], v[220:227], v[60:63]
	v_mfma_f32_16x16x128_f8f6f4 v[56:59], v[16:23], v[220:227], v[56:59]
	v_mfma_f32_16x16x128_f8f6f4 v[44:47], v[24:31], v[228:235], v[44:47]
	v_mfma_f32_16x16x128_f8f6f4 v[40:43], v[16:23], v[228:235], v[40:43]
	v_mfma_f32_16x16x128_f8f6f4 v[84:87], v[8:15], v[204:211], v[84:87]
	v_mfma_f32_16x16x128_f8f6f4 v[80:83], v[0:7], v[204:211], v[80:83]
	v_mfma_f32_16x16x128_f8f6f4 v[68:71], v[8:15], v[212:219], v[68:71]
	v_mfma_f32_16x16x128_f8f6f4 v[64:67], v[0:7], v[212:219], v[64:67]
	v_mfma_f32_16x16x128_f8f6f4 v[52:55], v[8:15], v[220:227], v[52:55]
	v_mfma_f32_16x16x128_f8f6f4 v[48:51], v[0:7], v[220:227], v[48:51]
	v_mfma_f32_16x16x128_f8f6f4 v[36:39], v[8:15], v[228:235], v[36:39]
	v_mfma_f32_16x16x128_f8f6f4 v[32:35], v[0:7], v[228:235], v[32:35]
	s_barrier
	s_add_i32 s70, 0, 0x18000
	s_add_i32 s71, 0, 0x1c000
	v_add_u32_e32 v12, s70, v195
	v_add_u32_e32 v28, s71, v195
	ds_read_b128 v[0:3], v12
	ds_read_b128 v[4:7], v12 offset:1024
	ds_read_b128 v[8:11], v12 offset:2048
	ds_read_b128 v[12:15], v12 offset:3072
	ds_read_b128 v[16:19], v28
	ds_read_b128 v[20:23], v28 offset:1024
	ds_read_b128 v[24:27], v28 offset:2048
	ds_read_b128 v[28:31], v28 offset:3072
	s_mov_b32 m0, s59
	v_lshl_add_u64 v[236:237], s[40:41], 0, v[166:167]
	ds_read_b128 v[204:207], v201 offset:32768
	ds_read_b128 v[208:211], v201 offset:33792
	ds_read_b128 v[212:215], v201 offset:34816
	ds_read_b128 v[216:219], v201 offset:35840
	ds_read_b128 v[220:223], v201 offset:36864
	ds_read_b128 v[224:227], v201 offset:37888
	ds_read_b128 v[228:231], v201 offset:38912
	ds_read_b128 v[232:235], v201 offset:39936
	global_load_lds_dwordx4 v[236:237], off
	v_lshl_add_u64 v[236:237], s[40:41], 0, v[170:171]
	s_mov_b32 m0, s60
	s_nop 0
	global_load_lds_dwordx4 v[236:237], off
	s_waitcnt vmcnt(8)
	s_waitcnt lgkmcnt(0)
	s_barrier
; #define PG8_STAGE(bufoff, gbase, o0, o1) do { \
;         __builtin_amdgcn_global_load_lds((const unsigned*)((const char*)(gbase) + (o0)), (LAS unsigned*)(lds + (bufoff) + ldsw), 16, 0, 0); \
;         __builtin_amdgcn_global_load_lds((const unsigned*)((const char*)(gbase) + (o1)), (LAS unsigned*)(lds + (bufoff) + ldsw + 8192), 16, 0, 0); } while (0)
; #define PG8_LDA(dst, b, h) do { _Pragma("unroll") for (int m = 0; m < 4; ++m) _Pragma("unroll") for (int k = 0; k < 2; ++k) dst[m][k] = *(const LAS bf16x8*)(lds + PG8_SA(b, h) + aoff + m * 2048 + k * 1024); } while (0)
; #define PG8_WAIT_V(n) asm volatile("s_waitcnt vmcnt(" #n ")" ::: "memory")
; #define PG8_WAIT_L(n) asm volatile("s_waitcnt lgkmcnt(" #n ")" ::: "memory")
; #define PG8_BAR __builtin_amdgcn_s_barrier()
; #define PG8_SCHED __builtin_amdgcn_sched_barrier(0)
; template <class Epi, class Sched, class Prob>
; __device__ __forceinline__ void gemm_phase(LAS unsigned char* lds, LAS unsigned char* lds_epi, const Prob g, const Sched& S, const Epi& E, int wid) {
;     ...
;             PG8_WAIT_V(8); PG8_WAIT_L(0); PG8_BAR; PG8_MMA(0, 0, At, B0); PG8_MMA(0, 1, At, B1); PG8_BAR; PG8_SCHED;
;             PG8_LDA(At, 1, 1); PG8_STAGE(PG8_SB(1, 0), b3, vB0, vB1); PG8_STAGE(PG8_SB(1, 1), b3 + hstepB, vB0, vB1); PG8_STAGE(PG8_SA(1, 0), a3, cA00, cA01);
;             PG8_WAIT_V(8); PG8_WAIT_L(0); PG8_BAR; PG8_MMA(1, 0, At, B0); PG8_MMA(1, 1, At, B1); PG8_BAR; PG8_SCHED;
;         }
	s_waitcnt lgkmcnt(0)
	v_mfma_f32_16x16x128_f8f6f4 v[156:159], v[0:7], v[204:211], v[156:159]
	v_mfma_f32_16x16x128_f8f6f4 v[152:155], v[8:15], v[204:211], v[152:155]
	v_mfma_f32_16x16x128_f8f6f4 v[140:143], v[0:7], v[212:219], v[140:143]
	v_mfma_f32_16x16x128_f8f6f4 v[136:139], v[8:15], v[212:219], v[136:139]
	v_mfma_f32_16x16x128_f8f6f4 v[124:127], v[0:7], v[220:227], v[124:127]
	v_mfma_f32_16x16x128_f8f6f4 v[120:123], v[8:15], v[220:227], v[120:123]
	v_mfma_f32_16x16x128_f8f6f4 v[108:111], v[0:7], v[228:235], v[108:111]
	v_mfma_f32_16x16x128_f8f6f4 v[104:107], v[8:15], v[228:235], v[104:107]
	v_mfma_f32_16x16x128_f8f6f4 v[148:151], v[16:23], v[204:211], v[148:151]
	v_mfma_f32_16x16x128_f8f6f4 v[144:147], v[24:31], v[204:211], v[144:147]
	v_mfma_f32_16x16x128_f8f6f4 v[132:135], v[16:23], v[212:219], v[132:135]
	v_mfma_f32_16x16x128_f8f6f4 v[128:131], v[24:31], v[212:219], v[128:131]
	v_mfma_f32_16x16x128_f8f6f4 v[116:119], v[16:23], v[220:227], v[116:119]
	v_mfma_f32_16x16x128_f8f6f4 v[112:115], v[24:31], v[220:227], v[112:115]
	v_mfma_f32_16x16x128_f8f6f4 v[100:103], v[16:23], v[228:235], v[100:103]
	v_mfma_f32_16x16x128_f8f6f4 v[96:99], v[24:31], v[228:235], v[96:99]
	s_barrier
	s_add_i32 s40, s70, s97
	v_lshl_add_u64 v[186:187], v[186:187], 0, s[18:19]
	s_mov_b32 m0, s40
	ds_read_b128 v[204:207], v201 offset:49152
	ds_read_b128 v[208:211], v201 offset:50176
	ds_read_b128 v[212:215], v201 offset:51200
	ds_read_b128 v[216:219], v201 offset:52224
	ds_read_b128 v[220:223], v201 offset:53248
	ds_read_b128 v[224:227], v201 offset:54272
	ds_read_b128 v[228:231], v201 offset:55296
	ds_read_b128 v[232:235], v201 offset:56320
	global_load_lds_dwordx4 v[186:187], off
	v_lshl_add_u64 v[186:187], v[188:189], 0, s[18:19]
	s_add_i32 m0, s40, 0x2000
	v_lshl_add_u64 v[184:185], v[184:185], 0, s[20:21]
	s_add_i32 s40, s71, s97
	global_load_lds_dwordx4 v[186:187], off
	v_lshl_add_u64 v[186:187], v[184:185], 0, v[160:161]
	s_mov_b32 m0, s40
	v_lshl_add_u64 v[184:185], v[184:185], 0, v[162:163]
	global_load_lds_dwordx4 v[186:187], off
	s_add_i32 m0, s40, 0x2000
	s_nop 0
	global_load_lds_dwordx4 v[184:185], off
	v_lshl_add_u64 v[184:185], v[190:191], 0, s[18:19]
	s_mov_b32 m0, s61
	s_nop 0
	global_load_lds_dwordx4 v[184:185], off
	v_lshl_add_u64 v[184:185], v[192:193], 0, s[18:19]
	s_mov_b32 m0, s62
	s_nop 0
	global_load_lds_dwordx4 v[184:185], off
	s_waitcnt vmcnt(8)
	s_waitcnt lgkmcnt(0)
	s_barrier
	s_waitcnt lgkmcnt(0)
	v_mfma_f32_16x16x128_f8f6f4 v[92:95], v[0:7], v[204:211], v[92:95]
	v_mfma_f32_16x16x128_f8f6f4 v[88:91], v[8:15], v[204:211], v[88:91]
	v_mfma_f32_16x16x128_f8f6f4 v[76:79], v[0:7], v[212:219], v[76:79]
	v_mfma_f32_16x16x128_f8f6f4 v[72:75], v[8:15], v[212:219], v[72:75]
	v_mfma_f32_16x16x128_f8f6f4 v[60:63], v[0:7], v[220:227], v[60:63]
	v_mfma_f32_16x16x128_f8f6f4 v[56:59], v[8:15], v[220:227], v[56:59]
	v_mfma_f32_16x16x128_f8f6f4 v[44:47], v[0:7], v[228:235], v[44:47]
	v_mfma_f32_16x16x128_f8f6f4 v[40:43], v[8:15], v[228:235], v[40:43]
	v_mfma_f32_16x16x128_f8f6f4 v[84:87], v[16:23], v[204:211], v[84:87]
	v_mfma_f32_16x16x128_f8f6f4 v[80:83], v[24:31], v[204:211], v[80:83]
	v_mfma_f32_16x16x128_f8f6f4 v[68:71], v[16:23], v[212:219], v[68:71]
	v_mfma_f32_16x16x128_f8f6f4 v[64:67], v[24:31], v[212:219], v[64:67]
	v_mfma_f32_16x16x128_f8f6f4 v[52:55], v[16:23], v[220:227], v[52:55]
	v_mfma_f32_16x16x128_f8f6f4 v[48:51], v[24:31], v[220:227], v[48:51]
	v_mfma_f32_16x16x128_f8f6f4 v[36:39], v[16:23], v[228:235], v[36:39]
	v_mfma_f32_16x16x128_f8f6f4 v[32:35], v[24:31], v[228:235], v[32:35]
	s_barrier
	s_add_i32 s69, s69, 2
	s_add_u32 s36, s36, 0x100
	s_addc_u32 s37, s37, 0
	s_cmp_gt_u32 s69, 13
	v_lshl_add_u64 v[182:183], v[182:183], 0, s[22:23]
	s_cbranch_scc0 .LBB0_2091
	v_readlane_b32 s36, v254, 27
	v_readlane_b32 s37, v254, 28
	s_and_b64 vcc, exec, s[36:37]
	s_cbranch_vccz .LBB0_2094
	s_barrier

; #define PG8_STAGE(bufoff, gbase, o0, o1) do { \
;         __builtin_amdgcn_global_load_lds((const unsigned*)((const char*)(gbase) + (o0)), (LAS unsigned*)(lds + (bufoff) + ldsw), 16, 0, 0); \
;         __builtin_amdgcn_global_load_lds((const unsigned*)((const char*)(gbase) + (o1)), (LAS unsigned*)(lds + (bufoff) + ldsw + 8192), 16, 0, 0); } while (0)
; #define PG8_LDA(dst, b, h) do { _Pragma("unroll") for (int m = 0; m < 4; ++m) _Pragma("unroll") for (int k = 0; k < 2; ++k) dst[m][k] = *(const LAS bf16x8*)(lds + PG8_SA(b, h) + aoff + m * 2048 + k * 1024); } while (0)
; #define PG8_LDB(dst, b, h) do { _Pragma("unroll") for (int n = 0; n < 2; ++n) _Pragma("unroll") for (int k = 0; k < 2; ++k) dst[n][k] = *(const LAS bf16x8*)(lds + PG8_SB(b, h) + boff + n * 2048 + k * 1024); } while (0)
; #define PG8_WAIT_V(n) asm volatile("s_waitcnt vmcnt(" #n ")" ::: "memory")
; #define PG8_WAIT_L(n) asm volatile("s_waitcnt lgkmcnt(" #n ")" ::: "memory")
; #define PG8_BAR __builtin_amdgcn_s_barrier()
; template <class Epi, class Sched, class Prob>
; __device__ __forceinline__ void gemm_phase(LAS unsigned char* lds, LAS unsigned char* lds_epi, const Prob g, const Sched& S, const Epi& E, int wid) {
;     ...
;         const bool has_next = S.next(ui + 1, nxt);
;         const char* nA = has_next ? g.a_base(nxt) : cA; const char* nB = has_next ? g.b_base(nxt) : cB;
; _Pragma("clang loop unroll(disable)")
;         for (int t = 0; t < nt; t += 2) {
;             const bool last = (t == nt - 2);
;             const char* a1 = cA + (size_t)(t + 1) * kstep;
;             const char* a2 = last ? nA : cA + (size_t)(t + 2) * kstep; const char* b2 = last ? nB : cB + (size_t)(t + 2) * kstep;
;             const char* a3 = a2 + kstep; const char* b3 = b2 + kstep;
;             PG8_LDB(B0, 0, 0); PG8_LDB(B1, 0, 1); PG8_SCHED; PG8_LDA(At, 0, 0); PG8_STAGE(PG8_SA(1, 1), a1, cA10, cA11);
;             PG8_WAIT_V(8); PG8_WAIT_L(0); PG8_BAR; PG8_MMA(0, 0, At, B0); PG8_MMA(0, 1, At, B1); PG8_BAR; PG8_SCHED;
;             PG8_LDA(At, 0, 1); PG8_STAGE(PG8_SB(0, 0), b2, vB0, vB1); PG8_STAGE(PG8_SB(0, 1), b2 + hstepB, vB0, vB1); PG8_STAGE(PG8_SA(0, 0), a2, cA00, cA01);
;             PG8_WAIT_V(8); PG8_WAIT_L(0); PG8_BAR; PG8_MMA(1, 0, At, B0); PG8_MMA(1, 1, At, B1); PG8_BAR; PG8_SCHED;
;             PG8_LDB(B0, 1, 0); PG8_LDB(B1, 1, 1); PG8_SCHED; PG8_LDA(At, 1, 0); PG8_STAGE(PG8_SA(0, 1), a2, cA10, cA11);
.LBB0_2172:
	s_add_u32 s36, s36, 0x80
	v_mov_b32_e32 v32, 0
	s_addc_u32 s37, s37, 0
	v_lshl_add_u64 v[186:187], v[0:1], 0, s[22:23]
	s_mov_b32 s64, -2
	ds_read_b128 v[24:27], v161
	ds_read_b128 v[28:31], v161 offset:1024
	ds_read_b128 v[16:19], v161 offset:2048
	ds_read_b128 v[20:23], v161 offset:3072
	ds_read_b128 v[8:11], v207
	ds_read_b128 v[12:15], v207 offset:1024
	ds_read_b128 v[0:3], v207 offset:2048
	ds_read_b128 v[4:7], v207 offset:3072
	s_add_u32 s40, s36, 0x80
	s_addc_u32 s41, s37, 0
	s_cmp_eq_u32 s64, 52
	s_cselect_b64 vcc, -1, 0
	s_cselect_b32 s41, s31, s41
	s_cselect_b32 s40, s30, s40
	v_cndmask_b32_e32 v189, v187, v185, vcc
	v_cndmask_b32_e32 v188, v186, v184, vcc
	v_lshl_add_u64 v[212:213], s[36:37], 0, v[182:183]
	s_add_i32 m0, s33, 0xc000
	ds_read_b128 v[190:193], v208
	ds_read_b128 v[194:197], v208 offset:1024
	ds_read_b128 v[216:219], v208 offset:2048
	ds_read_b128 v[220:223], v208 offset:3072
	ds_read_b128 v[224:227], v208 offset:4096
	ds_read_b128 v[228:231], v208 offset:5120
	ds_read_b128 v[238:241], v208 offset:6144
	ds_read_b128 v[242:245], v208 offset:7168
	global_load_lds_dwordx4 v[212:213], off
	v_lshl_add_u64 v[212:213], s[36:37], 0, v[180:181]
	s_add_i32 m0, s33, 0xe000
	s_nop 0
	global_load_lds_dwordx4 v[212:213], off
	s_waitcnt vmcnt(8)
	s_waitcnt lgkmcnt(0)
	s_barrier
	s_waitcnt lgkmcnt(0)
	v_mfma_f32_16x16x128_f8f6f4 v[156:159], v[24:31], v[190:197], 0
	v_mfma_f32_16x16x128_f8f6f4 v[152:155], v[16:23], v[190:197], 0
	v_mfma_f32_16x16x128_f8f6f4 v[140:143], v[24:31], v[216:223], 0
	v_mfma_f32_16x16x128_f8f6f4 v[136:139], v[16:23], v[216:223], 0
	v_mfma_f32_16x16x128_f8f6f4 v[124:127], v[24:31], v[224:231], 0
	v_mfma_f32_16x16x128_f8f6f4 v[120:123], v[16:23], v[224:231], 0
	v_mfma_f32_16x16x128_f8f6f4 v[108:111], v[24:31], v[238:245], 0
	v_mfma_f32_16x16x128_f8f6f4 v[104:107], v[16:23], v[238:245], 0
	v_mfma_f32_16x16x128_f8f6f4 v[148:151], v[8:15], v[190:197], 0
	v_mfma_f32_16x16x128_f8f6f4 v[144:147], v[0:7], v[190:197], 0
	v_mfma_f32_16x16x128_f8f6f4 v[132:135], v[8:15], v[216:223], 0
	v_mfma_f32_16x16x128_f8f6f4 v[128:131], v[0:7], v[216:223], 0
	v_mfma_f32_16x16x128_f8f6f4 v[116:119], v[8:15], v[224:231], 0
	v_mfma_f32_16x16x128_f8f6f4 v[112:115], v[0:7], v[224:231], 0
	v_mfma_f32_16x16x128_f8f6f4 v[100:103], v[8:15], v[238:245], 0
	v_mfma_f32_16x16x128_f8f6f4 v[96:99], v[0:7], v[238:245], 0
	s_barrier
	s_add_i32 s65, s58, s97
	v_lshl_add_u64 v[190:191], v[188:189], 0, v[162:163]
	s_mov_b32 m0, s65
	ds_read_b128 v[216:219], v208 offset:16384
	ds_read_b128 v[220:223], v208 offset:17408
	ds_read_b128 v[224:227], v208 offset:18432
	ds_read_b128 v[228:231], v208 offset:19456
	ds_read_b128 v[238:241], v208 offset:20480
	ds_read_b128 v[242:245], v208 offset:21504
	ds_read_b128 v[246:249], v208 offset:22528
	ds_read_b128 v[250:253], v208 offset:23552
	global_load_lds_dwordx4 v[190:191], off
	v_lshl_add_u64 v[192:193], v[188:189], 0, v[164:165]
	s_add_i32 m0, s65, 0x2000
	v_lshl_add_u64 v[194:195], v[188:189], 0, s[16:17]
	s_add_i32 s65, s59, s97
	global_load_lds_dwordx4 v[192:193], off
	v_lshl_add_u64 v[196:197], v[194:195], 0, v[162:163]
	s_mov_b32 m0, s65
	v_lshl_add_u64 v[194:195], v[194:195], 0, v[164:165]
	global_load_lds_dwordx4 v[196:197], off
	s_add_i32 m0, s65, 0x2000
	v_lshl_add_u64 v[196:197], s[40:41], 0, v[174:175]
	global_load_lds_dwordx4 v[194:195], off
	v_lshl_add_u64 v[194:195], s[40:41], 0, v[170:171]
	s_mov_b32 m0, s33
	s_nop 0
	global_load_lds_dwordx4 v[194:195], off
	s_mov_b32 m0, s35
	s_nop 0
	global_load_lds_dwordx4 v[196:197], off
	s_waitcnt vmcnt(8)
	s_waitcnt lgkmcnt(0)
	s_barrier
	s_waitcnt lgkmcnt(0)
	v_mfma_f32_16x16x128_f8f6f4 v[92:95], v[24:31], v[216:223], 0
	v_mfma_f32_16x16x128_f8f6f4 v[88:91], v[16:23], v[216:223], 0
	v_mfma_f32_16x16x128_f8f6f4 v[76:79], v[24:31], v[224:231], 0
	v_mfma_f32_16x16x128_f8f6f4 v[72:75], v[16:23], v[224:231], 0
	v_mfma_f32_16x16x128_f8f6f4 v[60:63], v[24:31], v[238:245], 0
	v_mfma_f32_16x16x128_f8f6f4 v[56:59], v[16:23], v[238:245], 0
	v_mfma_f32_16x16x128_f8f6f4 v[44:47], v[24:31], v[246:253], 0
	v_mfma_f32_16x16x128_f8f6f4 v[40:43], v[16:23], v[246:253], 0
	v_mfma_f32_16x16x128_f8f6f4 v[84:87], v[8:15], v[216:223], 0
	v_mfma_f32_16x16x128_f8f6f4 v[80:83], v[0:7], v[216:223], 0
	v_mfma_f32_16x16x128_f8f6f4 v[68:71], v[8:15], v[224:231], 0
	v_mfma_f32_16x16x128_f8f6f4 v[64:67], v[0:7], v[224:231], 0
	v_mfma_f32_16x16x128_f8f6f4 v[52:55], v[8:15], v[238:245], 0
	v_mfma_f32_16x16x128_f8f6f4 v[48:51], v[0:7], v[238:245], 0
	v_mfma_f32_16x16x128_f8f6f4 v[36:39], v[8:15], v[246:253], 0
	v_mfma_f32_16x16x128_f8f6f4 v[32:35], v[0:7], v[246:253], 0
	s_barrier
	s_add_i32 s65, 0, 0x18000
	s_add_i32 s66, 0, 0x1c000
	v_add_u32_e32 v12, s65, v204
	v_add_u32_e32 v28, s66, v204
	ds_read_b128 v[0:3], v12
	ds_read_b128 v[4:7], v12 offset:1024
	ds_read_b128 v[8:11], v12 offset:2048
	ds_read_b128 v[12:15], v12 offset:3072
	ds_read_b128 v[16:19], v28
	ds_read_b128 v[20:23], v28 offset:1024
	ds_read_b128 v[24:27], v28 offset:2048
	ds_read_b128 v[28:31], v28 offset:3072
	s_mov_b32 m0, s48
	v_lshl_add_u64 v[212:213], s[40:41], 0, v[172:173]
	ds_read_b128 v[216:219], v208 offset:32768
	ds_read_b128 v[220:223], v208 offset:33792
	ds_read_b128 v[224:227], v208 offset:34816
	ds_read_b128 v[228:231], v208 offset:35840
	ds_read_b128 v[238:241], v208 offset:36864
	ds_read_b128 v[242:245], v208 offset:37888
	ds_read_b128 v[246:249], v208 offset:38912
	ds_read_b128 v[250:253], v208 offset:39936
	global_load_lds_dwordx4 v[212:213], off
	v_lshl_add_u64 v[212:213], s[40:41], 0, v[176:177]
	s_mov_b32 m0, s52
	s_nop 0
	global_load_lds_dwordx4 v[212:213], off
	s_waitcnt vmcnt(8)
	s_waitcnt lgkmcnt(0)
	s_barrier
; #define PG8_STAGE(bufoff, gbase, o0, o1) do { \
;         __builtin_amdgcn_global_load_lds((const unsigned*)((const char*)(gbase) + (o0)), (LAS unsigned*)(lds + (bufoff) + ldsw), 16, 0, 0); \
;         __builtin_amdgcn_global_load_lds((const unsigned*)((const char*)(gbase) + (o1)), (LAS unsigned*)(lds + (bufoff) + ldsw + 8192), 16, 0, 0); } while (0)
; #define PG8_LDA(dst, b, h) do { _Pragma("unroll") for (int m = 0; m < 4; ++m) _Pragma("unroll") for (int k = 0; k < 2; ++k) dst[m][k] = *(const LAS bf16x8*)(lds + PG8_SA(b, h) + aoff + m * 2048 + k * 1024); } while (0)
; #define PG8_LDB(dst, b, h) do { _Pragma("unroll") for (int n = 0; n < 2; ++n) _Pragma("unroll") for (int k = 0; k < 2; ++k) dst[n][k] = *(const LAS bf16x8*)(lds + PG8_SB(b, h) + boff + n * 2048 + k * 1024); } while (0)
; #define PG8_WAIT_V(n) asm volatile("s_waitcnt vmcnt(" #n ")" ::: "memory")
; #define PG8_WAIT_L(n) asm volatile("s_waitcnt lgkmcnt(" #n ")" ::: "memory")
; #define PG8_BAR __builtin_amdgcn_s_barrier()
; #define PG8_SCHED __builtin_amdgcn_sched_barrier(0)
; template <class Epi, class Sched, class Prob>
; __device__ __forceinline__ void gemm_phase(LAS unsigned char* lds, LAS unsigned char* lds_epi, const Prob g, const Sched& S, const Epi& E, int wid) {
;     ...
;             PG8_LDB(B0, 0, 0); PG8_LDB(B1, 0, 1); PG8_SCHED; PG8_LDA(At, 0, 0); PG8_STAGE(PG8_SA(1, 1), a1, cA10, cA11);
;             PG8_WAIT_V(8); PG8_WAIT_L(0); PG8_BAR; PG8_MMA(0, 0, At, B0); PG8_MMA(0, 1, At, B1); PG8_BAR; PG8_SCHED;
;             PG8_LDA(At, 0, 1); PG8_STAGE(PG8_SB(0, 0), b2, vB0, vB1); PG8_STAGE(PG8_SB(0, 1), b2 + hstepB, vB0, vB1); PG8_STAGE(PG8_SA(0, 0), a2, cA00, cA01);
;             PG8_WAIT_V(8); PG8_WAIT_L(0); PG8_BAR; PG8_MMA(1, 0, At, B0); PG8_MMA(1, 1, At, B1); PG8_BAR; PG8_SCHED;
;             PG8_LDB(B0, 1, 0); PG8_LDB(B1, 1, 1); PG8_SCHED; PG8_LDA(At, 1, 0); PG8_STAGE(PG8_SA(0, 1), a2, cA10, cA11);
;             PG8_WAIT_V(8); PG8_WAIT_L(0); PG8_BAR; PG8_MMA(0, 0, At, B0); PG8_MMA(0, 1, At, B1); PG8_BAR; PG8_SCHED;
;             PG8_LDA(At, 1, 1); PG8_STAGE(PG8_SB(1, 0), b3, vB0, vB1); PG8_STAGE(PG8_SB(1, 1), b3 + hstepB, vB0, vB1); PG8_STAGE(PG8_SA(1, 0), a3, cA00, cA01);
;             PG8_WAIT_V(8); PG8_WAIT_L(0); PG8_BAR; PG8_MMA(1, 0, At, B0); PG8_MMA(1, 1, At, B1); PG8_BAR; PG8_SCHED;
	s_waitcnt lgkmcnt(0)
	v_mfma_f32_16x16x128_f8f6f4 v[156:159], v[0:7], v[216:223], v[156:159]
	v_mfma_f32_16x16x128_f8f6f4 v[152:155], v[8:15], v[216:223], v[152:155]
	v_mfma_f32_16x16x128_f8f6f4 v[140:143], v[0:7], v[224:231], v[140:143]
	v_mfma_f32_16x16x128_f8f6f4 v[136:139], v[8:15], v[224:231], v[136:139]
	v_mfma_f32_16x16x128_f8f6f4 v[124:127], v[0:7], v[238:245], v[124:127]
	v_mfma_f32_16x16x128_f8f6f4 v[120:123], v[8:15], v[238:245], v[120:123]
	v_mfma_f32_16x16x128_f8f6f4 v[108:111], v[0:7], v[246:253], v[108:111]
	v_mfma_f32_16x16x128_f8f6f4 v[104:107], v[8:15], v[246:253], v[104:107]
	v_mfma_f32_16x16x128_f8f6f4 v[148:151], v[16:23], v[216:223], v[148:151]
	v_mfma_f32_16x16x128_f8f6f4 v[144:147], v[24:31], v[216:223], v[144:147]
	v_mfma_f32_16x16x128_f8f6f4 v[132:135], v[16:23], v[224:231], v[132:135]
	v_mfma_f32_16x16x128_f8f6f4 v[128:131], v[24:31], v[224:231], v[128:131]
	v_mfma_f32_16x16x128_f8f6f4 v[116:119], v[16:23], v[238:245], v[116:119]
	v_mfma_f32_16x16x128_f8f6f4 v[112:115], v[24:31], v[238:245], v[112:115]
	v_mfma_f32_16x16x128_f8f6f4 v[100:103], v[16:23], v[246:253], v[100:103]
	v_mfma_f32_16x16x128_f8f6f4 v[96:99], v[24:31], v[246:253], v[96:99]
	s_barrier
	s_add_i32 s40, s65, s97
	v_lshl_add_u64 v[190:191], v[190:191], 0, s[18:19]
	s_mov_b32 m0, s40
	ds_read_b128 v[216:219], v208 offset:49152
	ds_read_b128 v[220:223], v208 offset:50176
	ds_read_b128 v[224:227], v208 offset:51200
	ds_read_b128 v[228:231], v208 offset:52224
	ds_read_b128 v[238:241], v208 offset:53248
	ds_read_b128 v[242:245], v208 offset:54272
	ds_read_b128 v[246:249], v208 offset:55296
	ds_read_b128 v[250:253], v208 offset:56320
	global_load_lds_dwordx4 v[190:191], off
	v_lshl_add_u64 v[190:191], v[192:193], 0, s[18:19]
	s_add_i32 m0, s40, 0x2000
	v_lshl_add_u64 v[188:189], v[188:189], 0, s[20:21]
	s_add_i32 s40, s66, s97
	global_load_lds_dwordx4 v[190:191], off
	v_lshl_add_u64 v[190:191], v[188:189], 0, v[162:163]
	s_mov_b32 m0, s40
	v_lshl_add_u64 v[188:189], v[188:189], 0, v[164:165]
	global_load_lds_dwordx4 v[190:191], off
	s_add_i32 m0, s40, 0x2000
	s_nop 0
	global_load_lds_dwordx4 v[188:189], off
	v_lshl_add_u64 v[188:189], v[194:195], 0, s[18:19]
	s_mov_b32 m0, s54
	s_nop 0
	global_load_lds_dwordx4 v[188:189], off
	v_lshl_add_u64 v[188:189], v[196:197], 0, s[18:19]
	s_mov_b32 m0, s55
	s_nop 0
	global_load_lds_dwordx4 v[188:189], off
	s_waitcnt vmcnt(8)
	s_waitcnt lgkmcnt(0)
	s_barrier
	s_waitcnt lgkmcnt(0)
	v_mfma_f32_16x16x128_f8f6f4 v[92:95], v[0:7], v[216:223], v[92:95]
	v_mfma_f32_16x16x128_f8f6f4 v[88:91], v[8:15], v[216:223], v[88:91]
	v_mfma_f32_16x16x128_f8f6f4 v[76:79], v[0:7], v[224:231], v[76:79]
	v_mfma_f32_16x16x128_f8f6f4 v[72:75], v[8:15], v[224:231], v[72:75]
	v_mfma_f32_16x16x128_f8f6f4 v[60:63], v[0:7], v[238:245], v[60:63]
	v_mfma_f32_16x16x128_f8f6f4 v[56:59], v[8:15], v[238:245], v[56:59]
	v_mfma_f32_16x16x128_f8f6f4 v[44:47], v[0:7], v[246:253], v[44:47]
	v_mfma_f32_16x16x128_f8f6f4 v[40:43], v[8:15], v[246:253], v[40:43]
	v_mfma_f32_16x16x128_f8f6f4 v[84:87], v[16:23], v[216:223], v[84:87]
	v_mfma_f32_16x16x128_f8f6f4 v[80:83], v[24:31], v[216:223], v[80:83]
	v_mfma_f32_16x16x128_f8f6f4 v[68:71], v[16:23], v[224:231], v[68:71]
	v_mfma_f32_16x16x128_f8f6f4 v[64:67], v[24:31], v[224:231], v[64:67]
	v_mfma_f32_16x16x128_f8f6f4 v[52:55], v[16:23], v[238:245], v[52:55]
	v_mfma_f32_16x16x128_f8f6f4 v[48:51], v[24:31], v[238:245], v[48:51]
	v_mfma_f32_16x16x128_f8f6f4 v[36:39], v[16:23], v[246:253], v[36:39]
	v_mfma_f32_16x16x128_f8f6f4 v[32:35], v[24:31], v[246:253], v[32:35]
	s_barrier
	s_add_i32 s64, s64, 2
	s_add_u32 s36, s36, 0x100
	s_addc_u32 s37, s37, 0
	s_cmp_gt_u32 s64, 53
	v_lshl_add_u64 v[186:187], v[186:187], 0, s[22:23]
.LBB0_2173:
	ds_read_b128 v[24:27], v161
	ds_read_b128 v[28:31], v161 offset:1024
	ds_read_b128 v[16:19], v161 offset:2048
	ds_read_b128 v[20:23], v161 offset:3072
	ds_read_b128 v[8:11], v207
	ds_read_b128 v[12:15], v207 offset:1024
	ds_read_b128 v[0:3], v207 offset:2048
	ds_read_b128 v[4:7], v207 offset:3072
	s_add_u32 s40, s36, 0x80
	s_addc_u32 s41, s37, 0
	s_cmp_eq_u32 s64, 52
	s_cselect_b64 vcc, -1, 0
	s_cselect_b32 s41, s31, s41
	s_cselect_b32 s40, s30, s40
	v_cndmask_b32_e32 v189, v187, v185, vcc
	v_cndmask_b32_e32 v188, v186, v184, vcc
	v_lshl_add_u64 v[212:213], s[36:37], 0, v[182:183]
	s_add_i32 m0, s33, 0xc000
	ds_read_b128 v[190:193], v208
	ds_read_b128 v[194:197], v208 offset:1024
	ds_read_b128 v[216:219], v208 offset:2048
	ds_read_b128 v[220:223], v208 offset:3072
	ds_read_b128 v[224:227], v208 offset:4096
	ds_read_b128 v[228:231], v208 offset:5120
	ds_read_b128 v[238:241], v208 offset:6144
	ds_read_b128 v[242:245], v208 offset:7168
	global_load_lds_dwordx4 v[212:213], off
	v_lshl_add_u64 v[212:213], s[36:37], 0, v[180:181]
	s_add_i32 m0, s33, 0xe000
	s_nop 0
	global_load_lds_dwordx4 v[212:213], off
	s_waitcnt vmcnt(8)
	s_waitcnt lgkmcnt(0)
	s_barrier
	s_waitcnt lgkmcnt(0)
	v_mfma_f32_16x16x128_f8f6f4 v[156:159], v[24:31], v[190:197], v[156:159]
	v_mfma_f32_16x16x128_f8f6f4 v[152:155], v[16:23], v[190:197], v[152:155]
	v_mfma_f32_16x16x128_f8f6f4 v[140:143], v[24:31], v[216:223], v[140:143]
	v_mfma_f32_16x16x128_f8f6f4 v[136:139], v[16:23], v[216:223], v[136:139]
	v_mfma_f32_16x16x128_f8f6f4 v[124:127], v[24:31], v[224:231], v[124:127]
	v_mfma_f32_16x16x128_f8f6f4 v[120:123], v[16:23], v[224:231], v[120:123]
	v_mfma_f32_16x16x128_f8f6f4 v[108:111], v[24:31], v[238:245], v[108:111]
	v_mfma_f32_16x16x128_f8f6f4 v[104:107], v[16:23], v[238:245], v[104:107]
	v_mfma_f32_16x16x128_f8f6f4 v[148:151], v[8:15], v[190:197], v[148:151]
	v_mfma_f32_16x16x128_f8f6f4 v[144:147], v[0:7], v[190:197], v[144:147]
	v_mfma_f32_16x16x128_f8f6f4 v[132:135], v[8:15], v[216:223], v[132:135]
	v_mfma_f32_16x16x128_f8f6f4 v[128:131], v[0:7], v[216:223], v[128:131]
	v_mfma_f32_16x16x128_f8f6f4 v[116:119], v[8:15], v[224:231], v[116:119]
	v_mfma_f32_16x16x128_f8f6f4 v[112:115], v[0:7], v[224:231], v[112:115]
	v_mfma_f32_16x16x128_f8f6f4 v[100:103], v[8:15], v[238:245], v[100:103]
	v_mfma_f32_16x16x128_f8f6f4 v[96:99], v[0:7], v[238:245], v[96:99]
	s_barrier
; #define PG8_STAGE(bufoff, gbase, o0, o1) do { \
;         __builtin_amdgcn_global_load_lds((const unsigned*)((const char*)(gbase) + (o0)), (LAS unsigned*)(lds + (bufoff) + ldsw), 16, 0, 0); \
;         __builtin_amdgcn_global_load_lds((const unsigned*)((const char*)(gbase) + (o1)), (LAS unsigned*)(lds + (bufoff) + ldsw + 8192), 16, 0, 0); } while (0)
; #define PG8_LDA(dst, b, h) do { _Pragma("unroll") for (int m = 0; m < 4; ++m) _Pragma("unroll") for (int k = 0; k < 2; ++k) dst[m][k] = *(const LAS bf16x8*)(lds + PG8_SA(b, h) + aoff + m * 2048 + k * 1024); } while (0)
; #define PG8_LDB(dst, b, h) do { _Pragma("unroll") for (int n = 0; n < 2; ++n) _Pragma("unroll") for (int k = 0; k < 2; ++k) dst[n][k] = *(const LAS bf16x8*)(lds + PG8_SB(b, h) + boff + n * 2048 + k * 1024); } while (0)
; #define PG8_WAIT_V(n) asm volatile("s_waitcnt vmcnt(" #n ")" ::: "memory")
; #define PG8_WAIT_L(n) asm volatile("s_waitcnt lgkmcnt(" #n ")" ::: "memory")
; #define PG8_BAR __builtin_amdgcn_s_barrier()
; #define PG8_SCHED __builtin_amdgcn_sched_barrier(0)
; template <class Epi, class Sched, class Prob>
; __device__ __forceinline__ void gemm_phase(LAS unsigned char* lds, LAS unsigned char* lds_epi, const Prob g, const Sched& S, const Epi& E, int wid) {
;     ...
;             PG8_LDA(At, 0, 1); PG8_STAGE(PG8_SB(0, 0), b2, vB0, vB1); PG8_STAGE(PG8_SB(0, 1), b2 + hstepB, vB0, vB1); PG8_STAGE(PG8_SA(0, 0), a2, cA00, cA01);
;             PG8_WAIT_V(8); PG8_WAIT_L(0); PG8_BAR; PG8_MMA(1, 0, At, B0); PG8_MMA(1, 1, At, B1); PG8_BAR; PG8_SCHED;
;             PG8_LDB(B0, 1, 0); PG8_LDB(B1, 1, 1); PG8_SCHED; PG8_LDA(At, 1, 0); PG8_STAGE(PG8_SA(0, 1), a2, cA10, cA11);
	s_add_i32 s65, s58, s97
	v_lshl_add_u64 v[190:191], v[188:189], 0, v[162:163]
	s_mov_b32 m0, s65
	ds_read_b128 v[216:219], v208 offset:16384
	ds_read_b128 v[220:223], v208 offset:17408
	ds_read_b128 v[224:227], v208 offset:18432
	ds_read_b128 v[228:231], v208 offset:19456
	ds_read_b128 v[238:241], v208 offset:20480
	ds_read_b128 v[242:245], v208 offset:21504
	ds_read_b128 v[246:249], v208 offset:22528
	ds_read_b128 v[250:253], v208 offset:23552
	global_load_lds_dwordx4 v[190:191], off
	v_lshl_add_u64 v[192:193], v[188:189], 0, v[164:165]
	s_add_i32 m0, s65, 0x2000
	v_lshl_add_u64 v[194:195], v[188:189], 0, s[16:17]
	s_add_i32 s65, s59, s97
	global_load_lds_dwordx4 v[192:193], off
	v_lshl_add_u64 v[196:197], v[194:195], 0, v[162:163]
	s_mov_b32 m0, s65
	v_lshl_add_u64 v[194:195], v[194:195], 0, v[164:165]
	global_load_lds_dwordx4 v[196:197], off
	s_add_i32 m0, s65, 0x2000
	v_lshl_add_u64 v[196:197], s[40:41], 0, v[174:175]
	global_load_lds_dwordx4 v[194:195], off
	v_lshl_add_u64 v[194:195], s[40:41], 0, v[170:171]
	s_mov_b32 m0, s33
	s_nop 0
	global_load_lds_dwordx4 v[194:195], off
	s_mov_b32 m0, s35
	s_nop 0
	global_load_lds_dwordx4 v[196:197], off
	s_waitcnt vmcnt(8)
	s_waitcnt lgkmcnt(0)
	s_barrier
	s_waitcnt lgkmcnt(0)
	v_mfma_f32_16x16x128_f8f6f4 v[92:95], v[24:31], v[216:223], v[92:95]
	v_mfma_f32_16x16x128_f8f6f4 v[88:91], v[16:23], v[216:223], v[88:91]
	v_mfma_f32_16x16x128_f8f6f4 v[76:79], v[24:31], v[224:231], v[76:79]
	v_mfma_f32_16x16x128_f8f6f4 v[72:75], v[16:23], v[224:231], v[72:75]
	v_mfma_f32_16x16x128_f8f6f4 v[60:63], v[24:31], v[238:245], v[60:63]
	v_mfma_f32_16x16x128_f8f6f4 v[56:59], v[16:23], v[238:245], v[56:59]
	v_mfma_f32_16x16x128_f8f6f4 v[44:47], v[24:31], v[246:253], v[44:47]
	v_mfma_f32_16x16x128_f8f6f4 v[40:43], v[16:23], v[246:253], v[40:43]
	v_mfma_f32_16x16x128_f8f6f4 v[84:87], v[8:15], v[216:223], v[84:87]
	v_mfma_f32_16x16x128_f8f6f4 v[80:83], v[0:7], v[216:223], v[80:83]
	v_mfma_f32_16x16x128_f8f6f4 v[68:71], v[8:15], v[224:231], v[68:71]
	v_mfma_f32_16x16x128_f8f6f4 v[64:67], v[0:7], v[224:231], v[64:67]
	v_mfma_f32_16x16x128_f8f6f4 v[52:55], v[8:15], v[238:245], v[52:55]
	v_mfma_f32_16x16x128_f8f6f4 v[48:51], v[0:7], v[238:245], v[48:51]
	v_mfma_f32_16x16x128_f8f6f4 v[36:39], v[8:15], v[246:253], v[36:39]
	v_mfma_f32_16x16x128_f8f6f4 v[32:35], v[0:7], v[246:253], v[32:35]
	s_barrier
	s_add_i32 s65, 0, 0x18000
	s_add_i32 s66, 0, 0x1c000
	v_add_u32_e32 v12, s65, v204
	v_add_u32_e32 v28, s66, v204
	ds_read_b128 v[0:3], v12
	ds_read_b128 v[4:7], v12 offset:1024
	ds_read_b128 v[8:11], v12 offset:2048
	ds_read_b128 v[12:15], v12 offset:3072
	ds_read_b128 v[16:19], v28
	ds_read_b128 v[20:23], v28 offset:1024
	ds_read_b128 v[24:27], v28 offset:2048
	ds_read_b128 v[28:31], v28 offset:3072
	s_mov_b32 m0, s48
	v_lshl_add_u64 v[212:213], s[40:41], 0, v[172:173]
	ds_read_b128 v[216:219], v208 offset:32768
	ds_read_b128 v[220:223], v208 offset:33792
	ds_read_b128 v[224:227], v208 offset:34816
	ds_read_b128 v[228:231], v208 offset:35840
	ds_read_b128 v[238:241], v208 offset:36864
	ds_read_b128 v[242:245], v208 offset:37888
	ds_read_b128 v[246:249], v208 offset:38912
	ds_read_b128 v[250:253], v208 offset:39936
	global_load_lds_dwordx4 v[212:213], off
	v_lshl_add_u64 v[212:213], s[40:41], 0, v[176:177]
	s_mov_b32 m0, s52
	s_nop 0
	global_load_lds_dwordx4 v[212:213], off
	s_waitcnt vmcnt(8)
	s_waitcnt lgkmcnt(0)
	s_barrier
; #define PG8_STAGE(bufoff, gbase, o0, o1) do { \
;         __builtin_amdgcn_global_load_lds((const unsigned*)((const char*)(gbase) + (o0)), (LAS unsigned*)(lds + (bufoff) + ldsw), 16, 0, 0); \
;         __builtin_amdgcn_global_load_lds((const unsigned*)((const char*)(gbase) + (o1)), (LAS unsigned*)(lds + (bufoff) + ldsw + 8192), 16, 0, 0); } while (0)
; #define PG8_LDA(dst, b, h) do { _Pragma("unroll") for (int m = 0; m < 4; ++m) _Pragma("unroll") for (int k = 0; k < 2; ++k) dst[m][k] = *(const LAS bf16x8*)(lds + PG8_SA(b, h) + aoff + m * 2048 + k * 1024); } while (0)
; #define PG8_WAIT_V(n) asm volatile("s_waitcnt vmcnt(" #n ")" ::: "memory")
; #define PG8_WAIT_L(n) asm volatile("s_waitcnt lgkmcnt(" #n ")" ::: "memory")
; #define PG8_BAR __builtin_amdgcn_s_barrier()
; #define PG8_SCHED __builtin_amdgcn_sched_barrier(0)
; template <class Epi, class Sched, class Prob>
; __device__ __forceinline__ void gemm_phase(LAS unsigned char* lds, LAS unsigned char* lds_epi, const Prob g, const Sched& S, const Epi& E, int wid) {
;     ...
;             PG8_WAIT_V(8); PG8_WAIT_L(0); PG8_BAR; PG8_MMA(0, 0, At, B0); PG8_MMA(0, 1, At, B1); PG8_BAR; PG8_SCHED;
;             PG8_LDA(At, 1, 1); PG8_STAGE(PG8_SB(1, 0), b3, vB0, vB1); PG8_STAGE(PG8_SB(1, 1), b3 + hstepB, vB0, vB1); PG8_STAGE(PG8_SA(1, 0), a3, cA00, cA01);
;             PG8_WAIT_V(8); PG8_WAIT_L(0); PG8_BAR; PG8_MMA(1, 0, At, B0); PG8_MMA(1, 1, At, B1); PG8_BAR; PG8_SCHED;
;         }
;         if constexpr (Prob::FP8) asm volatile("s_nop 7\n\ts_nop 7\n\ts_nop 7" ::: "memory");
	s_waitcnt lgkmcnt(0)
	v_mfma_f32_16x16x128_f8f6f4 v[156:159], v[0:7], v[216:223], v[156:159]
	v_mfma_f32_16x16x128_f8f6f4 v[152:155], v[8:15], v[216:223], v[152:155]
	v_mfma_f32_16x16x128_f8f6f4 v[140:143], v[0:7], v[224:231], v[140:143]
	v_mfma_f32_16x16x128_f8f6f4 v[136:139], v[8:15], v[224:231], v[136:139]
	v_mfma_f32_16x16x128_f8f6f4 v[124:127], v[0:7], v[238:245], v[124:127]
	v_mfma_f32_16x16x128_f8f6f4 v[120:123], v[8:15], v[238:245], v[120:123]
	v_mfma_f32_16x16x128_f8f6f4 v[108:111], v[0:7], v[246:253], v[108:111]
	v_mfma_f32_16x16x128_f8f6f4 v[104:107], v[8:15], v[246:253], v[104:107]
	v_mfma_f32_16x16x128_f8f6f4 v[148:151], v[16:23], v[216:223], v[148:151]
	v_mfma_f32_16x16x128_f8f6f4 v[144:147], v[24:31], v[216:223], v[144:147]
	v_mfma_f32_16x16x128_f8f6f4 v[132:135], v[16:23], v[224:231], v[132:135]
	v_mfma_f32_16x16x128_f8f6f4 v[128:131], v[24:31], v[224:231], v[128:131]
	v_mfma_f32_16x16x128_f8f6f4 v[116:119], v[16:23], v[238:245], v[116:119]
	v_mfma_f32_16x16x128_f8f6f4 v[112:115], v[24:31], v[238:245], v[112:115]
	v_mfma_f32_16x16x128_f8f6f4 v[100:103], v[16:23], v[246:253], v[100:103]
	v_mfma_f32_16x16x128_f8f6f4 v[96:99], v[24:31], v[246:253], v[96:99]
	s_barrier
	s_add_i32 s40, s65, s97
	v_lshl_add_u64 v[190:191], v[190:191], 0, s[18:19]
	s_mov_b32 m0, s40
	ds_read_b128 v[216:219], v208 offset:49152
	ds_read_b128 v[220:223], v208 offset:50176
	ds_read_b128 v[224:227], v208 offset:51200
	ds_read_b128 v[228:231], v208 offset:52224
	ds_read_b128 v[238:241], v208 offset:53248
	ds_read_b128 v[242:245], v208 offset:54272
	ds_read_b128 v[246:249], v208 offset:55296
	ds_read_b128 v[250:253], v208 offset:56320
	global_load_lds_dwordx4 v[190:191], off
	v_lshl_add_u64 v[190:191], v[192:193], 0, s[18:19]
	s_add_i32 m0, s40, 0x2000
	v_lshl_add_u64 v[188:189], v[188:189], 0, s[20:21]
	s_add_i32 s40, s66, s97
	global_load_lds_dwordx4 v[190:191], off
	v_lshl_add_u64 v[190:191], v[188:189], 0, v[162:163]
	s_mov_b32 m0, s40
	v_lshl_add_u64 v[188:189], v[188:189], 0, v[164:165]
	global_load_lds_dwordx4 v[190:191], off
	s_add_i32 m0, s40, 0x2000
	s_nop 0
	global_load_lds_dwordx4 v[188:189], off
	v_lshl_add_u64 v[188:189], v[194:195], 0, s[18:19]
	s_mov_b32 m0, s54
	s_nop 0
	global_load_lds_dwordx4 v[188:189], off
	v_lshl_add_u64 v[188:189], v[196:197], 0, s[18:19]
	s_mov_b32 m0, s55
	s_nop 0
	global_load_lds_dwordx4 v[188:189], off
	s_waitcnt vmcnt(8)
	s_waitcnt lgkmcnt(0)
	s_barrier
	s_waitcnt lgkmcnt(0)
	v_mfma_f32_16x16x128_f8f6f4 v[92:95], v[0:7], v[216:223], v[92:95]
	v_mfma_f32_16x16x128_f8f6f4 v[88:91], v[8:15], v[216:223], v[88:91]
	v_mfma_f32_16x16x128_f8f6f4 v[76:79], v[0:7], v[224:231], v[76:79]
	v_mfma_f32_16x16x128_f8f6f4 v[72:75], v[8:15], v[224:231], v[72:75]
	v_mfma_f32_16x16x128_f8f6f4 v[60:63], v[0:7], v[238:245], v[60:63]
	v_mfma_f32_16x16x128_f8f6f4 v[56:59], v[8:15], v[238:245], v[56:59]
	v_mfma_f32_16x16x128_f8f6f4 v[44:47], v[0:7], v[246:253], v[44:47]
	v_mfma_f32_16x16x128_f8f6f4 v[40:43], v[8:15], v[246:253], v[40:43]
	v_mfma_f32_16x16x128_f8f6f4 v[84:87], v[16:23], v[216:223], v[84:87]
	v_mfma_f32_16x16x128_f8f6f4 v[80:83], v[24:31], v[216:223], v[80:83]
	v_mfma_f32_16x16x128_f8f6f4 v[68:71], v[16:23], v[224:231], v[68:71]
	v_mfma_f32_16x16x128_f8f6f4 v[64:67], v[24:31], v[224:231], v[64:67]
	v_mfma_f32_16x16x128_f8f6f4 v[52:55], v[16:23], v[238:245], v[52:55]
	v_mfma_f32_16x16x128_f8f6f4 v[48:51], v[24:31], v[238:245], v[48:51]
	v_mfma_f32_16x16x128_f8f6f4 v[36:39], v[16:23], v[246:253], v[36:39]
	v_mfma_f32_16x16x128_f8f6f4 v[32:35], v[24:31], v[246:253], v[32:35]
	s_barrier
	s_add_i32 s64, s64, 2
	s_add_u32 s36, s36, 0x100
	s_addc_u32 s37, s37, 0
	s_cmp_gt_u32 s64, 53
	v_lshl_add_u64 v[186:187], v[186:187], 0, s[22:23]
	s_cbranch_scc0 .LBB0_2173
	s_nop 7
	s_nop 7
	s_nop 7
	v_readlane_b32 s36, v254, 27
	v_readlane_b32 s37, v254, 28
	s_and_b64 vcc, exec, s[36:37]
	s_cbranch_vccz .LBB0_2176
	s_barrier

; #define PG8_STAGE(bufoff, gbase, o0, o1) do { \
;         __builtin_amdgcn_global_load_lds((const unsigned*)((const char*)(gbase) + (o0)), (LAS unsigned*)(lds + (bufoff) + ldsw), 16, 0, 0); \
;         __builtin_amdgcn_global_load_lds((const unsigned*)((const char*)(gbase) + (o1)), (LAS unsigned*)(lds + (bufoff) + ldsw + 8192), 16, 0, 0); } while (0)
; #define PG8_LDA(dst, b, h) do { _Pragma("unroll") for (int m = 0; m < 4; ++m) _Pragma("unroll") for (int k = 0; k < 2; ++k) dst[m][k] = *(const LAS bf16x8*)(lds + PG8_SA(b, h) + aoff + m * 2048 + k * 1024); } while (0)
; #define PG8_LDB(dst, b, h) do { _Pragma("unroll") for (int n = 0; n < 2; ++n) _Pragma("unroll") for (int k = 0; k < 2; ++k) dst[n][k] = *(const LAS bf16x8*)(lds + PG8_SB(b, h) + boff + n * 2048 + k * 1024); } while (0)
; #define PG8_WAIT_V(n) asm volatile("s_waitcnt vmcnt(" #n ")" ::: "memory")
; #define PG8_WAIT_L(n) asm volatile("s_waitcnt lgkmcnt(" #n ")" ::: "memory")
; #define PG8_BAR __builtin_amdgcn_s_barrier()
; #define PG8_SCHED __builtin_amdgcn_sched_barrier(0)
; template <class Epi, class Sched, class Prob>
; __device__ __forceinline__ void gemm_phase(LAS unsigned char* lds, LAS unsigned char* lds_epi, const Prob g, const Sched& S, const Epi& E, int wid) {
;     ...
;         for (int t = 0; t < nt; t += 2) {
;             const bool last = (t == nt - 2);
;             const char* a1 = cA + (size_t)(t + 1) * kstep;
;             const char* a2 = last ? nA : cA + (size_t)(t + 2) * kstep; const char* b2 = last ? nB : cB + (size_t)(t + 2) * kstep;
;             const char* a3 = a2 + kstep; const char* b3 = b2 + kstep;
;             PG8_LDB(B0, 0, 0); PG8_LDB(B1, 0, 1); PG8_SCHED; PG8_LDA(At, 0, 0); PG8_STAGE(PG8_SA(1, 1), a1, cA10, cA11);
;             PG8_WAIT_V(8); PG8_WAIT_L(0); PG8_BAR; PG8_MMA(0, 0, At, B0); PG8_MMA(0, 1, At, B1); PG8_BAR; PG8_SCHED;
;             PG8_LDA(At, 0, 1); PG8_STAGE(PG8_SB(0, 0), b2, vB0, vB1); PG8_STAGE(PG8_SB(0, 1), b2 + hstepB, vB0, vB1); PG8_STAGE(PG8_SA(0, 0), a2, cA00, cA01);
;             PG8_WAIT_V(8); PG8_WAIT_L(0); PG8_BAR; PG8_MMA(1, 0, At, B0); PG8_MMA(1, 1, At, B1); PG8_BAR; PG8_SCHED;
.LBB0_2191:
	ds_read_b128 v[24:27], v161
	ds_read_b128 v[28:31], v161 offset:1024
	ds_read_b128 v[16:19], v161 offset:2048
	ds_read_b128 v[20:23], v161 offset:3072
	ds_read_b128 v[8:11], v186
	ds_read_b128 v[12:15], v186 offset:1024
	ds_read_b128 v[0:3], v186 offset:2048
	ds_read_b128 v[4:7], v186 offset:3072
	s_add_u32 s18, s14, s16
	s_addc_u32 s19, s15, s17
	s_add_u32 s18, s18, 0x41000100
	s_addc_u32 s19, s19, 0
	s_add_u32 s47, s31, s16
	s_addc_u32 s48, s33, s17
	s_cmpk_eq_i32 s16, 0x600
	s_cselect_b32 s21, s5, s19
	s_cselect_b32 s20, s4, s18
	s_cselect_b32 s19, s11, s48
	s_cselect_b32 s18, s10, s47
	s_mov_b32 m0, s35
	v_lshl_add_u64 v[208:209], v[176:177], 0, s[16:17]
	ds_read_b128 v[178:181], v187
	ds_read_b128 v[182:185], v187 offset:1024
	ds_read_b128 v[190:193], v187 offset:2048
	ds_read_b128 v[194:197], v187 offset:3072
	ds_read_b128 v[200:203], v187 offset:4096
	ds_read_b128 v[204:207], v187 offset:5120
	ds_read_b128 v[216:219], v187 offset:6144
	ds_read_b128 v[220:223], v187 offset:7168
	global_load_lds_dwordx4 v[208:209], off
	v_lshl_add_u64 v[208:209], v[174:175], 0, s[16:17]
	s_mov_b32 m0, s36
	s_nop 0
	global_load_lds_dwordx4 v[208:209], off
	s_waitcnt vmcnt(8)
	s_waitcnt lgkmcnt(0)
	s_barrier
	s_waitcnt lgkmcnt(0)
	v_mfma_f32_16x16x128_f8f6f4 v[156:159], v[24:31], v[178:185], v[156:159]
	v_mfma_f32_16x16x128_f8f6f4 v[152:155], v[16:23], v[178:185], v[152:155]
	v_mfma_f32_16x16x128_f8f6f4 v[148:151], v[24:31], v[190:197], v[148:151]
	v_mfma_f32_16x16x128_f8f6f4 v[144:147], v[16:23], v[190:197], v[144:147]
	v_mfma_f32_16x16x128_f8f6f4 v[140:143], v[24:31], v[200:207], v[140:143]
	v_mfma_f32_16x16x128_f8f6f4 v[136:139], v[16:23], v[200:207], v[136:139]
	v_mfma_f32_16x16x128_f8f6f4 v[132:135], v[24:31], v[216:223], v[132:135]
	v_mfma_f32_16x16x128_f8f6f4 v[128:131], v[16:23], v[216:223], v[128:131]
	v_mfma_f32_16x16x128_f8f6f4 v[124:127], v[8:15], v[178:185], v[124:127]
	v_mfma_f32_16x16x128_f8f6f4 v[120:123], v[0:7], v[178:185], v[120:123]
	v_mfma_f32_16x16x128_f8f6f4 v[116:119], v[8:15], v[190:197], v[116:119]
	v_mfma_f32_16x16x128_f8f6f4 v[112:115], v[0:7], v[190:197], v[112:115]
	v_mfma_f32_16x16x128_f8f6f4 v[108:111], v[8:15], v[200:207], v[108:111]
	v_mfma_f32_16x16x128_f8f6f4 v[104:107], v[0:7], v[200:207], v[104:107]
	v_mfma_f32_16x16x128_f8f6f4 v[100:103], v[8:15], v[216:223], v[100:103]
	v_mfma_f32_16x16x128_f8f6f4 v[96:99], v[0:7], v[216:223], v[96:99]
	s_barrier
	s_mov_b32 m0, s37
	v_lshl_add_u64 v[178:179], s[18:19], 0, v[162:163]
	s_add_u32 s48, s18, 0xe0000
	ds_read_b128 v[190:193], v187 offset:16384
	ds_read_b128 v[194:197], v187 offset:17408
	ds_read_b128 v[200:203], v187 offset:18432
	ds_read_b128 v[204:207], v187 offset:19456
	ds_read_b128 v[216:219], v187 offset:20480
	ds_read_b128 v[220:223], v187 offset:21504
	ds_read_b128 v[224:227], v187 offset:22528
	ds_read_b128 v[228:231], v187 offset:23552
	global_load_lds_dwordx4 v[178:179], off
	v_lshl_add_u64 v[180:181], s[18:19], 0, v[164:165]
	s_mov_b32 m0, s40
	s_addc_u32 s49, s19, 0
	global_load_lds_dwordx4 v[180:181], off
	v_lshl_add_u64 v[182:183], s[48:49], 0, v[162:163]
	s_mov_b32 m0, s41
	v_lshl_add_u64 v[184:185], s[20:21], 0, v[168:169]
	global_load_lds_dwordx4 v[182:183], off
	v_lshl_add_u64 v[182:183], s[48:49], 0, v[164:165]
	s_mov_b32 m0, s42
	s_nop 0
	global_load_lds_dwordx4 v[182:183], off
	v_lshl_add_u64 v[182:183], s[20:21], 0, v[166:167]
	s_mov_b32 m0, s25
	s_nop 0
	global_load_lds_dwordx4 v[182:183], off
	s_mov_b32 m0, s26
	s_nop 0
	global_load_lds_dwordx4 v[184:185], off
	s_waitcnt vmcnt(8)
	s_waitcnt lgkmcnt(0)
	s_barrier
	s_waitcnt lgkmcnt(0)
	v_mfma_f32_16x16x128_f8f6f4 v[92:95], v[24:31], v[190:197], v[92:95]
	v_mfma_f32_16x16x128_f8f6f4 v[88:91], v[16:23], v[190:197], v[88:91]
	v_mfma_f32_16x16x128_f8f6f4 v[84:87], v[24:31], v[200:207], v[84:87]
	v_mfma_f32_16x16x128_f8f6f4 v[80:83], v[16:23], v[200:207], v[80:83]
	v_mfma_f32_16x16x128_f8f6f4 v[76:79], v[24:31], v[216:223], v[76:79]
	v_mfma_f32_16x16x128_f8f6f4 v[72:75], v[16:23], v[216:223], v[72:75]
	v_mfma_f32_16x16x128_f8f6f4 v[68:71], v[24:31], v[224:231], v[68:71]
	v_mfma_f32_16x16x128_f8f6f4 v[64:67], v[16:23], v[224:231], v[64:67]
	v_mfma_f32_16x16x128_f8f6f4 v[60:63], v[8:15], v[190:197], v[60:63]
	v_mfma_f32_16x16x128_f8f6f4 v[56:59], v[0:7], v[190:197], v[56:59]
	v_mfma_f32_16x16x128_f8f6f4 v[52:55], v[8:15], v[200:207], v[52:55]
	v_mfma_f32_16x16x128_f8f6f4 v[48:51], v[0:7], v[200:207], v[48:51]
	v_mfma_f32_16x16x128_f8f6f4 v[44:47], v[8:15], v[216:223], v[44:47]
	v_mfma_f32_16x16x128_f8f6f4 v[40:43], v[0:7], v[216:223], v[40:43]
	v_mfma_f32_16x16x128_f8f6f4 v[36:39], v[8:15], v[224:231], v[36:39]
	v_mfma_f32_16x16x128_f8f6f4 v[32:35], v[0:7], v[224:231], v[32:35]
	s_barrier
; #define PG8_STAGE(bufoff, gbase, o0, o1) do { \
;         __builtin_amdgcn_global_load_lds((const unsigned*)((const char*)(gbase) + (o0)), (LAS unsigned*)(lds + (bufoff) + ldsw), 16, 0, 0); \
;         __builtin_amdgcn_global_load_lds((const unsigned*)((const char*)(gbase) + (o1)), (LAS unsigned*)(lds + (bufoff) + ldsw + 8192), 16, 0, 0); } while (0)
; #define PG8_LDA(dst, b, h) do { _Pragma("unroll") for (int m = 0; m < 4; ++m) _Pragma("unroll") for (int k = 0; k < 2; ++k) dst[m][k] = *(const LAS bf16x8*)(lds + PG8_SA(b, h) + aoff + m * 2048 + k * 1024); } while (0)
; #define PG8_LDB(dst, b, h) do { _Pragma("unroll") for (int n = 0; n < 2; ++n) _Pragma("unroll") for (int k = 0; k < 2; ++k) dst[n][k] = *(const LAS bf16x8*)(lds + PG8_SB(b, h) + boff + n * 2048 + k * 1024); } while (0)
; #define PG8_WAIT_V(n) asm volatile("s_waitcnt vmcnt(" #n ")" ::: "memory")
; #define PG8_WAIT_L(n) asm volatile("s_waitcnt lgkmcnt(" #n ")" ::: "memory")
; #define PG8_BAR __builtin_amdgcn_s_barrier()
; #define PG8_SCHED __builtin_amdgcn_sched_barrier(0)
; template <class Epi, class Sched, class Prob>
; __device__ __forceinline__ void gemm_phase(LAS unsigned char* lds, LAS unsigned char* lds_epi, const Prob g, const Sched& S, const Epi& E, int wid) {
;     ...
;             PG8_LDB(B0, 1, 0); PG8_LDB(B1, 1, 1); PG8_SCHED; PG8_LDA(At, 1, 0); PG8_STAGE(PG8_SA(0, 1), a2, cA10, cA11);
;             PG8_WAIT_V(8); PG8_WAIT_L(0); PG8_BAR; PG8_MMA(0, 0, At, B0); PG8_MMA(0, 1, At, B1); PG8_BAR; PG8_SCHED;
;             PG8_LDA(At, 1, 1); PG8_STAGE(PG8_SB(1, 0), b3, vB0, vB1); PG8_STAGE(PG8_SB(1, 1), b3 + hstepB, vB0, vB1); PG8_STAGE(PG8_SA(1, 0), a3, cA00, cA01);
;             PG8_WAIT_V(8); PG8_WAIT_L(0); PG8_BAR; PG8_MMA(1, 0, At, B0); PG8_MMA(1, 1, At, B1); PG8_BAR; PG8_SCHED;
;         }
;         if constexpr (Prob::FP8) asm volatile("s_nop 7\n\ts_nop 7\n\ts_nop 7" ::: "memory");
;         if (wr == 0) PG8_BAR;
	ds_read_b128 v[0:3], v188
	ds_read_b128 v[4:7], v188 offset:1024
	ds_read_b128 v[8:11], v188 offset:2048
	ds_read_b128 v[12:15], v188 offset:3072
	ds_read_b128 v[16:19], v189
	ds_read_b128 v[20:23], v189 offset:1024
	ds_read_b128 v[24:27], v189 offset:2048
	ds_read_b128 v[28:31], v189 offset:3072
	s_mov_b32 m0, s27
	v_lshl_add_u64 v[208:209], s[20:21], 0, v[170:171]
	ds_read_b128 v[190:193], v187 offset:32768
	ds_read_b128 v[194:197], v187 offset:33792
	ds_read_b128 v[200:203], v187 offset:34816
	ds_read_b128 v[204:207], v187 offset:35840
	ds_read_b128 v[216:219], v187 offset:36864
	ds_read_b128 v[220:223], v187 offset:37888
	ds_read_b128 v[224:227], v187 offset:38912
	ds_read_b128 v[228:231], v187 offset:39936
	global_load_lds_dwordx4 v[208:209], off
	v_lshl_add_u64 v[208:209], s[20:21], 0, v[172:173]
	s_mov_b32 m0, s28
	s_nop 0
	global_load_lds_dwordx4 v[208:209], off
	s_waitcnt vmcnt(8)
	s_waitcnt lgkmcnt(0)
	s_barrier
	s_waitcnt lgkmcnt(0)
	v_mfma_f32_16x16x128_f8f6f4 v[156:159], v[0:7], v[190:197], v[156:159]
	v_mfma_f32_16x16x128_f8f6f4 v[152:155], v[8:15], v[190:197], v[152:155]
	v_mfma_f32_16x16x128_f8f6f4 v[148:151], v[0:7], v[200:207], v[148:151]
	v_mfma_f32_16x16x128_f8f6f4 v[144:147], v[8:15], v[200:207], v[144:147]
	v_mfma_f32_16x16x128_f8f6f4 v[140:143], v[0:7], v[216:223], v[140:143]
	v_mfma_f32_16x16x128_f8f6f4 v[136:139], v[8:15], v[216:223], v[136:139]
	v_mfma_f32_16x16x128_f8f6f4 v[132:135], v[0:7], v[224:231], v[132:135]
	v_mfma_f32_16x16x128_f8f6f4 v[128:131], v[8:15], v[224:231], v[128:131]
	v_mfma_f32_16x16x128_f8f6f4 v[124:127], v[16:23], v[190:197], v[124:127]
	v_mfma_f32_16x16x128_f8f6f4 v[120:123], v[24:31], v[190:197], v[120:123]
	v_mfma_f32_16x16x128_f8f6f4 v[116:119], v[16:23], v[200:207], v[116:119]
	v_mfma_f32_16x16x128_f8f6f4 v[112:115], v[24:31], v[200:207], v[112:115]
	v_mfma_f32_16x16x128_f8f6f4 v[108:111], v[16:23], v[216:223], v[108:111]
	v_mfma_f32_16x16x128_f8f6f4 v[104:107], v[24:31], v[216:223], v[104:107]
	v_mfma_f32_16x16x128_f8f6f4 v[100:103], v[16:23], v[224:231], v[100:103]
	v_mfma_f32_16x16x128_f8f6f4 v[96:99], v[24:31], v[224:231], v[96:99]
	s_barrier
	s_mov_b32 m0, s43
	v_lshl_add_u64 v[178:179], v[178:179], 0, s[12:13]
	s_add_u32 s18, s18, 0xe0080
	ds_read_b128 v[190:193], v187 offset:49152
	ds_read_b128 v[194:197], v187 offset:50176
	ds_read_b128 v[200:203], v187 offset:51200
	ds_read_b128 v[204:207], v187 offset:52224
	ds_read_b128 v[216:219], v187 offset:53248
	ds_read_b128 v[220:223], v187 offset:54272
	ds_read_b128 v[224:227], v187 offset:55296
	ds_read_b128 v[228:231], v187 offset:56320
	global_load_lds_dwordx4 v[178:179], off
	v_lshl_add_u64 v[178:179], v[180:181], 0, s[12:13]
	s_mov_b32 m0, s44
	s_addc_u32 s19, s19, 0
	global_load_lds_dwordx4 v[178:179], off
	v_lshl_add_u64 v[178:179], s[18:19], 0, v[162:163]
	s_mov_b32 m0, s45
	s_nop 0
	global_load_lds_dwordx4 v[178:179], off
	v_lshl_add_u64 v[178:179], s[18:19], 0, v[164:165]
	s_mov_b32 m0, s46
	s_nop 0
	global_load_lds_dwordx4 v[178:179], off
	v_lshl_add_u64 v[178:179], v[182:183], 0, s[12:13]
	s_mov_b32 m0, s29
	s_nop 0
	global_load_lds_dwordx4 v[178:179], off
	v_lshl_add_u64 v[178:179], v[184:185], 0, s[12:13]
	s_mov_b32 m0, s30
	s_nop 0
	global_load_lds_dwordx4 v[178:179], off
	s_waitcnt vmcnt(8)
	s_waitcnt lgkmcnt(0)
	s_barrier
	s_waitcnt lgkmcnt(0)
	v_mfma_f32_16x16x128_f8f6f4 v[92:95], v[0:7], v[190:197], v[92:95]
	v_mfma_f32_16x16x128_f8f6f4 v[88:91], v[8:15], v[190:197], v[88:91]
	v_mfma_f32_16x16x128_f8f6f4 v[84:87], v[0:7], v[200:207], v[84:87]
	v_mfma_f32_16x16x128_f8f6f4 v[80:83], v[8:15], v[200:207], v[80:83]
	v_mfma_f32_16x16x128_f8f6f4 v[76:79], v[0:7], v[216:223], v[76:79]
	v_mfma_f32_16x16x128_f8f6f4 v[72:75], v[8:15], v[216:223], v[72:75]
	v_mfma_f32_16x16x128_f8f6f4 v[68:71], v[0:7], v[224:231], v[68:71]
	v_mfma_f32_16x16x128_f8f6f4 v[64:67], v[8:15], v[224:231], v[64:67]
	v_mfma_f32_16x16x128_f8f6f4 v[60:63], v[16:23], v[190:197], v[60:63]
	v_mfma_f32_16x16x128_f8f6f4 v[56:59], v[24:31], v[190:197], v[56:59]
	v_mfma_f32_16x16x128_f8f6f4 v[52:55], v[16:23], v[200:207], v[52:55]
	v_mfma_f32_16x16x128_f8f6f4 v[48:51], v[24:31], v[200:207], v[48:51]
	v_mfma_f32_16x16x128_f8f6f4 v[44:47], v[16:23], v[216:223], v[44:47]
	v_mfma_f32_16x16x128_f8f6f4 v[40:43], v[24:31], v[216:223], v[40:43]
	v_mfma_f32_16x16x128_f8f6f4 v[36:39], v[16:23], v[224:231], v[36:39]
	v_mfma_f32_16x16x128_f8f6f4 v[32:35], v[24:31], v[224:231], v[32:35]
	s_barrier
	s_add_i32 s34, s34, 2
	s_add_u32 s16, s16, 0x100
	s_addc_u32 s17, s17, 0
	s_cmp_gt_u32 s34, 11
	s_cbranch_scc0 .LBB0_2191
	s_nop 7
	s_nop 7
	s_nop 7
	v_readlane_b32 s4, v254, 27
	v_readlane_b32 s5, v254, 28
	s_and_b64 vcc, exec, s[4:5]
	s_cbranch_vccz .LBB0_2194
	s_barrier
